# wave reductions: ds_bpermute xor-butterfly hops replaced by DPP moves (8,4,2,1) and permlane16/32 swaps; on top of hand-written grid barrier
# speedup vs baseline: 1.0246x; 1.0036x over previous
; __device__ __forceinline__ unsigned cvt_pk_bf16(float lo, float hi) { const f32x2 v = {lo, hi}; const bf16x2_t b = __builtin_convertvector(v, bf16x2_t); return __builtin_bit_cast(unsigned, b); }
; __device__ __forceinline__ void rms_mod_store(const f32x4 (&x)[8], const float* g, const float* scale, const float* shift, bf16_t* orow, f32x4 (&y)[8], int lane) {
;     float ss = 0.f;
; #pragma unroll
;     for (int j = 0; j < 8; ++j) ss += x[j][0] * x[j][0] + x[j][1] * x[j][1] + x[j][2] * x[j][2] + x[j][3] * x[j][3];
;     ss = wave_sum(ss);
;     const float rinv = rsqrtf(ss * (1.0f / DM) + EPS);
; #pragma unroll
;     for (int j = 0; j < 8; ++j) { const int c = j * 256 + lane * 4;
;         const f32x4 gv = *(const f32x4*)(g + c), sc = *(const f32x4*)(scale + c), sh = *(const f32x4*)(shift + c);
;         y[j] = x[j] * rinv * gv * (1.0f + sc) + sh; }
; #pragma unroll
;     for (int j = 0; j < 8; ++j) { const int c = j * 256 + lane * 4; u32x2 w; w.x = cvt_pk_bf16(y[j][0], y[j][1]); w.y = cvt_pk_bf16(y[j][2], y[j][3]); *(u32x2*)(orow + c) = w; }
; }
; __device__ __forceinline__ void ph_norm1_tables(const Params& p) {
;     ...
;     for (int it = blockIdx.x; it < N1_ROWITEMS; it += gridDim.x) {
;         {
;             const int row = it * 8 + wave; const int rr = row < NLAT ? (row >> 11) : 4;
;             const float* xr = row < NLAT ? p.in[I_X] + (size_t)row * DM : p.in[I_CTX] + (size_t)(row - NLAT) * DM;
;             f32x4 x[8], y[8];
; #pragma unroll
;             for (int j = 0; j < 8; ++j) x[j] = *(const f32x4*)(xr + j * 256 + lane * 4);
;             const float* m = mod + (size_t)rr * 12288;
;             rms_mod_store(x, p.in[I_N1G], m + DM, m, (bf16_t*)(ws + WS_H) + (size_t)row * DM, y, lane);
;         }
;     }
.LBB0_147:
	s_or_b64 exec, exec, s[6:7]
	v_lshl_add_u64 v[2:3], v[2:3], 0, v[54:55]
	global_load_dwordx4 v[30:33], v[2:3], off
	global_load_dwordx4 v[26:29], v[2:3], off offset:1024
	global_load_dwordx4 v[22:25], v[2:3], off offset:2048
	global_load_dwordx4 v[14:17], v[2:3], off offset:3072
	v_add_co_u32_e32 v6, vcc, s10, v2
	v_min_i32_e32 v65, 0x2000, v52
	s_nop 0
	v_addc_co_u32_e32 v7, vcc, 0, v3, vcc
	global_load_dwordx4 v[10:13], v[6:7], off offset:1024
	global_load_dwordx4 v[18:21], v[6:7], off
	global_load_dwordx4 v[2:5], v[6:7], off offset:3072
	s_nop 0
	global_load_dwordx4 v[6:9], v[6:7], off offset:2048
	v_ashrrev_i32_e32 v65, 11, v65
	v_mul_hi_i32_i24_e32 v95, 0xc000, v65
	v_mul_i32_i24_e32 v94, 0xc000, v65
	v_lshl_add_u64 v[162:163], s[0:1], 0, v[94:95]
	v_mov_b32_e32 v59, v39
	v_lshl_add_u64 v[158:159], v[162:163], 0, s[4:5]
	v_lshl_add_u64 v[114:115], v[158:159], 0, v[58:59]
	v_mov_b32_e32 v61, v39
	v_lshl_add_u64 v[122:123], v[162:163], 0, v[54:55]
	v_lshl_add_u64 v[102:103], v[158:159], 0, v[54:55]
	v_lshl_add_u64 v[118:119], v[158:159], 0, v[56:57]
	v_lshl_add_u64 v[110:111], v[158:159], 0, v[38:39]
	v_lshl_add_u64 v[126:127], v[158:159], 0, v[60:61]
	global_load_dwordx4 v[34:37], v[40:41], off
	global_load_dwordx4 v[74:77], v[40:41], off offset:1024
	global_load_dwordx4 v[78:81], v[40:41], off offset:2048
	global_load_dwordx4 v[82:85], v[40:41], off offset:3072
	global_load_dwordx4 v[86:89], v[42:43], off
	global_load_dwordx4 v[90:93], v[44:45], off
	v_mov_b32_e32 v63, v39
	global_load_dwordx4 v[94:97], v[122:123], off offset:1024
	global_load_dwordx4 v[98:101], v[122:123], off offset:2048
	s_nop 0
	global_load_dwordx4 v[102:105], v[102:103], off
	s_nop 0
	global_load_dwordx4 v[106:109], v[122:123], off
	s_nop 0
	global_load_dwordx4 v[110:113], v[110:111], off
	s_nop 0
	global_load_dwordx4 v[114:117], v[114:115], off
	s_nop 0
	global_load_dwordx4 v[118:121], v[118:119], off
	s_nop 0
	global_load_dwordx4 v[122:125], v[122:123], off offset:3072
	s_nop 0
	global_load_dwordx4 v[126:129], v[126:127], off
	v_lshlrev_b64 v[166:167], 12, v[52:53]
	s_add_i32 s12, s12, s94
	s_cmpk_lt_i32 s12, 0x480
	v_add_u32_e32 v52, s8, v52
	s_waitcnt vmcnt(22)
	v_mul_f32_e32 v59, v31, v31
	s_waitcnt vmcnt(21)
	v_mul_f32_e32 v65, v27, v27
	s_waitcnt vmcnt(20)
	v_mul_f32_e32 v67, v23, v23
	v_fmac_f32_e32 v59, v30, v30
	v_fmac_f32_e32 v65, v26, v26
	s_waitcnt vmcnt(19)
	v_mul_f32_e32 v146, v15, v15
	v_fmac_f32_e32 v67, v22, v22
	v_fmac_f32_e32 v59, v32, v32
	v_fmac_f32_e32 v65, v28, v28
	s_waitcnt vmcnt(18)
	v_mov_b32_e32 v132, v11
	s_waitcnt vmcnt(17)
	v_mov_b32_e32 v133, v19
	v_fmac_f32_e32 v146, v14, v14
	v_fmac_f32_e32 v67, v24, v24
	v_mov_b32_e32 v130, v10
	v_mov_b32_e32 v131, v18
	v_fmac_f32_e32 v59, v33, v33
	v_fmac_f32_e32 v65, v29, v29
	v_pk_mul_f32 v[132:133], v[132:133], v[132:133]
	v_fmac_f32_e32 v146, v16, v16
	v_mov_b32_e32 v134, v12
	v_mov_b32_e32 v135, v20
	s_waitcnt vmcnt(16)
	v_mov_b32_e32 v140, v3
	s_waitcnt vmcnt(15)
	v_mov_b32_e32 v141, v7
	v_fmac_f32_e32 v67, v25, v25
	v_add_f32_e32 v59, v59, v65
	v_pk_fma_f32 v[130:131], v[130:131], v[130:131], v[132:133]
	v_mov_b32_e32 v136, v13
	v_mov_b32_e32 v137, v21
	v_mov_b32_e32 v138, v2
	v_mov_b32_e32 v139, v6
	v_fmac_f32_e32 v146, v17, v17
	v_pk_mul_f32 v[140:141], v[140:141], v[140:141]
	v_add_f32_e32 v59, v67, v59
	v_pk_fma_f32 v[130:131], v[134:135], v[134:135], v[130:131]
	v_mov_b32_e32 v142, v4
	v_mov_b32_e32 v143, v8
	v_pk_fma_f32 v[132:133], v[138:139], v[138:139], v[140:141]
	v_add_f32_e32 v59, v146, v59
	v_pk_fma_f32 v[130:131], v[136:137], v[136:137], v[130:131]
	v_mov_b32_e32 v144, v5
	v_mov_b32_e32 v145, v9
	v_pk_fma_f32 v[132:133], v[142:143], v[142:143], v[132:133]
	v_add_f32_e32 v59, v131, v59
	v_pk_fma_f32 v[132:133], v[144:145], v[144:145], v[132:133]
	v_add_f32_e32 v59, v130, v59
	v_add_f32_e32 v59, v133, v59
	v_add_f32_e32 v59, v132, v59
	v_mov_b32_e32 v67, v59
	s_nop 1
	v_permlane32_swap_b32_e32 v67, v59
	v_lshl_add_u64 v[130:131], v[162:163], 0, v[60:61]
	v_lshl_add_u64 v[138:139], v[158:159], 0, v[62:63]
	global_load_dwordx4 v[130:133], v[130:131], off
	s_nop 0
	global_load_dwordx4 v[134:137], v[46:47], off
	v_mov_b32_e32 v65, v39
	s_waitcnt lgkmcnt(0)
	v_add_f32_e32 v59, v59, v67
	global_load_dwordx4 v[138:141], v[138:139], off
	v_lshl_add_u64 v[142:143], v[162:163], 0, v[62:63]
	v_mov_b32_e32 v67, v39
	global_load_dwordx4 v[142:145], v[142:143], off
	v_lshl_add_u64 v[150:151], v[162:163], 0, v[64:65]
	v_lshl_add_u64 v[146:147], v[158:159], 0, v[64:65]
	v_lshl_add_u64 v[158:159], v[158:159], 0, v[66:67]
	global_load_dwordx4 v[146:149], v[146:147], off
	s_nop 0
	global_load_dwordx4 v[150:153], v[150:151], off
	v_lshl_add_u64 v[162:163], v[162:163], 0, v[66:67]
	global_load_dwordx4 v[154:157], v[48:49], off
	v_mov_b32_e32 v61, v59
	s_nop 1
	v_permlane16_swap_b32_e32 v61, v59
	global_load_dwordx4 v[158:161], v[158:159], off
	s_waitcnt vmcnt(14)
	v_pk_add_f32 v[104:105], v[104:105], 1.0 op_sel_hi:[1,0]
	global_load_dwordx4 v[162:165], v[162:163], off
	v_pk_add_f32 v[102:103], v[102:103], 1.0 op_sel_hi:[1,0]
	s_waitcnt lgkmcnt(0)
	v_add_f32_e32 v59, v59, v61
	s_nop 1
	v_mov_b32_dpp v61, v59 row_ror:8 row_mask:0xf bank_mask:0xf
	s_waitcnt lgkmcnt(0)
; __device__ __forceinline__ unsigned cvt_pk_bf16(float lo, float hi) { const f32x2 v = {lo, hi}; const bf16x2_t b = __builtin_convertvector(v, bf16x2_t); return __builtin_bit_cast(unsigned, b); }
; __device__ __forceinline__ float wave_sum(float v) {
; #pragma unroll
;     for (int o = 32; o >= 1; o >>= 1) v += __shfl_xor(v, o);
;     return v;
; }
; __device__ __forceinline__ void rms_mod_store(const f32x4 (&x)[8], const float* g, const float* scale, const float* shift, bf16_t* orow, f32x4 (&y)[8], int lane) {
;     ...
;     const float rinv = rsqrtf(ss * (1.0f / DM) + EPS);
; #pragma unroll
;     for (int j = 0; j < 8; ++j) { const int c = j * 256 + lane * 4;
;         const f32x4 gv = *(const f32x4*)(g + c), sc = *(const f32x4*)(scale + c), sh = *(const f32x4*)(shift + c);
;         y[j] = x[j] * rinv * gv * (1.0f + sc) + sh; }
; #pragma unroll
;     for (int j = 0; j < 8; ++j) { const int c = j * 256 + lane * 4; u32x2 w; w.x = cvt_pk_bf16(y[j][0], y[j][1]); w.y = cvt_pk_bf16(y[j][2], y[j][3]); *(u32x2*)(orow + c) = w; }
	v_add_f32_e32 v59, v59, v61
	s_nop 1
	v_mov_b32_dpp v61, v59 row_shl:4 row_mask:0xf bank_mask:0x5
	v_mov_b32_dpp v61, v59 row_shr:4 row_mask:0xf bank_mask:0xa
	s_waitcnt lgkmcnt(0)
	v_add_f32_e32 v59, v59, v61
	s_nop 1
	v_mov_b32_dpp v61, v59 quad_perm:[2,3,0,1] row_mask:0xf bank_mask:0xf
	s_waitcnt lgkmcnt(0)
	v_add_f32_e32 v59, v59, v61
	s_nop 1
	v_mov_b32_dpp v61, v59 quad_perm:[1,0,3,2] row_mask:0xf bank_mask:0xf
	s_waitcnt lgkmcnt(0)
	v_add_f32_e32 v59, v59, v61
	v_fmamk_f32 v59, v59, 0x3a000000, v73
	v_mul_f32_e32 v61, 0x4b800000, v59
	v_cmp_gt_f32_e32 vcc, s11, v59
	s_nop 1
	v_cndmask_b32_e32 v59, v59, v61, vcc
	v_rsq_f32_e32 v59, v59
	s_nop 0
	v_mul_f32_e32 v53, 0x45800000, v59
	v_cndmask_b32_e32 v168, v59, v53, vcc
	v_pk_mul_f32 v[32:33], v[32:33], v[168:169] op_sel_hi:[1,0]
	v_pk_mul_f32 v[30:31], v[30:31], v[168:169] op_sel_hi:[1,0]
	v_pk_mul_f32 v[28:29], v[28:29], v[168:169] op_sel_hi:[1,0]
	v_pk_mul_f32 v[26:27], v[26:27], v[168:169] op_sel_hi:[1,0]
	v_pk_mul_f32 v[30:31], v[34:35], v[30:31]
	v_pk_mul_f32 v[32:33], v[36:37], v[32:33]
	v_pk_mul_f32 v[26:27], v[74:75], v[26:27]
	v_pk_mul_f32 v[28:29], v[76:77], v[28:29]
	s_waitcnt vmcnt(11)
	v_pk_add_f32 v[34:35], v[120:121], 1.0 op_sel_hi:[1,0]
	v_pk_add_f32 v[36:37], v[118:119], 1.0 op_sel_hi:[1,0]
	v_pk_mul_f32 v[24:25], v[24:25], v[168:169] op_sel_hi:[1,0]
	v_pk_mul_f32 v[22:23], v[22:23], v[168:169] op_sel_hi:[1,0]
	v_pk_fma_f32 v[28:29], v[34:35], v[28:29], v[96:97]
	v_pk_fma_f32 v[26:27], v[36:37], v[26:27], v[94:95]
	v_pk_mul_f32 v[22:23], v[78:79], v[22:23]
	v_pk_mul_f32 v[24:25], v[80:81], v[24:25]
	v_pk_add_f32 v[34:35], v[112:113], 1.0 op_sel_hi:[1,0]
	v_pk_add_f32 v[36:37], v[110:111], 1.0 op_sel_hi:[1,0]
	v_pk_mul_f32 v[16:17], v[16:17], v[168:169] op_sel_hi:[1,0]
	v_pk_mul_f32 v[14:15], v[14:15], v[168:169] op_sel_hi:[1,0]
	v_pk_fma_f32 v[24:25], v[34:35], v[24:25], v[100:101]
	v_pk_fma_f32 v[22:23], v[36:37], v[22:23], v[98:99]
	v_pk_mul_f32 v[14:15], v[82:83], v[14:15]
	v_pk_mul_f32 v[16:17], v[84:85], v[16:17]
	v_pk_add_f32 v[34:35], v[116:117], 1.0 op_sel_hi:[1,0]
	v_pk_add_f32 v[36:37], v[114:115], 1.0 op_sel_hi:[1,0]
	v_pk_mul_f32 v[20:21], v[20:21], v[168:169] op_sel_hi:[1,0]
	v_pk_mul_f32 v[18:19], v[18:19], v[168:169] op_sel_hi:[1,0]
	s_waitcnt vmcnt(10)
	v_pk_fma_f32 v[16:17], v[34:35], v[16:17], v[124:125]
	v_pk_fma_f32 v[14:15], v[36:37], v[14:15], v[122:123]
	v_pk_mul_f32 v[18:19], v[86:87], v[18:19]
	v_pk_mul_f32 v[20:21], v[88:89], v[20:21]
	s_waitcnt vmcnt(9)
	v_pk_add_f32 v[34:35], v[128:129], 1.0 op_sel_hi:[1,0]
	v_pk_add_f32 v[36:37], v[126:127], 1.0 op_sel_hi:[1,0]
	v_pk_mul_f32 v[12:13], v[12:13], v[168:169] op_sel_hi:[1,0]
	v_pk_mul_f32 v[10:11], v[10:11], v[168:169] op_sel_hi:[1,0]
	s_waitcnt vmcnt(8)
	v_pk_fma_f32 v[20:21], v[34:35], v[20:21], v[132:133]
	v_pk_fma_f32 v[18:19], v[36:37], v[18:19], v[130:131]
	v_pk_mul_f32 v[10:11], v[10:11], v[90:91]
	v_pk_mul_f32 v[12:13], v[12:13], v[92:93]
	s_waitcnt vmcnt(6)
	v_pk_add_f32 v[34:35], v[140:141], 1.0 op_sel_hi:[1,0]
	v_pk_add_f32 v[36:37], v[138:139], 1.0 op_sel_hi:[1,0]
	v_pk_mul_f32 v[8:9], v[8:9], v[168:169] op_sel_hi:[1,0]
	v_pk_mul_f32 v[6:7], v[6:7], v[168:169] op_sel_hi:[1,0]
	s_waitcnt vmcnt(5)
	v_pk_fma_f32 v[12:13], v[12:13], v[34:35], v[144:145]
	v_pk_fma_f32 v[10:11], v[10:11], v[36:37], v[142:143]
	v_pk_mul_f32 v[6:7], v[6:7], v[134:135]
	v_pk_mul_f32 v[8:9], v[8:9], v[136:137]
	s_waitcnt vmcnt(4)
	v_pk_add_f32 v[34:35], v[148:149], 1.0 op_sel_hi:[1,0]
	v_pk_add_f32 v[36:37], v[146:147], 1.0 op_sel_hi:[1,0]
	v_pk_mul_f32 v[4:5], v[4:5], v[168:169] op_sel_hi:[1,0]
	v_pk_mul_f32 v[2:3], v[2:3], v[168:169] op_sel_hi:[1,0]
	v_pk_fma_f32 v[32:33], v[104:105], v[32:33], v[108:109]
	v_pk_fma_f32 v[30:31], v[102:103], v[30:31], v[106:107]
	s_waitcnt vmcnt(3)
	v_pk_fma_f32 v[8:9], v[8:9], v[34:35], v[152:153]
	v_pk_fma_f32 v[6:7], v[6:7], v[36:37], v[150:151]
	s_waitcnt vmcnt(2)
	v_pk_mul_f32 v[2:3], v[2:3], v[154:155]
	v_pk_mul_f32 v[4:5], v[4:5], v[156:157]
	s_waitcnt vmcnt(1)
	v_pk_add_f32 v[34:35], v[160:161], 1.0 op_sel_hi:[1,0]
	v_pk_add_f32 v[36:37], v[158:159], 1.0 op_sel_hi:[1,0]
	s_waitcnt vmcnt(0)
	v_pk_fma_f32 v[4:5], v[4:5], v[34:35], v[164:165]
	v_pk_fma_f32 v[2:3], v[2:3], v[36:37], v[162:163]
	v_cvt_pk_bf16_f32 v30, v30, v31
	v_cvt_pk_bf16_f32 v31, v32, v33
	v_lshl_add_u64 v[32:33], v[50:51], 0, v[166:167]
	v_cvt_pk_bf16_f32 v14, v14, v15
	v_cvt_pk_bf16_f32 v15, v16, v17
	v_cvt_pk_bf16_f32 v26, v26, v27
	v_cvt_pk_bf16_f32 v27, v28, v29
	v_cvt_pk_bf16_f32 v22, v22, v23
	v_cvt_pk_bf16_f32 v23, v24, v25
	global_store_dwordx2 v[32:33], v[14:15], off offset:1536
	v_cvt_pk_bf16_f32 v14, v18, v19
	v_cvt_pk_bf16_f32 v15, v20, v21
	v_cvt_pk_bf16_f32 v10, v10, v11
	v_cvt_pk_bf16_f32 v11, v12, v13
	v_cvt_pk_bf16_f32 v6, v6, v7
	v_cvt_pk_bf16_f32 v7, v8, v9
	v_cvt_pk_bf16_f32 v2, v2, v3
	v_cvt_pk_bf16_f32 v3, v4, v5
	global_store_dwordx2 v[32:33], v[30:31], off
	global_store_dwordx2 v[32:33], v[26:27], off offset:512
	global_store_dwordx2 v[32:33], v[22:23], off offset:1024
	global_store_dwordx2 v[32:33], v[14:15], off offset:2048
	global_store_dwordx2 v[32:33], v[10:11], off offset:2560
	global_store_dwordx2 v[32:33], v[6:7], off offset:3072
	global_store_dwordx2 v[32:33], v[2:3], off offset:3584
	s_cbranch_scc0 .LBB0_152

; #define LAS __attribute__((address_space(3)))
; __device__ __forceinline__ unsigned cvt_pk_bf16(float lo, float hi) { const f32x2 v = {lo, hi}; const bf16x2_t b = __builtin_convertvector(v, bf16x2_t); return __builtin_bit_cast(unsigned, b); }
; __device__ __forceinline__ void sgu_unit(const Params& p, int l, int un, LAS unsigned char* lds) {
;     ...
;     const int cc = un >> 2, h = un & 3; const int row0 = cc * 128;
;     LAS bf16_t* Wl = (LAS bf16_t*)lds;
;     LAS bf16_t* Vl = (LAS bf16_t*)(lds + 128 * 136 * 2);
;     const float* Wg = p.in[I_SGUW] + ((size_t)l * 4 + h) * 128 * 128;
;     f32x4 wq[8]; u32x4 vv[16];
; #pragma unroll
;     for (int i = 0; i < 8; ++i) wq[i] = *(const f32x4*)(Wg + (i * 512 + tid) * 4);
; #pragma unroll
;     for (int qi = 0; qi < 16; ++qi) vv[qi] = *(const u32x4*)(P + (size_t)(row0 + wave * 16 + qi) * INP + C_SGU_V + lane * 8);
; #pragma unroll
;     for (int i = 0; i < 8; ++i) { const int e4 = (i * 512 + tid) * 4, r = e4 >> 7, c = e4 & 127; const f32x4 v = wq[i];
;         u32x2 w; w.x = cvt_pk_bf16(v[0], v[1]); w.y = cvt_pk_bf16(v[2], v[3]); *(LAS u32x2*)(Wl + r * 136 + c) = w; }
.LBB0_474:
	s_and_b64 vcc, exec, s[2:3]
	s_cbranch_vccz .LBB0_539
	s_cmpk_gt_i32 s31, 0x47f
	s_cbranch_scc0 .LBB0_511
	s_cmpk_gt_u32 s31, 0x59f
	s_cbranch_scc1 .LBB0_510
	v_mov_b32_e32 v64, v0
	s_mov_b64 s[0:1], 0
	s_add_u32 s42, s84, s0
	s_addc_u32 s43, s85, s1
	s_add_u32 s14, s42, 0x1f1b8000
	s_addc_u32 s15, s43, 0
	s_and_b32 s0, s31, 3
	v_readlane_b32 s44, v251, 16
	s_lshl_b32 s19, s0, 7
	v_readlane_b32 s45, v251, 17
	v_readlane_b32 s46, v251, 18
	v_readlane_b32 s47, v251, 19
	v_readlane_b32 s48, v251, 20
	v_readlane_b32 s49, v251, 21
	v_readlane_b32 s50, v251, 22
	v_readlane_b32 s51, v251, 23
	s_lshl_b32 s1, s31, 5
	s_or_b32 s4, s19, s18
	v_readlane_b32 s52, v251, 24
	v_readlane_b32 s53, v251, 25
	v_readlane_b32 s54, v251, 26
	v_readlane_b32 s55, v251, 27
	s_mov_b64 s[44:45], s[48:49]
	s_add_i32 s1, s1, 0x7fff7000
	s_lshl_b64 s[2:3], s[4:5], 9
	s_mov_b64 s[46:47], s[50:51]
	s_add_u32 s2, s46, s2
	v_lshlrev_b32_e32 v2, 2, v64
	s_addc_u32 s3, s47, s3
	v_ashrrev_i32_e32 v3, 31, v2
	v_add_u32_e32 v62, 0x800, v2
	v_lshl_add_u64 v[4:5], v[2:3], 2, s[2:3]
	v_ashrrev_i32_e32 v63, 31, v62
	v_lshl_add_u64 v[6:7], v[62:63], 2, s[2:3]
	global_load_dwordx4 v[66:69], v[4:5], off
	global_load_dwordx4 v[70:73], v[6:7], off
	v_add_u32_e32 v126, 0x1000, v2
	v_ashrrev_i32_e32 v127, 31, v126
	v_add_u32_e32 v128, 0x1800, v2
	v_lshl_add_u64 v[4:5], v[126:127], 2, s[2:3]
	v_ashrrev_i32_e32 v129, 31, v128
	v_lshl_add_u64 v[6:7], v[128:129], 2, s[2:3]
	global_load_dwordx4 v[98:101], v[4:5], off
	global_load_dwordx4 v[102:105], v[6:7], off
	v_add_u32_e32 v130, 0x2000, v2
	v_ashrrev_i32_e32 v131, 31, v130
	v_add_u32_e32 v132, 0x2800, v2
	v_lshl_add_u64 v[4:5], v[130:131], 2, s[2:3]
	v_ashrrev_i32_e32 v133, 31, v132
	v_lshl_add_u64 v[6:7], v[132:133], 2, s[2:3]
	global_load_dwordx4 v[106:109], v[4:5], off
	global_load_dwordx4 v[110:113], v[6:7], off
	v_add_u32_e32 v134, 0x3000, v2
	v_add_u32_e32 v136, 0x3800, v2
	v_ashrrev_i32_e32 v135, 31, v134
	v_ashrrev_i32_e32 v137, 31, v136
	v_ashrrev_i32_e32 v127, 6, v64
	v_lshl_add_u64 v[4:5], v[134:135], 2, s[2:3]
	v_lshl_add_u64 v[2:3], v[136:137], 2, s[2:3]
	s_and_b32 s60, s1, 0x7fffff80
	v_lshlrev_b32_e32 v65, 4, v127
	v_and_b32_e32 v8, 63, v64
	global_load_dwordx4 v[114:117], v[4:5], off
	global_load_dwordx4 v[118:121], v[2:3], off
	v_add_u32_e32 v9, s60, v65
	v_mov_b64_e32 v[2:3], s[14:15]
	s_movk_i32 s1, 0x1e00
	v_mad_i64_i32 v[4:5], s[2:3], v9, s1, v[2:3]
	v_lshlrev_b32_e32 v206, 4, v8
	v_or_b32_e32 v6, 1, v9
	v_lshl_add_u64 v[4:5], v[4:5], 0, v[206:207]
	v_mad_i64_i32 v[6:7], s[2:3], v6, s1, v[2:3]
	v_lshl_add_u64 v[6:7], v[6:7], 0, v[206:207]
	global_load_dwordx4 v[122:125], v[4:5], off offset:1024
	global_load_dwordx4 v[58:61], v[6:7], off offset:1024
	v_or_b32_e32 v4, 2, v9
	v_or_b32_e32 v6, 3, v9
	v_mad_i64_i32 v[4:5], s[2:3], v4, s1, v[2:3]
	v_mad_i64_i32 v[6:7], s[2:3], v6, s1, v[2:3]
	v_lshl_add_u64 v[4:5], v[4:5], 0, v[206:207]
	v_lshl_add_u64 v[6:7], v[6:7], 0, v[206:207]
	global_load_dwordx4 v[54:57], v[4:5], off offset:1024
	global_load_dwordx4 v[50:53], v[6:7], off offset:1024
	v_or_b32_e32 v4, 4, v9
	v_or_b32_e32 v6, 5, v9
	v_mad_i64_i32 v[4:5], s[2:3], v4, s1, v[2:3]
	v_mad_i64_i32 v[6:7], s[2:3], v6, s1, v[2:3]
	v_lshl_add_u64 v[4:5], v[4:5], 0, v[206:207]
	v_lshl_add_u64 v[6:7], v[6:7], 0, v[206:207]
	global_load_dwordx4 v[46:49], v[4:5], off offset:1024
	global_load_dwordx4 v[42:45], v[6:7], off offset:1024
	v_or_b32_e32 v4, 6, v9
	v_or_b32_e32 v6, 7, v9
	v_mad_i64_i32 v[4:5], s[2:3], v4, s1, v[2:3]
	v_mad_i64_i32 v[6:7], s[2:3], v6, s1, v[2:3]
	v_lshl_add_u64 v[4:5], v[4:5], 0, v[206:207]
	v_lshl_add_u64 v[6:7], v[6:7], 0, v[206:207]
	global_load_dwordx4 v[38:41], v[4:5], off offset:1024
	global_load_dwordx4 v[34:37], v[6:7], off offset:1024
	v_or_b32_e32 v4, 8, v9
	v_or_b32_e32 v6, 9, v9
	v_mad_i64_i32 v[4:5], s[2:3], v4, s1, v[2:3]
	v_mad_i64_i32 v[6:7], s[2:3], v6, s1, v[2:3]
	v_lshl_add_u64 v[4:5], v[4:5], 0, v[206:207]
	v_lshl_add_u64 v[6:7], v[6:7], 0, v[206:207]
	global_load_dwordx4 v[30:33], v[4:5], off offset:1024
	global_load_dwordx4 v[26:29], v[6:7], off offset:1024
	v_or_b32_e32 v4, 10, v9
	v_or_b32_e32 v6, 11, v9
	v_mad_i64_i32 v[4:5], s[2:3], v4, s1, v[2:3]
	v_mad_i64_i32 v[6:7], s[2:3], v6, s1, v[2:3]
	v_lshl_add_u64 v[4:5], v[4:5], 0, v[206:207]
	v_lshl_add_u64 v[6:7], v[6:7], 0, v[206:207]
	global_load_dwordx4 v[22:25], v[4:5], off offset:1024
	global_load_dwordx4 v[18:21], v[6:7], off offset:1024
	v_or_b32_e32 v4, 12, v9
	v_or_b32_e32 v6, 13, v9
	v_mad_i64_i32 v[4:5], s[2:3], v4, s1, v[2:3]
	v_mad_i64_i32 v[6:7], s[2:3], v6, s1, v[2:3]
	v_lshl_add_u64 v[4:5], v[4:5], 0, v[206:207]
	v_lshl_add_u64 v[6:7], v[6:7], 0, v[206:207]
	v_lshlrev_b32_e32 v129, 3, v64
	global_load_dwordx4 v[14:17], v[4:5], off offset:1024
	global_load_dwordx4 v[10:13], v[6:7], off offset:1024
	v_or_b32_e32 v4, 14, v9
	v_or_b32_e32 v6, 15, v9
	v_and_b32_e32 v63, 0xf8, v129
	v_mad_i64_i32 v[4:5], s[2:3], v4, s1, v[2:3]
	v_mad_i64_i32 v[2:3], s[2:3], v6, s1, v[2:3]
	v_add_u32_e32 v138, 0, v63
	v_bfe_i32 v63, v64, 5, 25
	s_movk_i32 s44, 0x110
	v_lshl_add_u64 v[4:5], v[4:5], 0, v[206:207]
	v_lshl_add_u64 v[2:3], v[2:3], 0, v[206:207]
	s_waitcnt vmcnt(21)
	v_cvt_pk_bf16_f32 v66, v66, v67
	v_cvt_pk_bf16_f32 v67, v68, v69
	v_mad_u64_u32 v[68:69], s[2:3], v63, s44, v[138:139]
	global_load_dwordx4 v[6:9], v[4:5], off offset:1024
	s_nop 0
	global_load_dwordx4 v[2:5], v[2:3], off offset:1024
	ds_write_b64 v68, v[66:67]
	v_ashrrev_i32_e32 v66, 7, v62
	s_waitcnt vmcnt(22)
	v_cvt_pk_bf16_f32 v62, v70, v71
	v_cvt_pk_bf16_f32 v63, v72, v73
	v_mad_u64_u32 v[66:67], s[2:3], v66, s44, v[138:139]
	ds_write_b64 v66, v[62:63]
	v_ashrrev_i32_e32 v66, 7, v126
	s_waitcnt vmcnt(21)
; #define LAS __attribute__((address_space(3)))
; __device__ __forceinline__ unsigned cvt_pk_bf16(float lo, float hi) { const f32x2 v = {lo, hi}; const bf16x2_t b = __builtin_convertvector(v, bf16x2_t); return __builtin_bit_cast(unsigned, b); }
; __device__ __forceinline__ float bflo(unsigned w) { return __uint_as_float(w << 16); }
; __device__ __forceinline__ float bfhi(unsigned w) { return __uint_as_float(w & 0xffff0000u); }
; __device__ __forceinline__ unsigned short f2bf(float f) { return (unsigned short)(cvt_pk_bf16(f, 0.f) & 0xffffu); }
; __device__ __forceinline__ float wave_sum(float v) {
; #pragma unroll
;     for (int o = 32; o >= 1; o >>= 1) v += __shfl_xor(v, o);
;     return v;
; }
; __device__ __forceinline__ void sgu_unit(const Params& p, int l, int un, LAS unsigned char* lds) {
;     ...
;     for (int i = 0; i < 8; ++i) { const int e4 = (i * 512 + tid) * 4, r = e4 >> 7, c = e4 & 127; const f32x4 v = wq[i];
;         u32x2 w; w.x = cvt_pk_bf16(v[0], v[1]); w.y = cvt_pk_bf16(v[2], v[3]); *(LAS u32x2*)(Wl + r * 136 + c) = w; }
; #pragma unroll
;     for (int qi = 0; qi < 16; ++qi) { const int q = wave * 16 + qi;
;         const u32x4 v = vv[qi]; float f[8] = {bflo(v.x), bfhi(v.x), bflo(v.y), bfhi(v.y), bflo(v.z), bfhi(v.z), bflo(v.w), bfhi(v.w)}; float ss = 0.f;
; #pragma unroll
;         for (int j = 0; j < 8; ++j) { f[j] = gelu_tanh(f[j]); ss += f[j] * f[j]; }
;         ss = wave_sum(ss); const float rinv = rsqrtf(ss * (1.0f / 512.0f) + EPS);
;         if ((lane >> 4) == h) { const int c0 = (lane & 15) * 8; const float* g = p.in[I_SGUNG] + l * 512 + h * 128 + c0;
; #pragma unroll
;             for (int j = 0; j < 8; ++j) Vl[(c0 + j) * 136 + q] = f2bf(f[j] * rinv * g[j]); } }
	v_cvt_pk_bf16_f32 v62, v98, v99
	v_cvt_pk_bf16_f32 v63, v100, v101
	v_mad_u64_u32 v[66:67], s[2:3], v66, s44, v[138:139]
	ds_write_b64 v66, v[62:63]
	v_ashrrev_i32_e32 v66, 7, v128
	s_waitcnt vmcnt(20)
	v_cvt_pk_bf16_f32 v62, v102, v103
	v_cvt_pk_bf16_f32 v63, v104, v105
	v_mad_u64_u32 v[66:67], s[2:3], v66, s44, v[138:139]
	ds_write_b64 v66, v[62:63]
	v_ashrrev_i32_e32 v66, 7, v130
	s_waitcnt vmcnt(19)
	v_cvt_pk_bf16_f32 v62, v106, v107
	v_cvt_pk_bf16_f32 v63, v108, v109
	v_mad_u64_u32 v[66:67], s[2:3], v66, s44, v[138:139]
	ds_write_b64 v66, v[62:63]
	v_ashrrev_i32_e32 v66, 7, v132
	s_waitcnt vmcnt(18)
	v_cvt_pk_bf16_f32 v62, v110, v111
	v_cvt_pk_bf16_f32 v63, v112, v113
	v_mad_u64_u32 v[66:67], s[2:3], v66, s44, v[138:139]
	ds_write_b64 v66, v[62:63]
	v_ashrrev_i32_e32 v66, 7, v134
	s_waitcnt vmcnt(17)
	v_cvt_pk_bf16_f32 v62, v114, v115
	v_cvt_pk_bf16_f32 v63, v116, v117
	v_mad_u64_u32 v[66:67], s[2:3], v66, s44, v[138:139]
	ds_write_b64 v66, v[62:63]
	v_ashrrev_i32_e32 v66, 7, v136
	v_mad_u64_u32 v[66:67], s[2:3], v66, s44, v[138:139]
	s_waitcnt vmcnt(15)
	v_and_b32_e32 v67, 0xffff0000, v122
	v_mul_f32_e32 v77, 0x3dd2d3e8, v67
	v_fma_f32 v77, -v77, v67, s33
	v_mul_f32_e32 v77, v77, v67
	v_exp_f32_e32 v77, v77
	v_cvt_pk_bf16_f32 v62, v118, v119
	v_cvt_pk_bf16_f32 v63, v120, v121
	ds_write_b64 v66, v[62:63]
	v_lshlrev_b32_e32 v66, 16, v122
	v_add_f32_e32 v77, 1.0, v77
	v_mul_f32_e32 v73, 0x3dd2d3e8, v66
	v_rcp_f32_e32 v77, v77
	v_fma_f32 v73, -v73, v66, s33
	v_mul_f32_e32 v73, v73, v66
	v_lshlrev_b32_e32 v70, 16, v123
	v_exp_f32_e32 v73, v73
	v_mul_f32_e32 v102, v77, v67
	v_mul_f32_e32 v67, 0x3dd2d3e8, v70
	v_fma_f32 v67, -v67, v70, s33
	v_mul_f32_e32 v67, v67, v70
	v_add_f32_e32 v73, 1.0, v73
	v_exp_f32_e32 v67, v67
	v_rcp_f32_e32 v73, v73
	v_lshlrev_b32_e32 v72, 16, v124
	v_and_b32_e32 v71, 0xffff0000, v123
	v_add_f32_e32 v67, 1.0, v67
	v_mul_f32_e32 v77, 0x3dd2d3e8, v72
	v_mul_f32_e32 v104, v73, v66
	v_mul_f32_e32 v73, 0x3dd2d3e8, v71
	v_rcp_f32_e32 v67, v67
	v_fma_f32 v77, -v77, v72, s33
	v_fma_f32 v73, -v73, v71, s33
	v_mul_f32_e32 v77, v77, v72
	v_mul_f32_e32 v73, v73, v71
	v_exp_f32_e32 v77, v77
	v_and_b32_e32 v98, 0xffff0000, v124
	v_exp_f32_e32 v73, v73
	v_mul_f32_e32 v103, v67, v70
	v_mul_f32_e32 v70, 0x3dd2d3e8, v98
	v_fma_f32 v70, -v70, v98, s33
	v_add_f32_e32 v67, 1.0, v77
	v_mul_f32_e32 v70, v70, v98
	v_add_f32_e32 v73, 1.0, v73
	v_rcp_f32_e32 v67, v67
	v_exp_f32_e32 v70, v70
	v_rcp_f32_e32 v73, v73
	v_lshlrev_b32_e32 v105, 16, v125
	v_and_b32_e32 v106, 0xffff0000, v125
	v_mul_f32_e32 v99, v67, v72
	v_add_f32_e32 v67, 1.0, v70
	v_mul_f32_e32 v70, 0x3dd2d3e8, v105
	v_mul_f32_e32 v101, v73, v71
	v_fma_f32 v70, -v70, v105, s33
	v_mul_f32_e32 v71, 0x3dd2d3e8, v106
	v_mul_f32_e32 v70, v70, v105
	v_fma_f32 v71, -v71, v106, s33
	v_rcp_f32_e32 v67, v67
	v_exp_f32_e32 v70, v70
	v_mul_f32_e32 v71, v71, v106
	v_exp_f32_e32 v71, v71
	v_mul_f32_e32 v66, v102, v102
	v_mul_f32_e32 v100, v67, v98
	v_add_f32_e32 v67, 1.0, v70
	v_fmac_f32_e32 v66, v104, v104
	v_rcp_f32_e32 v67, v67
	v_add_f32_e32 v70, 1.0, v71
	v_fmac_f32_e32 v66, v103, v103
	v_rcp_f32_e32 v70, v70
	v_and_b32_e32 v62, 64, v249
	v_fmac_f32_e32 v66, v101, v101
	v_add_u32_e32 v62, 64, v62
	v_xor_b32_e32 v63, 32, v249
	v_fmac_f32_e32 v66, v99, v99
	v_cmp_lt_i32_e32 vcc, v63, v62
	v_fmac_f32_e32 v66, v100, v100
	v_mul_f32_e32 v98, v67, v105
	v_cndmask_b32_e32 v63, v249, v63, vcc
	v_fmac_f32_e32 v66, v98, v98
	v_mul_f32_e32 v77, v70, v106
	v_lshlrev_b32_e32 v68, 2, v63
	v_fmac_f32_e32 v66, v77, v77
	v_mov_b32_e32 v67, v66
	s_nop 1
	v_permlane32_swap_b32_e32 v67, v66
	v_xor_b32_e32 v63, 16, v249
	v_cmp_lt_i32_e32 vcc, v63, v62
	v_lshl_add_u32 v107, v127, 5, 0
	v_readlane_b32 s56, v251, 28
	v_cndmask_b32_e32 v63, v249, v63, vcc
	v_lshlrev_b32_e32 v69, 2, v63
	s_waitcnt lgkmcnt(0)
	v_add_f32_e32 v66, v66, v67
	v_mov_b32_e32 v67, v66
	s_nop 1
	v_permlane16_swap_b32_e32 v67, v66
	v_xor_b32_e32 v63, 8, v249
	v_cmp_lt_i32_e32 vcc, v63, v62
	v_readlane_b32 s57, v251, 29
	v_readlane_b32 s58, v251, 30
	v_cndmask_b32_e32 v63, v249, v63, vcc
	v_lshlrev_b32_e32 v70, 2, v63
	s_waitcnt lgkmcnt(0)
	v_add_f32_e32 v66, v66, v67
	s_nop 1
	v_mov_b32_dpp v67, v66 row_ror:8 row_mask:0xf bank_mask:0xf
	v_xor_b32_e32 v63, 4, v249
	v_cmp_lt_i32_e32 vcc, v63, v62
	v_readlane_b32 s59, v251, 31
	s_mov_b64 s[48:49], s[52:53]
	v_cndmask_b32_e32 v63, v249, v63, vcc
	v_lshlrev_b32_e32 v71, 2, v63
	v_xor_b32_e32 v63, 2, v249
	s_waitcnt lgkmcnt(0)
	v_add_f32_e32 v67, v66, v67
	v_cmp_lt_i32_e32 vcc, v63, v62
	s_nop 1
	v_mov_b32_dpp v105, v67 row_shl:4 row_mask:0xf bank_mask:0x5
	v_mov_b32_dpp v105, v67 row_shr:4 row_mask:0xf bank_mask:0xa
	v_bfe_u32 v66, v64, 4, 2
	v_cndmask_b32_e32 v63, v249, v63, vcc
	v_lshlrev_b32_e32 v72, 2, v63
	v_xor_b32_e32 v63, 1, v249
	v_cmp_lt_i32_e32 vcc, v63, v62
	s_mov_b64 s[50:51], s[54:55]
	s_nop 0
	v_cndmask_b32_e32 v62, v249, v63, vcc
	v_lshlrev_b32_e32 v73, 2, v62
	s_waitcnt lgkmcnt(0)
	v_add_f32_e32 v62, v67, v105
	s_nop 1
	v_mov_b32_dpp v63, v62 quad_perm:[2,3,0,1] row_mask:0xf bank_mask:0xf
	v_cmp_eq_u32_e32 vcc, s0, v66
	s_lshl_b32 s0, s0, 9
	v_and_b32_e32 v67, 0x78, v129
	s_add_u32 s0, s25, s0
	s_waitcnt lgkmcnt(0)
	v_add_f32_e32 v105, v62, v63
	s_nop 1
	v_mov_b32_dpp v106, v105 quad_perm:[1,0,3,2] row_mask:0xf bank_mask:0xf
	s_addc_u32 s1, s26, 0
	v_lshlrev_b32_e32 v206, 2, v67
	v_lshl_add_u64 v[62:63], s[0:1], 0, v[206:207]
	v_mad_u32_u24 v67, v67, s44, v107
	s_and_saveexec_b64 s[0:1], vcc
	s_cbranch_execz .LBB0_479
	s_waitcnt lgkmcnt(0)
	v_add_f32_e32 v105, v105, v106
	v_fmamk_f32 v105, v105, 0x3b000000, v246
	s_mov_b32 s2, 0x800000
	v_cmp_gt_f32_e64 s[2:3], s2, v105
	v_mul_f32_e32 v106, 0x4b800000, v105
	s_nop 0
	v_cndmask_b32_e64 v105, v105, v106, s[2:3]
	v_rsq_f32_e32 v105, v105
	s_nop 0
	v_mul_f32_e32 v106, 0x45800000, v105
	v_cndmask_b32_e64 v112, v105, v106, s[2:3]
	v_mul_f32_e32 v113, v104, v112
	global_load_dwordx4 v[104:107], v[62:63], off offset:16
	global_load_dwordx4 v[108:111], v[62:63], off
	v_mul_f32_e32 v102, v102, v112
	v_mul_f32_e32 v99, v99, v112
	v_mul_f32_e32 v101, v101, v112
	v_mul_f32_e32 v98, v98, v112
	v_mul_f32_e32 v77, v77, v112
	s_waitcnt vmcnt(1)
	v_mul_f32_e32 v99, v99, v104
	s_waitcnt vmcnt(0)
	v_mul_f32_e32 v102, v102, v109
	v_cvt_pk_bf16_f32 v102, v102, s0
	v_cvt_pk_bf16_f32 v99, v99, s0
	ds_write_b16 v67, v102 offset:35088
	v_mul_f32_e32 v102, v103, v112
	ds_write_b16 v67, v99 offset:35904
	v_mul_f32_e32 v99, v100, v112
	v_mul_f32_e32 v108, v113, v108
	v_mul_f32_e32 v102, v102, v110
	v_mul_f32_e32 v101, v101, v111
	v_mul_f32_e32 v99, v99, v105
	v_mul_f32_e32 v98, v98, v106
	v_mul_f32_e32 v77, v77, v107
	v_cvt_pk_bf16_f32 v108, v108, s0
	v_cvt_pk_bf16_f32 v102, v102, s0
	v_cvt_pk_bf16_f32 v101, v101, s0
	v_cvt_pk_bf16_f32 v99, v99, s0
	v_cvt_pk_bf16_f32 v98, v98, s0
	v_cvt_pk_bf16_f32 v77, v77, s0
	ds_write_b16 v67, v108 offset:34816
	ds_write_b16 v67, v102 offset:35360
	ds_write_b16 v67, v101 offset:35632
	ds_write_b16 v67, v99 offset:36176
	ds_write_b16 v67, v98 offset:36448
	ds_write_b16 v67, v77 offset:36720
; __device__ __forceinline__ float bflo(unsigned w) { return __uint_as_float(w << 16); }
; __device__ __forceinline__ float bfhi(unsigned w) { return __uint_as_float(w & 0xffff0000u); }
; __device__ __forceinline__ unsigned short f2bf(float f) { return (unsigned short)(cvt_pk_bf16(f, 0.f) & 0xffffu); }
; __device__ __forceinline__ void sgu_unit(const Params& p, int l, int un, LAS unsigned char* lds) {
;     ...
;     for (int qi = 0; qi < 16; ++qi) { const int q = wave * 16 + qi;
;         const u32x4 v = vv[qi]; float f[8] = {bflo(v.x), bfhi(v.x), bflo(v.y), bfhi(v.y), bflo(v.z), bfhi(v.z), bflo(v.w), bfhi(v.w)}; float ss = 0.f;
; #pragma unroll
;         for (int j = 0; j < 8; ++j) { f[j] = gelu_tanh(f[j]); ss += f[j] * f[j]; }
;         ss = wave_sum(ss); const float rinv = rsqrtf(ss * (1.0f / 512.0f) + EPS);
;         if ((lane >> 4) == h) { const int c0 = (lane & 15) * 8; const float* g = p.in[I_SGUNG] + l * 512 + h * 128 + c0;
; #pragma unroll
;             for (int j = 0; j < 8; ++j) Vl[(c0 + j) * 136 + q] = f2bf(f[j] * rinv * g[j]); } }
.LBB0_479:
	s_or_b64 exec, exec, s[0:1]
	s_waitcnt vmcnt(14)
	v_lshlrev_b32_e32 v77, 16, v58
	v_lshlrev_b32_e32 v98, 16, v59
	v_and_b32_e32 v100, 0xffff0000, v59
	v_mul_f32_e32 v59, 0x3dd2d3e8, v77
	v_fma_f32 v59, -v59, v77, s33
	v_mul_f32_e32 v59, v59, v77
	v_exp_f32_e32 v59, v59
	v_and_b32_e32 v58, 0xffff0000, v58
	v_lshlrev_b32_e32 v101, 16, v60
	v_and_b32_e32 v102, 0xffff0000, v60
	v_add_f32_e32 v59, 1.0, v59
	v_rcp_f32_e32 v59, v59
	v_mul_f32_e32 v60, 0x3dd2d3e8, v100
	v_fma_f32 v60, -v60, v100, s33
	v_mul_f32_e32 v60, v60, v100
	v_mul_f32_e32 v99, v59, v77
	v_mul_f32_e32 v59, 0x3dd2d3e8, v58
	v_fma_f32 v59, -v59, v58, s33
	v_mul_f32_e32 v59, v59, v58
	v_exp_f32_e32 v59, v59
	v_exp_f32_e32 v60, v60
	v_lshlrev_b32_e32 v103, 16, v61
	v_and_b32_e32 v104, 0xffff0000, v61
	v_add_f32_e32 v59, 1.0, v59
	v_rcp_f32_e32 v59, v59
	v_add_f32_e32 v60, 1.0, v60
	v_rcp_f32_e32 v60, v60
	v_mul_f32_e32 v61, 0x3dd2d3e8, v101
	v_mul_f32_e32 v59, v59, v58
	v_mul_f32_e32 v58, 0x3dd2d3e8, v98
	v_fma_f32 v58, -v58, v98, s33
	v_mul_f32_e32 v58, v58, v98
	v_exp_f32_e32 v58, v58
	v_fma_f32 v61, -v61, v101, s33
	v_mul_f32_e32 v77, 0x3dd2d3e8, v102
	v_mul_f32_e32 v61, v61, v101
	v_add_f32_e32 v58, 1.0, v58
	v_rcp_f32_e32 v58, v58
	v_fma_f32 v77, -v77, v102, s33
	v_mul_f32_e32 v60, v60, v100
	v_exp_f32_e32 v61, v61
	v_mul_f32_e32 v58, v58, v98
	v_mul_f32_e32 v98, 0x3dd2d3e8, v103
	v_mul_f32_e32 v77, v77, v102
	v_fma_f32 v98, -v98, v103, s33
	v_mul_f32_e32 v100, 0x3dd2d3e8, v104
	v_exp_f32_e32 v77, v77
	v_mul_f32_e32 v98, v98, v103
	v_fma_f32 v100, -v100, v104, s33
	v_exp_f32_e32 v98, v98
	v_mul_f32_e32 v100, v100, v104
	v_exp_f32_e32 v100, v100
	v_add_f32_e32 v61, 1.0, v61
	v_rcp_f32_e32 v61, v61
	v_add_f32_e32 v77, 1.0, v77
	v_mul_f32_e32 v105, v59, v59
	v_rcp_f32_e32 v77, v77
	v_add_f32_e32 v98, 1.0, v98
	v_fmac_f32_e32 v105, v99, v99
	v_rcp_f32_e32 v98, v98
	v_add_f32_e32 v100, 1.0, v100
	v_fmac_f32_e32 v105, v58, v58
	v_rcp_f32_e32 v100, v100
	v_fmac_f32_e32 v105, v60, v60
	v_mul_f32_e32 v61, v61, v101
	v_fmac_f32_e32 v105, v61, v61
	v_mul_f32_e32 v77, v77, v102
	v_fmac_f32_e32 v105, v77, v77
	v_mul_f32_e32 v98, v98, v103
	v_fmac_f32_e32 v105, v98, v98
	v_mul_f32_e32 v100, v100, v104
	v_fmac_f32_e32 v105, v100, v100
	ds_bpermute_b32 v101, v68, v105
	s_waitcnt lgkmcnt(0)
	v_add_f32_e32 v101, v105, v101
	v_mov_b32_e32 v102, v101
	s_nop 1
	v_permlane16_swap_b32_e32 v102, v101
	s_waitcnt lgkmcnt(0)
	v_add_f32_e32 v101, v101, v102
	s_nop 1
	v_mov_b32_dpp v102, v101 row_ror:8 row_mask:0xf bank_mask:0xf
	s_waitcnt lgkmcnt(0)
	v_add_f32_e32 v101, v101, v102
	s_nop 1
	v_mov_b32_dpp v102, v101 row_shl:4 row_mask:0xf bank_mask:0x5
	v_mov_b32_dpp v102, v101 row_shr:4 row_mask:0xf bank_mask:0xa
	s_waitcnt lgkmcnt(0)
	v_add_f32_e32 v101, v101, v102
	s_nop 1
	v_mov_b32_dpp v102, v101 quad_perm:[2,3,0,1] row_mask:0xf bank_mask:0xf
	s_waitcnt lgkmcnt(0)
	v_add_f32_e32 v101, v101, v102
	s_nop 1
	v_mov_b32_dpp v102, v101 quad_perm:[1,0,3,2] row_mask:0xf bank_mask:0xf
	s_and_saveexec_b64 s[0:1], vcc
	s_cbranch_execz .LBB0_481
	s_waitcnt lgkmcnt(0)
	v_add_f32_e32 v101, v101, v102
	v_fmamk_f32 v101, v101, 0x3b000000, v246
	s_mov_b32 s2, 0x800000
	v_cmp_gt_f32_e64 s[2:3], s2, v101
	v_mul_f32_e32 v102, 0x4b800000, v101
	s_nop 0
	v_cndmask_b32_e64 v101, v101, v102, s[2:3]
	v_rsq_f32_e32 v101, v101
	s_nop 0
	v_mul_f32_e32 v102, 0x45800000, v101
	v_cndmask_b32_e64 v101, v101, v102, s[2:3]
	global_load_dwordx4 v[102:105], v[62:63], off offset:16
	global_load_dwordx4 v[106:109], v[62:63], off
	v_mul_f32_e32 v58, v58, v101
	v_mul_f32_e32 v99, v99, v101
	v_mul_f32_e32 v59, v59, v101
	s_waitcnt vmcnt(0)
	v_mul_f32_e32 v58, v58, v108
	v_cvt_pk_bf16_f32 v58, v58, s0
	ds_write_b16 v67, v58 offset:35362
	v_mul_f32_e32 v58, v60, v101
	v_mul_f32_e32 v58, v58, v109
	v_cvt_pk_bf16_f32 v58, v58, s0
	ds_write_b16 v67, v58 offset:35634
	v_mul_f32_e32 v58, v61, v101
	v_mul_f32_e32 v58, v58, v102
	v_cvt_pk_bf16_f32 v58, v58, s0
	ds_write_b16 v67, v58 offset:35906
	v_mul_f32_e32 v58, v77, v101
	v_mul_f32_e32 v58, v58, v103
	v_cvt_pk_bf16_f32 v58, v58, s0
	ds_write_b16 v67, v58 offset:36178
	v_mul_f32_e32 v58, v98, v101
	v_mul_f32_e32 v58, v58, v104
	v_cvt_pk_bf16_f32 v58, v58, s0
	ds_write_b16 v67, v58 offset:36450
	v_mul_f32_e32 v58, v100, v101
	v_mul_f32_e32 v99, v99, v106
	v_mul_f32_e32 v59, v59, v107
	v_mul_f32_e32 v58, v58, v105
	v_cvt_pk_bf16_f32 v99, v99, s0
	v_cvt_pk_bf16_f32 v59, v59, s0
	v_cvt_pk_bf16_f32 v58, v58, s0
	ds_write_b16 v67, v99 offset:34818
	ds_write_b16 v67, v59 offset:35090
	ds_write_b16 v67, v58 offset:36722
; __device__ __forceinline__ float bflo(unsigned w) { return __uint_as_float(w << 16); }
; __device__ __forceinline__ float bfhi(unsigned w) { return __uint_as_float(w & 0xffff0000u); }
; __device__ __forceinline__ unsigned short f2bf(float f) { return (unsigned short)(cvt_pk_bf16(f, 0.f) & 0xffffu); }
; __device__ __forceinline__ void sgu_unit(const Params& p, int l, int un, LAS unsigned char* lds) {
;     ...
;     for (int qi = 0; qi < 16; ++qi) { const int q = wave * 16 + qi;
;         const u32x4 v = vv[qi]; float f[8] = {bflo(v.x), bfhi(v.x), bflo(v.y), bfhi(v.y), bflo(v.z), bfhi(v.z), bflo(v.w), bfhi(v.w)}; float ss = 0.f;
; #pragma unroll
;         for (int j = 0; j < 8; ++j) { f[j] = gelu_tanh(f[j]); ss += f[j] * f[j]; }
;         ss = wave_sum(ss); const float rinv = rsqrtf(ss * (1.0f / 512.0f) + EPS);
;         if ((lane >> 4) == h) { const int c0 = (lane & 15) * 8; const float* g = p.in[I_SGUNG] + l * 512 + h * 128 + c0;
; #pragma unroll
;             for (int j = 0; j < 8; ++j) Vl[(c0 + j) * 136 + q] = f2bf(f[j] * rinv * g[j]); } }
.LBB0_481:
	s_or_b64 exec, exec, s[0:1]
	s_waitcnt vmcnt(13)
	v_lshlrev_b32_e32 v58, 16, v54
	v_lshlrev_b32_e32 v59, 16, v55
	v_and_b32_e32 v61, 0xffff0000, v55
	v_mul_f32_e32 v55, 0x3dd2d3e8, v58
	v_fma_f32 v55, -v55, v58, s33
	v_mul_f32_e32 v55, v55, v58
	v_exp_f32_e32 v55, v55
	v_and_b32_e32 v54, 0xffff0000, v54
	v_lshlrev_b32_e32 v77, 16, v56
	v_and_b32_e32 v98, 0xffff0000, v56
	v_add_f32_e32 v55, 1.0, v55
	v_rcp_f32_e32 v55, v55
	v_mul_f32_e32 v56, 0x3dd2d3e8, v61
	v_fma_f32 v56, -v56, v61, s33
	v_mul_f32_e32 v56, v56, v61
	v_mul_f32_e32 v60, v55, v58
	v_mul_f32_e32 v55, 0x3dd2d3e8, v54
	v_fma_f32 v55, -v55, v54, s33
	v_mul_f32_e32 v55, v55, v54
	v_exp_f32_e32 v55, v55
	v_exp_f32_e32 v56, v56
	v_lshlrev_b32_e32 v99, 16, v57
	v_and_b32_e32 v100, 0xffff0000, v57
	v_add_f32_e32 v55, 1.0, v55
	v_rcp_f32_e32 v55, v55
	v_add_f32_e32 v56, 1.0, v56
	v_rcp_f32_e32 v56, v56
	v_mul_f32_e32 v57, 0x3dd2d3e8, v77
	v_mul_f32_e32 v55, v55, v54
	v_mul_f32_e32 v54, 0x3dd2d3e8, v59
	v_fma_f32 v54, -v54, v59, s33
	v_mul_f32_e32 v54, v54, v59
	v_exp_f32_e32 v54, v54
	v_fma_f32 v57, -v57, v77, s33
	v_mul_f32_e32 v58, 0x3dd2d3e8, v98
	v_mul_f32_e32 v57, v57, v77
	v_add_f32_e32 v54, 1.0, v54
	v_rcp_f32_e32 v54, v54
	v_fma_f32 v58, -v58, v98, s33
	v_mul_f32_e32 v56, v56, v61
	v_exp_f32_e32 v57, v57
	v_mul_f32_e32 v54, v54, v59
	v_mul_f32_e32 v59, 0x3dd2d3e8, v99
	v_mul_f32_e32 v58, v58, v98
	v_fma_f32 v59, -v59, v99, s33
	v_mul_f32_e32 v61, 0x3dd2d3e8, v100
	v_exp_f32_e32 v58, v58
	v_mul_f32_e32 v59, v59, v99
	v_fma_f32 v61, -v61, v100, s33
	v_exp_f32_e32 v59, v59
	v_mul_f32_e32 v61, v61, v100
	v_exp_f32_e32 v61, v61
	v_add_f32_e32 v57, 1.0, v57
	v_rcp_f32_e32 v57, v57
	v_add_f32_e32 v58, 1.0, v58
	v_mul_f32_e32 v101, v55, v55
	v_rcp_f32_e32 v58, v58
	v_add_f32_e32 v59, 1.0, v59
	v_fmac_f32_e32 v101, v60, v60
	v_rcp_f32_e32 v59, v59
	v_add_f32_e32 v61, 1.0, v61
	v_fmac_f32_e32 v101, v54, v54
	v_rcp_f32_e32 v61, v61
	v_fmac_f32_e32 v101, v56, v56
	v_mul_f32_e32 v57, v57, v77
	v_fmac_f32_e32 v101, v57, v57
	v_mul_f32_e32 v58, v58, v98
	v_fmac_f32_e32 v101, v58, v58
	v_mul_f32_e32 v59, v59, v99
	v_fmac_f32_e32 v101, v59, v59
	v_mul_f32_e32 v61, v61, v100
	v_fmac_f32_e32 v101, v61, v61
	ds_bpermute_b32 v77, v68, v101
	s_waitcnt lgkmcnt(0)
	v_add_f32_e32 v77, v101, v77
	v_mov_b32_e32 v98, v77
	s_nop 1
	v_permlane16_swap_b32_e32 v98, v77
	s_waitcnt lgkmcnt(0)
	v_add_f32_e32 v77, v77, v98
	s_nop 1
	v_mov_b32_dpp v98, v77 row_ror:8 row_mask:0xf bank_mask:0xf
	s_waitcnt lgkmcnt(0)
	v_add_f32_e32 v77, v77, v98
	s_nop 1
	v_mov_b32_dpp v98, v77 row_shl:4 row_mask:0xf bank_mask:0x5
	v_mov_b32_dpp v98, v77 row_shr:4 row_mask:0xf bank_mask:0xa
	s_waitcnt lgkmcnt(0)
	v_add_f32_e32 v77, v77, v98
	s_nop 1
	v_mov_b32_dpp v98, v77 quad_perm:[2,3,0,1] row_mask:0xf bank_mask:0xf
	s_waitcnt lgkmcnt(0)
	v_add_f32_e32 v77, v77, v98
	s_nop 1
	v_mov_b32_dpp v98, v77 quad_perm:[1,0,3,2] row_mask:0xf bank_mask:0xf
	s_and_saveexec_b64 s[0:1], vcc
	s_cbranch_execz .LBB0_483
	s_waitcnt lgkmcnt(0)
	v_add_f32_e32 v77, v77, v98
	v_fmamk_f32 v77, v77, 0x3b000000, v246
	s_mov_b32 s2, 0x800000
	v_cmp_gt_f32_e64 s[2:3], s2, v77
	v_mul_f32_e32 v98, 0x4b800000, v77
	s_nop 0
	v_cndmask_b32_e64 v77, v77, v98, s[2:3]
	v_rsq_f32_e32 v77, v77
	s_nop 0
	v_mul_f32_e32 v98, 0x45800000, v77
	v_cndmask_b32_e64 v77, v77, v98, s[2:3]
	global_load_dwordx4 v[98:101], v[62:63], off offset:16
	global_load_dwordx4 v[102:105], v[62:63], off
	v_mul_f32_e32 v54, v54, v77
	v_mul_f32_e32 v60, v60, v77
	v_mul_f32_e32 v55, v55, v77
	s_waitcnt vmcnt(0)
	v_mul_f32_e32 v54, v54, v104
	v_cvt_pk_bf16_f32 v54, v54, s0
	ds_write_b16 v67, v54 offset:35364
	v_mul_f32_e32 v54, v56, v77
	v_mul_f32_e32 v54, v54, v105
	v_cvt_pk_bf16_f32 v54, v54, s0
	ds_write_b16 v67, v54 offset:35636
	v_mul_f32_e32 v54, v57, v77
	v_mul_f32_e32 v54, v54, v98
	v_cvt_pk_bf16_f32 v54, v54, s0
	ds_write_b16 v67, v54 offset:35908
	v_mul_f32_e32 v54, v58, v77
	v_mul_f32_e32 v54, v54, v99
	v_cvt_pk_bf16_f32 v54, v54, s0
	ds_write_b16 v67, v54 offset:36180
	v_mul_f32_e32 v54, v59, v77
	v_mul_f32_e32 v54, v54, v100
	v_cvt_pk_bf16_f32 v54, v54, s0
	ds_write_b16 v67, v54 offset:36452
	v_mul_f32_e32 v54, v61, v77
	v_mul_f32_e32 v60, v60, v102
	v_mul_f32_e32 v55, v55, v103
	v_mul_f32_e32 v54, v54, v101
	v_cvt_pk_bf16_f32 v60, v60, s0
	v_cvt_pk_bf16_f32 v55, v55, s0
	v_cvt_pk_bf16_f32 v54, v54, s0
	ds_write_b16 v67, v60 offset:34820
	ds_write_b16 v67, v55 offset:35092
	ds_write_b16 v67, v54 offset:36724
; __device__ __forceinline__ float bflo(unsigned w) { return __uint_as_float(w << 16); }
; __device__ __forceinline__ float bfhi(unsigned w) { return __uint_as_float(w & 0xffff0000u); }
; __device__ __forceinline__ unsigned short f2bf(float f) { return (unsigned short)(cvt_pk_bf16(f, 0.f) & 0xffffu); }
; __device__ __forceinline__ void sgu_unit(const Params& p, int l, int un, LAS unsigned char* lds) {
;     ...
;     for (int qi = 0; qi < 16; ++qi) { const int q = wave * 16 + qi;
;         const u32x4 v = vv[qi]; float f[8] = {bflo(v.x), bfhi(v.x), bflo(v.y), bfhi(v.y), bflo(v.z), bfhi(v.z), bflo(v.w), bfhi(v.w)}; float ss = 0.f;
; #pragma unroll
;         for (int j = 0; j < 8; ++j) { f[j] = gelu_tanh(f[j]); ss += f[j] * f[j]; }
;         ss = wave_sum(ss); const float rinv = rsqrtf(ss * (1.0f / 512.0f) + EPS);
;         if ((lane >> 4) == h) { const int c0 = (lane & 15) * 8; const float* g = p.in[I_SGUNG] + l * 512 + h * 128 + c0;
; #pragma unroll
;             for (int j = 0; j < 8; ++j) Vl[(c0 + j) * 136 + q] = f2bf(f[j] * rinv * g[j]); } }
.LBB0_483:
	s_or_b64 exec, exec, s[0:1]
	s_waitcnt vmcnt(12)
	v_lshlrev_b32_e32 v54, 16, v50
	v_lshlrev_b32_e32 v55, 16, v51
	v_and_b32_e32 v57, 0xffff0000, v51
	v_mul_f32_e32 v51, 0x3dd2d3e8, v54
	v_fma_f32 v51, -v51, v54, s33
	v_mul_f32_e32 v51, v51, v54
	v_exp_f32_e32 v51, v51
	v_and_b32_e32 v50, 0xffff0000, v50
	v_lshlrev_b32_e32 v58, 16, v52
	v_and_b32_e32 v59, 0xffff0000, v52
	v_add_f32_e32 v51, 1.0, v51
	v_rcp_f32_e32 v51, v51
	v_mul_f32_e32 v52, 0x3dd2d3e8, v57
	v_fma_f32 v52, -v52, v57, s33
	v_mul_f32_e32 v52, v52, v57
	v_mul_f32_e32 v56, v51, v54
	v_mul_f32_e32 v51, 0x3dd2d3e8, v50
	v_fma_f32 v51, -v51, v50, s33
	v_mul_f32_e32 v51, v51, v50
	v_exp_f32_e32 v51, v51
	v_exp_f32_e32 v52, v52
	v_lshlrev_b32_e32 v60, 16, v53
	v_and_b32_e32 v61, 0xffff0000, v53
	v_add_f32_e32 v51, 1.0, v51
	v_rcp_f32_e32 v51, v51
	v_add_f32_e32 v52, 1.0, v52
	v_rcp_f32_e32 v52, v52
	v_mul_f32_e32 v53, 0x3dd2d3e8, v58
	v_mul_f32_e32 v51, v51, v50
	v_mul_f32_e32 v50, 0x3dd2d3e8, v55
	v_fma_f32 v50, -v50, v55, s33
	v_mul_f32_e32 v50, v50, v55
	v_exp_f32_e32 v50, v50
	v_fma_f32 v53, -v53, v58, s33
	v_mul_f32_e32 v54, 0x3dd2d3e8, v59
	v_mul_f32_e32 v53, v53, v58
	v_add_f32_e32 v50, 1.0, v50
	v_rcp_f32_e32 v50, v50
	v_fma_f32 v54, -v54, v59, s33
	v_mul_f32_e32 v52, v52, v57
	v_exp_f32_e32 v53, v53
	v_mul_f32_e32 v50, v50, v55
	v_mul_f32_e32 v55, 0x3dd2d3e8, v60
	v_mul_f32_e32 v54, v54, v59
	v_fma_f32 v55, -v55, v60, s33
	v_mul_f32_e32 v57, 0x3dd2d3e8, v61
	v_exp_f32_e32 v54, v54
	v_mul_f32_e32 v55, v55, v60
	v_fma_f32 v57, -v57, v61, s33
	v_exp_f32_e32 v55, v55
	v_mul_f32_e32 v57, v57, v61
	v_exp_f32_e32 v57, v57
	v_add_f32_e32 v53, 1.0, v53
	v_rcp_f32_e32 v53, v53
	v_add_f32_e32 v54, 1.0, v54
	v_mul_f32_e32 v77, v51, v51
	v_rcp_f32_e32 v54, v54
	v_add_f32_e32 v55, 1.0, v55
	v_fmac_f32_e32 v77, v56, v56
	v_rcp_f32_e32 v55, v55
	v_add_f32_e32 v57, 1.0, v57
	v_fmac_f32_e32 v77, v50, v50
	v_rcp_f32_e32 v57, v57
	v_fmac_f32_e32 v77, v52, v52
	v_mul_f32_e32 v53, v53, v58
	v_fmac_f32_e32 v77, v53, v53
	v_mul_f32_e32 v54, v54, v59
	v_fmac_f32_e32 v77, v54, v54
	v_mul_f32_e32 v55, v55, v60
	v_fmac_f32_e32 v77, v55, v55
	v_mul_f32_e32 v57, v57, v61
	v_fmac_f32_e32 v77, v57, v57
	ds_bpermute_b32 v58, v68, v77
	s_waitcnt lgkmcnt(0)
	v_add_f32_e32 v58, v77, v58
	v_mov_b32_e32 v59, v58
	s_nop 1
	v_permlane16_swap_b32_e32 v59, v58
	s_waitcnt lgkmcnt(0)
	v_add_f32_e32 v58, v58, v59
	s_nop 1
	v_mov_b32_dpp v59, v58 row_ror:8 row_mask:0xf bank_mask:0xf
	s_waitcnt lgkmcnt(0)
	v_add_f32_e32 v58, v58, v59
	s_nop 1
	v_mov_b32_dpp v59, v58 row_shl:4 row_mask:0xf bank_mask:0x5
	v_mov_b32_dpp v59, v58 row_shr:4 row_mask:0xf bank_mask:0xa
	s_waitcnt lgkmcnt(0)
	v_add_f32_e32 v58, v58, v59
	s_nop 1
	v_mov_b32_dpp v59, v58 quad_perm:[2,3,0,1] row_mask:0xf bank_mask:0xf
	s_waitcnt lgkmcnt(0)
	v_add_f32_e32 v58, v58, v59
	s_nop 1
	v_mov_b32_dpp v59, v58 quad_perm:[1,0,3,2] row_mask:0xf bank_mask:0xf
	s_and_saveexec_b64 s[0:1], vcc
	s_cbranch_execz .LBB0_485
	s_waitcnt lgkmcnt(0)
	v_add_f32_e32 v58, v58, v59
	v_fmamk_f32 v58, v58, 0x3b000000, v246
	s_mov_b32 s2, 0x800000
	v_cmp_gt_f32_e64 s[2:3], s2, v58
	v_mul_f32_e32 v59, 0x4b800000, v58
	s_nop 0
	v_cndmask_b32_e64 v58, v58, v59, s[2:3]
	v_rsq_f32_e32 v58, v58
	s_nop 0
	v_mul_f32_e32 v59, 0x45800000, v58
	v_cndmask_b32_e64 v77, v58, v59, s[2:3]
	global_load_dwordx4 v[58:61], v[62:63], off offset:16
	global_load_dwordx4 v[98:101], v[62:63], off
	v_mul_f32_e32 v50, v50, v77
	v_mul_f32_e32 v56, v56, v77
	v_mul_f32_e32 v51, v51, v77
	s_waitcnt vmcnt(0)
	v_mul_f32_e32 v50, v50, v100
	v_cvt_pk_bf16_f32 v50, v50, s0
	ds_write_b16 v67, v50 offset:35366
	v_mul_f32_e32 v50, v52, v77
	v_mul_f32_e32 v50, v50, v101
	v_cvt_pk_bf16_f32 v50, v50, s0
	ds_write_b16 v67, v50 offset:35638
	v_mul_f32_e32 v50, v53, v77
	v_mul_f32_e32 v50, v50, v58
	v_cvt_pk_bf16_f32 v50, v50, s0
	ds_write_b16 v67, v50 offset:35910
	v_mul_f32_e32 v50, v54, v77
	v_mul_f32_e32 v50, v50, v59
	v_cvt_pk_bf16_f32 v50, v50, s0
	ds_write_b16 v67, v50 offset:36182
	v_mul_f32_e32 v50, v55, v77
	v_mul_f32_e32 v50, v50, v60
	v_cvt_pk_bf16_f32 v50, v50, s0
	ds_write_b16 v67, v50 offset:36454
	v_mul_f32_e32 v50, v57, v77
	v_mul_f32_e32 v56, v56, v98
	v_mul_f32_e32 v51, v51, v99
	v_mul_f32_e32 v50, v50, v61
	v_cvt_pk_bf16_f32 v56, v56, s0
	v_cvt_pk_bf16_f32 v51, v51, s0
	v_cvt_pk_bf16_f32 v50, v50, s0
	ds_write_b16 v67, v56 offset:34822
	ds_write_b16 v67, v51 offset:35094
	ds_write_b16 v67, v50 offset:36726
; __device__ __forceinline__ float bflo(unsigned w) { return __uint_as_float(w << 16); }
; __device__ __forceinline__ float bfhi(unsigned w) { return __uint_as_float(w & 0xffff0000u); }
; __device__ __forceinline__ unsigned short f2bf(float f) { return (unsigned short)(cvt_pk_bf16(f, 0.f) & 0xffffu); }
; __device__ __forceinline__ void sgu_unit(const Params& p, int l, int un, LAS unsigned char* lds) {
;     ...
;     for (int qi = 0; qi < 16; ++qi) { const int q = wave * 16 + qi;
;         const u32x4 v = vv[qi]; float f[8] = {bflo(v.x), bfhi(v.x), bflo(v.y), bfhi(v.y), bflo(v.z), bfhi(v.z), bflo(v.w), bfhi(v.w)}; float ss = 0.f;
; #pragma unroll
;         for (int j = 0; j < 8; ++j) { f[j] = gelu_tanh(f[j]); ss += f[j] * f[j]; }
;         ss = wave_sum(ss); const float rinv = rsqrtf(ss * (1.0f / 512.0f) + EPS);
;         if ((lane >> 4) == h) { const int c0 = (lane & 15) * 8; const float* g = p.in[I_SGUNG] + l * 512 + h * 128 + c0;
; #pragma unroll
;             for (int j = 0; j < 8; ++j) Vl[(c0 + j) * 136 + q] = f2bf(f[j] * rinv * g[j]); } }
.LBB0_485:
	s_or_b64 exec, exec, s[0:1]
	s_waitcnt vmcnt(11)
	v_lshlrev_b32_e32 v50, 16, v46
	v_lshlrev_b32_e32 v51, 16, v47
	v_and_b32_e32 v53, 0xffff0000, v47
	v_mul_f32_e32 v47, 0x3dd2d3e8, v50
	v_fma_f32 v47, -v47, v50, s33
	v_mul_f32_e32 v47, v47, v50
	v_exp_f32_e32 v47, v47
	v_and_b32_e32 v46, 0xffff0000, v46
	v_lshlrev_b32_e32 v54, 16, v48
	v_and_b32_e32 v55, 0xffff0000, v48
	v_add_f32_e32 v47, 1.0, v47
	v_rcp_f32_e32 v47, v47
	v_mul_f32_e32 v48, 0x3dd2d3e8, v53
	v_fma_f32 v48, -v48, v53, s33
	v_mul_f32_e32 v48, v48, v53
	v_mul_f32_e32 v52, v47, v50
	v_mul_f32_e32 v47, 0x3dd2d3e8, v46
	v_fma_f32 v47, -v47, v46, s33
	v_mul_f32_e32 v47, v47, v46
	v_exp_f32_e32 v47, v47
	v_exp_f32_e32 v48, v48
	v_lshlrev_b32_e32 v56, 16, v49
	v_and_b32_e32 v57, 0xffff0000, v49
	v_add_f32_e32 v47, 1.0, v47
	v_rcp_f32_e32 v47, v47
	v_add_f32_e32 v48, 1.0, v48
	v_rcp_f32_e32 v48, v48
	v_mul_f32_e32 v49, 0x3dd2d3e8, v54
	v_mul_f32_e32 v47, v47, v46
	v_mul_f32_e32 v46, 0x3dd2d3e8, v51
	v_fma_f32 v46, -v46, v51, s33
	v_mul_f32_e32 v46, v46, v51
	v_exp_f32_e32 v46, v46
	v_fma_f32 v49, -v49, v54, s33
	v_mul_f32_e32 v50, 0x3dd2d3e8, v55
	v_mul_f32_e32 v49, v49, v54
	v_add_f32_e32 v46, 1.0, v46
	v_rcp_f32_e32 v46, v46
	v_fma_f32 v50, -v50, v55, s33
	v_mul_f32_e32 v48, v48, v53
	v_exp_f32_e32 v49, v49
	v_mul_f32_e32 v46, v46, v51
	v_mul_f32_e32 v51, 0x3dd2d3e8, v56
	v_mul_f32_e32 v50, v50, v55
	v_fma_f32 v51, -v51, v56, s33
	v_mul_f32_e32 v53, 0x3dd2d3e8, v57
	v_exp_f32_e32 v50, v50
	v_mul_f32_e32 v51, v51, v56
	v_fma_f32 v53, -v53, v57, s33
	v_exp_f32_e32 v51, v51
	v_mul_f32_e32 v53, v53, v57
	v_exp_f32_e32 v53, v53
	v_add_f32_e32 v49, 1.0, v49
	v_rcp_f32_e32 v49, v49
	v_add_f32_e32 v50, 1.0, v50
	v_mul_f32_e32 v58, v47, v47
	v_rcp_f32_e32 v50, v50
	v_add_f32_e32 v51, 1.0, v51
	v_fmac_f32_e32 v58, v52, v52
	v_rcp_f32_e32 v51, v51
	v_add_f32_e32 v53, 1.0, v53
	v_fmac_f32_e32 v58, v46, v46
	v_rcp_f32_e32 v53, v53
	v_fmac_f32_e32 v58, v48, v48
	v_mul_f32_e32 v49, v49, v54
	v_fmac_f32_e32 v58, v49, v49
	v_mul_f32_e32 v50, v50, v55
	v_fmac_f32_e32 v58, v50, v50
	v_mul_f32_e32 v51, v51, v56
	v_fmac_f32_e32 v58, v51, v51
	v_mul_f32_e32 v53, v53, v57
	v_fmac_f32_e32 v58, v53, v53
	ds_bpermute_b32 v54, v68, v58
	s_waitcnt lgkmcnt(0)
	v_add_f32_e32 v54, v58, v54
	v_mov_b32_e32 v55, v54
	s_nop 1
	v_permlane16_swap_b32_e32 v55, v54
	s_waitcnt lgkmcnt(0)
	v_add_f32_e32 v54, v54, v55
	s_nop 1
	v_mov_b32_dpp v55, v54 row_ror:8 row_mask:0xf bank_mask:0xf
	s_waitcnt lgkmcnt(0)
	v_add_f32_e32 v54, v54, v55
	s_nop 1
	v_mov_b32_dpp v55, v54 row_shl:4 row_mask:0xf bank_mask:0x5
	v_mov_b32_dpp v55, v54 row_shr:4 row_mask:0xf bank_mask:0xa
	s_waitcnt lgkmcnt(0)
	v_add_f32_e32 v54, v54, v55
	s_nop 1
	v_mov_b32_dpp v55, v54 quad_perm:[2,3,0,1] row_mask:0xf bank_mask:0xf
	s_waitcnt lgkmcnt(0)
	v_add_f32_e32 v54, v54, v55
	s_nop 1
	v_mov_b32_dpp v55, v54 quad_perm:[1,0,3,2] row_mask:0xf bank_mask:0xf
	s_and_saveexec_b64 s[0:1], vcc
	s_cbranch_execz .LBB0_487
	s_waitcnt lgkmcnt(0)
	v_add_f32_e32 v54, v54, v55
	v_fmamk_f32 v54, v54, 0x3b000000, v246
	s_mov_b32 s2, 0x800000
	v_cmp_gt_f32_e64 s[2:3], s2, v54
	v_mul_f32_e32 v55, 0x4b800000, v54
	s_nop 0
	v_cndmask_b32_e64 v54, v54, v55, s[2:3]
	v_rsq_f32_e32 v54, v54
	s_nop 0
	v_mul_f32_e32 v55, 0x45800000, v54
	v_cndmask_b32_e64 v77, v54, v55, s[2:3]
	global_load_dwordx4 v[54:57], v[62:63], off offset:16
	global_load_dwordx4 v[58:61], v[62:63], off
	v_mul_f32_e32 v46, v46, v77
	v_mul_f32_e32 v52, v52, v77
	v_mul_f32_e32 v47, v47, v77
	s_waitcnt vmcnt(0)
	v_mul_f32_e32 v46, v46, v60
	v_cvt_pk_bf16_f32 v46, v46, s0
	ds_write_b16 v67, v46 offset:35368
	v_mul_f32_e32 v46, v48, v77
	v_mul_f32_e32 v46, v46, v61
	v_cvt_pk_bf16_f32 v46, v46, s0
	ds_write_b16 v67, v46 offset:35640
	v_mul_f32_e32 v46, v49, v77
	v_mul_f32_e32 v46, v46, v54
	v_cvt_pk_bf16_f32 v46, v46, s0
	ds_write_b16 v67, v46 offset:35912
	v_mul_f32_e32 v46, v50, v77
	v_mul_f32_e32 v46, v46, v55
	v_cvt_pk_bf16_f32 v46, v46, s0
	ds_write_b16 v67, v46 offset:36184
	v_mul_f32_e32 v46, v51, v77
	v_mul_f32_e32 v46, v46, v56
	v_cvt_pk_bf16_f32 v46, v46, s0
	ds_write_b16 v67, v46 offset:36456
	v_mul_f32_e32 v46, v53, v77
	v_mul_f32_e32 v52, v52, v58
	v_mul_f32_e32 v47, v47, v59
	v_mul_f32_e32 v46, v46, v57
	v_cvt_pk_bf16_f32 v52, v52, s0
	v_cvt_pk_bf16_f32 v47, v47, s0
	v_cvt_pk_bf16_f32 v46, v46, s0
	ds_write_b16 v67, v52 offset:34824
	ds_write_b16 v67, v47 offset:35096
	ds_write_b16 v67, v46 offset:36728
; __device__ __forceinline__ float bflo(unsigned w) { return __uint_as_float(w << 16); }
; __device__ __forceinline__ float bfhi(unsigned w) { return __uint_as_float(w & 0xffff0000u); }
; __device__ __forceinline__ unsigned short f2bf(float f) { return (unsigned short)(cvt_pk_bf16(f, 0.f) & 0xffffu); }
; __device__ __forceinline__ void sgu_unit(const Params& p, int l, int un, LAS unsigned char* lds) {
;     ...
;     for (int qi = 0; qi < 16; ++qi) { const int q = wave * 16 + qi;
;         const u32x4 v = vv[qi]; float f[8] = {bflo(v.x), bfhi(v.x), bflo(v.y), bfhi(v.y), bflo(v.z), bfhi(v.z), bflo(v.w), bfhi(v.w)}; float ss = 0.f;
; #pragma unroll
;         for (int j = 0; j < 8; ++j) { f[j] = gelu_tanh(f[j]); ss += f[j] * f[j]; }
;         ss = wave_sum(ss); const float rinv = rsqrtf(ss * (1.0f / 512.0f) + EPS);
;         if ((lane >> 4) == h) { const int c0 = (lane & 15) * 8; const float* g = p.in[I_SGUNG] + l * 512 + h * 128 + c0;
; #pragma unroll
;             for (int j = 0; j < 8; ++j) Vl[(c0 + j) * 136 + q] = f2bf(f[j] * rinv * g[j]); } }
.LBB0_487:
	s_or_b64 exec, exec, s[0:1]
	s_waitcnt vmcnt(10)
	v_lshlrev_b32_e32 v46, 16, v42
	v_lshlrev_b32_e32 v47, 16, v43
	v_and_b32_e32 v49, 0xffff0000, v43
	v_mul_f32_e32 v43, 0x3dd2d3e8, v46
	v_fma_f32 v43, -v43, v46, s33
	v_mul_f32_e32 v43, v43, v46
	v_exp_f32_e32 v43, v43
	v_and_b32_e32 v42, 0xffff0000, v42
	v_lshlrev_b32_e32 v50, 16, v44
	v_and_b32_e32 v51, 0xffff0000, v44
	v_add_f32_e32 v43, 1.0, v43
	v_rcp_f32_e32 v43, v43
	v_mul_f32_e32 v44, 0x3dd2d3e8, v49
	v_fma_f32 v44, -v44, v49, s33
	v_mul_f32_e32 v44, v44, v49
	v_mul_f32_e32 v48, v43, v46
	v_mul_f32_e32 v43, 0x3dd2d3e8, v42
	v_fma_f32 v43, -v43, v42, s33
	v_mul_f32_e32 v43, v43, v42
	v_exp_f32_e32 v43, v43
	v_exp_f32_e32 v44, v44
	v_lshlrev_b32_e32 v52, 16, v45
	v_and_b32_e32 v53, 0xffff0000, v45
	v_add_f32_e32 v43, 1.0, v43
	v_rcp_f32_e32 v43, v43
	v_add_f32_e32 v44, 1.0, v44
	v_rcp_f32_e32 v44, v44
	v_mul_f32_e32 v45, 0x3dd2d3e8, v50
	v_mul_f32_e32 v43, v43, v42
	v_mul_f32_e32 v42, 0x3dd2d3e8, v47
	v_fma_f32 v42, -v42, v47, s33
	v_mul_f32_e32 v42, v42, v47
	v_exp_f32_e32 v42, v42
	v_fma_f32 v45, -v45, v50, s33
	v_mul_f32_e32 v46, 0x3dd2d3e8, v51
	v_mul_f32_e32 v45, v45, v50
	v_add_f32_e32 v42, 1.0, v42
	v_rcp_f32_e32 v42, v42
	v_fma_f32 v46, -v46, v51, s33
	v_mul_f32_e32 v44, v44, v49
	v_exp_f32_e32 v45, v45
	v_mul_f32_e32 v42, v42, v47
	v_mul_f32_e32 v47, 0x3dd2d3e8, v52
	v_mul_f32_e32 v46, v46, v51
	v_fma_f32 v47, -v47, v52, s33
	v_mul_f32_e32 v49, 0x3dd2d3e8, v53
	v_exp_f32_e32 v46, v46
	v_mul_f32_e32 v47, v47, v52
	v_fma_f32 v49, -v49, v53, s33
	v_exp_f32_e32 v47, v47
	v_mul_f32_e32 v49, v49, v53
	v_exp_f32_e32 v49, v49
	v_add_f32_e32 v45, 1.0, v45
	v_rcp_f32_e32 v45, v45
	v_add_f32_e32 v46, 1.0, v46
	v_mul_f32_e32 v54, v43, v43
	v_rcp_f32_e32 v46, v46
	v_add_f32_e32 v47, 1.0, v47
	v_fmac_f32_e32 v54, v48, v48
	v_rcp_f32_e32 v47, v47
	v_add_f32_e32 v49, 1.0, v49
	v_fmac_f32_e32 v54, v42, v42
	v_rcp_f32_e32 v49, v49
	v_fmac_f32_e32 v54, v44, v44
	v_mul_f32_e32 v45, v45, v50
	v_fmac_f32_e32 v54, v45, v45
	v_mul_f32_e32 v46, v46, v51
	v_fmac_f32_e32 v54, v46, v46
	v_mul_f32_e32 v47, v47, v52
	v_fmac_f32_e32 v54, v47, v47
	v_mul_f32_e32 v49, v49, v53
	v_fmac_f32_e32 v54, v49, v49
	v_mov_b32_e32 v50, v54
	s_nop 1
	v_permlane32_swap_b32_e32 v50, v54
	s_waitcnt lgkmcnt(0)
	v_add_f32_e32 v50, v54, v50
	v_mov_b32_e32 v51, v50
	s_nop 1
	v_permlane16_swap_b32_e32 v51, v50
	s_waitcnt lgkmcnt(0)
	v_add_f32_e32 v50, v50, v51
	s_nop 1
	v_mov_b32_dpp v51, v50 row_ror:8 row_mask:0xf bank_mask:0xf
	s_waitcnt lgkmcnt(0)
	v_add_f32_e32 v50, v50, v51
	s_nop 1
	v_mov_b32_dpp v51, v50 row_shl:4 row_mask:0xf bank_mask:0x5
	v_mov_b32_dpp v51, v50 row_shr:4 row_mask:0xf bank_mask:0xa
	s_waitcnt lgkmcnt(0)
	v_add_f32_e32 v50, v50, v51
	s_nop 1
	v_mov_b32_dpp v51, v50 quad_perm:[2,3,0,1] row_mask:0xf bank_mask:0xf
	s_waitcnt lgkmcnt(0)
	v_add_f32_e32 v50, v50, v51
	s_nop 1
	v_mov_b32_dpp v51, v50 quad_perm:[1,0,3,2] row_mask:0xf bank_mask:0xf
	s_and_saveexec_b64 s[0:1], vcc
	s_cbranch_execz .LBB0_489
	s_waitcnt lgkmcnt(0)
	v_add_f32_e32 v50, v50, v51
	v_fmamk_f32 v50, v50, 0x3b000000, v246
	s_mov_b32 s2, 0x800000
	v_cmp_gt_f32_e64 s[2:3], s2, v50
	v_mul_f32_e32 v51, 0x4b800000, v50
	s_nop 0
	v_cndmask_b32_e64 v50, v50, v51, s[2:3]
	v_rsq_f32_e32 v50, v50
	s_nop 0
	v_mul_f32_e32 v51, 0x45800000, v50
	v_cndmask_b32_e64 v58, v50, v51, s[2:3]
	global_load_dwordx4 v[50:53], v[62:63], off offset:16
	global_load_dwordx4 v[54:57], v[62:63], off
	v_mul_f32_e32 v42, v42, v58
	v_mul_f32_e32 v48, v48, v58
	v_mul_f32_e32 v43, v43, v58
	s_waitcnt vmcnt(0)
	v_mul_f32_e32 v42, v42, v56
	v_cvt_pk_bf16_f32 v42, v42, s0
	ds_write_b16 v67, v42 offset:35370
	v_mul_f32_e32 v42, v44, v58
	v_mul_f32_e32 v42, v42, v57
	v_cvt_pk_bf16_f32 v42, v42, s0
	ds_write_b16 v67, v42 offset:35642
	v_mul_f32_e32 v42, v45, v58
	v_mul_f32_e32 v42, v42, v50
	v_cvt_pk_bf16_f32 v42, v42, s0
	ds_write_b16 v67, v42 offset:35914
	v_mul_f32_e32 v42, v46, v58
	v_mul_f32_e32 v42, v42, v51
	v_cvt_pk_bf16_f32 v42, v42, s0
	ds_write_b16 v67, v42 offset:36186
	v_mul_f32_e32 v42, v47, v58
	v_mul_f32_e32 v42, v42, v52
	v_cvt_pk_bf16_f32 v42, v42, s0
	ds_write_b16 v67, v42 offset:36458
	v_mul_f32_e32 v42, v49, v58
	v_mul_f32_e32 v48, v48, v54
	v_mul_f32_e32 v43, v43, v55
	v_mul_f32_e32 v42, v42, v53
	v_cvt_pk_bf16_f32 v48, v48, s0
	v_cvt_pk_bf16_f32 v43, v43, s0
	v_cvt_pk_bf16_f32 v42, v42, s0
	ds_write_b16 v67, v48 offset:34826
	ds_write_b16 v67, v43 offset:35098
	ds_write_b16 v67, v42 offset:36730
; __device__ __forceinline__ float bflo(unsigned w) { return __uint_as_float(w << 16); }
; __device__ __forceinline__ float bfhi(unsigned w) { return __uint_as_float(w & 0xffff0000u); }
; __device__ __forceinline__ unsigned short f2bf(float f) { return (unsigned short)(cvt_pk_bf16(f, 0.f) & 0xffffu); }
; __device__ __forceinline__ void sgu_unit(const Params& p, int l, int un, LAS unsigned char* lds) {
;     ...
;     for (int qi = 0; qi < 16; ++qi) { const int q = wave * 16 + qi;
;         const u32x4 v = vv[qi]; float f[8] = {bflo(v.x), bfhi(v.x), bflo(v.y), bfhi(v.y), bflo(v.z), bfhi(v.z), bflo(v.w), bfhi(v.w)}; float ss = 0.f;
; #pragma unroll
;         for (int j = 0; j < 8; ++j) { f[j] = gelu_tanh(f[j]); ss += f[j] * f[j]; }
;         ss = wave_sum(ss); const float rinv = rsqrtf(ss * (1.0f / 512.0f) + EPS);
;         if ((lane >> 4) == h) { const int c0 = (lane & 15) * 8; const float* g = p.in[I_SGUNG] + l * 512 + h * 128 + c0;
; #pragma unroll
;             for (int j = 0; j < 8; ++j) Vl[(c0 + j) * 136 + q] = f2bf(f[j] * rinv * g[j]); } }
.LBB0_489:
	s_or_b64 exec, exec, s[0:1]
	s_waitcnt vmcnt(9)
	v_lshlrev_b32_e32 v42, 16, v38
	v_lshlrev_b32_e32 v43, 16, v39
	v_and_b32_e32 v45, 0xffff0000, v39
	v_mul_f32_e32 v39, 0x3dd2d3e8, v42
	v_fma_f32 v39, -v39, v42, s33
	v_mul_f32_e32 v39, v39, v42
	v_exp_f32_e32 v39, v39
	v_and_b32_e32 v38, 0xffff0000, v38
	v_lshlrev_b32_e32 v46, 16, v40
	v_and_b32_e32 v47, 0xffff0000, v40
	v_add_f32_e32 v39, 1.0, v39
	v_rcp_f32_e32 v39, v39
	v_mul_f32_e32 v40, 0x3dd2d3e8, v45
	v_fma_f32 v40, -v40, v45, s33
	v_mul_f32_e32 v40, v40, v45
	v_mul_f32_e32 v44, v39, v42
	v_mul_f32_e32 v39, 0x3dd2d3e8, v38
	v_fma_f32 v39, -v39, v38, s33
	v_mul_f32_e32 v39, v39, v38
	v_exp_f32_e32 v39, v39
	v_exp_f32_e32 v40, v40
	v_lshlrev_b32_e32 v48, 16, v41
	v_and_b32_e32 v49, 0xffff0000, v41
	v_add_f32_e32 v39, 1.0, v39
	v_rcp_f32_e32 v39, v39
	v_add_f32_e32 v40, 1.0, v40
	v_rcp_f32_e32 v40, v40
	v_mul_f32_e32 v41, 0x3dd2d3e8, v46
	v_mul_f32_e32 v39, v39, v38
	v_mul_f32_e32 v38, 0x3dd2d3e8, v43
	v_fma_f32 v38, -v38, v43, s33
	v_mul_f32_e32 v38, v38, v43
	v_exp_f32_e32 v38, v38
	v_fma_f32 v41, -v41, v46, s33
	v_mul_f32_e32 v42, 0x3dd2d3e8, v47
	v_mul_f32_e32 v41, v41, v46
	v_add_f32_e32 v38, 1.0, v38
	v_rcp_f32_e32 v38, v38
	v_fma_f32 v42, -v42, v47, s33
	v_mul_f32_e32 v40, v40, v45
	v_exp_f32_e32 v41, v41
	v_mul_f32_e32 v38, v38, v43
	v_mul_f32_e32 v43, 0x3dd2d3e8, v48
	v_mul_f32_e32 v42, v42, v47
	v_fma_f32 v43, -v43, v48, s33
	v_mul_f32_e32 v45, 0x3dd2d3e8, v49
	v_exp_f32_e32 v42, v42
	v_mul_f32_e32 v43, v43, v48
	v_fma_f32 v45, -v45, v49, s33
	v_exp_f32_e32 v43, v43
	v_mul_f32_e32 v45, v45, v49
	v_exp_f32_e32 v45, v45
	v_add_f32_e32 v41, 1.0, v41
	v_rcp_f32_e32 v41, v41
	v_add_f32_e32 v42, 1.0, v42
	v_mul_f32_e32 v50, v39, v39
	v_rcp_f32_e32 v42, v42
	v_add_f32_e32 v43, 1.0, v43
	v_fmac_f32_e32 v50, v44, v44
	v_rcp_f32_e32 v43, v43
	v_add_f32_e32 v45, 1.0, v45
	v_fmac_f32_e32 v50, v38, v38
	v_rcp_f32_e32 v45, v45
	v_fmac_f32_e32 v50, v40, v40
	v_mul_f32_e32 v41, v41, v46
	v_fmac_f32_e32 v50, v41, v41
	v_mul_f32_e32 v42, v42, v47
	v_fmac_f32_e32 v50, v42, v42
	v_mul_f32_e32 v43, v43, v48
	v_fmac_f32_e32 v50, v43, v43
	v_mul_f32_e32 v45, v45, v49
	v_fmac_f32_e32 v50, v45, v45
	v_mov_b32_e32 v46, v50
	s_nop 1
	v_permlane32_swap_b32_e32 v46, v50
	s_waitcnt lgkmcnt(0)
	v_add_f32_e32 v46, v50, v46
	v_mov_b32_e32 v47, v46
	s_nop 1
	v_permlane16_swap_b32_e32 v47, v46
	s_waitcnt lgkmcnt(0)
	v_add_f32_e32 v46, v46, v47
	s_nop 1
	v_mov_b32_dpp v47, v46 row_ror:8 row_mask:0xf bank_mask:0xf
	s_waitcnt lgkmcnt(0)
	v_add_f32_e32 v46, v46, v47
	s_nop 1
	v_mov_b32_dpp v47, v46 row_shl:4 row_mask:0xf bank_mask:0x5
	v_mov_b32_dpp v47, v46 row_shr:4 row_mask:0xf bank_mask:0xa
	s_waitcnt lgkmcnt(0)
	v_add_f32_e32 v46, v46, v47
	s_nop 1
	v_mov_b32_dpp v47, v46 quad_perm:[2,3,0,1] row_mask:0xf bank_mask:0xf
	s_waitcnt lgkmcnt(0)
	v_add_f32_e32 v46, v46, v47
	s_nop 1
	v_mov_b32_dpp v47, v46 quad_perm:[1,0,3,2] row_mask:0xf bank_mask:0xf
	s_and_saveexec_b64 s[0:1], vcc
	s_cbranch_execz .LBB0_491
	s_waitcnt lgkmcnt(0)
	v_add_f32_e32 v46, v46, v47
	v_fmamk_f32 v46, v46, 0x3b000000, v246
	s_mov_b32 s2, 0x800000
	v_cmp_gt_f32_e64 s[2:3], s2, v46
	v_mul_f32_e32 v47, 0x4b800000, v46
	s_nop 0
	v_cndmask_b32_e64 v46, v46, v47, s[2:3]
	v_rsq_f32_e32 v46, v46
	s_nop 0
	v_mul_f32_e32 v47, 0x45800000, v46
	v_cndmask_b32_e64 v54, v46, v47, s[2:3]
	global_load_dwordx4 v[46:49], v[62:63], off offset:16
	global_load_dwordx4 v[50:53], v[62:63], off
	v_mul_f32_e32 v38, v38, v54
	v_mul_f32_e32 v44, v44, v54
	v_mul_f32_e32 v39, v39, v54
	s_waitcnt vmcnt(0)
	v_mul_f32_e32 v38, v38, v52
	v_cvt_pk_bf16_f32 v38, v38, s0
	ds_write_b16 v67, v38 offset:35372
	v_mul_f32_e32 v38, v40, v54
	v_mul_f32_e32 v38, v38, v53
	v_cvt_pk_bf16_f32 v38, v38, s0
	ds_write_b16 v67, v38 offset:35644
	v_mul_f32_e32 v38, v41, v54
	v_mul_f32_e32 v38, v38, v46
	v_cvt_pk_bf16_f32 v38, v38, s0
	ds_write_b16 v67, v38 offset:35916
	v_mul_f32_e32 v38, v42, v54
	v_mul_f32_e32 v38, v38, v47
	v_cvt_pk_bf16_f32 v38, v38, s0
	ds_write_b16 v67, v38 offset:36188
	v_mul_f32_e32 v38, v43, v54
	v_mul_f32_e32 v38, v38, v48
	v_cvt_pk_bf16_f32 v38, v38, s0
	ds_write_b16 v67, v38 offset:36460
	v_mul_f32_e32 v38, v45, v54
	v_mul_f32_e32 v44, v44, v50
	v_mul_f32_e32 v39, v39, v51
	v_mul_f32_e32 v38, v38, v49
	v_cvt_pk_bf16_f32 v44, v44, s0
	v_cvt_pk_bf16_f32 v39, v39, s0
	v_cvt_pk_bf16_f32 v38, v38, s0
	ds_write_b16 v67, v44 offset:34828
	ds_write_b16 v67, v39 offset:35100
	ds_write_b16 v67, v38 offset:36732
; __device__ __forceinline__ float bflo(unsigned w) { return __uint_as_float(w << 16); }
; __device__ __forceinline__ float bfhi(unsigned w) { return __uint_as_float(w & 0xffff0000u); }
; __device__ __forceinline__ unsigned short f2bf(float f) { return (unsigned short)(cvt_pk_bf16(f, 0.f) & 0xffffu); }
; __device__ __forceinline__ void sgu_unit(const Params& p, int l, int un, LAS unsigned char* lds) {
;     ...
;     for (int qi = 0; qi < 16; ++qi) { const int q = wave * 16 + qi;
;         const u32x4 v = vv[qi]; float f[8] = {bflo(v.x), bfhi(v.x), bflo(v.y), bfhi(v.y), bflo(v.z), bfhi(v.z), bflo(v.w), bfhi(v.w)}; float ss = 0.f;
; #pragma unroll
;         for (int j = 0; j < 8; ++j) { f[j] = gelu_tanh(f[j]); ss += f[j] * f[j]; }
;         ss = wave_sum(ss); const float rinv = rsqrtf(ss * (1.0f / 512.0f) + EPS);
;         if ((lane >> 4) == h) { const int c0 = (lane & 15) * 8; const float* g = p.in[I_SGUNG] + l * 512 + h * 128 + c0;
; #pragma unroll
;             for (int j = 0; j < 8; ++j) Vl[(c0 + j) * 136 + q] = f2bf(f[j] * rinv * g[j]); } }
.LBB0_491:
	s_or_b64 exec, exec, s[0:1]
	s_waitcnt vmcnt(8)
	v_lshlrev_b32_e32 v38, 16, v34
	v_lshlrev_b32_e32 v39, 16, v35
	v_and_b32_e32 v41, 0xffff0000, v35
	v_mul_f32_e32 v35, 0x3dd2d3e8, v38
	v_fma_f32 v35, -v35, v38, s33
	v_mul_f32_e32 v35, v35, v38
	v_exp_f32_e32 v35, v35
	v_and_b32_e32 v34, 0xffff0000, v34
	v_lshlrev_b32_e32 v42, 16, v36
	v_and_b32_e32 v43, 0xffff0000, v36
	v_add_f32_e32 v35, 1.0, v35
	v_rcp_f32_e32 v35, v35
	v_mul_f32_e32 v36, 0x3dd2d3e8, v41
	v_fma_f32 v36, -v36, v41, s33
	v_mul_f32_e32 v36, v36, v41
	v_mul_f32_e32 v40, v35, v38
	v_mul_f32_e32 v35, 0x3dd2d3e8, v34
	v_fma_f32 v35, -v35, v34, s33
	v_mul_f32_e32 v35, v35, v34
	v_exp_f32_e32 v35, v35
	v_exp_f32_e32 v36, v36
	v_lshlrev_b32_e32 v44, 16, v37
	v_and_b32_e32 v45, 0xffff0000, v37
	v_add_f32_e32 v35, 1.0, v35
	v_rcp_f32_e32 v35, v35
	v_add_f32_e32 v36, 1.0, v36
	v_rcp_f32_e32 v36, v36
	v_mul_f32_e32 v37, 0x3dd2d3e8, v42
	v_mul_f32_e32 v35, v35, v34
	v_mul_f32_e32 v34, 0x3dd2d3e8, v39
	v_fma_f32 v34, -v34, v39, s33
	v_mul_f32_e32 v34, v34, v39
	v_exp_f32_e32 v34, v34
	v_fma_f32 v37, -v37, v42, s33
	v_mul_f32_e32 v38, 0x3dd2d3e8, v43
	v_mul_f32_e32 v37, v37, v42
	v_add_f32_e32 v34, 1.0, v34
	v_rcp_f32_e32 v34, v34
	v_fma_f32 v38, -v38, v43, s33
	v_mul_f32_e32 v36, v36, v41
	v_exp_f32_e32 v37, v37
	v_mul_f32_e32 v34, v34, v39
	v_mul_f32_e32 v39, 0x3dd2d3e8, v44
	v_mul_f32_e32 v38, v38, v43
	v_fma_f32 v39, -v39, v44, s33
	v_mul_f32_e32 v41, 0x3dd2d3e8, v45
	v_exp_f32_e32 v38, v38
	v_mul_f32_e32 v39, v39, v44
	v_fma_f32 v41, -v41, v45, s33
	v_exp_f32_e32 v39, v39
	v_mul_f32_e32 v41, v41, v45
	v_exp_f32_e32 v41, v41
	v_add_f32_e32 v37, 1.0, v37
	v_rcp_f32_e32 v37, v37
	v_add_f32_e32 v38, 1.0, v38
	v_mul_f32_e32 v46, v35, v35
	v_rcp_f32_e32 v38, v38
	v_add_f32_e32 v39, 1.0, v39
	v_fmac_f32_e32 v46, v40, v40
	v_rcp_f32_e32 v39, v39
	v_add_f32_e32 v41, 1.0, v41
	v_fmac_f32_e32 v46, v34, v34
	v_rcp_f32_e32 v41, v41
	v_fmac_f32_e32 v46, v36, v36
	v_mul_f32_e32 v37, v37, v42
	v_fmac_f32_e32 v46, v37, v37
	v_mul_f32_e32 v38, v38, v43
	v_fmac_f32_e32 v46, v38, v38
	v_mul_f32_e32 v39, v39, v44
	v_fmac_f32_e32 v46, v39, v39
	v_mul_f32_e32 v41, v41, v45
	v_fmac_f32_e32 v46, v41, v41
	v_mov_b32_e32 v42, v46
	s_nop 1
	v_permlane32_swap_b32_e32 v42, v46
	s_waitcnt lgkmcnt(0)
	v_add_f32_e32 v42, v46, v42
	v_mov_b32_e32 v43, v42
	s_nop 1
	v_permlane16_swap_b32_e32 v43, v42
	s_waitcnt lgkmcnt(0)
	v_add_f32_e32 v42, v42, v43
	s_nop 1
	v_mov_b32_dpp v43, v42 row_ror:8 row_mask:0xf bank_mask:0xf
	s_waitcnt lgkmcnt(0)
	v_add_f32_e32 v42, v42, v43
	s_nop 1
	v_mov_b32_dpp v43, v42 row_shl:4 row_mask:0xf bank_mask:0x5
	v_mov_b32_dpp v43, v42 row_shr:4 row_mask:0xf bank_mask:0xa
	s_waitcnt lgkmcnt(0)
	v_add_f32_e32 v42, v42, v43
	s_nop 1
	v_mov_b32_dpp v43, v42 quad_perm:[2,3,0,1] row_mask:0xf bank_mask:0xf
	s_waitcnt lgkmcnt(0)
	v_add_f32_e32 v42, v42, v43
	s_nop 1
	v_mov_b32_dpp v43, v42 quad_perm:[1,0,3,2] row_mask:0xf bank_mask:0xf
	s_and_saveexec_b64 s[0:1], vcc
	s_cbranch_execz .LBB0_493
	s_waitcnt lgkmcnt(0)
	v_add_f32_e32 v42, v42, v43
	v_fmamk_f32 v42, v42, 0x3b000000, v246
	s_mov_b32 s2, 0x800000
	v_cmp_gt_f32_e64 s[2:3], s2, v42
	v_mul_f32_e32 v43, 0x4b800000, v42
	s_nop 0
	v_cndmask_b32_e64 v42, v42, v43, s[2:3]
	v_rsq_f32_e32 v42, v42
	s_nop 0
	v_mul_f32_e32 v43, 0x45800000, v42
	v_cndmask_b32_e64 v50, v42, v43, s[2:3]
	global_load_dwordx4 v[42:45], v[62:63], off offset:16
	global_load_dwordx4 v[46:49], v[62:63], off
	v_mul_f32_e32 v34, v34, v50
	v_mul_f32_e32 v40, v40, v50
	v_mul_f32_e32 v35, v35, v50
	s_waitcnt vmcnt(0)
	v_mul_f32_e32 v34, v34, v48
	v_cvt_pk_bf16_f32 v34, v34, s0
	ds_write_b16 v67, v34 offset:35374
	v_mul_f32_e32 v34, v36, v50
	v_mul_f32_e32 v34, v34, v49
	v_cvt_pk_bf16_f32 v34, v34, s0
	ds_write_b16 v67, v34 offset:35646
	v_mul_f32_e32 v34, v37, v50
	v_mul_f32_e32 v34, v34, v42
	v_cvt_pk_bf16_f32 v34, v34, s0
	ds_write_b16 v67, v34 offset:35918
	v_mul_f32_e32 v34, v38, v50
	v_mul_f32_e32 v34, v34, v43
	v_cvt_pk_bf16_f32 v34, v34, s0
	ds_write_b16 v67, v34 offset:36190
	v_mul_f32_e32 v34, v39, v50
	v_mul_f32_e32 v34, v34, v44
	v_cvt_pk_bf16_f32 v34, v34, s0
	ds_write_b16 v67, v34 offset:36462
	v_mul_f32_e32 v34, v41, v50
	v_mul_f32_e32 v40, v40, v46
	v_mul_f32_e32 v35, v35, v47
	v_mul_f32_e32 v34, v34, v45
	v_cvt_pk_bf16_f32 v40, v40, s0
	v_cvt_pk_bf16_f32 v35, v35, s0
	v_cvt_pk_bf16_f32 v34, v34, s0
	ds_write_b16 v67, v40 offset:34830
	ds_write_b16 v67, v35 offset:35102
	ds_write_b16 v67, v34 offset:36734
; __device__ __forceinline__ float bflo(unsigned w) { return __uint_as_float(w << 16); }
; __device__ __forceinline__ float bfhi(unsigned w) { return __uint_as_float(w & 0xffff0000u); }
; __device__ __forceinline__ unsigned short f2bf(float f) { return (unsigned short)(cvt_pk_bf16(f, 0.f) & 0xffffu); }
; __device__ __forceinline__ void sgu_unit(const Params& p, int l, int un, LAS unsigned char* lds) {
;     ...
;     for (int qi = 0; qi < 16; ++qi) { const int q = wave * 16 + qi;
;         const u32x4 v = vv[qi]; float f[8] = {bflo(v.x), bfhi(v.x), bflo(v.y), bfhi(v.y), bflo(v.z), bfhi(v.z), bflo(v.w), bfhi(v.w)}; float ss = 0.f;
; #pragma unroll
;         for (int j = 0; j < 8; ++j) { f[j] = gelu_tanh(f[j]); ss += f[j] * f[j]; }
;         ss = wave_sum(ss); const float rinv = rsqrtf(ss * (1.0f / 512.0f) + EPS);
;         if ((lane >> 4) == h) { const int c0 = (lane & 15) * 8; const float* g = p.in[I_SGUNG] + l * 512 + h * 128 + c0;
; #pragma unroll
;             for (int j = 0; j < 8; ++j) Vl[(c0 + j) * 136 + q] = f2bf(f[j] * rinv * g[j]); } }
.LBB0_493:
	s_or_b64 exec, exec, s[0:1]
	s_waitcnt vmcnt(7)
	v_lshlrev_b32_e32 v34, 16, v30
	v_lshlrev_b32_e32 v35, 16, v31
	v_and_b32_e32 v37, 0xffff0000, v31
	v_mul_f32_e32 v31, 0x3dd2d3e8, v34
	v_fma_f32 v31, -v31, v34, s33
	v_mul_f32_e32 v31, v31, v34
	v_exp_f32_e32 v31, v31
	v_and_b32_e32 v30, 0xffff0000, v30
	v_lshlrev_b32_e32 v38, 16, v32
	v_and_b32_e32 v39, 0xffff0000, v32
	v_add_f32_e32 v31, 1.0, v31
	v_rcp_f32_e32 v31, v31
	v_mul_f32_e32 v32, 0x3dd2d3e8, v37
	v_fma_f32 v32, -v32, v37, s33
	v_mul_f32_e32 v32, v32, v37
	v_mul_f32_e32 v36, v31, v34
	v_mul_f32_e32 v31, 0x3dd2d3e8, v30
	v_fma_f32 v31, -v31, v30, s33
	v_mul_f32_e32 v31, v31, v30
	v_exp_f32_e32 v31, v31
	v_exp_f32_e32 v32, v32
	v_lshlrev_b32_e32 v40, 16, v33
	v_and_b32_e32 v41, 0xffff0000, v33
	v_add_f32_e32 v31, 1.0, v31
	v_rcp_f32_e32 v31, v31
	v_add_f32_e32 v32, 1.0, v32
	v_rcp_f32_e32 v32, v32
	v_mul_f32_e32 v33, 0x3dd2d3e8, v38
	v_mul_f32_e32 v31, v31, v30
	v_mul_f32_e32 v30, 0x3dd2d3e8, v35
	v_fma_f32 v30, -v30, v35, s33
	v_mul_f32_e32 v30, v30, v35
	v_exp_f32_e32 v30, v30
	v_fma_f32 v33, -v33, v38, s33
	v_mul_f32_e32 v34, 0x3dd2d3e8, v39
	v_mul_f32_e32 v33, v33, v38
	v_add_f32_e32 v30, 1.0, v30
	v_rcp_f32_e32 v30, v30
	v_fma_f32 v34, -v34, v39, s33
	v_mul_f32_e32 v32, v32, v37
	v_exp_f32_e32 v33, v33
	v_mul_f32_e32 v30, v30, v35
	v_mul_f32_e32 v35, 0x3dd2d3e8, v40
	v_mul_f32_e32 v34, v34, v39
	v_fma_f32 v35, -v35, v40, s33
	v_mul_f32_e32 v37, 0x3dd2d3e8, v41
	v_exp_f32_e32 v34, v34
	v_mul_f32_e32 v35, v35, v40
	v_fma_f32 v37, -v37, v41, s33
	v_exp_f32_e32 v35, v35
	v_mul_f32_e32 v37, v37, v41
	v_exp_f32_e32 v37, v37
	v_add_f32_e32 v33, 1.0, v33
	v_rcp_f32_e32 v33, v33
	v_add_f32_e32 v34, 1.0, v34
	v_mul_f32_e32 v42, v31, v31
	v_rcp_f32_e32 v34, v34
	v_add_f32_e32 v35, 1.0, v35
	v_fmac_f32_e32 v42, v36, v36
	v_rcp_f32_e32 v35, v35
	v_add_f32_e32 v37, 1.0, v37
	v_fmac_f32_e32 v42, v30, v30
	v_rcp_f32_e32 v37, v37
	v_fmac_f32_e32 v42, v32, v32
	v_mul_f32_e32 v33, v33, v38
	v_fmac_f32_e32 v42, v33, v33
	v_mul_f32_e32 v34, v34, v39
	v_fmac_f32_e32 v42, v34, v34
	v_mul_f32_e32 v35, v35, v40
	v_fmac_f32_e32 v42, v35, v35
	v_mul_f32_e32 v37, v37, v41
	v_fmac_f32_e32 v42, v37, v37
	v_mov_b32_e32 v38, v42
	s_nop 1
	v_permlane32_swap_b32_e32 v38, v42
	s_waitcnt lgkmcnt(0)
	v_add_f32_e32 v38, v42, v38
	v_mov_b32_e32 v39, v38
	s_nop 1
	v_permlane16_swap_b32_e32 v39, v38
	s_waitcnt lgkmcnt(0)
	v_add_f32_e32 v38, v38, v39
	s_nop 1
	v_mov_b32_dpp v39, v38 row_ror:8 row_mask:0xf bank_mask:0xf
	s_waitcnt lgkmcnt(0)
	v_add_f32_e32 v38, v38, v39
	s_nop 1
	v_mov_b32_dpp v39, v38 row_shl:4 row_mask:0xf bank_mask:0x5
	v_mov_b32_dpp v39, v38 row_shr:4 row_mask:0xf bank_mask:0xa
	s_waitcnt lgkmcnt(0)
	v_add_f32_e32 v38, v38, v39
	s_nop 1
	v_mov_b32_dpp v39, v38 quad_perm:[2,3,0,1] row_mask:0xf bank_mask:0xf
	s_waitcnt lgkmcnt(0)
	v_add_f32_e32 v38, v38, v39
	s_nop 1
	v_mov_b32_dpp v39, v38 quad_perm:[1,0,3,2] row_mask:0xf bank_mask:0xf
	s_and_saveexec_b64 s[0:1], vcc
	s_cbranch_execz .LBB0_495
	s_waitcnt lgkmcnt(0)
	v_add_f32_e32 v38, v38, v39
	v_fmamk_f32 v38, v38, 0x3b000000, v246
	s_mov_b32 s2, 0x800000
	v_cmp_gt_f32_e64 s[2:3], s2, v38
	v_mul_f32_e32 v39, 0x4b800000, v38
	s_nop 0
	v_cndmask_b32_e64 v38, v38, v39, s[2:3]
	v_rsq_f32_e32 v38, v38
	s_nop 0
	v_mul_f32_e32 v39, 0x45800000, v38
	v_cndmask_b32_e64 v46, v38, v39, s[2:3]
	global_load_dwordx4 v[38:41], v[62:63], off offset:16
	global_load_dwordx4 v[42:45], v[62:63], off
	v_mul_f32_e32 v30, v30, v46
	v_mul_f32_e32 v36, v36, v46
	v_mul_f32_e32 v31, v31, v46
	s_waitcnt vmcnt(0)
	v_mul_f32_e32 v30, v30, v44
	v_cvt_pk_bf16_f32 v30, v30, s0
	ds_write_b16 v67, v30 offset:35376
	v_mul_f32_e32 v30, v32, v46
	v_mul_f32_e32 v30, v30, v45
	v_cvt_pk_bf16_f32 v30, v30, s0
	ds_write_b16 v67, v30 offset:35648
	v_mul_f32_e32 v30, v33, v46
	v_mul_f32_e32 v30, v30, v38
	v_cvt_pk_bf16_f32 v30, v30, s0
	ds_write_b16 v67, v30 offset:35920
	v_mul_f32_e32 v30, v34, v46
	v_mul_f32_e32 v30, v30, v39
	v_cvt_pk_bf16_f32 v30, v30, s0
	ds_write_b16 v67, v30 offset:36192
	v_mul_f32_e32 v30, v35, v46
	v_mul_f32_e32 v30, v30, v40
	v_cvt_pk_bf16_f32 v30, v30, s0
	ds_write_b16 v67, v30 offset:36464
	v_mul_f32_e32 v30, v37, v46
	v_mul_f32_e32 v36, v36, v42
	v_mul_f32_e32 v31, v31, v43
	v_mul_f32_e32 v30, v30, v41
	v_cvt_pk_bf16_f32 v36, v36, s0
	v_cvt_pk_bf16_f32 v31, v31, s0
	v_cvt_pk_bf16_f32 v30, v30, s0
	ds_write_b16 v67, v36 offset:34832
	ds_write_b16 v67, v31 offset:35104
	ds_write_b16 v67, v30 offset:36736
; __device__ __forceinline__ float bflo(unsigned w) { return __uint_as_float(w << 16); }
; __device__ __forceinline__ float bfhi(unsigned w) { return __uint_as_float(w & 0xffff0000u); }
; __device__ __forceinline__ unsigned short f2bf(float f) { return (unsigned short)(cvt_pk_bf16(f, 0.f) & 0xffffu); }
; __device__ __forceinline__ float wave_sum(float v) {
; #pragma unroll
;     for (int o = 32; o >= 1; o >>= 1) v += __shfl_xor(v, o);
;     return v;
; }
; __device__ __forceinline__ void sgu_unit(const Params& p, int l, int un, LAS unsigned char* lds) {
;     ...
;     for (int qi = 0; qi < 16; ++qi) { const int q = wave * 16 + qi;
;         const u32x4 v = vv[qi]; float f[8] = {bflo(v.x), bfhi(v.x), bflo(v.y), bfhi(v.y), bflo(v.z), bfhi(v.z), bflo(v.w), bfhi(v.w)}; float ss = 0.f;
; #pragma unroll
;         for (int j = 0; j < 8; ++j) { f[j] = gelu_tanh(f[j]); ss += f[j] * f[j]; }
;         ss = wave_sum(ss); const float rinv = rsqrtf(ss * (1.0f / 512.0f) + EPS);
;         if ((lane >> 4) == h) { const int c0 = (lane & 15) * 8; const float* g = p.in[I_SGUNG] + l * 512 + h * 128 + c0;
; #pragma unroll
;             for (int j = 0; j < 8; ++j) Vl[(c0 + j) * 136 + q] = f2bf(f[j] * rinv * g[j]); } }
.LBB0_495:
	s_or_b64 exec, exec, s[0:1]
	s_waitcnt vmcnt(6)
	v_lshlrev_b32_e32 v30, 16, v26
	v_lshlrev_b32_e32 v31, 16, v27
	v_and_b32_e32 v33, 0xffff0000, v27
	v_mul_f32_e32 v27, 0x3dd2d3e8, v30
	v_fma_f32 v27, -v27, v30, s33
	v_mul_f32_e32 v27, v27, v30
	v_exp_f32_e32 v27, v27
	v_and_b32_e32 v26, 0xffff0000, v26
	v_lshlrev_b32_e32 v34, 16, v28
	v_and_b32_e32 v35, 0xffff0000, v28
	v_add_f32_e32 v27, 1.0, v27
	v_rcp_f32_e32 v27, v27
	v_mul_f32_e32 v28, 0x3dd2d3e8, v33
	v_fma_f32 v28, -v28, v33, s33
	v_mul_f32_e32 v28, v28, v33
	v_mul_f32_e32 v32, v27, v30
	v_mul_f32_e32 v27, 0x3dd2d3e8, v26
	v_fma_f32 v27, -v27, v26, s33
	v_mul_f32_e32 v27, v27, v26
	v_exp_f32_e32 v27, v27
	v_exp_f32_e32 v28, v28
	v_lshlrev_b32_e32 v36, 16, v29
	v_and_b32_e32 v37, 0xffff0000, v29
	v_add_f32_e32 v27, 1.0, v27
	v_rcp_f32_e32 v27, v27
	v_add_f32_e32 v28, 1.0, v28
	v_rcp_f32_e32 v28, v28
	v_mul_f32_e32 v29, 0x3dd2d3e8, v34
	v_mul_f32_e32 v27, v27, v26
	v_mul_f32_e32 v26, 0x3dd2d3e8, v31
	v_fma_f32 v26, -v26, v31, s33
	v_mul_f32_e32 v26, v26, v31
	v_exp_f32_e32 v26, v26
	v_fma_f32 v29, -v29, v34, s33
	v_mul_f32_e32 v30, 0x3dd2d3e8, v35
	v_mul_f32_e32 v29, v29, v34
	v_add_f32_e32 v26, 1.0, v26
	v_rcp_f32_e32 v26, v26
	v_fma_f32 v30, -v30, v35, s33
	v_mul_f32_e32 v28, v28, v33
	v_exp_f32_e32 v29, v29
	v_mul_f32_e32 v26, v26, v31
	v_mul_f32_e32 v31, 0x3dd2d3e8, v36
	v_mul_f32_e32 v30, v30, v35
	v_fma_f32 v31, -v31, v36, s33
	v_mul_f32_e32 v33, 0x3dd2d3e8, v37
	v_exp_f32_e32 v30, v30
	v_mul_f32_e32 v31, v31, v36
	v_fma_f32 v33, -v33, v37, s33
	v_exp_f32_e32 v31, v31
	v_mul_f32_e32 v33, v33, v37
	v_exp_f32_e32 v33, v33
	v_add_f32_e32 v29, 1.0, v29
	v_rcp_f32_e32 v29, v29
	v_add_f32_e32 v30, 1.0, v30
	v_mul_f32_e32 v38, v27, v27
	v_rcp_f32_e32 v30, v30
	v_add_f32_e32 v31, 1.0, v31
	v_fmac_f32_e32 v38, v32, v32
	v_rcp_f32_e32 v31, v31
	v_add_f32_e32 v33, 1.0, v33
	v_fmac_f32_e32 v38, v26, v26
	v_rcp_f32_e32 v33, v33
	v_fmac_f32_e32 v38, v28, v28
	v_mul_f32_e32 v29, v29, v34
	v_fmac_f32_e32 v38, v29, v29
	v_mul_f32_e32 v30, v30, v35
	v_fmac_f32_e32 v38, v30, v30
	v_mul_f32_e32 v31, v31, v36
	v_fmac_f32_e32 v38, v31, v31
	v_mul_f32_e32 v33, v33, v37
	v_fmac_f32_e32 v38, v33, v33
	v_mov_b32_e32 v34, v38
	s_nop 1
	v_permlane32_swap_b32_e32 v34, v38
	s_waitcnt lgkmcnt(0)
	v_add_f32_e32 v34, v38, v34
	v_mov_b32_e32 v35, v34
	s_nop 1
	v_permlane16_swap_b32_e32 v35, v34
	s_waitcnt lgkmcnt(0)
	v_add_f32_e32 v34, v34, v35
	s_nop 1
	v_mov_b32_dpp v35, v34 row_ror:8 row_mask:0xf bank_mask:0xf
	s_waitcnt lgkmcnt(0)
	v_add_f32_e32 v34, v34, v35
	s_nop 1
	v_mov_b32_dpp v35, v34 row_shl:4 row_mask:0xf bank_mask:0x5
	v_mov_b32_dpp v35, v34 row_shr:4 row_mask:0xf bank_mask:0xa
	s_waitcnt lgkmcnt(0)
	v_add_f32_e32 v34, v34, v35
	s_nop 1
	v_mov_b32_dpp v35, v34 quad_perm:[2,3,0,1] row_mask:0xf bank_mask:0xf
	s_waitcnt lgkmcnt(0)
	v_add_f32_e32 v34, v34, v35
	s_nop 1
	v_mov_b32_dpp v35, v34 quad_perm:[1,0,3,2] row_mask:0xf bank_mask:0xf
	s_and_saveexec_b64 s[0:1], vcc
	s_cbranch_execz .LBB0_497
	s_waitcnt lgkmcnt(0)
	v_add_f32_e32 v34, v34, v35
	v_fmamk_f32 v34, v34, 0x3b000000, v246
	s_mov_b32 s2, 0x800000
	v_cmp_gt_f32_e64 s[2:3], s2, v34
	v_mul_f32_e32 v35, 0x4b800000, v34
	s_nop 0
	v_cndmask_b32_e64 v34, v34, v35, s[2:3]
	v_rsq_f32_e32 v34, v34
	s_nop 0
	v_mul_f32_e32 v35, 0x45800000, v34
	v_cndmask_b32_e64 v42, v34, v35, s[2:3]
	global_load_dwordx4 v[34:37], v[62:63], off offset:16
	global_load_dwordx4 v[38:41], v[62:63], off
	v_mul_f32_e32 v26, v26, v42
	v_mul_f32_e32 v32, v32, v42
	v_mul_f32_e32 v27, v27, v42
	s_waitcnt vmcnt(0)
	v_mul_f32_e32 v26, v26, v40
	v_cvt_pk_bf16_f32 v26, v26, s0
	ds_write_b16 v67, v26 offset:35378
	v_mul_f32_e32 v26, v28, v42
	v_mul_f32_e32 v26, v26, v41
	v_cvt_pk_bf16_f32 v26, v26, s0
	ds_write_b16 v67, v26 offset:35650
	v_mul_f32_e32 v26, v29, v42
	v_mul_f32_e32 v26, v26, v34
	v_cvt_pk_bf16_f32 v26, v26, s0
	ds_write_b16 v67, v26 offset:35922
	v_mul_f32_e32 v26, v30, v42
	v_mul_f32_e32 v26, v26, v35
	v_cvt_pk_bf16_f32 v26, v26, s0
	ds_write_b16 v67, v26 offset:36194
	v_mul_f32_e32 v26, v31, v42
	v_mul_f32_e32 v26, v26, v36
	v_cvt_pk_bf16_f32 v26, v26, s0
	ds_write_b16 v67, v26 offset:36466
	v_mul_f32_e32 v26, v33, v42
	v_mul_f32_e32 v32, v32, v38
	v_mul_f32_e32 v27, v27, v39
	v_mul_f32_e32 v26, v26, v37
	v_cvt_pk_bf16_f32 v32, v32, s0
	v_cvt_pk_bf16_f32 v27, v27, s0
	v_cvt_pk_bf16_f32 v26, v26, s0
	ds_write_b16 v67, v32 offset:34834
	ds_write_b16 v67, v27 offset:35106
	ds_write_b16 v67, v26 offset:36738
; __device__ __forceinline__ float bflo(unsigned w) { return __uint_as_float(w << 16); }
; __device__ __forceinline__ float bfhi(unsigned w) { return __uint_as_float(w & 0xffff0000u); }
; __device__ __forceinline__ unsigned short f2bf(float f) { return (unsigned short)(cvt_pk_bf16(f, 0.f) & 0xffffu); }
; __device__ __forceinline__ float wave_sum(float v) {
; #pragma unroll
;     for (int o = 32; o >= 1; o >>= 1) v += __shfl_xor(v, o);
;     return v;
; }
; __device__ __forceinline__ void sgu_unit(const Params& p, int l, int un, LAS unsigned char* lds) {
;     ...
;     for (int qi = 0; qi < 16; ++qi) { const int q = wave * 16 + qi;
;         const u32x4 v = vv[qi]; float f[8] = {bflo(v.x), bfhi(v.x), bflo(v.y), bfhi(v.y), bflo(v.z), bfhi(v.z), bflo(v.w), bfhi(v.w)}; float ss = 0.f;
; #pragma unroll
;         for (int j = 0; j < 8; ++j) { f[j] = gelu_tanh(f[j]); ss += f[j] * f[j]; }
;         ss = wave_sum(ss); const float rinv = rsqrtf(ss * (1.0f / 512.0f) + EPS);
;         if ((lane >> 4) == h) { const int c0 = (lane & 15) * 8; const float* g = p.in[I_SGUNG] + l * 512 + h * 128 + c0;
; #pragma unroll
;             for (int j = 0; j < 8; ++j) Vl[(c0 + j) * 136 + q] = f2bf(f[j] * rinv * g[j]); } }
.LBB0_497:
	s_or_b64 exec, exec, s[0:1]
	s_waitcnt vmcnt(5)
	v_lshlrev_b32_e32 v26, 16, v22
	v_lshlrev_b32_e32 v27, 16, v23
	v_and_b32_e32 v29, 0xffff0000, v23
	v_mul_f32_e32 v23, 0x3dd2d3e8, v26
	v_fma_f32 v23, -v23, v26, s33
	v_mul_f32_e32 v23, v23, v26
	v_exp_f32_e32 v23, v23
	v_and_b32_e32 v22, 0xffff0000, v22
	v_lshlrev_b32_e32 v30, 16, v24
	v_and_b32_e32 v31, 0xffff0000, v24
	v_add_f32_e32 v23, 1.0, v23
	v_rcp_f32_e32 v23, v23
	v_mul_f32_e32 v24, 0x3dd2d3e8, v29
	v_fma_f32 v24, -v24, v29, s33
	v_mul_f32_e32 v24, v24, v29
	v_mul_f32_e32 v28, v23, v26
	v_mul_f32_e32 v23, 0x3dd2d3e8, v22
	v_fma_f32 v23, -v23, v22, s33
	v_mul_f32_e32 v23, v23, v22
	v_exp_f32_e32 v23, v23
	v_exp_f32_e32 v24, v24
	v_lshlrev_b32_e32 v32, 16, v25
	v_and_b32_e32 v33, 0xffff0000, v25
	v_add_f32_e32 v23, 1.0, v23
	v_rcp_f32_e32 v23, v23
	v_add_f32_e32 v24, 1.0, v24
	v_rcp_f32_e32 v24, v24
	v_mul_f32_e32 v25, 0x3dd2d3e8, v30
	v_mul_f32_e32 v23, v23, v22
	v_mul_f32_e32 v22, 0x3dd2d3e8, v27
	v_fma_f32 v22, -v22, v27, s33
	v_mul_f32_e32 v22, v22, v27
	v_exp_f32_e32 v22, v22
	v_fma_f32 v25, -v25, v30, s33
	v_mul_f32_e32 v26, 0x3dd2d3e8, v31
	v_mul_f32_e32 v25, v25, v30
	v_add_f32_e32 v22, 1.0, v22
	v_rcp_f32_e32 v22, v22
	v_fma_f32 v26, -v26, v31, s33
	v_mul_f32_e32 v24, v24, v29
	v_exp_f32_e32 v25, v25
	v_mul_f32_e32 v22, v22, v27
	v_mul_f32_e32 v27, 0x3dd2d3e8, v32
	v_mul_f32_e32 v26, v26, v31
	v_fma_f32 v27, -v27, v32, s33
	v_mul_f32_e32 v29, 0x3dd2d3e8, v33
	v_exp_f32_e32 v26, v26
	v_mul_f32_e32 v27, v27, v32
	v_fma_f32 v29, -v29, v33, s33
	v_exp_f32_e32 v27, v27
	v_mul_f32_e32 v29, v29, v33
	v_exp_f32_e32 v29, v29
	v_add_f32_e32 v25, 1.0, v25
	v_rcp_f32_e32 v25, v25
	v_add_f32_e32 v26, 1.0, v26
	v_mul_f32_e32 v34, v23, v23
	v_rcp_f32_e32 v26, v26
	v_add_f32_e32 v27, 1.0, v27
	v_fmac_f32_e32 v34, v28, v28
	v_rcp_f32_e32 v27, v27
	v_add_f32_e32 v29, 1.0, v29
	v_fmac_f32_e32 v34, v22, v22
	v_rcp_f32_e32 v29, v29
	v_fmac_f32_e32 v34, v24, v24
	v_mul_f32_e32 v25, v25, v30
	v_fmac_f32_e32 v34, v25, v25
	v_mul_f32_e32 v26, v26, v31
	v_fmac_f32_e32 v34, v26, v26
	v_mul_f32_e32 v27, v27, v32
	v_fmac_f32_e32 v34, v27, v27
	v_mul_f32_e32 v29, v29, v33
	v_fmac_f32_e32 v34, v29, v29
	v_mov_b32_e32 v30, v34
	s_nop 1
	v_permlane32_swap_b32_e32 v30, v34
	s_waitcnt lgkmcnt(0)
	v_add_f32_e32 v30, v34, v30
	v_mov_b32_e32 v31, v30
	s_nop 1
	v_permlane16_swap_b32_e32 v31, v30
	s_waitcnt lgkmcnt(0)
	v_add_f32_e32 v30, v30, v31
	s_nop 1
	v_mov_b32_dpp v31, v30 row_ror:8 row_mask:0xf bank_mask:0xf
	s_waitcnt lgkmcnt(0)
	v_add_f32_e32 v30, v30, v31
	s_nop 1
	v_mov_b32_dpp v31, v30 row_shl:4 row_mask:0xf bank_mask:0x5
	v_mov_b32_dpp v31, v30 row_shr:4 row_mask:0xf bank_mask:0xa
	s_waitcnt lgkmcnt(0)
	v_add_f32_e32 v30, v30, v31
	s_nop 1
	v_mov_b32_dpp v31, v30 quad_perm:[2,3,0,1] row_mask:0xf bank_mask:0xf
	s_waitcnt lgkmcnt(0)
	v_add_f32_e32 v30, v30, v31
	s_nop 1
	v_mov_b32_dpp v31, v30 quad_perm:[1,0,3,2] row_mask:0xf bank_mask:0xf
	s_and_saveexec_b64 s[0:1], vcc
	s_cbranch_execz .LBB0_499
	s_waitcnt lgkmcnt(0)
	v_add_f32_e32 v30, v30, v31
	v_fmamk_f32 v30, v30, 0x3b000000, v246
	s_mov_b32 s2, 0x800000
	v_cmp_gt_f32_e64 s[2:3], s2, v30
	v_mul_f32_e32 v31, 0x4b800000, v30
	s_nop 0
	v_cndmask_b32_e64 v30, v30, v31, s[2:3]
	v_rsq_f32_e32 v30, v30
	s_nop 0
	v_mul_f32_e32 v31, 0x45800000, v30
	v_cndmask_b32_e64 v38, v30, v31, s[2:3]
	global_load_dwordx4 v[30:33], v[62:63], off offset:16
	global_load_dwordx4 v[34:37], v[62:63], off
	v_mul_f32_e32 v22, v22, v38
	v_mul_f32_e32 v28, v28, v38
	v_mul_f32_e32 v23, v23, v38
	s_waitcnt vmcnt(0)
	v_mul_f32_e32 v22, v22, v36
	v_cvt_pk_bf16_f32 v22, v22, s0
	ds_write_b16 v67, v22 offset:35380
	v_mul_f32_e32 v22, v24, v38
	v_mul_f32_e32 v22, v22, v37
	v_cvt_pk_bf16_f32 v22, v22, s0
	ds_write_b16 v67, v22 offset:35652
	v_mul_f32_e32 v22, v25, v38
	v_mul_f32_e32 v22, v22, v30
	v_cvt_pk_bf16_f32 v22, v22, s0
	ds_write_b16 v67, v22 offset:35924
	v_mul_f32_e32 v22, v26, v38
	v_mul_f32_e32 v22, v22, v31
	v_cvt_pk_bf16_f32 v22, v22, s0
	ds_write_b16 v67, v22 offset:36196
	v_mul_f32_e32 v22, v27, v38
	v_mul_f32_e32 v22, v22, v32
	v_cvt_pk_bf16_f32 v22, v22, s0
	ds_write_b16 v67, v22 offset:36468
	v_mul_f32_e32 v22, v29, v38
	v_mul_f32_e32 v28, v28, v34
	v_mul_f32_e32 v23, v23, v35
	v_mul_f32_e32 v22, v22, v33
	v_cvt_pk_bf16_f32 v28, v28, s0
	v_cvt_pk_bf16_f32 v23, v23, s0
	v_cvt_pk_bf16_f32 v22, v22, s0
	ds_write_b16 v67, v28 offset:34836
	ds_write_b16 v67, v23 offset:35108
	ds_write_b16 v67, v22 offset:36740
; __device__ __forceinline__ float bflo(unsigned w) { return __uint_as_float(w << 16); }
; __device__ __forceinline__ float bfhi(unsigned w) { return __uint_as_float(w & 0xffff0000u); }
; __device__ __forceinline__ unsigned short f2bf(float f) { return (unsigned short)(cvt_pk_bf16(f, 0.f) & 0xffffu); }
; __device__ __forceinline__ float wave_sum(float v) {
; #pragma unroll
;     for (int o = 32; o >= 1; o >>= 1) v += __shfl_xor(v, o);
;     return v;
; }
; __device__ __forceinline__ void sgu_unit(const Params& p, int l, int un, LAS unsigned char* lds) {
;     ...
;     for (int qi = 0; qi < 16; ++qi) { const int q = wave * 16 + qi;
;         const u32x4 v = vv[qi]; float f[8] = {bflo(v.x), bfhi(v.x), bflo(v.y), bfhi(v.y), bflo(v.z), bfhi(v.z), bflo(v.w), bfhi(v.w)}; float ss = 0.f;
; #pragma unroll
;         for (int j = 0; j < 8; ++j) { f[j] = gelu_tanh(f[j]); ss += f[j] * f[j]; }
;         ss = wave_sum(ss); const float rinv = rsqrtf(ss * (1.0f / 512.0f) + EPS);
;         if ((lane >> 4) == h) { const int c0 = (lane & 15) * 8; const float* g = p.in[I_SGUNG] + l * 512 + h * 128 + c0;
; #pragma unroll
;             for (int j = 0; j < 8; ++j) Vl[(c0 + j) * 136 + q] = f2bf(f[j] * rinv * g[j]); } }
.LBB0_499:
	s_or_b64 exec, exec, s[0:1]
	s_waitcnt vmcnt(4)
	v_lshlrev_b32_e32 v22, 16, v18
	v_lshlrev_b32_e32 v23, 16, v19
	v_and_b32_e32 v25, 0xffff0000, v19
	v_mul_f32_e32 v19, 0x3dd2d3e8, v22
	v_fma_f32 v19, -v19, v22, s33
	v_mul_f32_e32 v19, v19, v22
	v_exp_f32_e32 v19, v19
	v_and_b32_e32 v18, 0xffff0000, v18
	v_lshlrev_b32_e32 v26, 16, v20
	v_and_b32_e32 v27, 0xffff0000, v20
	v_add_f32_e32 v19, 1.0, v19
	v_rcp_f32_e32 v19, v19
	v_mul_f32_e32 v20, 0x3dd2d3e8, v25
	v_fma_f32 v20, -v20, v25, s33
	v_mul_f32_e32 v20, v20, v25
	v_mul_f32_e32 v24, v19, v22
	v_mul_f32_e32 v19, 0x3dd2d3e8, v18
	v_fma_f32 v19, -v19, v18, s33
	v_mul_f32_e32 v19, v19, v18
	v_exp_f32_e32 v19, v19
	v_exp_f32_e32 v20, v20
	v_lshlrev_b32_e32 v28, 16, v21
	v_and_b32_e32 v29, 0xffff0000, v21
	v_add_f32_e32 v19, 1.0, v19
	v_rcp_f32_e32 v19, v19
	v_add_f32_e32 v20, 1.0, v20
	v_rcp_f32_e32 v20, v20
	v_mul_f32_e32 v21, 0x3dd2d3e8, v26
	v_mul_f32_e32 v19, v19, v18
	v_mul_f32_e32 v18, 0x3dd2d3e8, v23
	v_fma_f32 v18, -v18, v23, s33
	v_mul_f32_e32 v18, v18, v23
	v_exp_f32_e32 v18, v18
	v_fma_f32 v21, -v21, v26, s33
	v_mul_f32_e32 v22, 0x3dd2d3e8, v27
	v_mul_f32_e32 v21, v21, v26
	v_add_f32_e32 v18, 1.0, v18
	v_rcp_f32_e32 v18, v18
	v_fma_f32 v22, -v22, v27, s33
	v_mul_f32_e32 v20, v20, v25
	v_exp_f32_e32 v21, v21
	v_mul_f32_e32 v18, v18, v23
	v_mul_f32_e32 v23, 0x3dd2d3e8, v28
	v_mul_f32_e32 v22, v22, v27
	v_fma_f32 v23, -v23, v28, s33
	v_mul_f32_e32 v25, 0x3dd2d3e8, v29
	v_exp_f32_e32 v22, v22
	v_mul_f32_e32 v23, v23, v28
	v_fma_f32 v25, -v25, v29, s33
	v_exp_f32_e32 v23, v23
	v_mul_f32_e32 v25, v25, v29
	v_exp_f32_e32 v25, v25
	v_add_f32_e32 v21, 1.0, v21
	v_rcp_f32_e32 v21, v21
	v_add_f32_e32 v22, 1.0, v22
	v_mul_f32_e32 v30, v19, v19
	v_rcp_f32_e32 v22, v22
	v_add_f32_e32 v23, 1.0, v23
	v_fmac_f32_e32 v30, v24, v24
	v_rcp_f32_e32 v23, v23
	v_add_f32_e32 v25, 1.0, v25
	v_fmac_f32_e32 v30, v18, v18
	v_rcp_f32_e32 v25, v25
	v_fmac_f32_e32 v30, v20, v20
	v_mul_f32_e32 v21, v21, v26
	v_fmac_f32_e32 v30, v21, v21
	v_mul_f32_e32 v22, v22, v27
	v_fmac_f32_e32 v30, v22, v22
	v_mul_f32_e32 v23, v23, v28
	v_fmac_f32_e32 v30, v23, v23
	v_mul_f32_e32 v25, v25, v29
	v_fmac_f32_e32 v30, v25, v25
	v_mov_b32_e32 v26, v30
	s_nop 1
	v_permlane32_swap_b32_e32 v26, v30
	s_waitcnt lgkmcnt(0)
	v_add_f32_e32 v26, v30, v26
	v_mov_b32_e32 v27, v26
	s_nop 1
	v_permlane16_swap_b32_e32 v27, v26
	s_waitcnt lgkmcnt(0)
	v_add_f32_e32 v26, v26, v27
	s_nop 1
	v_mov_b32_dpp v27, v26 row_ror:8 row_mask:0xf bank_mask:0xf
	s_waitcnt lgkmcnt(0)
	v_add_f32_e32 v26, v26, v27
	s_nop 1
	v_mov_b32_dpp v27, v26 row_shl:4 row_mask:0xf bank_mask:0x5
	v_mov_b32_dpp v27, v26 row_shr:4 row_mask:0xf bank_mask:0xa
	s_waitcnt lgkmcnt(0)
	v_add_f32_e32 v26, v26, v27
	s_nop 1
	v_mov_b32_dpp v27, v26 quad_perm:[2,3,0,1] row_mask:0xf bank_mask:0xf
	s_waitcnt lgkmcnt(0)
	v_add_f32_e32 v26, v26, v27
	s_nop 1
	v_mov_b32_dpp v27, v26 quad_perm:[1,0,3,2] row_mask:0xf bank_mask:0xf
	s_and_saveexec_b64 s[0:1], vcc
	s_cbranch_execz .LBB0_501
	s_waitcnt lgkmcnt(0)
	v_add_f32_e32 v26, v26, v27
	v_fmamk_f32 v26, v26, 0x3b000000, v246
	s_mov_b32 s2, 0x800000
	v_cmp_gt_f32_e64 s[2:3], s2, v26
	v_mul_f32_e32 v27, 0x4b800000, v26
	s_nop 0
	v_cndmask_b32_e64 v26, v26, v27, s[2:3]
	v_rsq_f32_e32 v26, v26
	s_nop 0
	v_mul_f32_e32 v27, 0x45800000, v26
	v_cndmask_b32_e64 v34, v26, v27, s[2:3]
	global_load_dwordx4 v[26:29], v[62:63], off offset:16
	global_load_dwordx4 v[30:33], v[62:63], off
	v_mul_f32_e32 v18, v18, v34
	v_mul_f32_e32 v24, v24, v34
	v_mul_f32_e32 v19, v19, v34
	s_waitcnt vmcnt(0)
	v_mul_f32_e32 v18, v18, v32
	v_cvt_pk_bf16_f32 v18, v18, s0
	ds_write_b16 v67, v18 offset:35382
	v_mul_f32_e32 v18, v20, v34
	v_mul_f32_e32 v18, v18, v33
	v_cvt_pk_bf16_f32 v18, v18, s0
	ds_write_b16 v67, v18 offset:35654
	v_mul_f32_e32 v18, v21, v34
	v_mul_f32_e32 v18, v18, v26
	v_cvt_pk_bf16_f32 v18, v18, s0
	ds_write_b16 v67, v18 offset:35926
	v_mul_f32_e32 v18, v22, v34
	v_mul_f32_e32 v18, v18, v27
	v_cvt_pk_bf16_f32 v18, v18, s0
	ds_write_b16 v67, v18 offset:36198
	v_mul_f32_e32 v18, v23, v34
	v_mul_f32_e32 v18, v18, v28
	v_cvt_pk_bf16_f32 v18, v18, s0
	ds_write_b16 v67, v18 offset:36470
	v_mul_f32_e32 v18, v25, v34
	v_mul_f32_e32 v24, v24, v30
	v_mul_f32_e32 v19, v19, v31
	v_mul_f32_e32 v18, v18, v29
	v_cvt_pk_bf16_f32 v24, v24, s0
	v_cvt_pk_bf16_f32 v19, v19, s0
	v_cvt_pk_bf16_f32 v18, v18, s0
	ds_write_b16 v67, v24 offset:34838
	ds_write_b16 v67, v19 offset:35110
	ds_write_b16 v67, v18 offset:36742
; __device__ __forceinline__ float bflo(unsigned w) { return __uint_as_float(w << 16); }
; __device__ __forceinline__ float bfhi(unsigned w) { return __uint_as_float(w & 0xffff0000u); }
; __device__ __forceinline__ unsigned short f2bf(float f) { return (unsigned short)(cvt_pk_bf16(f, 0.f) & 0xffffu); }
; __device__ __forceinline__ float wave_sum(float v) {
; #pragma unroll
;     for (int o = 32; o >= 1; o >>= 1) v += __shfl_xor(v, o);
;     return v;
; }
; __device__ __forceinline__ void sgu_unit(const Params& p, int l, int un, LAS unsigned char* lds) {
;     ...
;     for (int qi = 0; qi < 16; ++qi) { const int q = wave * 16 + qi;
;         const u32x4 v = vv[qi]; float f[8] = {bflo(v.x), bfhi(v.x), bflo(v.y), bfhi(v.y), bflo(v.z), bfhi(v.z), bflo(v.w), bfhi(v.w)}; float ss = 0.f;
; #pragma unroll
;         for (int j = 0; j < 8; ++j) { f[j] = gelu_tanh(f[j]); ss += f[j] * f[j]; }
;         ss = wave_sum(ss); const float rinv = rsqrtf(ss * (1.0f / 512.0f) + EPS);
;         if ((lane >> 4) == h) { const int c0 = (lane & 15) * 8; const float* g = p.in[I_SGUNG] + l * 512 + h * 128 + c0;
; #pragma unroll
;             for (int j = 0; j < 8; ++j) Vl[(c0 + j) * 136 + q] = f2bf(f[j] * rinv * g[j]); } }
.LBB0_501:
	s_or_b64 exec, exec, s[0:1]
	s_waitcnt vmcnt(3)
	v_lshlrev_b32_e32 v18, 16, v14
	v_lshlrev_b32_e32 v19, 16, v15
	v_and_b32_e32 v21, 0xffff0000, v15
	v_mul_f32_e32 v15, 0x3dd2d3e8, v18
	v_fma_f32 v15, -v15, v18, s33
	v_mul_f32_e32 v15, v15, v18
	v_exp_f32_e32 v15, v15
	v_and_b32_e32 v14, 0xffff0000, v14
	v_lshlrev_b32_e32 v22, 16, v16
	v_and_b32_e32 v23, 0xffff0000, v16
	v_add_f32_e32 v15, 1.0, v15
	v_rcp_f32_e32 v15, v15
	v_mul_f32_e32 v16, 0x3dd2d3e8, v21
	v_fma_f32 v16, -v16, v21, s33
	v_mul_f32_e32 v16, v16, v21
	v_mul_f32_e32 v20, v15, v18
	v_mul_f32_e32 v15, 0x3dd2d3e8, v14
	v_fma_f32 v15, -v15, v14, s33
	v_mul_f32_e32 v15, v15, v14
	v_exp_f32_e32 v15, v15
	v_exp_f32_e32 v16, v16
	v_lshlrev_b32_e32 v24, 16, v17
	v_and_b32_e32 v25, 0xffff0000, v17
	v_add_f32_e32 v15, 1.0, v15
	v_rcp_f32_e32 v15, v15
	v_add_f32_e32 v16, 1.0, v16
	v_rcp_f32_e32 v16, v16
	v_mul_f32_e32 v17, 0x3dd2d3e8, v22
	v_mul_f32_e32 v15, v15, v14
	v_mul_f32_e32 v14, 0x3dd2d3e8, v19
	v_fma_f32 v14, -v14, v19, s33
	v_mul_f32_e32 v14, v14, v19
	v_exp_f32_e32 v14, v14
	v_fma_f32 v17, -v17, v22, s33
	v_mul_f32_e32 v18, 0x3dd2d3e8, v23
	v_mul_f32_e32 v17, v17, v22
	v_add_f32_e32 v14, 1.0, v14
	v_rcp_f32_e32 v14, v14
	v_fma_f32 v18, -v18, v23, s33
	v_mul_f32_e32 v16, v16, v21
	v_exp_f32_e32 v17, v17
	v_mul_f32_e32 v14, v14, v19
	v_mul_f32_e32 v19, 0x3dd2d3e8, v24
	v_mul_f32_e32 v18, v18, v23
	v_fma_f32 v19, -v19, v24, s33
	v_mul_f32_e32 v21, 0x3dd2d3e8, v25
	v_exp_f32_e32 v18, v18
	v_mul_f32_e32 v19, v19, v24
	v_fma_f32 v21, -v21, v25, s33
	v_exp_f32_e32 v19, v19
	v_mul_f32_e32 v21, v21, v25
	v_exp_f32_e32 v21, v21
	v_add_f32_e32 v17, 1.0, v17
	v_rcp_f32_e32 v17, v17
	v_add_f32_e32 v18, 1.0, v18
	v_mul_f32_e32 v26, v15, v15
	v_rcp_f32_e32 v18, v18
	v_add_f32_e32 v19, 1.0, v19
	v_fmac_f32_e32 v26, v20, v20
	v_rcp_f32_e32 v19, v19
	v_add_f32_e32 v21, 1.0, v21
	v_fmac_f32_e32 v26, v14, v14
	v_rcp_f32_e32 v21, v21
	v_fmac_f32_e32 v26, v16, v16
	v_mul_f32_e32 v17, v17, v22
	v_fmac_f32_e32 v26, v17, v17
	v_mul_f32_e32 v18, v18, v23
	v_fmac_f32_e32 v26, v18, v18
	v_mul_f32_e32 v19, v19, v24
	v_fmac_f32_e32 v26, v19, v19
	v_mul_f32_e32 v21, v21, v25
	v_fmac_f32_e32 v26, v21, v21
	v_mov_b32_e32 v22, v26
	s_nop 1
	v_permlane32_swap_b32_e32 v22, v26
	s_waitcnt lgkmcnt(0)
	v_add_f32_e32 v22, v26, v22
	v_mov_b32_e32 v23, v22
	s_nop 1
	v_permlane16_swap_b32_e32 v23, v22
	s_waitcnt lgkmcnt(0)
	v_add_f32_e32 v22, v22, v23
	s_nop 1
	v_mov_b32_dpp v23, v22 row_ror:8 row_mask:0xf bank_mask:0xf
	s_waitcnt lgkmcnt(0)
	v_add_f32_e32 v22, v22, v23
	s_nop 1
	v_mov_b32_dpp v23, v22 row_shl:4 row_mask:0xf bank_mask:0x5
	v_mov_b32_dpp v23, v22 row_shr:4 row_mask:0xf bank_mask:0xa
	s_waitcnt lgkmcnt(0)
	v_add_f32_e32 v22, v22, v23
	s_nop 1
	v_mov_b32_dpp v23, v22 quad_perm:[2,3,0,1] row_mask:0xf bank_mask:0xf
	s_waitcnt lgkmcnt(0)
	v_add_f32_e32 v22, v22, v23
	s_nop 1
	v_mov_b32_dpp v23, v22 quad_perm:[1,0,3,2] row_mask:0xf bank_mask:0xf
	s_and_saveexec_b64 s[0:1], vcc
	s_cbranch_execz .LBB0_503
	s_waitcnt lgkmcnt(0)
	v_add_f32_e32 v22, v22, v23
	v_fmamk_f32 v22, v22, 0x3b000000, v246
	s_mov_b32 s2, 0x800000
	v_cmp_gt_f32_e64 s[2:3], s2, v22
	v_mul_f32_e32 v23, 0x4b800000, v22
	s_nop 0
	v_cndmask_b32_e64 v22, v22, v23, s[2:3]
	v_rsq_f32_e32 v22, v22
	s_nop 0
	v_mul_f32_e32 v23, 0x45800000, v22
	v_cndmask_b32_e64 v30, v22, v23, s[2:3]
	global_load_dwordx4 v[22:25], v[62:63], off offset:16
	global_load_dwordx4 v[26:29], v[62:63], off
	v_mul_f32_e32 v14, v14, v30
	v_mul_f32_e32 v20, v20, v30
	v_mul_f32_e32 v15, v15, v30
	s_waitcnt vmcnt(0)
	v_mul_f32_e32 v14, v14, v28
	v_cvt_pk_bf16_f32 v14, v14, s0
	ds_write_b16 v67, v14 offset:35384
	v_mul_f32_e32 v14, v16, v30
	v_mul_f32_e32 v14, v14, v29
	v_cvt_pk_bf16_f32 v14, v14, s0
	ds_write_b16 v67, v14 offset:35656
	v_mul_f32_e32 v14, v17, v30
	v_mul_f32_e32 v14, v14, v22
	v_cvt_pk_bf16_f32 v14, v14, s0
	ds_write_b16 v67, v14 offset:35928
	v_mul_f32_e32 v14, v18, v30
	v_mul_f32_e32 v14, v14, v23
	v_cvt_pk_bf16_f32 v14, v14, s0
	ds_write_b16 v67, v14 offset:36200
	v_mul_f32_e32 v14, v19, v30
	v_mul_f32_e32 v14, v14, v24
	v_cvt_pk_bf16_f32 v14, v14, s0
	ds_write_b16 v67, v14 offset:36472
	v_mul_f32_e32 v14, v21, v30
	v_mul_f32_e32 v20, v20, v26
	v_mul_f32_e32 v15, v15, v27
	v_mul_f32_e32 v14, v14, v25
	v_cvt_pk_bf16_f32 v20, v20, s0
	v_cvt_pk_bf16_f32 v15, v15, s0
	v_cvt_pk_bf16_f32 v14, v14, s0
	ds_write_b16 v67, v20 offset:34840
	ds_write_b16 v67, v15 offset:35112
	ds_write_b16 v67, v14 offset:36744
; __device__ __forceinline__ float bflo(unsigned w) { return __uint_as_float(w << 16); }
; __device__ __forceinline__ float bfhi(unsigned w) { return __uint_as_float(w & 0xffff0000u); }
; __device__ __forceinline__ unsigned short f2bf(float f) { return (unsigned short)(cvt_pk_bf16(f, 0.f) & 0xffffu); }
; __device__ __forceinline__ float wave_sum(float v) {
; #pragma unroll
;     for (int o = 32; o >= 1; o >>= 1) v += __shfl_xor(v, o);
;     return v;
; }
; __device__ __forceinline__ void sgu_unit(const Params& p, int l, int un, LAS unsigned char* lds) {
;     ...
;     for (int qi = 0; qi < 16; ++qi) { const int q = wave * 16 + qi;
;         const u32x4 v = vv[qi]; float f[8] = {bflo(v.x), bfhi(v.x), bflo(v.y), bfhi(v.y), bflo(v.z), bfhi(v.z), bflo(v.w), bfhi(v.w)}; float ss = 0.f;
; #pragma unroll
;         for (int j = 0; j < 8; ++j) { f[j] = gelu_tanh(f[j]); ss += f[j] * f[j]; }
;         ss = wave_sum(ss); const float rinv = rsqrtf(ss * (1.0f / 512.0f) + EPS);
;         if ((lane >> 4) == h) { const int c0 = (lane & 15) * 8; const float* g = p.in[I_SGUNG] + l * 512 + h * 128 + c0;
; #pragma unroll
;             for (int j = 0; j < 8; ++j) Vl[(c0 + j) * 136 + q] = f2bf(f[j] * rinv * g[j]); } }
.LBB0_503:
	s_or_b64 exec, exec, s[0:1]
	s_waitcnt vmcnt(2)
	v_lshlrev_b32_e32 v14, 16, v10
	v_lshlrev_b32_e32 v15, 16, v11
	v_and_b32_e32 v17, 0xffff0000, v11
	v_mul_f32_e32 v11, 0x3dd2d3e8, v14
	v_fma_f32 v11, -v11, v14, s33
	v_mul_f32_e32 v11, v11, v14
	v_exp_f32_e32 v11, v11
	v_and_b32_e32 v10, 0xffff0000, v10
	v_lshlrev_b32_e32 v18, 16, v12
	v_and_b32_e32 v19, 0xffff0000, v12
	v_add_f32_e32 v11, 1.0, v11
	v_rcp_f32_e32 v11, v11
	v_mul_f32_e32 v12, 0x3dd2d3e8, v17
	v_fma_f32 v12, -v12, v17, s33
	v_mul_f32_e32 v12, v12, v17
	v_mul_f32_e32 v16, v11, v14
	v_mul_f32_e32 v11, 0x3dd2d3e8, v10
	v_fma_f32 v11, -v11, v10, s33
	v_mul_f32_e32 v11, v11, v10
	v_exp_f32_e32 v11, v11
	v_exp_f32_e32 v12, v12
	v_lshlrev_b32_e32 v20, 16, v13
	v_and_b32_e32 v21, 0xffff0000, v13
	v_add_f32_e32 v11, 1.0, v11
	v_rcp_f32_e32 v11, v11
	v_add_f32_e32 v12, 1.0, v12
	v_rcp_f32_e32 v12, v12
	v_mul_f32_e32 v13, 0x3dd2d3e8, v18
	v_mul_f32_e32 v11, v11, v10
	v_mul_f32_e32 v10, 0x3dd2d3e8, v15
	v_fma_f32 v10, -v10, v15, s33
	v_mul_f32_e32 v10, v10, v15
	v_exp_f32_e32 v10, v10
	v_fma_f32 v13, -v13, v18, s33
	v_mul_f32_e32 v14, 0x3dd2d3e8, v19
	v_mul_f32_e32 v13, v13, v18
	v_add_f32_e32 v10, 1.0, v10
	v_rcp_f32_e32 v10, v10
	v_fma_f32 v14, -v14, v19, s33
	v_mul_f32_e32 v12, v12, v17
	v_exp_f32_e32 v13, v13
	v_mul_f32_e32 v10, v10, v15
	v_mul_f32_e32 v15, 0x3dd2d3e8, v20
	v_mul_f32_e32 v14, v14, v19
	v_fma_f32 v15, -v15, v20, s33
	v_mul_f32_e32 v17, 0x3dd2d3e8, v21
	v_exp_f32_e32 v14, v14
	v_mul_f32_e32 v15, v15, v20
	v_fma_f32 v17, -v17, v21, s33
	v_exp_f32_e32 v15, v15
	v_mul_f32_e32 v17, v17, v21
	v_exp_f32_e32 v17, v17
	v_add_f32_e32 v13, 1.0, v13
	v_rcp_f32_e32 v13, v13
	v_add_f32_e32 v14, 1.0, v14
	v_mul_f32_e32 v22, v11, v11
	v_rcp_f32_e32 v14, v14
	v_add_f32_e32 v15, 1.0, v15
	v_fmac_f32_e32 v22, v16, v16
	v_rcp_f32_e32 v15, v15
	v_add_f32_e32 v17, 1.0, v17
	v_fmac_f32_e32 v22, v10, v10
	v_rcp_f32_e32 v17, v17
	v_fmac_f32_e32 v22, v12, v12
	v_mul_f32_e32 v13, v13, v18
	v_fmac_f32_e32 v22, v13, v13
	v_mul_f32_e32 v14, v14, v19
	v_fmac_f32_e32 v22, v14, v14
	v_mul_f32_e32 v15, v15, v20
	v_fmac_f32_e32 v22, v15, v15
	v_mul_f32_e32 v17, v17, v21
	v_fmac_f32_e32 v22, v17, v17
	v_mov_b32_e32 v18, v22
	s_nop 1
	v_permlane32_swap_b32_e32 v18, v22
	s_waitcnt lgkmcnt(0)
	v_add_f32_e32 v18, v22, v18
	v_mov_b32_e32 v19, v18
	s_nop 1
	v_permlane16_swap_b32_e32 v19, v18
	s_waitcnt lgkmcnt(0)
	v_add_f32_e32 v18, v18, v19
	s_nop 1
	v_mov_b32_dpp v19, v18 row_ror:8 row_mask:0xf bank_mask:0xf
	s_waitcnt lgkmcnt(0)
	v_add_f32_e32 v18, v18, v19
	s_nop 1
	v_mov_b32_dpp v19, v18 row_shl:4 row_mask:0xf bank_mask:0x5
	v_mov_b32_dpp v19, v18 row_shr:4 row_mask:0xf bank_mask:0xa
	s_waitcnt lgkmcnt(0)
	v_add_f32_e32 v18, v18, v19
	s_nop 1
	v_mov_b32_dpp v19, v18 quad_perm:[2,3,0,1] row_mask:0xf bank_mask:0xf
	s_waitcnt lgkmcnt(0)
	v_add_f32_e32 v18, v18, v19
	s_nop 1
	v_mov_b32_dpp v19, v18 quad_perm:[1,0,3,2] row_mask:0xf bank_mask:0xf
	s_and_saveexec_b64 s[0:1], vcc
	s_cbranch_execz .LBB0_505
	s_waitcnt lgkmcnt(0)
	v_add_f32_e32 v18, v18, v19
	v_fmamk_f32 v18, v18, 0x3b000000, v246
	s_mov_b32 s2, 0x800000
	v_cmp_gt_f32_e64 s[2:3], s2, v18
	v_mul_f32_e32 v19, 0x4b800000, v18
	s_nop 0
	v_cndmask_b32_e64 v18, v18, v19, s[2:3]
	v_rsq_f32_e32 v18, v18
	s_nop 0
	v_mul_f32_e32 v19, 0x45800000, v18
	v_cndmask_b32_e64 v26, v18, v19, s[2:3]
	global_load_dwordx4 v[18:21], v[62:63], off offset:16
	global_load_dwordx4 v[22:25], v[62:63], off
	v_mul_f32_e32 v10, v10, v26
	v_mul_f32_e32 v16, v16, v26
	v_mul_f32_e32 v11, v11, v26
	s_waitcnt vmcnt(0)
	v_mul_f32_e32 v10, v10, v24
	v_cvt_pk_bf16_f32 v10, v10, s0
	ds_write_b16 v67, v10 offset:35386
	v_mul_f32_e32 v10, v12, v26
	v_mul_f32_e32 v10, v10, v25
	v_cvt_pk_bf16_f32 v10, v10, s0
	ds_write_b16 v67, v10 offset:35658
	v_mul_f32_e32 v10, v13, v26
	v_mul_f32_e32 v10, v10, v18
	v_cvt_pk_bf16_f32 v10, v10, s0
	ds_write_b16 v67, v10 offset:35930
	v_mul_f32_e32 v10, v14, v26
	v_mul_f32_e32 v10, v10, v19
	v_cvt_pk_bf16_f32 v10, v10, s0
	ds_write_b16 v67, v10 offset:36202
	v_mul_f32_e32 v10, v15, v26
	v_mul_f32_e32 v10, v10, v20
	v_cvt_pk_bf16_f32 v10, v10, s0
	ds_write_b16 v67, v10 offset:36474
	v_mul_f32_e32 v10, v17, v26
	v_mul_f32_e32 v16, v16, v22
	v_mul_f32_e32 v11, v11, v23
	v_mul_f32_e32 v10, v10, v21
	v_cvt_pk_bf16_f32 v16, v16, s0
	v_cvt_pk_bf16_f32 v11, v11, s0
	v_cvt_pk_bf16_f32 v10, v10, s0
	ds_write_b16 v67, v16 offset:34842
	ds_write_b16 v67, v11 offset:35114
	ds_write_b16 v67, v10 offset:36746
; __device__ __forceinline__ float bflo(unsigned w) { return __uint_as_float(w << 16); }
; __device__ __forceinline__ float bfhi(unsigned w) { return __uint_as_float(w & 0xffff0000u); }
; __device__ __forceinline__ unsigned short f2bf(float f) { return (unsigned short)(cvt_pk_bf16(f, 0.f) & 0xffffu); }
; __device__ __forceinline__ float wave_sum(float v) {
; #pragma unroll
;     for (int o = 32; o >= 1; o >>= 1) v += __shfl_xor(v, o);
;     return v;
; }
; __device__ __forceinline__ void sgu_unit(const Params& p, int l, int un, LAS unsigned char* lds) {
;     ...
;     for (int qi = 0; qi < 16; ++qi) { const int q = wave * 16 + qi;
;         const u32x4 v = vv[qi]; float f[8] = {bflo(v.x), bfhi(v.x), bflo(v.y), bfhi(v.y), bflo(v.z), bfhi(v.z), bflo(v.w), bfhi(v.w)}; float ss = 0.f;
; #pragma unroll
;         for (int j = 0; j < 8; ++j) { f[j] = gelu_tanh(f[j]); ss += f[j] * f[j]; }
;         ss = wave_sum(ss); const float rinv = rsqrtf(ss * (1.0f / 512.0f) + EPS);
;         if ((lane >> 4) == h) { const int c0 = (lane & 15) * 8; const float* g = p.in[I_SGUNG] + l * 512 + h * 128 + c0;
; #pragma unroll
;             for (int j = 0; j < 8; ++j) Vl[(c0 + j) * 136 + q] = f2bf(f[j] * rinv * g[j]); } }
.LBB0_505:
	s_or_b64 exec, exec, s[0:1]
	s_waitcnt vmcnt(1)
	v_lshlrev_b32_e32 v10, 16, v6
	v_lshlrev_b32_e32 v11, 16, v7
	v_and_b32_e32 v13, 0xffff0000, v7
	v_mul_f32_e32 v7, 0x3dd2d3e8, v10
	v_fma_f32 v7, -v7, v10, s33
	v_mul_f32_e32 v7, v7, v10
	v_exp_f32_e32 v7, v7
	v_and_b32_e32 v6, 0xffff0000, v6
	v_lshlrev_b32_e32 v14, 16, v8
	v_and_b32_e32 v15, 0xffff0000, v8
	v_add_f32_e32 v7, 1.0, v7
	v_rcp_f32_e32 v7, v7
	v_mul_f32_e32 v8, 0x3dd2d3e8, v13
	v_fma_f32 v8, -v8, v13, s33
	v_mul_f32_e32 v8, v8, v13
	v_mul_f32_e32 v12, v7, v10
	v_mul_f32_e32 v7, 0x3dd2d3e8, v6
	v_fma_f32 v7, -v7, v6, s33
	v_mul_f32_e32 v7, v7, v6
	v_exp_f32_e32 v7, v7
	v_exp_f32_e32 v8, v8
	v_lshlrev_b32_e32 v16, 16, v9
	v_and_b32_e32 v17, 0xffff0000, v9
	v_add_f32_e32 v7, 1.0, v7
	v_rcp_f32_e32 v7, v7
	v_add_f32_e32 v8, 1.0, v8
	v_rcp_f32_e32 v8, v8
	v_mul_f32_e32 v9, 0x3dd2d3e8, v14
	v_mul_f32_e32 v7, v7, v6
	v_mul_f32_e32 v6, 0x3dd2d3e8, v11
	v_fma_f32 v6, -v6, v11, s33
	v_mul_f32_e32 v6, v6, v11
	v_exp_f32_e32 v6, v6
	v_fma_f32 v9, -v9, v14, s33
	v_mul_f32_e32 v10, 0x3dd2d3e8, v15
	v_mul_f32_e32 v9, v9, v14
	v_add_f32_e32 v6, 1.0, v6
	v_rcp_f32_e32 v6, v6
	v_fma_f32 v10, -v10, v15, s33
	v_mul_f32_e32 v8, v8, v13
	v_exp_f32_e32 v9, v9
	v_mul_f32_e32 v6, v6, v11
	v_mul_f32_e32 v11, 0x3dd2d3e8, v16
	v_mul_f32_e32 v10, v10, v15
	v_fma_f32 v11, -v11, v16, s33
	v_mul_f32_e32 v13, 0x3dd2d3e8, v17
	v_exp_f32_e32 v10, v10
	v_mul_f32_e32 v11, v11, v16
	v_fma_f32 v13, -v13, v17, s33
	v_exp_f32_e32 v11, v11
	v_mul_f32_e32 v13, v13, v17
	v_exp_f32_e32 v13, v13
	v_add_f32_e32 v9, 1.0, v9
	v_rcp_f32_e32 v9, v9
	v_add_f32_e32 v10, 1.0, v10
	v_mul_f32_e32 v18, v7, v7
	v_rcp_f32_e32 v10, v10
	v_add_f32_e32 v11, 1.0, v11
	v_fmac_f32_e32 v18, v12, v12
	v_rcp_f32_e32 v11, v11
	v_add_f32_e32 v13, 1.0, v13
	v_fmac_f32_e32 v18, v6, v6
	v_rcp_f32_e32 v13, v13
	v_fmac_f32_e32 v18, v8, v8
	v_mul_f32_e32 v9, v9, v14
	v_fmac_f32_e32 v18, v9, v9
	v_mul_f32_e32 v10, v10, v15
	v_fmac_f32_e32 v18, v10, v10
	v_mul_f32_e32 v11, v11, v16
	v_fmac_f32_e32 v18, v11, v11
	v_mul_f32_e32 v13, v13, v17
	v_fmac_f32_e32 v18, v13, v13
	v_mov_b32_e32 v14, v18
	s_nop 1
	v_permlane32_swap_b32_e32 v14, v18
	s_waitcnt lgkmcnt(0)
	v_add_f32_e32 v14, v18, v14
	v_mov_b32_e32 v15, v14
	s_nop 1
	v_permlane16_swap_b32_e32 v15, v14
	s_waitcnt lgkmcnt(0)
	v_add_f32_e32 v14, v14, v15
	s_nop 1
	v_mov_b32_dpp v15, v14 row_ror:8 row_mask:0xf bank_mask:0xf
	s_waitcnt lgkmcnt(0)
	v_add_f32_e32 v14, v14, v15
	s_nop 1
	v_mov_b32_dpp v15, v14 row_shl:4 row_mask:0xf bank_mask:0x5
	v_mov_b32_dpp v15, v14 row_shr:4 row_mask:0xf bank_mask:0xa
	s_waitcnt lgkmcnt(0)
	v_add_f32_e32 v14, v14, v15
	s_nop 1
	v_mov_b32_dpp v15, v14 quad_perm:[2,3,0,1] row_mask:0xf bank_mask:0xf
	s_waitcnt lgkmcnt(0)
	v_add_f32_e32 v14, v14, v15
	s_nop 1
	v_mov_b32_dpp v15, v14 quad_perm:[1,0,3,2] row_mask:0xf bank_mask:0xf
	s_and_saveexec_b64 s[0:1], vcc
	s_cbranch_execz .LBB0_507
	s_waitcnt lgkmcnt(0)
	v_add_f32_e32 v14, v14, v15
	v_fmamk_f32 v14, v14, 0x3b000000, v246
	s_mov_b32 s2, 0x800000
	v_cmp_gt_f32_e64 s[2:3], s2, v14
	v_mul_f32_e32 v15, 0x4b800000, v14
	s_nop 0
	v_cndmask_b32_e64 v14, v14, v15, s[2:3]
	v_rsq_f32_e32 v14, v14
	s_nop 0
	v_mul_f32_e32 v15, 0x45800000, v14
	v_cndmask_b32_e64 v22, v14, v15, s[2:3]
	global_load_dwordx4 v[14:17], v[62:63], off offset:16
	global_load_dwordx4 v[18:21], v[62:63], off
	v_mul_f32_e32 v6, v6, v22
	v_mul_f32_e32 v12, v12, v22
	v_mul_f32_e32 v7, v7, v22
	s_waitcnt vmcnt(0)
	v_mul_f32_e32 v6, v6, v20
	v_cvt_pk_bf16_f32 v6, v6, s0
	ds_write_b16 v67, v6 offset:35388
	v_mul_f32_e32 v6, v8, v22
	v_mul_f32_e32 v6, v6, v21
	v_cvt_pk_bf16_f32 v6, v6, s0
	ds_write_b16 v67, v6 offset:35660
	v_mul_f32_e32 v6, v9, v22
	v_mul_f32_e32 v6, v6, v14
	v_cvt_pk_bf16_f32 v6, v6, s0
	ds_write_b16 v67, v6 offset:35932
	v_mul_f32_e32 v6, v10, v22
	v_mul_f32_e32 v6, v6, v15
	v_cvt_pk_bf16_f32 v6, v6, s0
	ds_write_b16 v67, v6 offset:36204
	v_mul_f32_e32 v6, v11, v22
	v_mul_f32_e32 v6, v6, v16
	v_cvt_pk_bf16_f32 v6, v6, s0
	ds_write_b16 v67, v6 offset:36476
	v_mul_f32_e32 v6, v13, v22
	v_mul_f32_e32 v12, v12, v18
	v_mul_f32_e32 v7, v7, v19
	v_mul_f32_e32 v6, v6, v17
	v_cvt_pk_bf16_f32 v12, v12, s0
	v_cvt_pk_bf16_f32 v7, v7, s0
	v_cvt_pk_bf16_f32 v6, v6, s0
	ds_write_b16 v67, v12 offset:34844
	ds_write_b16 v67, v7 offset:35116
	ds_write_b16 v67, v6 offset:36748
; __device__ __forceinline__ float bflo(unsigned w) { return __uint_as_float(w << 16); }
; __device__ __forceinline__ float bfhi(unsigned w) { return __uint_as_float(w & 0xffff0000u); }
; __device__ __forceinline__ unsigned short f2bf(float f) { return (unsigned short)(cvt_pk_bf16(f, 0.f) & 0xffffu); }
; __device__ __forceinline__ float wave_sum(float v) {
; #pragma unroll
;     for (int o = 32; o >= 1; o >>= 1) v += __shfl_xor(v, o);
;     return v;
; }
; __device__ __forceinline__ void sgu_unit(const Params& p, int l, int un, LAS unsigned char* lds) {
;     ...
;     for (int qi = 0; qi < 16; ++qi) { const int q = wave * 16 + qi;
;         const u32x4 v = vv[qi]; float f[8] = {bflo(v.x), bfhi(v.x), bflo(v.y), bfhi(v.y), bflo(v.z), bfhi(v.z), bflo(v.w), bfhi(v.w)}; float ss = 0.f;
; #pragma unroll
;         for (int j = 0; j < 8; ++j) { f[j] = gelu_tanh(f[j]); ss += f[j] * f[j]; }
;         ss = wave_sum(ss); const float rinv = rsqrtf(ss * (1.0f / 512.0f) + EPS);
;         if ((lane >> 4) == h) { const int c0 = (lane & 15) * 8; const float* g = p.in[I_SGUNG] + l * 512 + h * 128 + c0;
; #pragma unroll
;             for (int j = 0; j < 8; ++j) Vl[(c0 + j) * 136 + q] = f2bf(f[j] * rinv * g[j]); } }
.LBB0_507:
	s_or_b64 exec, exec, s[0:1]
	s_waitcnt vmcnt(0)
	v_lshlrev_b32_e32 v6, 16, v2
	v_lshlrev_b32_e32 v7, 16, v3
	v_and_b32_e32 v9, 0xffff0000, v3
	v_mul_f32_e32 v3, 0x3dd2d3e8, v6
	v_fma_f32 v3, -v3, v6, s33
	v_mul_f32_e32 v3, v3, v6
	v_exp_f32_e32 v3, v3
	v_and_b32_e32 v2, 0xffff0000, v2
	v_lshlrev_b32_e32 v10, 16, v4
	v_and_b32_e32 v11, 0xffff0000, v4
	v_add_f32_e32 v3, 1.0, v3
	v_rcp_f32_e32 v3, v3
	v_mul_f32_e32 v4, 0x3dd2d3e8, v9
	v_fma_f32 v4, -v4, v9, s33
	v_mul_f32_e32 v4, v4, v9
	v_mul_f32_e32 v8, v3, v6
	v_mul_f32_e32 v3, 0x3dd2d3e8, v2
	v_fma_f32 v3, -v3, v2, s33
	v_mul_f32_e32 v3, v3, v2
	v_exp_f32_e32 v3, v3
	v_exp_f32_e32 v4, v4
	v_lshlrev_b32_e32 v12, 16, v5
	v_and_b32_e32 v13, 0xffff0000, v5
	v_add_f32_e32 v3, 1.0, v3
	v_rcp_f32_e32 v3, v3
	v_add_f32_e32 v4, 1.0, v4
	v_rcp_f32_e32 v4, v4
	v_mul_f32_e32 v5, 0x3dd2d3e8, v10
	v_mul_f32_e32 v3, v3, v2
	v_mul_f32_e32 v2, 0x3dd2d3e8, v7
	v_fma_f32 v2, -v2, v7, s33
	v_mul_f32_e32 v2, v2, v7
	v_exp_f32_e32 v2, v2
	v_fma_f32 v5, -v5, v10, s33
	v_mul_f32_e32 v6, 0x3dd2d3e8, v11
	v_mul_f32_e32 v5, v5, v10
	v_add_f32_e32 v2, 1.0, v2
	v_rcp_f32_e32 v2, v2
	v_fma_f32 v6, -v6, v11, s33
	v_mul_f32_e32 v4, v4, v9
	v_exp_f32_e32 v5, v5
	v_mul_f32_e32 v2, v2, v7
	v_mul_f32_e32 v7, 0x3dd2d3e8, v12
	v_mul_f32_e32 v6, v6, v11
	v_fma_f32 v7, -v7, v12, s33
	v_mul_f32_e32 v9, 0x3dd2d3e8, v13
	v_exp_f32_e32 v6, v6
	v_mul_f32_e32 v7, v7, v12
	v_fma_f32 v9, -v9, v13, s33
	v_exp_f32_e32 v7, v7
	v_mul_f32_e32 v9, v9, v13
	v_exp_f32_e32 v9, v9
	v_add_f32_e32 v5, 1.0, v5
	v_rcp_f32_e32 v5, v5
	v_add_f32_e32 v6, 1.0, v6
	v_mul_f32_e32 v14, v3, v3
	v_rcp_f32_e32 v6, v6
	v_add_f32_e32 v7, 1.0, v7
	v_fmac_f32_e32 v14, v8, v8
	v_rcp_f32_e32 v7, v7
	v_add_f32_e32 v9, 1.0, v9
	v_fmac_f32_e32 v14, v2, v2
	v_rcp_f32_e32 v9, v9
	v_fmac_f32_e32 v14, v4, v4
	v_mul_f32_e32 v5, v5, v10
	v_fmac_f32_e32 v14, v5, v5
	v_mul_f32_e32 v6, v6, v11
	v_fmac_f32_e32 v14, v6, v6
	v_mul_f32_e32 v7, v7, v12
	v_fmac_f32_e32 v14, v7, v7
	v_mul_f32_e32 v9, v9, v13
	v_fmac_f32_e32 v14, v9, v9
	v_mov_b32_e32 v10, v14
	s_nop 1
	v_permlane32_swap_b32_e32 v10, v14
	s_waitcnt lgkmcnt(0)
	v_add_f32_e32 v10, v14, v10
	v_mov_b32_e32 v11, v10
	s_nop 1
	v_permlane16_swap_b32_e32 v11, v10
	s_waitcnt lgkmcnt(0)
	v_add_f32_e32 v10, v10, v11
	s_nop 1
	v_mov_b32_dpp v11, v10 row_ror:8 row_mask:0xf bank_mask:0xf
	s_waitcnt lgkmcnt(0)
	v_add_f32_e32 v10, v10, v11
	s_nop 1
	v_mov_b32_dpp v11, v10 row_shl:4 row_mask:0xf bank_mask:0x5
	v_mov_b32_dpp v11, v10 row_shr:4 row_mask:0xf bank_mask:0xa
	s_waitcnt lgkmcnt(0)
	v_add_f32_e32 v10, v10, v11
	s_nop 1
	v_mov_b32_dpp v11, v10 quad_perm:[2,3,0,1] row_mask:0xf bank_mask:0xf
	s_waitcnt lgkmcnt(0)
	v_add_f32_e32 v10, v10, v11
	s_nop 1
	v_mov_b32_dpp v11, v10 quad_perm:[1,0,3,2] row_mask:0xf bank_mask:0xf
	s_and_saveexec_b64 s[0:1], vcc
	s_cbranch_execz .LBB0_509
	s_waitcnt lgkmcnt(0)
	v_add_f32_e32 v10, v10, v11
	v_fmamk_f32 v10, v10, 0x3b000000, v246
	s_mov_b32 s2, 0x800000
	v_cmp_gt_f32_e32 vcc, s2, v10
	v_mul_f32_e32 v11, 0x4b800000, v10
	s_nop 0
	v_cndmask_b32_e32 v10, v10, v11, vcc
	v_rsq_f32_e32 v10, v10
	s_nop 0
	v_mul_f32_e32 v11, 0x45800000, v10
	v_cndmask_b32_e32 v18, v10, v11, vcc
	global_load_dwordx4 v[10:13], v[62:63], off offset:16
	global_load_dwordx4 v[14:17], v[62:63], off
	v_mul_f32_e32 v2, v2, v18
	v_mul_f32_e32 v8, v8, v18
	v_mul_f32_e32 v3, v3, v18
	s_waitcnt vmcnt(0)
	v_mul_f32_e32 v2, v2, v16
	v_cvt_pk_bf16_f32 v2, v2, s0
	ds_write_b16 v67, v2 offset:35390
	v_mul_f32_e32 v2, v4, v18
	v_mul_f32_e32 v2, v2, v17
	v_cvt_pk_bf16_f32 v2, v2, s0
	ds_write_b16 v67, v2 offset:35662
	v_mul_f32_e32 v2, v5, v18
	v_mul_f32_e32 v2, v2, v10
	v_cvt_pk_bf16_f32 v2, v2, s0
	ds_write_b16 v67, v2 offset:35934
	v_mul_f32_e32 v2, v6, v18
	v_mul_f32_e32 v2, v2, v11
	v_cvt_pk_bf16_f32 v2, v2, s0
	ds_write_b16 v67, v2 offset:36206
	v_mul_f32_e32 v2, v7, v18
	v_mul_f32_e32 v2, v2, v12
	v_cvt_pk_bf16_f32 v2, v2, s0
	ds_write_b16 v67, v2 offset:36478
	v_mul_f32_e32 v2, v9, v18
	v_mul_f32_e32 v8, v8, v14
	v_mul_f32_e32 v3, v3, v15
	v_mul_f32_e32 v2, v2, v13
	v_cvt_pk_bf16_f32 v8, v8, s0
	v_cvt_pk_bf16_f32 v3, v3, s0
	v_cvt_pk_bf16_f32 v2, v2, s0
	ds_write_b16 v67, v8 offset:34846
	ds_write_b16 v67, v3 offset:35118
	ds_write_b16 v67, v2 offset:36750

; __device__ __forceinline__ unsigned cvt_pk_bf16(float lo, float hi) { const f32x2 v = {lo, hi}; const bf16x2_t b = __builtin_convertvector(v, bf16x2_t); return __builtin_bit_cast(unsigned, b); }
; __device__ __forceinline__ float bf2f(unsigned short b) { return __uint_as_float(((unsigned)b) << 16); }
; __device__ __forceinline__ float bflo(unsigned w) { return __uint_as_float(w << 16); }
; __device__ __forceinline__ float bfhi(unsigned w) { return __uint_as_float(w & 0xffff0000u); }
; template <bool MAIN, bool CONV>
; __device__ __forceinline__ void b_row(const Params& p, unsigned char* ws, int l, int row, int lane) {
;     ...
;         { float f[8]; float ss = 0.f;
;           if (lane < 48) { const u32x4 v = vq; f[0] = bflo(v.x); f[1] = bfhi(v.x); f[2] = bflo(v.y); f[3] = bfhi(v.y); f[4] = bflo(v.z); f[5] = bfhi(v.z); f[6] = bflo(v.w); f[7] = bfhi(v.w);
;     #pragma unroll
;               for (int j = 0; j < 8; ++j) ss += f[j] * f[j]; }
;           else {
;     #pragma unroll
;               for (int j = 0; j < 8; ++j) f[j] = 0.f; }
;           ss = wave_sum(ss); const float rinv = rsqrtf(ss * (1.0f / 384.0f) + EPS);
;           if (lane < 48) { u32x4 w;
;               w.x = cvt_pk_bf16(f[0] * rinv * gq0[0], f[1] * rinv * gq0[1]); w.y = cvt_pk_bf16(f[2] * rinv * gq0[2], f[3] * rinv * gq0[3]);
;               w.z = cvt_pk_bf16(f[4] * rinv * gq1[0], f[5] * rinv * gq1[1]); w.w = cvt_pk_bf16(f[6] * rinv * gq1[2], f[7] * rinv * gq1[3]);
;               *(u32x4*)((bf16_t*)(ws + WS_QA) + (size_t)row * 384 + lane * 8) = w; } }
;         { const u32x2 v = vkv; const float f0 = bflo(v.x), f1 = bfhi(v.x), f2 = bflo(v.y), f3 = bfhi(v.y);
;           const float ss = wave_sum(f0 * f0 + f1 * f1 + f2 * f2 + f3 * f3); const float rinv = rsqrtf(ss * (1.0f / 256.0f) + EPS);
;           u32x2 w; w.x = cvt_pk_bf16(f0 * rinv * gkv[0], f1 * rinv * gkv[1]); w.y = cvt_pk_bf16(f2 * rinv * gkv[2], f3 * rinv * gkv[3]);
;           *(u32x2*)((bf16_t*)(ws + WS_KVA) + (size_t)row * 256 + lane * 4) = w; }
;         { float v = bf2f(vkr); const float partner = __shfl_xor(v, 16);
.LBB0_525:
	s_or_b64 exec, exec, s[0:1]
	s_waitcnt vmcnt(13)
	v_and_b32_e32 v70, 64, v249
	v_add_u32_e32 v117, 64, v70
	v_xor_b32_e32 v70, 32, v249
	v_cmp_lt_i32_e32 vcc, v70, v117
	s_nop 1
	v_cndmask_b32_e32 v70, v249, v70, vcc
	v_lshlrev_b32_e32 v71, 2, v70
	v_mov_b32_e32 v70, v116
	s_nop 1
	v_permlane32_swap_b32_e32 v70, v116
	s_waitcnt lgkmcnt(0)
	v_add_f32_e32 v72, v116, v70
	v_xor_b32_e32 v70, 16, v249
	v_cmp_lt_i32_e32 vcc, v70, v117
	s_nop 1
	v_cndmask_b32_e32 v70, v249, v70, vcc
	v_lshlrev_b32_e32 v70, 2, v70
	v_mov_b32_e32 v73, v72
	s_nop 1
	v_permlane16_swap_b32_e32 v73, v72
	s_waitcnt lgkmcnt(0)
	v_add_f32_e32 v73, v72, v73
	v_xor_b32_e32 v72, 8, v249
	v_cmp_lt_i32_e32 vcc, v72, v117
	s_nop 1
	v_cndmask_b32_e32 v72, v249, v72, vcc
	v_lshlrev_b32_e32 v72, 2, v72
	s_nop 1
	v_mov_b32_dpp v116, v73 row_ror:8 row_mask:0xf bank_mask:0xf
	s_waitcnt lgkmcnt(0)
	v_add_f32_e32 v116, v73, v116
	v_xor_b32_e32 v73, 4, v249
	v_cmp_lt_i32_e32 vcc, v73, v117
	s_nop 1
	v_cndmask_b32_e32 v73, v249, v73, vcc
	v_lshlrev_b32_e32 v73, 2, v73
	s_nop 1
	v_mov_b32_dpp v118, v116 row_shl:4 row_mask:0xf bank_mask:0x5
	v_mov_b32_dpp v118, v116 row_shr:4 row_mask:0xf bank_mask:0xa
	s_waitcnt lgkmcnt(0)
	v_add_f32_e32 v118, v116, v118
	v_xor_b32_e32 v116, 2, v249
	v_cmp_lt_i32_e32 vcc, v116, v117
	s_nop 1
	v_cndmask_b32_e32 v116, v249, v116, vcc
	v_lshlrev_b32_e32 v116, 2, v116
	s_nop 1
	v_mov_b32_dpp v119, v118 quad_perm:[2,3,0,1] row_mask:0xf bank_mask:0xf
	s_waitcnt lgkmcnt(0)
	v_add_f32_e32 v118, v118, v119
	v_xor_b32_e32 v119, 1, v249
	v_cmp_lt_i32_e32 vcc, v119, v117
	s_nop 1
	v_cndmask_b32_e32 v117, v249, v119, vcc
	v_lshlrev_b32_e32 v117, 2, v117
	s_nop 1
	v_mov_b32_dpp v119, v118 quad_perm:[1,0,3,2] row_mask:0xf bank_mask:0xf
	s_and_saveexec_b64 s[0:1], s[36:37]
	s_cbranch_execz .LBB0_527
	s_waitcnt lgkmcnt(0)
	v_add_f32_e32 v118, v118, v119
	v_fmamk_f32 v118, v118, 0x3b2aaaab, v246
	s_mov_b32 s2, 0x800000
	v_mul_f32_e32 v119, 0x4b800000, v118
	v_cmp_gt_f32_e32 vcc, s2, v118
	s_movk_i32 s2, 0x300
	s_nop 0
	v_cndmask_b32_e32 v118, v118, v119, vcc
	v_rsq_f32_e32 v118, v118
	s_nop 0
	v_mul_f32_e32 v119, 0x45800000, v118
	v_cndmask_b32_e32 v118, v118, v119, vcc
	v_pk_mul_f32 v[106:107], v[106:107], v[118:119] op_sel_hi:[1,0]
	v_pk_mul_f32 v[108:109], v[108:109], v[118:119] op_sel_hi:[1,0]
	s_waitcnt vmcnt(10)
	v_pk_mul_f32 v[66:67], v[66:67], v[106:107]
	v_pk_mul_f32 v[68:69], v[68:69], v[108:109]
	v_cvt_pk_bf16_f32 v66, v66, v67
	v_cvt_pk_bf16_f32 v67, v68, v69
	v_pk_mul_f32 v[68:69], v[110:111], v[118:119] op_sel_hi:[1,0]
	s_nop 0
	v_pk_mul_f32 v[58:59], v[58:59], v[68:69]
	s_nop 0
	v_cvt_pk_bf16_f32 v68, v58, v59
	v_pk_mul_f32 v[58:59], v[112:113], v[118:119] op_sel_hi:[1,0]
	s_nop 0
	v_pk_mul_f32 v[58:59], v[60:61], v[58:59]
	s_nop 0
	v_cvt_pk_bf16_f32 v69, v58, v59
	v_mad_i64_i32 v[58:59], s[2:3], v98, s2, v[90:91]
	global_store_dwordx4 v[58:59], v[66:69], off
.LBB0_527:
	s_or_b64 exec, exec, s[0:1]
	s_waitcnt vmcnt(11)
	v_add_u32_e32 v59, 0xffffe000, v98
	v_ashrrev_i32_e32 v58, 11, v98
	v_lshrrev_b32_e32 v59, 8, v59
	s_waitcnt vmcnt(10)
	v_lshlrev_b32_e32 v66, 16, v104
	v_and_b32_e32 v67, 0xffff0000, v104
	v_cndmask_b32_e64 v106, v59, v58, s[42:43]
	v_lshlrev_b32_e32 v58, 16, v105
	v_and_b32_e32 v59, 0xffff0000, v105
	v_pk_mul_f32 v[68:69], v[66:67], v[66:67]
	v_pk_mul_f32 v[60:61], v[58:59], v[58:59]
	v_add_f32_e32 v68, v68, v69
	v_add_f32_e32 v60, v60, v68
	v_add_f32_e32 v60, v61, v60
	v_mov_b32_e32 v61, v60
	s_nop 1
	v_permlane32_swap_b32_e32 v61, v60
	s_mov_b32 s0, 0x800000
	s_movk_i32 s3, 0x900
	s_movk_i32 s2, 0x180
	s_waitcnt lgkmcnt(0)
	v_add_f32_e32 v60, v60, v61
	v_mov_b32_e32 v61, v60
	s_nop 1
	v_permlane16_swap_b32_e32 v61, v60
	s_waitcnt lgkmcnt(0)
	v_add_f32_e32 v60, v60, v61
	s_nop 1
	v_mov_b32_dpp v61, v60 row_ror:8 row_mask:0xf bank_mask:0xf
	s_waitcnt lgkmcnt(0)
	v_add_f32_e32 v60, v60, v61
	s_nop 1
	v_mov_b32_dpp v61, v60 row_shl:4 row_mask:0xf bank_mask:0x5
	v_mov_b32_dpp v61, v60 row_shr:4 row_mask:0xf bank_mask:0xa
	s_waitcnt lgkmcnt(0)
	v_add_f32_e32 v60, v60, v61
	s_nop 1
	v_mov_b32_dpp v61, v60 quad_perm:[2,3,0,1] row_mask:0xf bank_mask:0xf
	s_waitcnt lgkmcnt(0)
	v_add_f32_e32 v60, v60, v61
	s_nop 1
	v_mov_b32_dpp v61, v60 quad_perm:[1,0,3,2] row_mask:0xf bank_mask:0xf
	s_waitcnt lgkmcnt(0)
	v_add_f32_e32 v60, v60, v61
	v_fmamk_f32 v60, v60, 0x3b800000, v246
	v_cmp_gt_f32_e32 vcc, s0, v60
	v_mul_f32_e32 v61, 0x4b800000, v60
	s_nop 0
	v_cndmask_b32_e32 v60, v60, v61, vcc
	v_rsq_f32_e32 v60, v60
	s_nop 0
	v_mul_f32_e32 v61, 0x45800000, v60
	v_cndmask_b32_e32 v60, v60, v61, vcc
	v_pk_mul_f32 v[66:67], v[60:61], v[66:67] op_sel_hi:[0,1]
	v_pk_mul_f32 v[58:59], v[60:61], v[58:59] op_sel_hi:[0,1]
	s_waitcnt vmcnt(9)
	v_pk_mul_f32 v[62:63], v[62:63], v[66:67]
	v_pk_mul_f32 v[58:59], v[64:65], v[58:59]
	v_cvt_pk_bf16_f32 v62, v62, v63
	v_cvt_pk_bf16_f32 v63, v58, v59
	v_lshlrev_b64 v[58:59], 9, v[98:99]
	v_lshl_add_u64 v[58:59], v[80:81], 0, v[58:59]
	global_store_dwordx2 v[58:59], v[62:63], off
	v_lshlrev_b32_e32 v58, 16, v114
	ds_bpermute_b32 v59, v70, v58
	v_lshlrev_b32_e32 v65, 2, v106
	s_waitcnt lgkmcnt(0)
; __device__ __forceinline__ unsigned cvt_pk_bf16(float lo, float hi) { const f32x2 v = {lo, hi}; const bf16x2_t b = __builtin_convertvector(v, bf16x2_t); return __builtin_bit_cast(unsigned, b); }
; __device__ __forceinline__ float bf2f(unsigned short b) { return __uint_as_float(((unsigned)b) << 16); }
; __device__ __forceinline__ float bflo(unsigned w) { return __uint_as_float(w << 16); }
; __device__ __forceinline__ float bfhi(unsigned w) { return __uint_as_float(w & 0xffff0000u); }
; __device__ __forceinline__ unsigned short f2bf(float f) { return (unsigned short)(cvt_pk_bf16(f, 0.f) & 0xffffu); }
; template <bool MAIN, bool CONV>
; __device__ __forceinline__ void b_row(const Params& p, unsigned char* ws, int l, int row, int lane) {
;     ...
;         { float v = bf2f(vkr); const float partner = __shfl_xor(v, 16);
;           if (lat) { const int jj = lane & 31; const float cs = rope.x, sn = rope.y;
;               v = jj < 16 ? (v * cs - partner * sn) : (v * cs + partner * sn); }
;           const int key = lat ? CTX + t : t; const unsigned short o = f2bf(v);
;           bf16_t* kc = (bf16_t*)(ws + WS_KC);
;     #pragma unroll
;           for (int h = 0; h < 4; ++h) kc[((size_t)(b * 4 + h) * NKEY + key) * 192 + 128 + lane] = o; }
;         { const u32x4 v = vs5; const int g = lane >> 1, half = lane & 1;
;           *(u32x4*)((bf16_t*)(ws + WS_UPK) + ((size_t)g * 768 + (row >> 4)) * 512 + (row & 15) * 16 + half * 8) = v; }
;     }
;     if (CONV) {
;         { float zp[8], zc[8], zn[8];
;     ...
;           CONV_Z(zc, ca, ch); CONV_Z(zp, pa, ph); CONV_Z(zn, na, nh);
;     ...
;           float bgf[8] = {bflo(bg.x), bfhi(bg.x), bflo(bg.y), bfhi(bg.y), bflo(bg.z), bfhi(bg.z), bflo(bg.w), bfhi(bg.w)};
;           const float w0[8] = {cw0a[0], cw0a[1], cw0a[2], cw0a[3], cw0b[0], cw0b[1], cw0b[2], cw0b[3]}, w1[8] = {cw1a[0], cw1a[1], cw1a[2], cw1a[3], cw1b[0], cw1b[1], cw1b[2], cw1b[3]},
;                       w2[8] = {cw2a[0], cw2a[1], cw2a[2], cw2a[3], cw2b[0], cw2b[1], cw2b[2], cw2b[3]};
;           float o[8];
;     #pragma unroll
;           for (int j = 0; j < 8; ++j) o[j] = bgf[j] * (w0[j] * zp[j] + w1[j] * zc[j] + w2[j] * zn[j]);
;           u32x4 w; w.x = cvt_pk_bf16(o[0], o[1]); w.y = cvt_pk_bf16(o[2], o[3]); w.z = cvt_pk_bf16(o[4], o[5]); w.w = cvt_pk_bf16(o[6], o[7]);
;           *(u32x4*)(CAT + (size_t)row * DM + 1536 + c0) = w; }
	v_mul_f32_e32 v59, v103, v59
	v_cndmask_b32_e64 v59, v59, -v59, s[40:41]
	v_fmac_f32_e32 v59, v102, v58
	v_cndmask_b32_e64 v59, v58, v59, s[42:43]
	v_add_u32_e32 v58, 0x100, v77
	v_cndmask_b32_e64 v58, v115, v58, s[42:43]
	v_cvt_pk_bf16_f32 v64, v59, s0
	v_mov_b32_e32 v59, v207
	v_mad_i64_i32 v[60:61], s[0:1], v65, s3, v[58:59]
	v_mad_u64_u32 v[62:63], s[0:1], v60, s2, v[82:83]
	v_or_b32_e32 v60, 1, v65
	v_mad_i32_i24 v63, v61, s2, v63
	v_mad_i64_i32 v[60:61], s[0:1], v60, s3, v[58:59]
	global_store_short v[62:63], v64, off
	v_mad_u64_u32 v[62:63], s[0:1], v60, s2, v[82:83]
	v_or_b32_e32 v60, 2, v65
	v_mad_i32_i24 v63, v61, s2, v63
	v_mad_i64_i32 v[60:61], s[0:1], v60, s3, v[58:59]
	global_store_short v[62:63], v64, off
	v_mad_u64_u32 v[62:63], s[0:1], v60, s2, v[82:83]
	v_or_b32_e32 v60, 3, v65
	v_mad_i64_i32 v[58:59], s[0:1], v60, s3, v[58:59]
	v_mad_i32_i24 v63, v61, s2, v63
	v_mad_u64_u32 v[60:61], s[0:1], v58, s2, v[82:83]
	v_ashrrev_i32_e32 v58, 4, v98
	v_mad_i32_i24 v61, v59, s2, v61
	v_ashrrev_i32_e32 v59, 31, v58
	v_lshl_add_u64 v[58:59], v[58:59], 0, v[86:87]
	global_store_short v[60:61], v64, off
	v_lshlrev_b64 v[58:59], 10, v[58:59]
	v_lshlrev_b32_e32 v60, 5, v98
	v_lshl_add_u64 v[58:59], s[16:17], 0, v[58:59]
	v_and_b32_e32 v60, 0x1e0, v60
	v_mov_b32_e32 v61, v207
	v_lshl_add_u64 v[58:59], v[58:59], 0, v[60:61]
	v_lshlrev_b32_e32 v60, 1, v88
	v_lshl_add_u64 v[58:59], v[58:59], 0, v[60:61]
	global_store_short v[62:63], v64, off
	global_store_dwordx4 v[58:59], v[26:29], off
	s_waitcnt vmcnt(12)
	v_lshlrev_b32_e32 v58, 16, v2
	v_and_b32_e32 v59, 0xffff0000, v2
	v_lshlrev_b32_e32 v26, 16, v14
	v_and_b32_e32 v27, 0xffff0000, v14
	v_lshlrev_b32_e32 v28, 16, v10
	v_and_b32_e32 v29, 0xffff0000, v10
	v_lshlrev_b32_e32 v14, 16, v15
	v_and_b32_e32 v15, 0xffff0000, v15
	v_lshlrev_b32_e32 v10, 16, v11
	v_and_b32_e32 v11, 0xffff0000, v11
	v_pk_mul_f32 v[10:11], v[14:15], v[10:11]
	v_lshlrev_b32_e32 v14, 16, v19
	v_and_b32_e32 v15, 0xffff0000, v19
	v_lshlrev_b32_e32 v2, 16, v3
	v_and_b32_e32 v3, 0xffff0000, v3
	v_pk_mul_f32 v[26:27], v[26:27], v[28:29]
	v_lshlrev_b32_e32 v28, 16, v18
	v_and_b32_e32 v29, 0xffff0000, v18
	v_pk_mul_f32 v[2:3], v[2:3], v[14:15]
	v_lshlrev_b32_e32 v14, 16, v31
	v_and_b32_e32 v15, 0xffff0000, v31
	v_lshlrev_b32_e32 v18, 16, v23
	v_and_b32_e32 v19, 0xffff0000, v23
	s_waitcnt vmcnt(8)
	v_pk_mul_f32 v[10:11], v[10:11], v[56:57]
	v_pk_mul_f32 v[28:29], v[58:59], v[28:29]
	v_lshlrev_b32_e32 v58, 16, v30
	v_and_b32_e32 v59, 0xffff0000, v30
	v_lshlrev_b32_e32 v60, 16, v22
	v_and_b32_e32 v61, 0xffff0000, v22
	v_pk_mul_f32 v[14:15], v[18:19], v[14:15]
	v_pk_fma_f32 v[2:3], v[2:3], v[48:49], v[10:11]
	v_pk_mul_f32 v[58:59], v[60:61], v[58:59]
	v_lshlrev_b32_e32 v60, 16, v6
	v_and_b32_e32 v61, 0xffff0000, v6
	v_lshlrev_b32_e32 v6, 16, v7
	v_and_b32_e32 v7, 0xffff0000, v7
	s_waitcnt vmcnt(6)
	v_pk_fma_f32 v[2:3], v[14:15], v[52:53], v[2:3]
	v_lshlrev_b32_e32 v10, 16, v12
	v_pk_mul_f32 v[6:7], v[2:3], v[6:7]
	v_lshlrev_b32_e32 v2, 16, v16
	v_and_b32_e32 v3, 0xffff0000, v16
	v_and_b32_e32 v11, 0xffff0000, v12
	v_pk_mul_f32 v[2:3], v[2:3], v[10:11]
	v_lshlrev_b32_e32 v10, 16, v20
	v_and_b32_e32 v11, 0xffff0000, v20
	v_lshlrev_b32_e32 v14, 16, v4
	v_and_b32_e32 v15, 0xffff0000, v4
	v_pk_mul_f32 v[10:11], v[14:15], v[10:11]
	v_lshlrev_b32_e32 v14, 16, v32
	v_and_b32_e32 v15, 0xffff0000, v32
	v_lshlrev_b32_e32 v18, 16, v24
	v_and_b32_e32 v19, 0xffff0000, v24
	v_pk_mul_f32 v[2:3], v[2:3], v[42:43]
	v_pk_mul_f32 v[14:15], v[18:19], v[14:15]
	v_pk_fma_f32 v[2:3], v[10:11], v[34:35], v[2:3]
	v_lshlrev_b32_e32 v18, 16, v8
	v_and_b32_e32 v19, 0xffff0000, v8
	v_pk_fma_f32 v[2:3], v[14:15], v[38:39], v[2:3]
	v_lshlrev_b32_e32 v12, 16, v13
	v_pk_mul_f32 v[10:11], v[2:3], v[18:19]
	v_lshlrev_b32_e32 v2, 16, v17
	v_and_b32_e32 v3, 0xffff0000, v17
	v_and_b32_e32 v13, 0xffff0000, v13
	v_pk_mul_f32 v[2:3], v[2:3], v[12:13]
	v_lshlrev_b32_e32 v12, 16, v21
	v_and_b32_e32 v13, 0xffff0000, v21
	v_lshlrev_b32_e32 v4, 16, v5
	v_and_b32_e32 v5, 0xffff0000, v5
	v_pk_mul_f32 v[4:5], v[4:5], v[12:13]
	v_lshlrev_b32_e32 v12, 16, v33
	v_and_b32_e32 v13, 0xffff0000, v33
	v_lshlrev_b32_e32 v14, 16, v25
	v_and_b32_e32 v15, 0xffff0000, v25
	v_pk_mul_f32 v[2:3], v[2:3], v[44:45]
	v_pk_mul_f32 v[12:13], v[14:15], v[12:13]
	v_pk_fma_f32 v[2:3], v[4:5], v[36:37], v[2:3]
	v_lshlrev_b32_e32 v8, 16, v9
	v_and_b32_e32 v9, 0xffff0000, v9
	v_pk_fma_f32 v[2:3], v[12:13], v[40:41], v[2:3]
	v_pk_mul_f32 v[26:27], v[26:27], v[54:55]
	v_pk_mul_f32 v[8:9], v[2:3], v[8:9]
	v_cvt_pk_bf16_f32 v3, v6, v7
	v_lshlrev_b64 v[6:7], 12, v[98:99]
	v_pk_fma_f32 v[26:27], v[28:29], v[46:47], v[26:27]
	v_lshl_add_u64 v[6:7], s[20:21], 0, v[6:7]
	v_pk_fma_f32 v[26:27], v[58:59], v[50:51], v[26:27]
	v_lshl_add_u64 v[6:7], v[6:7], 0, v[206:207]
	v_pk_mul_f32 v[26:27], v[26:27], v[60:61]
	v_add_co_u32_e32 v6, vcc, 0x2d1b8000, v6
	v_cvt_pk_bf16_f32 v2, v26, v27
	v_cvt_pk_bf16_f32 v4, v10, v11
	v_cvt_pk_bf16_f32 v5, v8, v9
	v_addc_co_u32_e32 v7, vcc, 0, v7, vcc
	s_mov_b64 s[0:1], 0
	global_store_dwordx4 v[6:7], v[2:5], off offset:3072

; __device__ __forceinline__ unsigned cvt_pk_bf16(float lo, float hi) { const f32x2 v = {lo, hi}; const bf16x2_t b = __builtin_convertvector(v, bf16x2_t); return __builtin_bit_cast(unsigned, b); }
; __device__ __forceinline__ float bflo(unsigned w) { return __uint_as_float(w << 16); }
; __device__ __forceinline__ float bfhi(unsigned w) { return __uint_as_float(w & 0xffff0000u); }
; template <bool MAIN, bool CONV>
; __device__ __forceinline__ void b_row(const Params& p, unsigned char* ws, int l, int row, int lane) {
;     ...
;         { float f[8]; float ss = 0.f;
;           if (lane < 48) { const u32x4 v = vq; f[0] = bflo(v.x); f[1] = bfhi(v.x); f[2] = bflo(v.y); f[3] = bfhi(v.y); f[4] = bflo(v.z); f[5] = bfhi(v.z); f[6] = bflo(v.w); f[7] = bfhi(v.w);
;     #pragma unroll
;               for (int j = 0; j < 8; ++j) ss += f[j] * f[j]; }
;           else {
;     #pragma unroll
;               for (int j = 0; j < 8; ++j) f[j] = 0.f; }
;           ss = wave_sum(ss); const float rinv = rsqrtf(ss * (1.0f / 384.0f) + EPS);
;           if (lane < 48) { u32x4 w;
;               w.x = cvt_pk_bf16(f[0] * rinv * gq0[0], f[1] * rinv * gq0[1]); w.y = cvt_pk_bf16(f[2] * rinv * gq0[2], f[3] * rinv * gq0[3]);
;               w.z = cvt_pk_bf16(f[4] * rinv * gq1[0], f[5] * rinv * gq1[1]); w.w = cvt_pk_bf16(f[6] * rinv * gq1[2], f[7] * rinv * gq1[3]);
;               *(u32x4*)((bf16_t*)(ws + WS_QA) + (size_t)row * 384 + lane * 8) = w; } }
.LBB0_537:
	s_or_b64 exec, exec, s[0:1]
	s_waitcnt vmcnt(4)
	v_and_b32_e32 v18, 64, v249
	v_add_u32_e32 v36, 64, v18
	v_xor_b32_e32 v18, 32, v249
	v_cmp_lt_i32_e32 vcc, v18, v36
	s_nop 1
	v_cndmask_b32_e32 v18, v249, v18, vcc
	v_lshlrev_b32_e32 v19, 2, v18
	v_mov_b32_e32 v18, v35
	s_nop 1
	v_permlane32_swap_b32_e32 v18, v35
	s_waitcnt lgkmcnt(0)
	v_add_f32_e32 v20, v35, v18
	v_xor_b32_e32 v18, 16, v249
	v_cmp_lt_i32_e32 vcc, v18, v36
	s_nop 1
	v_cndmask_b32_e32 v18, v249, v18, vcc
	v_lshlrev_b32_e32 v18, 2, v18
	v_mov_b32_e32 v21, v20
	s_nop 1
	v_permlane16_swap_b32_e32 v21, v20
	s_waitcnt lgkmcnt(0)
	v_add_f32_e32 v21, v20, v21
	v_xor_b32_e32 v20, 8, v249
	v_cmp_lt_i32_e32 vcc, v20, v36
	s_nop 1
	v_cndmask_b32_e32 v20, v249, v20, vcc
	v_lshlrev_b32_e32 v20, 2, v20
	s_nop 1
	v_mov_b32_dpp v35, v21 row_ror:8 row_mask:0xf bank_mask:0xf
	s_waitcnt lgkmcnt(0)
	v_add_f32_e32 v35, v21, v35
	v_xor_b32_e32 v21, 4, v249
	v_cmp_lt_i32_e32 vcc, v21, v36
	s_nop 1
	v_cndmask_b32_e32 v21, v249, v21, vcc
	v_lshlrev_b32_e32 v21, 2, v21
	s_nop 1
	v_mov_b32_dpp v37, v35 row_shl:4 row_mask:0xf bank_mask:0x5
	v_mov_b32_dpp v37, v35 row_shr:4 row_mask:0xf bank_mask:0xa
	s_waitcnt lgkmcnt(0)
	v_add_f32_e32 v37, v35, v37
	v_xor_b32_e32 v35, 2, v249
	v_cmp_lt_i32_e32 vcc, v35, v36
	s_nop 1
	v_cndmask_b32_e32 v35, v249, v35, vcc
	v_lshlrev_b32_e32 v35, 2, v35
	s_nop 1
	v_mov_b32_dpp v38, v37 quad_perm:[2,3,0,1] row_mask:0xf bank_mask:0xf
	s_waitcnt lgkmcnt(0)
	v_add_f32_e32 v37, v37, v38
	v_xor_b32_e32 v38, 1, v249
	v_cmp_lt_i32_e32 vcc, v38, v36
	s_nop 1
	v_cndmask_b32_e32 v36, v249, v38, vcc
	v_lshlrev_b32_e32 v36, 2, v36
	s_nop 1
	v_mov_b32_dpp v38, v37 quad_perm:[1,0,3,2] row_mask:0xf bank_mask:0xf
	s_and_saveexec_b64 s[0:1], s[36:37]
	s_cbranch_execz .LBB0_467
	s_waitcnt lgkmcnt(0)
	v_add_f32_e32 v37, v37, v38
	v_fmamk_f32 v37, v37, 0x3b2aaaab, v246
	s_mov_b32 s2, 0x800000
	v_mul_f32_e32 v38, 0x4b800000, v37
	v_cmp_gt_f32_e32 vcc, s2, v37
	s_movk_i32 s2, 0x300
	s_nop 0
	v_cndmask_b32_e32 v37, v37, v38, vcc
	v_rsq_f32_e32 v37, v37
	s_nop 0
	v_mul_f32_e32 v38, 0x45800000, v37
	v_cndmask_b32_e32 v38, v37, v38, vcc
	v_pk_mul_f32 v[26:27], v[26:27], v[38:39] op_sel_hi:[1,0]
	v_pk_mul_f32 v[28:29], v[28:29], v[38:39] op_sel_hi:[1,0]
	s_waitcnt vmcnt(1)
	v_pk_mul_f32 v[14:15], v[14:15], v[26:27]
	v_pk_mul_f32 v[16:17], v[16:17], v[28:29]
	v_cvt_pk_bf16_f32 v14, v14, v15
	v_cvt_pk_bf16_f32 v15, v16, v17
	v_pk_mul_f32 v[16:17], v[30:31], v[38:39] op_sel_hi:[1,0]
	s_nop 0
	v_pk_mul_f32 v[6:7], v[6:7], v[16:17]
	s_nop 0
	v_cvt_pk_bf16_f32 v16, v6, v7
	v_pk_mul_f32 v[6:7], v[32:33], v[38:39] op_sel_hi:[1,0]
	s_nop 0
	v_pk_mul_f32 v[6:7], v[8:9], v[6:7]
	s_nop 0
	v_cvt_pk_bf16_f32 v17, v6, v7
	v_mad_i64_i32 v[6:7], s[2:3], v98, s2, v[90:91]
	global_store_dwordx4 v[6:7], v[14:17], off
	s_branch .LBB0_467

; #define ATT_DMAV(tile, slot) do { _Pragma("unroll") for (int i = 0; i < 3; ++i) { const int pc = (wv + 8 * i) < 18 ? (wv + 8 * i) : 17; \
;         __builtin_amdgcn_global_load_lds((const unsigned*)((const char*)Vbh + (size_t)(tile) * 128 + doffV[i]), (LAS unsigned*)(lds + VRING + (slot) * VT_BYTES + pc * 1024), 16, 0, 0); } } while (0)
; __device__ __forceinline__ void attn_unit(const bf16_t* Qrows  , const bf16_t* Kbh, const bf16_t* Vbh, int nkeys, bf16_t* Orows, LAS unsigned char* lds) {
;     ...
;         ATT_DMAV(j + 2, v0 == 0 ? 2 : v0 - 1);
.LBB0_1238:
	s_mul_i32 s12, s36, 0x4800
	s_add_i32 s13, s12, 0xffffb800
	s_cmp_lg_u32 s36, 0
	s_cselect_b32 s13, s13, 0x9000
	s_add_i32 s13, s13, 0
	s_add_i32 s13, s13, 0x12c00
	v_lshl_add_u64 v[168:169], v[158:159], 0, s[2:3]
	v_lshl_add_u64 v[82:83], v[168:169], 0, s[28:29]
	s_add_i32 m0, s13, s69
	v_lshl_add_u64 v[170:171], v[160:161], 0, s[2:3]
	global_load_lds_dwordx4 v[82:83], off
	v_lshl_add_u64 v[82:83], v[170:171], 0, s[28:29]
	s_add_i32 m0, s13, s70
	v_lshl_add_u64 v[172:173], v[162:163], 0, s[2:3]
	global_load_lds_dwordx4 v[82:83], off
	v_lshl_add_u64 v[82:83], v[172:173], 0, s[28:29]
	s_add_i32 m0, s13, s71
	v_and_b32_e32 v84, 64, v249
	global_load_lds_dwordx4 v[82:83], off
	v_max_f32_e32 v82, v67, v67
	v_max_f32_e32 v83, v66, v66
	v_max_f32_e32 v82, v83, v82
	v_max3_f32 v82, v82, v68, v69
	v_max3_f32 v82, v82, v70, v71
	v_max3_f32 v82, v82, v72, v73
	v_max3_f32 v82, v82, v74, v75
	v_xor_b32_e32 v83, 32, v249
	v_add_u32_e32 v84, 64, v84
	v_max3_f32 v82, v82, v76, v77
	v_cmp_lt_i32_e32 vcc, v83, v84
	v_max3_f32 v82, v82, v78, v79
	v_max3_f32 v82, v82, v80, v81
	v_cndmask_b32_e32 v83, v249, v83, vcc
	v_lshlrev_b32_e32 v180, 2, v83
	v_mov_b32_e32 v83, v82
	s_nop 1
	v_permlane32_swap_b32_e32 v83, v82
	s_waitcnt lgkmcnt(0)
	v_max_f32_e32 v83, v83, v83
	v_max_f32_e32 v82, v82, v83
	v_add_f32_e32 v83, 0x41000000, v183
	v_cmp_gt_f32_e32 vcc, v82, v83
	s_cbranch_vccz .LBB0_1240
	v_max_f32_e32 v82, v82, v82
	v_max_f32_e32 v83, v183, v183
	v_max_f32_e32 v83, v83, v82
	v_sub_f32_e32 v82, v183, v83
	v_exp_f32_e32 v82, v82
	v_mov_b32_e32 v183, v83
	v_pk_mul_f32 v[64:65], v[64:65], v[82:83] op_sel_hi:[1,0]
	v_pk_mul_f32 v[62:63], v[62:63], v[82:83] op_sel_hi:[1,0]
	v_pk_mul_f32 v[60:61], v[60:61], v[82:83] op_sel_hi:[1,0]
	v_pk_mul_f32 v[58:59], v[58:59], v[82:83] op_sel_hi:[1,0]
	v_pk_mul_f32 v[56:57], v[56:57], v[82:83] op_sel_hi:[1,0]
	v_pk_mul_f32 v[54:55], v[54:55], v[82:83] op_sel_hi:[1,0]
	v_pk_mul_f32 v[52:53], v[52:53], v[82:83] op_sel_hi:[1,0]
	v_pk_mul_f32 v[50:51], v[50:51], v[82:83] op_sel_hi:[1,0]
	v_pk_mul_f32 v[48:49], v[48:49], v[82:83] op_sel_hi:[1,0]
	v_pk_mul_f32 v[46:47], v[46:47], v[82:83] op_sel_hi:[1,0]
	v_pk_mul_f32 v[44:45], v[44:45], v[82:83] op_sel_hi:[1,0]
	v_pk_mul_f32 v[42:43], v[42:43], v[82:83] op_sel_hi:[1,0]
	v_pk_mul_f32 v[40:41], v[40:41], v[82:83] op_sel_hi:[1,0]
	v_pk_mul_f32 v[38:39], v[38:39], v[82:83] op_sel_hi:[1,0]
	v_pk_mul_f32 v[36:37], v[36:37], v[82:83] op_sel_hi:[1,0]
	v_pk_mul_f32 v[34:35], v[34:35], v[82:83] op_sel_hi:[1,0]
	v_pk_mul_f32 v[32:33], v[32:33], v[82:83] op_sel_hi:[1,0]
	v_pk_mul_f32 v[30:31], v[30:31], v[82:83] op_sel_hi:[1,0]
	v_pk_mul_f32 v[28:29], v[28:29], v[82:83] op_sel_hi:[1,0]
	v_pk_mul_f32 v[26:27], v[26:27], v[82:83] op_sel_hi:[1,0]
	v_pk_mul_f32 v[24:25], v[24:25], v[82:83] op_sel_hi:[1,0]
	v_pk_mul_f32 v[22:23], v[22:23], v[82:83] op_sel_hi:[1,0]
	v_pk_mul_f32 v[20:21], v[20:21], v[82:83] op_sel_hi:[1,0]
	v_pk_mul_f32 v[18:19], v[18:19], v[82:83] op_sel_hi:[1,0]
	v_pk_mul_f32 v[16:17], v[16:17], v[82:83] op_sel_hi:[1,0]
	v_pk_mul_f32 v[14:15], v[14:15], v[82:83] op_sel_hi:[1,0]
	v_pk_mul_f32 v[12:13], v[12:13], v[82:83] op_sel_hi:[1,0]
	v_pk_mul_f32 v[10:11], v[10:11], v[82:83] op_sel_hi:[1,0]
	v_pk_mul_f32 v[8:9], v[8:9], v[82:83] op_sel_hi:[1,0]
	v_pk_mul_f32 v[6:7], v[6:7], v[82:83] op_sel_hi:[1,0]
	v_pk_mul_f32 v[4:5], v[4:5], v[82:83] op_sel_hi:[1,0]
	v_pk_mul_f32 v[2:3], v[2:3], v[82:83] op_sel_hi:[1,0]
	v_mul_f32_e32 v186, v186, v82

; #define ATT_SYNC(full) do { if (full) asm volatile("s_waitcnt vmcnt(7)" ::: "memory"); else asm volatile("s_waitcnt vmcnt(0)" ::: "memory"); \
;         __builtin_amdgcn_s_barrier(); asm volatile("" ::: "memory"); } while (0)
; __device__ __forceinline__ void attn_unit(const bf16_t* Qrows  , const bf16_t* Kbh, const bf16_t* Vbh, int nkeys, bf16_t* Orows, LAS unsigned char* lds) {
;     ...
;     ATT_SYNC(false);
;     ATT_STEP(sA, sB, true, k1, v0);
.LBB0_1250:
	v_max_f32_e32 v82, v67, v67
	v_max_f32_e32 v83, v66, v66
	v_max_f32_e32 v82, v83, v82
	v_max3_f32 v82, v82, v68, v69
	v_max3_f32 v82, v82, v70, v71
	v_max3_f32 v82, v82, v72, v73
	v_max3_f32 v82, v82, v74, v75
	v_max3_f32 v82, v82, v76, v77
	v_max3_f32 v82, v82, v78, v79
	v_max3_f32 v82, v82, v80, v81
	v_mov_b32_e32 v83, v82
	s_nop 1
	v_permlane32_swap_b32_e32 v83, v82
	s_waitcnt vmcnt(0)
	s_barrier
	v_add_f32_e32 v150, 0x41000000, v183
	s_waitcnt lgkmcnt(0)
	v_max_f32_e32 v83, v83, v83
	v_max_f32_e32 v82, v82, v83
	v_cmp_gt_f32_e32 vcc, v82, v150
	s_cbranch_vccz .LBB0_1252
	v_max_f32_e32 v82, v82, v82
	v_max_f32_e32 v83, v183, v183
	v_max_f32_e32 v83, v83, v82
	v_sub_f32_e32 v82, v183, v83
	v_exp_f32_e32 v82, v82
	v_add_f32_e32 v150, 0x41000000, v83
	v_mov_b32_e32 v183, v83
	v_pk_mul_f32 v[64:65], v[64:65], v[82:83] op_sel_hi:[1,0]
	v_pk_mul_f32 v[62:63], v[62:63], v[82:83] op_sel_hi:[1,0]
	v_pk_mul_f32 v[60:61], v[60:61], v[82:83] op_sel_hi:[1,0]
	v_pk_mul_f32 v[58:59], v[58:59], v[82:83] op_sel_hi:[1,0]
	v_pk_mul_f32 v[56:57], v[56:57], v[82:83] op_sel_hi:[1,0]
	v_pk_mul_f32 v[54:55], v[54:55], v[82:83] op_sel_hi:[1,0]
	v_pk_mul_f32 v[52:53], v[52:53], v[82:83] op_sel_hi:[1,0]
	v_pk_mul_f32 v[50:51], v[50:51], v[82:83] op_sel_hi:[1,0]
	v_pk_mul_f32 v[48:49], v[48:49], v[82:83] op_sel_hi:[1,0]
	v_pk_mul_f32 v[46:47], v[46:47], v[82:83] op_sel_hi:[1,0]
	v_pk_mul_f32 v[44:45], v[44:45], v[82:83] op_sel_hi:[1,0]
	v_pk_mul_f32 v[42:43], v[42:43], v[82:83] op_sel_hi:[1,0]
	v_pk_mul_f32 v[40:41], v[40:41], v[82:83] op_sel_hi:[1,0]
	v_pk_mul_f32 v[38:39], v[38:39], v[82:83] op_sel_hi:[1,0]
	v_pk_mul_f32 v[36:37], v[36:37], v[82:83] op_sel_hi:[1,0]
	v_pk_mul_f32 v[34:35], v[34:35], v[82:83] op_sel_hi:[1,0]
	v_pk_mul_f32 v[32:33], v[32:33], v[82:83] op_sel_hi:[1,0]
	v_pk_mul_f32 v[30:31], v[30:31], v[82:83] op_sel_hi:[1,0]
	v_pk_mul_f32 v[28:29], v[28:29], v[82:83] op_sel_hi:[1,0]
	v_pk_mul_f32 v[26:27], v[26:27], v[82:83] op_sel_hi:[1,0]
	v_pk_mul_f32 v[24:25], v[24:25], v[82:83] op_sel_hi:[1,0]
	v_pk_mul_f32 v[22:23], v[22:23], v[82:83] op_sel_hi:[1,0]
	v_pk_mul_f32 v[20:21], v[20:21], v[82:83] op_sel_hi:[1,0]
	v_pk_mul_f32 v[18:19], v[18:19], v[82:83] op_sel_hi:[1,0]
	v_pk_mul_f32 v[16:17], v[16:17], v[82:83] op_sel_hi:[1,0]
	v_pk_mul_f32 v[14:15], v[14:15], v[82:83] op_sel_hi:[1,0]
	v_pk_mul_f32 v[12:13], v[12:13], v[82:83] op_sel_hi:[1,0]
	v_pk_mul_f32 v[10:11], v[10:11], v[82:83] op_sel_hi:[1,0]
	v_pk_mul_f32 v[8:9], v[8:9], v[82:83] op_sel_hi:[1,0]
	v_pk_mul_f32 v[6:7], v[6:7], v[82:83] op_sel_hi:[1,0]
	v_pk_mul_f32 v[4:5], v[4:5], v[82:83] op_sel_hi:[1,0]
	v_pk_mul_f32 v[2:3], v[2:3], v[82:83] op_sel_hi:[1,0]
	v_mul_f32_e32 v186, v186, v82
.LBB0_1252:
	s_mul_i32 s0, s14, 0x6400
	s_add_i32 s0, s0, 0
	v_add3_u32 v86, s0, v184, v206
	ds_read_b128 v[82:85], v86
	ds_read_b128 v[152:155], v86 offset:32
	ds_read_b128 v[156:159], v86 offset:64
	ds_read_b128 v[160:163], v86 offset:96
	ds_read_b128 v[164:167], v86 offset:128
	ds_read_b128 v[168:171], v86 offset:160
	ds_read_b128 v[188:191], v86 offset:192
	ds_read_b128 v[192:195], v86 offset:224
	ds_read_b128 v[196:199], v86 offset:256
	ds_read_b128 v[200:203], v86 offset:288
	ds_read_b128 v[216:219], v86 offset:320
	ds_read_b128 v[146:149], v86 offset:352
	s_mul_i32 s0, s36, 0x4800
	s_add_i32 s1, s0, 0
	s_add_i32 s1, s1, 0x12c00
	s_waitcnt lgkmcnt(0)
	v_mfma_f32_32x32x16_bf16 v[82:97], v[82:85], v[142:145], 0
	v_sub_f32_e32 v66, v66, v183
	v_exp_f32_e32 v66, v66
	v_sub_f32_e32 v78, v78, v183
	v_exp_f32_e32 v78, v78
	v_add_u32_e32 v151, s1, v181
	v_add_f32_e32 v142, 0, v66
	v_add_f32_e32 v142, v78, v142
	v_mfma_f32_32x32x16_bf16 v[82:97], v[152:155], v[138:141], v[82:97]
	v_sub_f32_e32 v67, v67, v183
	v_exp_f32_e32 v67, v67
	v_sub_f32_e32 v79, v79, v183
	v_exp_f32_e32 v79, v79
	v_add_f32_e32 v138, v67, v142
	v_cvt_pk_bf16_f32 v66, v66, v67
	v_add_f32_e32 v138, v79, v138
	v_mfma_f32_32x32x16_bf16 v[82:97], v[156:159], v[134:137], v[82:97]
	v_sub_f32_e32 v67, v68, v183
	v_exp_f32_e32 v67, v67
	v_sub_f32_e32 v80, v80, v183
	v_exp_f32_e32 v134, v80
	v_add_f32_e32 v68, v67, v138
	v_add_f32_e32 v68, v134, v68
	v_mfma_f32_32x32x16_bf16 v[82:97], v[160:163], v[130:133], v[82:97]
	v_sub_f32_e32 v69, v69, v183
	v_exp_f32_e32 v69, v69
	v_sub_f32_e32 v80, v81, v183
	v_exp_f32_e32 v81, v80
	v_cvt_pk_bf16_f32 v80, v78, v79
	v_add_f32_e32 v68, v69, v68
	v_cvt_pk_bf16_f32 v67, v67, v69
	v_add_f32_e32 v68, v81, v68
	v_cvt_pk_bf16_f32 v81, v134, v81
	v_mfma_f32_32x32x16_bf16 v[82:97], v[164:167], v[126:129], v[82:97]
	v_sub_f32_e32 v69, v70, v183
	v_exp_f32_e32 v69, v69
	s_nop 0
	v_add_f32_e32 v68, v69, v68
	v_mfma_f32_32x32x16_bf16 v[82:97], v[168:171], v[122:125], v[82:97]
	v_sub_f32_e32 v70, v71, v183
	v_exp_f32_e32 v70, v70
	s_nop 0
	v_add_f32_e32 v71, v70, v68
	v_cvt_pk_bf16_f32 v68, v69, v70
	v_mfma_f32_32x32x16_bf16 v[82:97], v[188:191], v[118:121], v[82:97]
	v_sub_f32_e32 v69, v72, v183
	v_exp_f32_e32 v69, v69
	s_nop 0
	v_add_f32_e32 v70, v69, v71
	v_mfma_f32_32x32x16_bf16 v[82:97], v[192:195], v[114:117], v[82:97]
	v_sub_f32_e32 v71, v73, v183
	v_exp_f32_e32 v71, v71
	s_nop 0
	v_add_f32_e32 v70, v71, v70
	v_cvt_pk_bf16_f32 v69, v69, v71
	v_sub_f32_e32 v71, v74, v183
	v_exp_f32_e32 v74, v71
	v_mfma_f32_32x32x16_bf16 v[82:97], v[196:199], v[110:113], v[82:97]
	v_add3_u32 v122, v151, v206, v182
	v_add_f32_e32 v78, v74, v70
	ds_read_b128 v[70:73], v122
	ds_read_b128 v[110:113], v122 offset:32
	v_mfma_f32_32x32x16_bf16 v[82:97], v[200:203], v[106:109], v[82:97]
	v_sub_f32_e32 v75, v75, v183
	ds_read_b128 v[106:109], v122 offset:4608
	ds_read_b128 v[114:117], v122 offset:4640
	v_exp_f32_e32 v75, v75
	s_nop 0
	v_add_f32_e32 v79, v75, v78
	v_cvt_pk_bf16_f32 v78, v74, v75
	v_mfma_f32_32x32x16_bf16 v[82:97], v[216:219], v[102:105], v[82:97]
	v_sub_f32_e32 v74, v76, v183
	ds_read_b128 v[102:105], v122 offset:9216
	ds_read_b128 v[118:121], v122 offset:9248
	v_exp_f32_e32 v74, v74
	s_nop 0
	v_add_f32_e32 v75, v74, v79
	v_sub_f32_e32 v76, v77, v183
	v_exp_f32_e32 v76, v76
	v_mfma_f32_32x32x16_bf16 v[82:97], v[146:149], v[98:101], v[82:97]
	v_add_f32_e32 v123, v76, v75
	v_cvt_pk_bf16_f32 v79, v74, v76
	ds_read_b128 v[74:77], v122 offset:13824
	ds_read_b128 v[98:101], v122 offset:13856
	s_waitcnt lgkmcnt(0)
; #define ATT_SYNC(full) do { if (full) asm volatile("s_waitcnt vmcnt(7)" ::: "memory"); else asm volatile("s_waitcnt vmcnt(0)" ::: "memory"); \
;         __builtin_amdgcn_s_barrier(); asm volatile("" ::: "memory"); } while (0)
; __device__ __forceinline__ void attn_unit(const bf16_t* Qrows  , const bf16_t* Kbh, const bf16_t* Vbh, int nkeys, bf16_t* Orows, LAS unsigned char* lds) {
;     ...
;     ATT_SYNC(false);
;     ATT_STEP(sB, sA, false, k1, v0);
	v_mfma_f32_32x32x16_bf16 v[50:65], v[70:73], v[66:69], v[50:65]
	v_mfma_f32_32x32x16_bf16 v[34:49], v[106:109], v[66:69], v[34:49]
	v_mfma_f32_32x32x16_bf16 v[18:33], v[102:105], v[66:69], v[18:33]
	v_mfma_f32_32x32x16_bf16 v[2:17], v[74:77], v[66:69], v[2:17]
	v_mfma_f32_32x32x16_bf16 v[50:65], v[110:113], v[78:81], v[50:65]
	v_mfma_f32_32x32x16_bf16 v[34:49], v[114:117], v[78:81], v[34:49]
	v_mfma_f32_32x32x16_bf16 v[18:33], v[118:121], v[78:81], v[18:33]
	v_mfma_f32_32x32x16_bf16 v[2:17], v[98:101], v[78:81], v[2:17]
	v_max_f32_e32 v66, v83, v83
	v_max_f32_e32 v67, v82, v82
	v_max_f32_e32 v66, v67, v66
	v_max3_f32 v66, v66, v84, v85
	v_max3_f32 v66, v66, v86, v87
	v_max3_f32 v66, v66, v88, v89
	v_max3_f32 v66, v66, v90, v91
	v_max3_f32 v66, v66, v92, v93
	v_max3_f32 v66, v66, v94, v95
	v_max3_f32 v67, v66, v96, v97
	v_mov_b32_e32 v68, v67
	s_nop 1
	v_permlane32_swap_b32_e32 v68, v67
	s_waitcnt vmcnt(0)
	s_barrier
	v_add_f32_e32 v66, v186, v123
	s_waitcnt lgkmcnt(0)
	v_max_f32_e32 v68, v68, v68
	v_max_f32_e32 v67, v67, v68
	v_cmp_gt_f32_e32 vcc, v67, v150
	s_cbranch_vccz .LBB0_1254
	v_max_f32_e32 v67, v67, v67
	v_max_f32_e32 v68, v183, v183
	v_max_f32_e32 v67, v68, v67
	v_sub_f32_e32 v68, v183, v67
	v_exp_f32_e32 v68, v68
	v_mov_b32_e32 v183, v67
	v_pk_mul_f32 v[64:65], v[64:65], v[68:69] op_sel_hi:[1,0]
	v_pk_mul_f32 v[62:63], v[62:63], v[68:69] op_sel_hi:[1,0]
	v_pk_mul_f32 v[60:61], v[60:61], v[68:69] op_sel_hi:[1,0]
	v_pk_mul_f32 v[58:59], v[58:59], v[68:69] op_sel_hi:[1,0]
	v_pk_mul_f32 v[56:57], v[56:57], v[68:69] op_sel_hi:[1,0]
	v_pk_mul_f32 v[54:55], v[54:55], v[68:69] op_sel_hi:[1,0]
	v_pk_mul_f32 v[52:53], v[52:53], v[68:69] op_sel_hi:[1,0]
	v_pk_mul_f32 v[50:51], v[50:51], v[68:69] op_sel_hi:[1,0]
	v_pk_mul_f32 v[48:49], v[48:49], v[68:69] op_sel_hi:[1,0]
	v_pk_mul_f32 v[46:47], v[46:47], v[68:69] op_sel_hi:[1,0]
	v_pk_mul_f32 v[44:45], v[44:45], v[68:69] op_sel_hi:[1,0]
	v_pk_mul_f32 v[42:43], v[42:43], v[68:69] op_sel_hi:[1,0]
	v_pk_mul_f32 v[40:41], v[40:41], v[68:69] op_sel_hi:[1,0]
	v_pk_mul_f32 v[38:39], v[38:39], v[68:69] op_sel_hi:[1,0]
	v_pk_mul_f32 v[36:37], v[36:37], v[68:69] op_sel_hi:[1,0]
	v_pk_mul_f32 v[34:35], v[34:35], v[68:69] op_sel_hi:[1,0]
	v_pk_mul_f32 v[32:33], v[32:33], v[68:69] op_sel_hi:[1,0]
	v_pk_mul_f32 v[30:31], v[30:31], v[68:69] op_sel_hi:[1,0]
	v_pk_mul_f32 v[28:29], v[28:29], v[68:69] op_sel_hi:[1,0]
	v_pk_mul_f32 v[26:27], v[26:27], v[68:69] op_sel_hi:[1,0]
	v_pk_mul_f32 v[24:25], v[24:25], v[68:69] op_sel_hi:[1,0]
	v_pk_mul_f32 v[22:23], v[22:23], v[68:69] op_sel_hi:[1,0]
	v_pk_mul_f32 v[20:21], v[20:21], v[68:69] op_sel_hi:[1,0]
	v_pk_mul_f32 v[18:19], v[18:19], v[68:69] op_sel_hi:[1,0]
	v_pk_mul_f32 v[16:17], v[16:17], v[68:69] op_sel_hi:[1,0]
	v_pk_mul_f32 v[14:15], v[14:15], v[68:69] op_sel_hi:[1,0]
	v_pk_mul_f32 v[12:13], v[12:13], v[68:69] op_sel_hi:[1,0]
	v_pk_mul_f32 v[10:11], v[10:11], v[68:69] op_sel_hi:[1,0]
	v_pk_mul_f32 v[8:9], v[8:9], v[68:69] op_sel_hi:[1,0]
	v_pk_mul_f32 v[6:7], v[6:7], v[68:69] op_sel_hi:[1,0]
	v_pk_mul_f32 v[4:5], v[4:5], v[68:69] op_sel_hi:[1,0]
	v_pk_mul_f32 v[2:3], v[2:3], v[68:69] op_sel_hi:[1,0]
	v_mul_f32_e32 v66, v66, v68
; #define LAS __attribute__((address_space(3)))
; __device__ __forceinline__ void attn_unit(const bf16_t* Qrows  , const bf16_t* Kbh, const bf16_t* Vbh, int nkeys, bf16_t* Orows, LAS unsigned char* lds) {
;     ...
;     __syncthreads();
;     lsum += __shfl_xor(lsum, 32);
;     LAS float* mb = (LAS float*)lds + (size_t)qg * 66 * 64 + lane;
;     if (kh == 1) {
; #pragma unroll
;         for (int db = 0; db < 4; ++db)
; #pragma unroll
;             for (int r = 0; r < 16; ++r) mb[(db * 16 + r) * 64] = o[db][r];
;         mb[64 * 64] = mrow; mb[65 * 64] = lsum;
.LBB0_1254:
	s_addk_i32 s0, 0x4800
	s_cmp_lg_u32 s36, 2
	s_cselect_b32 s0, s0, 0
	s_add_i32 s0, s0, 0
	v_sub_f32_e32 v72, v82, v183
	s_add_i32 s0, s0, 0x12c00
	v_exp_f32_e32 v98, v72
	v_sub_f32_e32 v72, v83, v183
	v_add_u32_e32 v67, s0, v181
	v_exp_f32_e32 v99, v72
	v_sub_f32_e32 v72, v84, v183
	v_add3_u32 v67, v67, v206, v182
	v_exp_f32_e32 v84, v72
	v_sub_f32_e32 v72, v85, v183
	ds_read_b128 v[68:71], v67
	v_exp_f32_e32 v85, v72
	v_sub_f32_e32 v72, v86, v183
	v_exp_f32_e32 v86, v72
	v_sub_f32_e32 v72, v87, v183
	v_exp_f32_e32 v87, v72
	v_sub_f32_e32 v72, v88, v183
	v_exp_f32_e32 v88, v72
	v_sub_f32_e32 v72, v89, v183
	v_exp_f32_e32 v89, v72
	v_cvt_pk_bf16_f32 v72, v98, v99
	v_cvt_pk_bf16_f32 v73, v84, v85
	v_cvt_pk_bf16_f32 v74, v86, v87
	v_cvt_pk_bf16_f32 v75, v88, v89
	v_sub_f32_e32 v90, v90, v183
	v_sub_f32_e32 v91, v91, v183
	s_waitcnt lgkmcnt(0)
	v_mfma_f32_32x32x16_bf16 v[50:65], v[68:71], v[72:75], v[50:65]
	ds_read_b128 v[68:71], v67 offset:4608
	ds_read_b128 v[76:79], v67 offset:32
	ds_read_b128 v[80:83], v67 offset:9216
	v_sub_f32_e32 v92, v92, v183
	v_exp_f32_e32 v90, v90
	v_exp_f32_e32 v91, v91
	v_exp_f32_e32 v92, v92
	s_waitcnt lgkmcnt(0)
	v_mfma_f32_32x32x16_bf16 v[34:49], v[68:71], v[72:75], v[34:49]
	ds_read_b128 v[68:71], v67 offset:13824
	v_mfma_f32_32x32x16_bf16 v[18:33], v[80:83], v[72:75], v[18:33]
	v_sub_f32_e32 v80, v93, v183
	v_exp_f32_e32 v93, v80
	v_sub_f32_e32 v80, v94, v183
	v_exp_f32_e32 v94, v80
	v_sub_f32_e32 v80, v95, v183
	v_exp_f32_e32 v95, v80
	v_sub_f32_e32 v80, v96, v183
	s_waitcnt lgkmcnt(0)
	v_mfma_f32_32x32x16_bf16 v[2:17], v[68:71], v[72:75], v[2:17]
	v_sub_f32_e32 v68, v97, v183
	v_exp_f32_e32 v96, v80
	v_exp_f32_e32 v97, v68
	v_cvt_pk_bf16_f32 v68, v90, v91
	v_cvt_pk_bf16_f32 v69, v92, v93
	v_cvt_pk_bf16_f32 v70, v94, v95
	v_cvt_pk_bf16_f32 v71, v96, v97
	s_nop 1
	v_mfma_f32_32x32x16_bf16 v[50:65], v[76:79], v[68:71], v[50:65]
	ds_read_b128 v[72:75], v67 offset:4640
	ds_read_b128 v[76:79], v67 offset:9248
	ds_read_b128 v[80:83], v67 offset:13856
	v_add_f32_e32 v67, 0, v98
	v_add_f32_e32 v67, v99, v67
	v_add_f32_e32 v67, v84, v67
	v_add_f32_e32 v67, v85, v67
	v_add_f32_e32 v67, v86, v67
	v_add_f32_e32 v67, v87, v67
	v_add_f32_e32 v67, v88, v67
	v_add_f32_e32 v67, v89, v67
	v_add_f32_e32 v67, v90, v67
	s_waitcnt lgkmcnt(0)
	v_mfma_f32_32x32x16_bf16 v[34:49], v[72:75], v[68:71], v[34:49]
	v_add_f32_e32 v67, v91, v67
	v_add_f32_e32 v67, v92, v67
	v_add_f32_e32 v67, v93, v67
	v_add_f32_e32 v67, v94, v67
	v_add_f32_e32 v67, v95, v67
	v_add_f32_e32 v67, v96, v67
	v_add_f32_e32 v67, v97, v67
	v_mfma_f32_32x32x16_bf16 v[18:33], v[76:79], v[68:71], v[18:33]
	v_add_f32_e32 v66, v66, v67
	v_mfma_f32_32x32x16_bf16 v[2:17], v[80:83], v[68:71], v[2:17]
	v_mov_b32_e32 v67, v66
	s_nop 1
	v_permlane32_swap_b32_e32 v67, v66
	v_mul_u32_u24_e32 v68, 0x4200, v178
	v_cmp_eq_u32_e32 vcc, 1, v179
	s_waitcnt vmcnt(0) lgkmcnt(0)
	s_barrier
	v_add_f32_e32 v66, v66, v67
	v_lshlrev_b32_e32 v67, 2, v177
	v_add3_u32 v69, 0, v68, v67
	s_and_saveexec_b64 s[0:1], vcc
	s_cbranch_execz .LBB0_1256
	ds_write2st64_b32 v69, v50, v51 offset1:1
	ds_write2st64_b32 v69, v52, v53 offset0:2 offset1:3
	ds_write2st64_b32 v69, v54, v55 offset0:4 offset1:5
	ds_write2st64_b32 v69, v56, v57 offset0:6 offset1:7
	ds_write2st64_b32 v69, v58, v59 offset0:8 offset1:9
	ds_write2st64_b32 v69, v60, v61 offset0:10 offset1:11
	ds_write2st64_b32 v69, v62, v63 offset0:12 offset1:13
	ds_write2st64_b32 v69, v64, v65 offset0:14 offset1:15
	ds_write2st64_b32 v69, v34, v35 offset0:16 offset1:17
	ds_write2st64_b32 v69, v36, v37 offset0:18 offset1:19
	ds_write2st64_b32 v69, v38, v39 offset0:20 offset1:21
	ds_write2st64_b32 v69, v40, v41 offset0:22 offset1:23
	ds_write2st64_b32 v69, v42, v43 offset0:24 offset1:25
	ds_write2st64_b32 v69, v44, v45 offset0:26 offset1:27
	ds_write2st64_b32 v69, v46, v47 offset0:28 offset1:29
	ds_write2st64_b32 v69, v48, v49 offset0:30 offset1:31
	ds_write2st64_b32 v69, v18, v19 offset0:32 offset1:33
	ds_write2st64_b32 v69, v20, v21 offset0:34 offset1:35
	ds_write2st64_b32 v69, v22, v23 offset0:36 offset1:37
	ds_write2st64_b32 v69, v24, v25 offset0:38 offset1:39
	ds_write2st64_b32 v69, v26, v27 offset0:40 offset1:41
	ds_write2st64_b32 v69, v28, v29 offset0:42 offset1:43
	ds_write2st64_b32 v69, v30, v31 offset0:44 offset1:45
	ds_write2st64_b32 v69, v32, v33 offset0:46 offset1:47
	ds_write2st64_b32 v69, v2, v3 offset0:48 offset1:49
	ds_write2st64_b32 v69, v4, v5 offset0:50 offset1:51
	ds_write2st64_b32 v69, v6, v7 offset0:52 offset1:53
	ds_write2st64_b32 v69, v8, v9 offset0:54 offset1:55
	ds_write2st64_b32 v69, v10, v11 offset0:56 offset1:57
	ds_write2st64_b32 v69, v12, v13 offset0:58 offset1:59
	ds_write2st64_b32 v69, v14, v15 offset0:60 offset1:61
	ds_write2st64_b32 v69, v16, v17 offset0:62 offset1:63
	ds_write2st64_b32 v69, v183, v66 offset0:64 offset1:65

; #define LAS __attribute__((address_space(3)))
;     __device__ __forceinline__ void init(const void* A_, const void* B_, int G_, int c_) { T.init(A_, B_, DM, DM, NLAT / 256, INP / 256, 1, 0, 0, G_, c_, 0); }
; __device__ __forceinline__ void sgu_unit(const Params& p, int l, int un, LAS unsigned char* lds) {
;     ...
;     const int cc = un >> 2, h = un & 3; const int row0 = cc * 128;
;     LAS bf16_t* Wl = (LAS bf16_t*)lds;
;     LAS bf16_t* Vl = (LAS bf16_t*)(lds + 128 * 136 * 2);
;     const float* Wg = p.in[I_SGUW] + ((size_t)l * 4 + h) * 128 * 128;
;     f32x4 wq[8]; u32x4 vv[16];
; #pragma unroll
;     for (int i = 0; i < 8; ++i) wq[i] = *(const f32x4*)(Wg + (i * 512 + tid) * 4);
; #pragma unroll
;     for (int qi = 0; qi < 16; ++qi) vv[qi] = *(const u32x4*)(P + (size_t)(row0 + wave * 16 + qi) * INP + C_SGU_V + lane * 8);
; __global__ void __launch_bounds__(512, 2) fwd(Params p) {
;     ...
;             { pg8::TileSched S; S.init(ws + WS_UPK, (bf16_t*)(ws + WS_G2B) + (size_t)l * 32 * 256 * 512, 512, 512, 3, 1, 32, (size_t)768 * 512 * 2, (size_t)256 * 512 * 2, G, c, (l == 0 && G == 256) ? 32 : 0);
;               pg8::EpiS2 E{(bf16_t*)(ws + WS_GB)};
;               pg8::Unit u0; if (S.next(0, u0)) { carry_wait(p, l); pg8::gemm_phase(lds, pg8::Desc{512, 512, 512}, S, E); }
;               else if (G == 256) { const int un = c - (l == 0 ? 128 : 96); if (un >= 0) sgu_unit(p, l, un, lds); } }
.LBB0_1258:
	v_readlane_b32 s0, v251, 50
	v_readlane_b32 s2, v252, 20
	v_readlane_b32 s1, v251, 51
	v_readlane_b32 s3, v252, 21
	s_and_b64 s[0:1], s[0:1], s[2:3]
	s_and_b64 s[0:1], s[0:1], exec
	s_cselect_b32 s0, 32, 0
	v_readlane_b32 s2, v255, 11
	s_mul_hi_u32 s1, s0, s2
	v_readlane_b32 s3, v255, 12
	s_mul_i32 s1, s1, s3
	s_sub_i32 s0, s0, s1
	s_sub_i32 s1, s0, s3
	s_cmp_ge_u32 s0, s3
	s_cselect_b32 s0, s1, s0
	s_sub_i32 s1, s0, s3
	s_cmp_ge_u32 s0, s3
	s_cselect_b32 s0, s1, s0
	v_readlane_b32 s1, v255, 42
	s_sub_i32 s0, s1, s0
	s_ashr_i32 s1, s0, 31
	s_abs_i32 s0, s0
	s_mul_hi_u32 s2, s0, s2
	s_mul_i32 s2, s2, s3
	s_sub_i32 s0, s0, s2
	s_sub_i32 s2, s0, s3
	s_cmp_ge_u32 s0, s3
	s_cselect_b32 s0, s2, s0
	s_sub_i32 s2, s0, s3
	s_cmp_ge_u32 s0, s3
	s_cselect_b32 s0, s2, s0
	s_xor_b32 s0, s0, s1
	s_sub_i32 s26, s0, s1
	s_cmpk_gt_i32 s26, 0x5f
	s_mov_b64 s[0:1], -1
	s_barrier
	s_cbranch_scc0 .LBB0_1294
	v_readlane_b32 s0, v252, 20
	v_readlane_b32 s1, v252, 21
	s_and_b64 s[0:1], s[0:1], exec
	s_movk_i32 s0, 0xff80
	s_cselect_b32 s0, s0, 0xffffffa0
	s_add_i32 s0, s0, s92
	v_readlane_b32 s12, v251, 50
	s_cmp_lt_i32 s0, 0
	v_readlane_b32 s13, v251, 51
	s_cselect_b64 s[2:3], -1, 0
	s_xor_b64 s[12:13], s[12:13], -1
	s_or_b64 s[2:3], s[2:3], s[12:13]
	s_and_b64 vcc, exec, s[2:3]
	s_cbranch_vccnz .LBB0_1293
	v_readlane_b32 s2, v252, 5
	v_readlane_b32 s44, v251, 16
	s_lshl_b32 s1, s0, 5
	s_lshl_b32 s0, s2, 9
	v_readlane_b32 s2, v253, 39
	v_readlane_b32 s48, v251, 20
	v_readlane_b32 s49, v251, 21
	v_readlane_b32 s3, v252, 6
	s_or_b32 s40, s0, s2
	s_mov_b32 s41, s5
	v_readlane_b32 s50, v251, 22
	v_readlane_b32 s51, v251, 23
	v_readlane_b32 s52, v251, 24
	v_readlane_b32 s53, v251, 25
	v_readlane_b32 s54, v251, 26
	v_readlane_b32 s55, v251, 27
	s_mov_b64 s[12:13], s[48:49]
	s_lshl_b64 s[2:3], s[40:41], 9
	s_mov_b64 s[14:15], s[50:51]
	v_mov_b32_e32 v64, v0
	s_add_u32 s2, s14, s2
	s_addc_u32 s3, s15, s3
	v_lshlrev_b32_e32 v2, 2, v64
	v_ashrrev_i32_e32 v3, 31, v2
	v_add_u32_e32 v62, 0x800, v2
	s_mov_b64 s[14:15], 0
	v_lshl_add_u64 v[4:5], v[2:3], 2, s[2:3]
	v_ashrrev_i32_e32 v63, 31, v62
	v_lshl_add_u64 v[6:7], v[62:63], 2, s[2:3]
	global_load_dwordx4 v[66:69], v[4:5], off
	global_load_dwordx4 v[70:73], v[6:7], off
	v_add_u32_e32 v102, 0x1000, v2
	v_ashrrev_i32_e32 v103, 31, v102
	v_add_u32_e32 v104, 0x1800, v2
	v_lshl_add_u64 v[4:5], v[102:103], 2, s[2:3]
	v_ashrrev_i32_e32 v105, 31, v104
	s_and_b32 s12, s1, 0x7fffff80
	s_mov_b32 s1, s5
	v_lshl_add_u64 v[6:7], v[104:105], 2, s[2:3]
	global_load_dwordx4 v[74:77], v[4:5], off
	global_load_dwordx4 v[78:81], v[6:7], off
	s_lshl_b64 s[0:1], s[0:1], 2
	v_readlane_b32 s13, v253, 41
	v_add_u32_e32 v106, 0x2000, v2
	s_add_u32 s0, s13, s0
	v_readlane_b32 s13, v253, 42
	v_ashrrev_i32_e32 v107, 31, v106
	v_add_u32_e32 v108, 0x2800, v2
	s_addc_u32 s1, s13, s1
	v_lshl_add_u64 v[4:5], v[106:107], 2, s[2:3]
	v_ashrrev_i32_e32 v109, 31, v108
	s_add_u32 s36, s84, s14
	v_lshl_add_u64 v[6:7], v[108:109], 2, s[2:3]
	global_load_dwordx4 v[82:85], v[4:5], off
	global_load_dwordx4 v[86:89], v[6:7], off
	s_addc_u32 s37, s85, s15
	v_add_u32_e32 v110, 0x3000, v2
	v_add_u32_e32 v112, 0x3800, v2
	s_add_u32 s38, s36, 0x1f1b8000
	v_ashrrev_i32_e32 v111, 31, v110
	v_ashrrev_i32_e32 v113, 31, v112
	v_ashrrev_i32_e32 v103, 6, v64
	s_addc_u32 s39, s37, 0
	v_lshl_add_u64 v[4:5], v[110:111], 2, s[2:3]
	v_lshl_add_u64 v[2:3], v[112:113], 2, s[2:3]
	v_lshlrev_b32_e32 v65, 4, v103
	v_and_b32_e32 v8, 63, v64
	global_load_dwordx4 v[90:93], v[4:5], off
	global_load_dwordx4 v[94:97], v[2:3], off
	v_add_u32_e32 v9, s12, v65
	v_mov_b64_e32 v[2:3], s[38:39]
	s_movk_i32 s13, 0x1e00
	v_mad_i64_i32 v[4:5], s[2:3], v9, s13, v[2:3]
	v_lshlrev_b32_e32 v206, 4, v8
	v_or_b32_e32 v6, 1, v9
	v_lshl_add_u64 v[4:5], v[4:5], 0, v[206:207]
	v_mad_i64_i32 v[6:7], s[2:3], v6, s13, v[2:3]
	v_lshl_add_u64 v[6:7], v[6:7], 0, v[206:207]
	global_load_dwordx4 v[98:101], v[4:5], off offset:1024
	global_load_dwordx4 v[58:61], v[6:7], off offset:1024
	v_or_b32_e32 v4, 2, v9
	v_or_b32_e32 v6, 3, v9
	v_mad_i64_i32 v[4:5], s[2:3], v4, s13, v[2:3]
	v_mad_i64_i32 v[6:7], s[2:3], v6, s13, v[2:3]
	v_lshl_add_u64 v[4:5], v[4:5], 0, v[206:207]
	v_lshl_add_u64 v[6:7], v[6:7], 0, v[206:207]
	global_load_dwordx4 v[54:57], v[4:5], off offset:1024
	global_load_dwordx4 v[50:53], v[6:7], off offset:1024
	v_or_b32_e32 v4, 4, v9
	v_or_b32_e32 v6, 5, v9
	v_mad_i64_i32 v[4:5], s[2:3], v4, s13, v[2:3]
	v_mad_i64_i32 v[6:7], s[2:3], v6, s13, v[2:3]
	v_lshl_add_u64 v[4:5], v[4:5], 0, v[206:207]
	v_lshl_add_u64 v[6:7], v[6:7], 0, v[206:207]
	global_load_dwordx4 v[46:49], v[4:5], off offset:1024
	global_load_dwordx4 v[42:45], v[6:7], off offset:1024
	v_or_b32_e32 v4, 6, v9
	v_or_b32_e32 v6, 7, v9
	v_mad_i64_i32 v[4:5], s[2:3], v4, s13, v[2:3]
	v_mad_i64_i32 v[6:7], s[2:3], v6, s13, v[2:3]
	v_lshl_add_u64 v[4:5], v[4:5], 0, v[206:207]
	v_lshl_add_u64 v[6:7], v[6:7], 0, v[206:207]
	global_load_dwordx4 v[38:41], v[4:5], off offset:1024
	global_load_dwordx4 v[34:37], v[6:7], off offset:1024
	v_or_b32_e32 v4, 8, v9
	v_or_b32_e32 v6, 9, v9
	v_mad_i64_i32 v[4:5], s[2:3], v4, s13, v[2:3]
	v_mad_i64_i32 v[6:7], s[2:3], v6, s13, v[2:3]
	v_lshl_add_u64 v[4:5], v[4:5], 0, v[206:207]
	v_lshl_add_u64 v[6:7], v[6:7], 0, v[206:207]
	global_load_dwordx4 v[30:33], v[4:5], off offset:1024
	global_load_dwordx4 v[26:29], v[6:7], off offset:1024
	v_or_b32_e32 v4, 10, v9
	v_or_b32_e32 v6, 11, v9
	v_mad_i64_i32 v[4:5], s[2:3], v4, s13, v[2:3]
	v_mad_i64_i32 v[6:7], s[2:3], v6, s13, v[2:3]
	v_lshl_add_u64 v[4:5], v[4:5], 0, v[206:207]
	v_lshl_add_u64 v[6:7], v[6:7], 0, v[206:207]
	global_load_dwordx4 v[22:25], v[4:5], off offset:1024
	global_load_dwordx4 v[18:21], v[6:7], off offset:1024
	v_or_b32_e32 v4, 12, v9
	v_or_b32_e32 v6, 13, v9
	v_mad_i64_i32 v[4:5], s[2:3], v4, s13, v[2:3]
	v_mad_i64_i32 v[6:7], s[2:3], v6, s13, v[2:3]
	v_lshl_add_u64 v[4:5], v[4:5], 0, v[206:207]
	v_lshl_add_u64 v[6:7], v[6:7], 0, v[206:207]
	v_lshlrev_b32_e32 v105, 3, v64
	global_load_dwordx4 v[14:17], v[4:5], off offset:1024
	global_load_dwordx4 v[10:13], v[6:7], off offset:1024
	v_or_b32_e32 v4, 14, v9
	v_or_b32_e32 v6, 15, v9
	v_and_b32_e32 v63, 0xf8, v105
	v_mad_i64_i32 v[4:5], s[2:3], v4, s13, v[2:3]
	v_mad_i64_i32 v[2:3], s[2:3], v6, s13, v[2:3]
	v_add_u32_e32 v114, 0, v63
	v_bfe_i32 v63, v64, 5, 25
	s_movk_i32 s13, 0x110
	v_lshl_add_u64 v[4:5], v[4:5], 0, v[206:207]
	v_lshl_add_u64 v[2:3], v[2:3], 0, v[206:207]
	s_waitcnt vmcnt(21)
; #define LAS __attribute__((address_space(3)))
; __device__ __forceinline__ unsigned cvt_pk_bf16(float lo, float hi) { const f32x2 v = {lo, hi}; const bf16x2_t b = __builtin_convertvector(v, bf16x2_t); return __builtin_bit_cast(unsigned, b); }
; __device__ __forceinline__ float bflo(unsigned w) { return __uint_as_float(w << 16); }
; __device__ __forceinline__ float bfhi(unsigned w) { return __uint_as_float(w & 0xffff0000u); }
; __device__ __forceinline__ float wave_sum(float v) {
; #pragma unroll
;     for (int o = 32; o >= 1; o >>= 1) v += __shfl_xor(v, o);
;     return v;
; }
; __device__ __forceinline__ void sgu_unit(const Params& p, int l, int un, LAS unsigned char* lds) {
;     ...
;     for (int i = 0; i < 8; ++i) { const int e4 = (i * 512 + tid) * 4, r = e4 >> 7, c = e4 & 127; const f32x4 v = wq[i];
;         u32x2 w; w.x = cvt_pk_bf16(v[0], v[1]); w.y = cvt_pk_bf16(v[2], v[3]); *(LAS u32x2*)(Wl + r * 136 + c) = w; }
; #pragma unroll
;     for (int qi = 0; qi < 16; ++qi) { const int q = wave * 16 + qi;
;         const u32x4 v = vv[qi]; float f[8] = {bflo(v.x), bfhi(v.x), bflo(v.y), bfhi(v.y), bflo(v.z), bfhi(v.z), bflo(v.w), bfhi(v.w)}; float ss = 0.f;
; #pragma unroll
;         for (int j = 0; j < 8; ++j) { f[j] = gelu_tanh(f[j]); ss += f[j] * f[j]; }
;         ss = wave_sum(ss); const float rinv = rsqrtf(ss * (1.0f / 512.0f) + EPS);
	v_cvt_pk_bf16_f32 v66, v66, v67
	v_cvt_pk_bf16_f32 v67, v68, v69
	v_mad_u64_u32 v[68:69], s[2:3], v63, s13, v[114:115]
	global_load_dwordx4 v[6:9], v[4:5], off offset:1024
	s_nop 0
	global_load_dwordx4 v[2:5], v[2:3], off offset:1024
	ds_write_b64 v68, v[66:67]
	v_ashrrev_i32_e32 v66, 7, v62
	s_waitcnt vmcnt(22)
	v_cvt_pk_bf16_f32 v62, v70, v71
	v_cvt_pk_bf16_f32 v63, v72, v73
	v_mad_u64_u32 v[66:67], s[2:3], v66, s13, v[114:115]
	ds_write_b64 v66, v[62:63]
	v_ashrrev_i32_e32 v66, 7, v102
	s_waitcnt vmcnt(21)
	v_cvt_pk_bf16_f32 v62, v74, v75
	v_cvt_pk_bf16_f32 v63, v76, v77
	v_mad_u64_u32 v[66:67], s[2:3], v66, s13, v[114:115]
	ds_write_b64 v66, v[62:63]
	v_ashrrev_i32_e32 v66, 7, v104
	s_waitcnt vmcnt(20)
	v_cvt_pk_bf16_f32 v62, v78, v79
	v_cvt_pk_bf16_f32 v63, v80, v81
	v_mad_u64_u32 v[66:67], s[2:3], v66, s13, v[114:115]
	ds_write_b64 v66, v[62:63]
	v_ashrrev_i32_e32 v66, 7, v106
	s_waitcnt vmcnt(19)
	v_cvt_pk_bf16_f32 v62, v82, v83
	v_cvt_pk_bf16_f32 v63, v84, v85
	v_mad_u64_u32 v[66:67], s[2:3], v66, s13, v[114:115]
	ds_write_b64 v66, v[62:63]
	v_ashrrev_i32_e32 v66, 7, v108
	s_waitcnt vmcnt(18)
	v_cvt_pk_bf16_f32 v62, v86, v87
	v_cvt_pk_bf16_f32 v63, v88, v89
	v_mad_u64_u32 v[66:67], s[2:3], v66, s13, v[114:115]
	ds_write_b64 v66, v[62:63]
	v_ashrrev_i32_e32 v66, 7, v110
	s_waitcnt vmcnt(17)
	v_cvt_pk_bf16_f32 v62, v90, v91
	v_cvt_pk_bf16_f32 v63, v92, v93
	v_mad_u64_u32 v[66:67], s[2:3], v66, s13, v[114:115]
	ds_write_b64 v66, v[62:63]
	v_ashrrev_i32_e32 v66, 7, v112
	v_mad_u64_u32 v[66:67], s[2:3], v66, s13, v[114:115]
	s_waitcnt vmcnt(15)
	v_and_b32_e32 v67, 0xffff0000, v98
	v_mul_f32_e32 v73, 0x3dd2d3e8, v67
	v_fma_f32 v73, -v73, v67, s33
	v_mul_f32_e32 v73, v73, v67
	v_exp_f32_e32 v73, v73
	v_cvt_pk_bf16_f32 v62, v94, v95
	v_cvt_pk_bf16_f32 v63, v96, v97
	ds_write_b64 v66, v[62:63]
	v_lshlrev_b32_e32 v66, 16, v98
	v_add_f32_e32 v73, 1.0, v73
	v_mul_f32_e32 v72, 0x3dd2d3e8, v66
	v_rcp_f32_e32 v73, v73
	v_fma_f32 v72, -v72, v66, s33
	v_mul_f32_e32 v72, v72, v66
	v_lshlrev_b32_e32 v69, 16, v99
	v_exp_f32_e32 v72, v72
	v_mul_f32_e32 v79, v73, v67
	v_mul_f32_e32 v67, 0x3dd2d3e8, v69
	v_fma_f32 v67, -v67, v69, s33
	v_mul_f32_e32 v67, v67, v69
	v_add_f32_e32 v72, 1.0, v72
	v_exp_f32_e32 v67, v67
	v_rcp_f32_e32 v72, v72
	v_lshlrev_b32_e32 v71, 16, v100
	v_and_b32_e32 v70, 0xffff0000, v99
	v_add_f32_e32 v67, 1.0, v67
	v_mul_f32_e32 v73, 0x3dd2d3e8, v71
	v_mul_f32_e32 v81, v72, v66
	v_mul_f32_e32 v72, 0x3dd2d3e8, v70
	v_rcp_f32_e32 v67, v67
	v_fma_f32 v73, -v73, v71, s33
	v_fma_f32 v72, -v72, v70, s33
	v_mul_f32_e32 v73, v73, v71
	v_mul_f32_e32 v72, v72, v70
	v_exp_f32_e32 v73, v73
	v_and_b32_e32 v74, 0xffff0000, v100
	v_exp_f32_e32 v72, v72
	v_mul_f32_e32 v80, v67, v69
	v_mul_f32_e32 v69, 0x3dd2d3e8, v74
	v_fma_f32 v69, -v69, v74, s33
	v_add_f32_e32 v67, 1.0, v73
	v_mul_f32_e32 v69, v69, v74
	v_add_f32_e32 v72, 1.0, v72
	v_rcp_f32_e32 v67, v67
	v_exp_f32_e32 v69, v69
	v_rcp_f32_e32 v72, v72
	v_lshlrev_b32_e32 v75, 16, v101
	v_and_b32_e32 v82, 0xffff0000, v101
	v_mul_f32_e32 v76, v67, v71
	v_add_f32_e32 v67, 1.0, v69
	v_mul_f32_e32 v69, 0x3dd2d3e8, v75
	v_mul_f32_e32 v78, v72, v70
	v_fma_f32 v69, -v69, v75, s33
	v_mul_f32_e32 v70, 0x3dd2d3e8, v82
	v_mul_f32_e32 v69, v69, v75
	v_fma_f32 v70, -v70, v82, s33
	v_rcp_f32_e32 v67, v67
	v_exp_f32_e32 v69, v69
	v_mul_f32_e32 v70, v70, v82
	v_exp_f32_e32 v70, v70
	v_mul_f32_e32 v66, v79, v79
	v_mul_f32_e32 v77, v67, v74
	v_add_f32_e32 v67, 1.0, v69
	v_fmac_f32_e32 v66, v81, v81
	v_rcp_f32_e32 v67, v67
	v_add_f32_e32 v69, 1.0, v70
	v_fmac_f32_e32 v66, v80, v80
	v_rcp_f32_e32 v69, v69
	v_and_b32_e32 v62, 64, v249
	v_fmac_f32_e32 v66, v78, v78
	v_add_u32_e32 v62, 64, v62
	v_xor_b32_e32 v63, 32, v249
	v_fmac_f32_e32 v66, v76, v76
	v_cmp_lt_i32_e32 vcc, v63, v62
	v_fmac_f32_e32 v66, v77, v77
	v_mul_f32_e32 v75, v67, v75
	v_cndmask_b32_e32 v63, v249, v63, vcc
	v_fmac_f32_e32 v66, v75, v75
	v_mul_f32_e32 v74, v69, v82
	v_lshlrev_b32_e32 v68, 2, v63
	v_fmac_f32_e32 v66, v74, v74
	v_mov_b32_e32 v67, v66
	s_nop 1
	v_permlane32_swap_b32_e32 v67, v66
	v_xor_b32_e32 v63, 16, v249
	v_cmp_lt_i32_e32 vcc, v63, v62
	v_and_b32_e32 v84, 0x78, v105
	v_readlane_b32 s2, v253, 40
	v_cndmask_b32_e32 v63, v249, v63, vcc
	v_lshlrev_b32_e32 v69, 2, v63
	s_waitcnt lgkmcnt(0)
	v_add_f32_e32 v66, v66, v67
	v_mov_b32_e32 v67, v66
	s_nop 1
	v_permlane16_swap_b32_e32 v67, v66
	v_xor_b32_e32 v63, 8, v249
	v_cmp_lt_i32_e32 vcc, v63, v62
	v_lshlrev_b32_e32 v206, 2, v84
	v_readlane_b32 s45, v251, 17
	v_cndmask_b32_e32 v63, v249, v63, vcc
	v_lshlrev_b32_e32 v70, 2, v63
	s_waitcnt lgkmcnt(0)
	v_add_f32_e32 v66, v66, v67
	s_nop 1
	v_mov_b32_dpp v67, v66 row_ror:8 row_mask:0xf bank_mask:0xf
	v_xor_b32_e32 v63, 4, v249
	v_cmp_lt_i32_e32 vcc, v63, v62
	v_readlane_b32 s46, v251, 18
	v_readlane_b32 s47, v251, 19
	v_cndmask_b32_e32 v63, v249, v63, vcc
	v_lshlrev_b32_e32 v71, 2, v63
	s_waitcnt lgkmcnt(0)
	v_add_f32_e32 v66, v66, v67
	v_xor_b32_e32 v63, 2, v249
	s_nop 1
	v_mov_b32_dpp v67, v66 row_shl:4 row_mask:0xf bank_mask:0x5
	v_mov_b32_dpp v67, v66 row_shr:4 row_mask:0xf bank_mask:0xa
	v_cmp_lt_i32_e32 vcc, v63, v62
	v_readlane_b32 s56, v251, 28
	v_readlane_b32 s57, v251, 29
	v_cndmask_b32_e32 v63, v249, v63, vcc
	v_lshlrev_b32_e32 v72, 2, v63
	v_xor_b32_e32 v63, 1, v249
	v_cmp_lt_i32_e32 vcc, v63, v62
	v_readlane_b32 s58, v251, 30
	v_readlane_b32 s59, v251, 31
	v_cndmask_b32_e32 v62, v249, v63, vcc
	s_waitcnt lgkmcnt(0)
	v_add_f32_e32 v63, v66, v67
	s_nop 1
	v_mov_b32_dpp v67, v63 quad_perm:[2,3,0,1] row_mask:0xf bank_mask:0xf
	v_lshlrev_b32_e32 v73, 2, v62
	v_bfe_u32 v66, v64, 4, 2
	v_cmp_eq_u32_e32 vcc, s2, v66
	s_mov_b64 s[16:17], s[52:53]
	s_waitcnt lgkmcnt(0)
	v_add_f32_e32 v82, v63, v67
	s_nop 1
	v_mov_b32_dpp v83, v82 quad_perm:[1,0,3,2] row_mask:0xf bank_mask:0xf
	v_lshl_add_u32 v67, v103, 5, 0
	v_lshl_add_u64 v[62:63], s[0:1], 0, v[206:207]
	v_mad_u32_u24 v67, v84, s13, v67
	s_mov_b64 s[18:19], s[54:55]
	s_and_saveexec_b64 s[0:1], vcc
	s_cbranch_execz .LBB0_1262
; __device__ __forceinline__ float bflo(unsigned w) { return __uint_as_float(w << 16); }
; __device__ __forceinline__ float bfhi(unsigned w) { return __uint_as_float(w & 0xffff0000u); }
; __device__ __forceinline__ unsigned short f2bf(float f) { return (unsigned short)(cvt_pk_bf16(f, 0.f) & 0xffffu); }
; __device__ __forceinline__ float wave_sum(float v) {
; #pragma unroll
;     for (int o = 32; o >= 1; o >>= 1) v += __shfl_xor(v, o);
;     return v;
; }
; __device__ __forceinline__ void sgu_unit(const Params& p, int l, int un, LAS unsigned char* lds) {
;     ...
;     for (int qi = 0; qi < 16; ++qi) { const int q = wave * 16 + qi;
;         const u32x4 v = vv[qi]; float f[8] = {bflo(v.x), bfhi(v.x), bflo(v.y), bfhi(v.y), bflo(v.z), bfhi(v.z), bflo(v.w), bfhi(v.w)}; float ss = 0.f;
; #pragma unroll
;         for (int j = 0; j < 8; ++j) { f[j] = gelu_tanh(f[j]); ss += f[j] * f[j]; }
;         ss = wave_sum(ss); const float rinv = rsqrtf(ss * (1.0f / 512.0f) + EPS);
;         if ((lane >> 4) == h) { const int c0 = (lane & 15) * 8; const float* g = p.in[I_SGUNG] + l * 512 + h * 128 + c0;
; #pragma unroll
;             for (int j = 0; j < 8; ++j) Vl[(c0 + j) * 136 + q] = f2bf(f[j] * rinv * g[j]); } }
	s_waitcnt lgkmcnt(0)
	v_add_f32_e32 v82, v82, v83
	v_fmamk_f32 v82, v82, 0x3b000000, v246
	s_mov_b32 s2, 0x800000
	v_cmp_gt_f32_e64 s[2:3], s2, v82
	v_mul_f32_e32 v83, 0x4b800000, v82
	s_nop 0
	v_cndmask_b32_e64 v82, v82, v83, s[2:3]
	v_rsq_f32_e32 v82, v82
	s_nop 0
	v_mul_f32_e32 v83, 0x45800000, v82
	v_cndmask_b32_e64 v90, v82, v83, s[2:3]
	global_load_dwordx4 v[82:85], v[62:63], off offset:16
	global_load_dwordx4 v[86:89], v[62:63], off
	v_mul_f32_e32 v79, v79, v90
	v_mul_f32_e32 v76, v76, v90
	v_mul_f32_e32 v81, v81, v90
	v_mul_f32_e32 v78, v78, v90
	v_mul_f32_e32 v75, v75, v90
	v_mul_f32_e32 v74, v74, v90
	s_waitcnt vmcnt(1)
	v_mul_f32_e32 v76, v76, v82
	s_waitcnt vmcnt(0)
	v_mul_f32_e32 v79, v79, v87
	v_cvt_pk_bf16_f32 v79, v79, s0
	v_cvt_pk_bf16_f32 v76, v76, s0
	ds_write_b16 v67, v79 offset:35088
	v_mul_f32_e32 v79, v80, v90
	ds_write_b16 v67, v76 offset:35904
	v_mul_f32_e32 v76, v77, v90
	v_mul_f32_e32 v81, v81, v86
	v_mul_f32_e32 v79, v79, v88
	v_mul_f32_e32 v78, v78, v89
	v_mul_f32_e32 v76, v76, v83
	v_mul_f32_e32 v75, v75, v84
	v_mul_f32_e32 v74, v74, v85
	v_cvt_pk_bf16_f32 v81, v81, s0
	v_cvt_pk_bf16_f32 v79, v79, s0
	v_cvt_pk_bf16_f32 v78, v78, s0
	v_cvt_pk_bf16_f32 v76, v76, s0
	v_cvt_pk_bf16_f32 v75, v75, s0
	v_cvt_pk_bf16_f32 v74, v74, s0
	ds_write_b16 v67, v81 offset:34816
	ds_write_b16 v67, v79 offset:35360
	ds_write_b16 v67, v78 offset:35632
	ds_write_b16 v67, v76 offset:36176
	ds_write_b16 v67, v75 offset:36448
	ds_write_b16 v67, v74 offset:36720
.LBB0_1262:
	s_or_b64 exec, exec, s[0:1]
	s_waitcnt vmcnt(14)
	v_lshlrev_b32_e32 v74, 16, v58
	v_lshlrev_b32_e32 v75, 16, v59
	v_and_b32_e32 v77, 0xffff0000, v59
	v_mul_f32_e32 v59, 0x3dd2d3e8, v74
	v_fma_f32 v59, -v59, v74, s33
	v_mul_f32_e32 v59, v59, v74
	v_exp_f32_e32 v59, v59
	v_and_b32_e32 v58, 0xffff0000, v58
	v_lshlrev_b32_e32 v78, 16, v60
	v_and_b32_e32 v79, 0xffff0000, v60
	v_add_f32_e32 v59, 1.0, v59
	v_rcp_f32_e32 v59, v59
	v_mul_f32_e32 v60, 0x3dd2d3e8, v77
	v_fma_f32 v60, -v60, v77, s33
	v_mul_f32_e32 v60, v60, v77
	v_mul_f32_e32 v76, v59, v74
	v_mul_f32_e32 v59, 0x3dd2d3e8, v58
	v_fma_f32 v59, -v59, v58, s33
	v_mul_f32_e32 v59, v59, v58
	v_exp_f32_e32 v59, v59
	v_exp_f32_e32 v60, v60
	v_lshlrev_b32_e32 v80, 16, v61
	v_and_b32_e32 v81, 0xffff0000, v61
	v_add_f32_e32 v59, 1.0, v59
	v_rcp_f32_e32 v59, v59
	v_add_f32_e32 v60, 1.0, v60
	v_rcp_f32_e32 v60, v60
	v_mul_f32_e32 v61, 0x3dd2d3e8, v78
	v_mul_f32_e32 v59, v59, v58
	v_mul_f32_e32 v58, 0x3dd2d3e8, v75
	v_fma_f32 v58, -v58, v75, s33
	v_mul_f32_e32 v58, v58, v75
	v_exp_f32_e32 v58, v58
	v_fma_f32 v61, -v61, v78, s33
	v_mul_f32_e32 v74, 0x3dd2d3e8, v79
	v_mul_f32_e32 v61, v61, v78
	v_add_f32_e32 v58, 1.0, v58
	v_rcp_f32_e32 v58, v58
	v_fma_f32 v74, -v74, v79, s33
	v_mul_f32_e32 v60, v60, v77
	v_exp_f32_e32 v61, v61
	v_mul_f32_e32 v58, v58, v75
	v_mul_f32_e32 v75, 0x3dd2d3e8, v80
	v_mul_f32_e32 v74, v74, v79
	v_fma_f32 v75, -v75, v80, s33
	v_mul_f32_e32 v77, 0x3dd2d3e8, v81
	v_exp_f32_e32 v74, v74
	v_mul_f32_e32 v75, v75, v80
	v_fma_f32 v77, -v77, v81, s33
	v_exp_f32_e32 v75, v75
	v_mul_f32_e32 v77, v77, v81
	v_exp_f32_e32 v77, v77
	v_add_f32_e32 v61, 1.0, v61
	v_rcp_f32_e32 v61, v61
	v_add_f32_e32 v74, 1.0, v74
	v_mul_f32_e32 v82, v59, v59
	v_rcp_f32_e32 v74, v74
	v_add_f32_e32 v75, 1.0, v75
	v_fmac_f32_e32 v82, v76, v76
	v_rcp_f32_e32 v75, v75
	v_add_f32_e32 v77, 1.0, v77
	v_fmac_f32_e32 v82, v58, v58
	v_rcp_f32_e32 v77, v77
	v_fmac_f32_e32 v82, v60, v60
	v_mul_f32_e32 v61, v61, v78
	v_fmac_f32_e32 v82, v61, v61
	v_mul_f32_e32 v74, v74, v79
	v_fmac_f32_e32 v82, v74, v74
	v_mul_f32_e32 v75, v75, v80
	v_fmac_f32_e32 v82, v75, v75
	v_mul_f32_e32 v77, v77, v81
	v_fmac_f32_e32 v82, v77, v77
	ds_bpermute_b32 v78, v68, v82
	s_waitcnt lgkmcnt(0)
	v_add_f32_e32 v78, v82, v78
	v_mov_b32_e32 v79, v78
	s_nop 1
	v_permlane16_swap_b32_e32 v79, v78
	s_waitcnt lgkmcnt(0)
	v_add_f32_e32 v78, v78, v79
	s_nop 1
	v_mov_b32_dpp v79, v78 row_ror:8 row_mask:0xf bank_mask:0xf
	s_waitcnt lgkmcnt(0)
	v_add_f32_e32 v78, v78, v79
	s_nop 1
	v_mov_b32_dpp v79, v78 row_shl:4 row_mask:0xf bank_mask:0x5
	v_mov_b32_dpp v79, v78 row_shr:4 row_mask:0xf bank_mask:0xa
	s_waitcnt lgkmcnt(0)
	v_add_f32_e32 v78, v78, v79
	s_nop 1
	v_mov_b32_dpp v79, v78 quad_perm:[2,3,0,1] row_mask:0xf bank_mask:0xf
	s_waitcnt lgkmcnt(0)
	v_add_f32_e32 v78, v78, v79
	s_nop 1
	v_mov_b32_dpp v79, v78 quad_perm:[1,0,3,2] row_mask:0xf bank_mask:0xf
	s_and_saveexec_b64 s[0:1], vcc
	s_cbranch_execz .LBB0_1264
	s_waitcnt lgkmcnt(0)
	v_add_f32_e32 v78, v78, v79
	v_fmamk_f32 v78, v78, 0x3b000000, v246
	s_mov_b32 s2, 0x800000
	v_cmp_gt_f32_e64 s[2:3], s2, v78
	v_mul_f32_e32 v79, 0x4b800000, v78
	s_nop 0
	v_cndmask_b32_e64 v78, v78, v79, s[2:3]
	v_rsq_f32_e32 v78, v78
	s_nop 0
	v_mul_f32_e32 v79, 0x45800000, v78
	v_cndmask_b32_e64 v86, v78, v79, s[2:3]
	global_load_dwordx4 v[78:81], v[62:63], off offset:16
	global_load_dwordx4 v[82:85], v[62:63], off
	v_mul_f32_e32 v58, v58, v86
	v_mul_f32_e32 v76, v76, v86
	v_mul_f32_e32 v59, v59, v86
	s_waitcnt vmcnt(0)
	v_mul_f32_e32 v58, v58, v84
	v_cvt_pk_bf16_f32 v58, v58, s0
	ds_write_b16 v67, v58 offset:35362
	v_mul_f32_e32 v58, v60, v86
	v_mul_f32_e32 v58, v58, v85
	v_cvt_pk_bf16_f32 v58, v58, s0
	ds_write_b16 v67, v58 offset:35634
	v_mul_f32_e32 v58, v61, v86
	v_mul_f32_e32 v58, v58, v78
	v_cvt_pk_bf16_f32 v58, v58, s0
	ds_write_b16 v67, v58 offset:35906
	v_mul_f32_e32 v58, v74, v86
	v_mul_f32_e32 v58, v58, v79
	v_cvt_pk_bf16_f32 v58, v58, s0
	ds_write_b16 v67, v58 offset:36178
	v_mul_f32_e32 v58, v75, v86
	v_mul_f32_e32 v58, v58, v80
	v_cvt_pk_bf16_f32 v58, v58, s0
	ds_write_b16 v67, v58 offset:36450
	v_mul_f32_e32 v58, v77, v86
	v_mul_f32_e32 v76, v76, v82
	v_mul_f32_e32 v59, v59, v83
	v_mul_f32_e32 v58, v58, v81
	v_cvt_pk_bf16_f32 v76, v76, s0
	v_cvt_pk_bf16_f32 v59, v59, s0
	v_cvt_pk_bf16_f32 v58, v58, s0
	ds_write_b16 v67, v76 offset:34818
	ds_write_b16 v67, v59 offset:35090
	ds_write_b16 v67, v58 offset:36722
; __device__ __forceinline__ float bflo(unsigned w) { return __uint_as_float(w << 16); }
; __device__ __forceinline__ float bfhi(unsigned w) { return __uint_as_float(w & 0xffff0000u); }
; __device__ __forceinline__ unsigned short f2bf(float f) { return (unsigned short)(cvt_pk_bf16(f, 0.f) & 0xffffu); }
; __device__ __forceinline__ float wave_sum(float v) {
; #pragma unroll
;     for (int o = 32; o >= 1; o >>= 1) v += __shfl_xor(v, o);
;     return v;
; }
; __device__ __forceinline__ void sgu_unit(const Params& p, int l, int un, LAS unsigned char* lds) {
;     ...
;     for (int qi = 0; qi < 16; ++qi) { const int q = wave * 16 + qi;
;         const u32x4 v = vv[qi]; float f[8] = {bflo(v.x), bfhi(v.x), bflo(v.y), bfhi(v.y), bflo(v.z), bfhi(v.z), bflo(v.w), bfhi(v.w)}; float ss = 0.f;
; #pragma unroll
;         for (int j = 0; j < 8; ++j) { f[j] = gelu_tanh(f[j]); ss += f[j] * f[j]; }
;         ss = wave_sum(ss); const float rinv = rsqrtf(ss * (1.0f / 512.0f) + EPS);
;         if ((lane >> 4) == h) { const int c0 = (lane & 15) * 8; const float* g = p.in[I_SGUNG] + l * 512 + h * 128 + c0;
; #pragma unroll
;             for (int j = 0; j < 8; ++j) Vl[(c0 + j) * 136 + q] = f2bf(f[j] * rinv * g[j]); } }
.LBB0_1264:
	s_or_b64 exec, exec, s[0:1]
	s_waitcnt vmcnt(13)
	v_lshlrev_b32_e32 v58, 16, v54
	v_lshlrev_b32_e32 v59, 16, v55
	v_and_b32_e32 v61, 0xffff0000, v55
	v_mul_f32_e32 v55, 0x3dd2d3e8, v58
	v_fma_f32 v55, -v55, v58, s33
	v_mul_f32_e32 v55, v55, v58
	v_exp_f32_e32 v55, v55
	v_and_b32_e32 v54, 0xffff0000, v54
	v_lshlrev_b32_e32 v74, 16, v56
	v_and_b32_e32 v75, 0xffff0000, v56
	v_add_f32_e32 v55, 1.0, v55
	v_rcp_f32_e32 v55, v55
	v_mul_f32_e32 v56, 0x3dd2d3e8, v61
	v_fma_f32 v56, -v56, v61, s33
	v_mul_f32_e32 v56, v56, v61
	v_mul_f32_e32 v60, v55, v58
	v_mul_f32_e32 v55, 0x3dd2d3e8, v54
	v_fma_f32 v55, -v55, v54, s33
	v_mul_f32_e32 v55, v55, v54
	v_exp_f32_e32 v55, v55
	v_exp_f32_e32 v56, v56
	v_lshlrev_b32_e32 v76, 16, v57
	v_and_b32_e32 v77, 0xffff0000, v57
	v_add_f32_e32 v55, 1.0, v55
	v_rcp_f32_e32 v55, v55
	v_add_f32_e32 v56, 1.0, v56
	v_rcp_f32_e32 v56, v56
	v_mul_f32_e32 v57, 0x3dd2d3e8, v74
	v_mul_f32_e32 v55, v55, v54
	v_mul_f32_e32 v54, 0x3dd2d3e8, v59
	v_fma_f32 v54, -v54, v59, s33
	v_mul_f32_e32 v54, v54, v59
	v_exp_f32_e32 v54, v54
	v_fma_f32 v57, -v57, v74, s33
	v_mul_f32_e32 v58, 0x3dd2d3e8, v75
	v_mul_f32_e32 v57, v57, v74
	v_add_f32_e32 v54, 1.0, v54
	v_rcp_f32_e32 v54, v54
	v_fma_f32 v58, -v58, v75, s33
	v_mul_f32_e32 v56, v56, v61
	v_exp_f32_e32 v57, v57
	v_mul_f32_e32 v54, v54, v59
	v_mul_f32_e32 v59, 0x3dd2d3e8, v76
	v_mul_f32_e32 v58, v58, v75
	v_fma_f32 v59, -v59, v76, s33
	v_mul_f32_e32 v61, 0x3dd2d3e8, v77
	v_exp_f32_e32 v58, v58
	v_mul_f32_e32 v59, v59, v76
	v_fma_f32 v61, -v61, v77, s33
	v_exp_f32_e32 v59, v59
	v_mul_f32_e32 v61, v61, v77
	v_exp_f32_e32 v61, v61
	v_add_f32_e32 v57, 1.0, v57
	v_rcp_f32_e32 v57, v57
	v_add_f32_e32 v58, 1.0, v58
	v_mul_f32_e32 v78, v55, v55
	v_rcp_f32_e32 v58, v58
	v_add_f32_e32 v59, 1.0, v59
	v_fmac_f32_e32 v78, v60, v60
	v_rcp_f32_e32 v59, v59
	v_add_f32_e32 v61, 1.0, v61
	v_fmac_f32_e32 v78, v54, v54
	v_rcp_f32_e32 v61, v61
	v_fmac_f32_e32 v78, v56, v56
	v_mul_f32_e32 v57, v57, v74
	v_fmac_f32_e32 v78, v57, v57
	v_mul_f32_e32 v58, v58, v75
	v_fmac_f32_e32 v78, v58, v58
	v_mul_f32_e32 v59, v59, v76
	v_fmac_f32_e32 v78, v59, v59
	v_mul_f32_e32 v61, v61, v77
	v_fmac_f32_e32 v78, v61, v61
	ds_bpermute_b32 v74, v68, v78
	s_waitcnt lgkmcnt(0)
	v_add_f32_e32 v74, v78, v74
	v_mov_b32_e32 v75, v74
	s_nop 1
	v_permlane16_swap_b32_e32 v75, v74
	s_waitcnt lgkmcnt(0)
	v_add_f32_e32 v74, v74, v75
	s_nop 1
	v_mov_b32_dpp v75, v74 row_ror:8 row_mask:0xf bank_mask:0xf
	s_waitcnt lgkmcnt(0)
	v_add_f32_e32 v74, v74, v75
	s_nop 1
	v_mov_b32_dpp v75, v74 row_shl:4 row_mask:0xf bank_mask:0x5
	v_mov_b32_dpp v75, v74 row_shr:4 row_mask:0xf bank_mask:0xa
	s_waitcnt lgkmcnt(0)
	v_add_f32_e32 v74, v74, v75
	s_nop 1
	v_mov_b32_dpp v75, v74 quad_perm:[2,3,0,1] row_mask:0xf bank_mask:0xf
	s_waitcnt lgkmcnt(0)
	v_add_f32_e32 v74, v74, v75
	s_nop 1
	v_mov_b32_dpp v75, v74 quad_perm:[1,0,3,2] row_mask:0xf bank_mask:0xf
	s_and_saveexec_b64 s[0:1], vcc
	s_cbranch_execz .LBB0_1266
	s_waitcnt lgkmcnt(0)
	v_add_f32_e32 v74, v74, v75
	v_fmamk_f32 v74, v74, 0x3b000000, v246
	s_mov_b32 s2, 0x800000
	v_cmp_gt_f32_e64 s[2:3], s2, v74
	v_mul_f32_e32 v75, 0x4b800000, v74
	s_nop 0
	v_cndmask_b32_e64 v74, v74, v75, s[2:3]
	v_rsq_f32_e32 v74, v74
	s_nop 0
	v_mul_f32_e32 v75, 0x45800000, v74
	v_cndmask_b32_e64 v82, v74, v75, s[2:3]
	global_load_dwordx4 v[74:77], v[62:63], off offset:16
	global_load_dwordx4 v[78:81], v[62:63], off
	v_mul_f32_e32 v54, v54, v82
	v_mul_f32_e32 v60, v60, v82
	v_mul_f32_e32 v55, v55, v82
	s_waitcnt vmcnt(0)
	v_mul_f32_e32 v54, v54, v80
	v_cvt_pk_bf16_f32 v54, v54, s0
	ds_write_b16 v67, v54 offset:35364
	v_mul_f32_e32 v54, v56, v82
	v_mul_f32_e32 v54, v54, v81
	v_cvt_pk_bf16_f32 v54, v54, s0
	ds_write_b16 v67, v54 offset:35636
	v_mul_f32_e32 v54, v57, v82
	v_mul_f32_e32 v54, v54, v74
	v_cvt_pk_bf16_f32 v54, v54, s0
	ds_write_b16 v67, v54 offset:35908
	v_mul_f32_e32 v54, v58, v82
	v_mul_f32_e32 v54, v54, v75
	v_cvt_pk_bf16_f32 v54, v54, s0
	ds_write_b16 v67, v54 offset:36180
	v_mul_f32_e32 v54, v59, v82
	v_mul_f32_e32 v54, v54, v76
	v_cvt_pk_bf16_f32 v54, v54, s0
	ds_write_b16 v67, v54 offset:36452
	v_mul_f32_e32 v54, v61, v82
	v_mul_f32_e32 v60, v60, v78
	v_mul_f32_e32 v55, v55, v79
	v_mul_f32_e32 v54, v54, v77
	v_cvt_pk_bf16_f32 v60, v60, s0
	v_cvt_pk_bf16_f32 v55, v55, s0
	v_cvt_pk_bf16_f32 v54, v54, s0
	ds_write_b16 v67, v60 offset:34820
	ds_write_b16 v67, v55 offset:35092
	ds_write_b16 v67, v54 offset:36724
; __device__ __forceinline__ float bflo(unsigned w) { return __uint_as_float(w << 16); }
; __device__ __forceinline__ float bfhi(unsigned w) { return __uint_as_float(w & 0xffff0000u); }
; __device__ __forceinline__ unsigned short f2bf(float f) { return (unsigned short)(cvt_pk_bf16(f, 0.f) & 0xffffu); }
; __device__ __forceinline__ float wave_sum(float v) {
; #pragma unroll
;     for (int o = 32; o >= 1; o >>= 1) v += __shfl_xor(v, o);
;     return v;
; }
; __device__ __forceinline__ void sgu_unit(const Params& p, int l, int un, LAS unsigned char* lds) {
;     ...
;     for (int qi = 0; qi < 16; ++qi) { const int q = wave * 16 + qi;
;         const u32x4 v = vv[qi]; float f[8] = {bflo(v.x), bfhi(v.x), bflo(v.y), bfhi(v.y), bflo(v.z), bfhi(v.z), bflo(v.w), bfhi(v.w)}; float ss = 0.f;
; #pragma unroll
;         for (int j = 0; j < 8; ++j) { f[j] = gelu_tanh(f[j]); ss += f[j] * f[j]; }
;         ss = wave_sum(ss); const float rinv = rsqrtf(ss * (1.0f / 512.0f) + EPS);
;         if ((lane >> 4) == h) { const int c0 = (lane & 15) * 8; const float* g = p.in[I_SGUNG] + l * 512 + h * 128 + c0;
; #pragma unroll
;             for (int j = 0; j < 8; ++j) Vl[(c0 + j) * 136 + q] = f2bf(f[j] * rinv * g[j]); } }
.LBB0_1266:
	s_or_b64 exec, exec, s[0:1]
	s_waitcnt vmcnt(12)
	v_lshlrev_b32_e32 v54, 16, v50
	v_lshlrev_b32_e32 v55, 16, v51
	v_and_b32_e32 v57, 0xffff0000, v51
	v_mul_f32_e32 v51, 0x3dd2d3e8, v54
	v_fma_f32 v51, -v51, v54, s33
	v_mul_f32_e32 v51, v51, v54
	v_exp_f32_e32 v51, v51
	v_and_b32_e32 v50, 0xffff0000, v50
	v_lshlrev_b32_e32 v58, 16, v52
	v_and_b32_e32 v59, 0xffff0000, v52
	v_add_f32_e32 v51, 1.0, v51
	v_rcp_f32_e32 v51, v51
	v_mul_f32_e32 v52, 0x3dd2d3e8, v57
	v_fma_f32 v52, -v52, v57, s33
	v_mul_f32_e32 v52, v52, v57
	v_mul_f32_e32 v56, v51, v54
	v_mul_f32_e32 v51, 0x3dd2d3e8, v50
	v_fma_f32 v51, -v51, v50, s33
	v_mul_f32_e32 v51, v51, v50
	v_exp_f32_e32 v51, v51
	v_exp_f32_e32 v52, v52
	v_lshlrev_b32_e32 v60, 16, v53
	v_and_b32_e32 v61, 0xffff0000, v53
	v_add_f32_e32 v51, 1.0, v51
	v_rcp_f32_e32 v51, v51
	v_add_f32_e32 v52, 1.0, v52
	v_rcp_f32_e32 v52, v52
	v_mul_f32_e32 v53, 0x3dd2d3e8, v58
	v_mul_f32_e32 v51, v51, v50
	v_mul_f32_e32 v50, 0x3dd2d3e8, v55
	v_fma_f32 v50, -v50, v55, s33
	v_mul_f32_e32 v50, v50, v55
	v_exp_f32_e32 v50, v50
	v_fma_f32 v53, -v53, v58, s33
	v_mul_f32_e32 v54, 0x3dd2d3e8, v59
	v_mul_f32_e32 v53, v53, v58
	v_add_f32_e32 v50, 1.0, v50
	v_rcp_f32_e32 v50, v50
	v_fma_f32 v54, -v54, v59, s33
	v_mul_f32_e32 v52, v52, v57
	v_exp_f32_e32 v53, v53
	v_mul_f32_e32 v50, v50, v55
	v_mul_f32_e32 v55, 0x3dd2d3e8, v60
	v_mul_f32_e32 v54, v54, v59
	v_fma_f32 v55, -v55, v60, s33
	v_mul_f32_e32 v57, 0x3dd2d3e8, v61
	v_exp_f32_e32 v54, v54
	v_mul_f32_e32 v55, v55, v60
	v_fma_f32 v57, -v57, v61, s33
	v_exp_f32_e32 v55, v55
	v_mul_f32_e32 v57, v57, v61
	v_exp_f32_e32 v57, v57
	v_add_f32_e32 v53, 1.0, v53
	v_rcp_f32_e32 v53, v53
	v_add_f32_e32 v54, 1.0, v54
	v_mul_f32_e32 v74, v51, v51
	v_rcp_f32_e32 v54, v54
	v_add_f32_e32 v55, 1.0, v55
	v_fmac_f32_e32 v74, v56, v56
	v_rcp_f32_e32 v55, v55
	v_add_f32_e32 v57, 1.0, v57
	v_fmac_f32_e32 v74, v50, v50
	v_rcp_f32_e32 v57, v57
	v_fmac_f32_e32 v74, v52, v52
	v_mul_f32_e32 v53, v53, v58
	v_fmac_f32_e32 v74, v53, v53
	v_mul_f32_e32 v54, v54, v59
	v_fmac_f32_e32 v74, v54, v54
	v_mul_f32_e32 v55, v55, v60
	v_fmac_f32_e32 v74, v55, v55
	v_mul_f32_e32 v57, v57, v61
	v_fmac_f32_e32 v74, v57, v57
	ds_bpermute_b32 v58, v68, v74
	s_waitcnt lgkmcnt(0)
	v_add_f32_e32 v58, v74, v58
	v_mov_b32_e32 v59, v58
	s_nop 1
	v_permlane16_swap_b32_e32 v59, v58
	s_waitcnt lgkmcnt(0)
	v_add_f32_e32 v58, v58, v59
	s_nop 1
	v_mov_b32_dpp v59, v58 row_ror:8 row_mask:0xf bank_mask:0xf
	s_waitcnt lgkmcnt(0)
	v_add_f32_e32 v58, v58, v59
	s_nop 1
	v_mov_b32_dpp v59, v58 row_shl:4 row_mask:0xf bank_mask:0x5
	v_mov_b32_dpp v59, v58 row_shr:4 row_mask:0xf bank_mask:0xa
	s_waitcnt lgkmcnt(0)
	v_add_f32_e32 v58, v58, v59
	s_nop 1
	v_mov_b32_dpp v59, v58 quad_perm:[2,3,0,1] row_mask:0xf bank_mask:0xf
	s_waitcnt lgkmcnt(0)
	v_add_f32_e32 v58, v58, v59
	s_nop 1
	v_mov_b32_dpp v59, v58 quad_perm:[1,0,3,2] row_mask:0xf bank_mask:0xf
	s_and_saveexec_b64 s[0:1], vcc
	s_cbranch_execz .LBB0_1268
	s_waitcnt lgkmcnt(0)
	v_add_f32_e32 v58, v58, v59
	v_fmamk_f32 v58, v58, 0x3b000000, v246
	s_mov_b32 s2, 0x800000
	v_cmp_gt_f32_e64 s[2:3], s2, v58
	v_mul_f32_e32 v59, 0x4b800000, v58
	s_nop 0
	v_cndmask_b32_e64 v58, v58, v59, s[2:3]
	v_rsq_f32_e32 v58, v58
	s_nop 0
	v_mul_f32_e32 v59, 0x45800000, v58
	v_cndmask_b32_e64 v78, v58, v59, s[2:3]
	global_load_dwordx4 v[58:61], v[62:63], off offset:16
	global_load_dwordx4 v[74:77], v[62:63], off
	v_mul_f32_e32 v50, v50, v78
	v_mul_f32_e32 v56, v56, v78
	v_mul_f32_e32 v51, v51, v78
	s_waitcnt vmcnt(0)
	v_mul_f32_e32 v50, v50, v76
	v_cvt_pk_bf16_f32 v50, v50, s0
	ds_write_b16 v67, v50 offset:35366
	v_mul_f32_e32 v50, v52, v78
	v_mul_f32_e32 v50, v50, v77
	v_cvt_pk_bf16_f32 v50, v50, s0
	ds_write_b16 v67, v50 offset:35638
	v_mul_f32_e32 v50, v53, v78
	v_mul_f32_e32 v50, v50, v58
	v_cvt_pk_bf16_f32 v50, v50, s0
	ds_write_b16 v67, v50 offset:35910
	v_mul_f32_e32 v50, v54, v78
	v_mul_f32_e32 v50, v50, v59
	v_cvt_pk_bf16_f32 v50, v50, s0
	ds_write_b16 v67, v50 offset:36182
	v_mul_f32_e32 v50, v55, v78
	v_mul_f32_e32 v50, v50, v60
	v_cvt_pk_bf16_f32 v50, v50, s0
	ds_write_b16 v67, v50 offset:36454
	v_mul_f32_e32 v50, v57, v78
	v_mul_f32_e32 v56, v56, v74
	v_mul_f32_e32 v51, v51, v75
	v_mul_f32_e32 v50, v50, v61
	v_cvt_pk_bf16_f32 v56, v56, s0
	v_cvt_pk_bf16_f32 v51, v51, s0
	v_cvt_pk_bf16_f32 v50, v50, s0
	ds_write_b16 v67, v56 offset:34822
	ds_write_b16 v67, v51 offset:35094
	ds_write_b16 v67, v50 offset:36726
; __device__ __forceinline__ float bflo(unsigned w) { return __uint_as_float(w << 16); }
; __device__ __forceinline__ float bfhi(unsigned w) { return __uint_as_float(w & 0xffff0000u); }
; __device__ __forceinline__ unsigned short f2bf(float f) { return (unsigned short)(cvt_pk_bf16(f, 0.f) & 0xffffu); }
; __device__ __forceinline__ float wave_sum(float v) {
; #pragma unroll
;     for (int o = 32; o >= 1; o >>= 1) v += __shfl_xor(v, o);
;     return v;
; }
; __device__ __forceinline__ void sgu_unit(const Params& p, int l, int un, LAS unsigned char* lds) {
;     ...
;     for (int qi = 0; qi < 16; ++qi) { const int q = wave * 16 + qi;
;         const u32x4 v = vv[qi]; float f[8] = {bflo(v.x), bfhi(v.x), bflo(v.y), bfhi(v.y), bflo(v.z), bfhi(v.z), bflo(v.w), bfhi(v.w)}; float ss = 0.f;
; #pragma unroll
;         for (int j = 0; j < 8; ++j) { f[j] = gelu_tanh(f[j]); ss += f[j] * f[j]; }
;         ss = wave_sum(ss); const float rinv = rsqrtf(ss * (1.0f / 512.0f) + EPS);
;         if ((lane >> 4) == h) { const int c0 = (lane & 15) * 8; const float* g = p.in[I_SGUNG] + l * 512 + h * 128 + c0;
; #pragma unroll
;             for (int j = 0; j < 8; ++j) Vl[(c0 + j) * 136 + q] = f2bf(f[j] * rinv * g[j]); } }
.LBB0_1268:
	s_or_b64 exec, exec, s[0:1]
	s_waitcnt vmcnt(11)
	v_lshlrev_b32_e32 v50, 16, v46
	v_lshlrev_b32_e32 v51, 16, v47
	v_and_b32_e32 v53, 0xffff0000, v47
	v_mul_f32_e32 v47, 0x3dd2d3e8, v50
	v_fma_f32 v47, -v47, v50, s33
	v_mul_f32_e32 v47, v47, v50
	v_exp_f32_e32 v47, v47
	v_and_b32_e32 v46, 0xffff0000, v46
	v_lshlrev_b32_e32 v54, 16, v48
	v_and_b32_e32 v55, 0xffff0000, v48
	v_add_f32_e32 v47, 1.0, v47
	v_rcp_f32_e32 v47, v47
	v_mul_f32_e32 v48, 0x3dd2d3e8, v53
	v_fma_f32 v48, -v48, v53, s33
	v_mul_f32_e32 v48, v48, v53
	v_mul_f32_e32 v52, v47, v50
	v_mul_f32_e32 v47, 0x3dd2d3e8, v46
	v_fma_f32 v47, -v47, v46, s33
	v_mul_f32_e32 v47, v47, v46
	v_exp_f32_e32 v47, v47
	v_exp_f32_e32 v48, v48
	v_lshlrev_b32_e32 v56, 16, v49
	v_and_b32_e32 v57, 0xffff0000, v49
	v_add_f32_e32 v47, 1.0, v47
	v_rcp_f32_e32 v47, v47
	v_add_f32_e32 v48, 1.0, v48
	v_rcp_f32_e32 v48, v48
	v_mul_f32_e32 v49, 0x3dd2d3e8, v54
	v_mul_f32_e32 v47, v47, v46
	v_mul_f32_e32 v46, 0x3dd2d3e8, v51
	v_fma_f32 v46, -v46, v51, s33
	v_mul_f32_e32 v46, v46, v51
	v_exp_f32_e32 v46, v46
	v_fma_f32 v49, -v49, v54, s33
	v_mul_f32_e32 v50, 0x3dd2d3e8, v55
	v_mul_f32_e32 v49, v49, v54
	v_add_f32_e32 v46, 1.0, v46
	v_rcp_f32_e32 v46, v46
	v_fma_f32 v50, -v50, v55, s33
	v_mul_f32_e32 v48, v48, v53
	v_exp_f32_e32 v49, v49
	v_mul_f32_e32 v46, v46, v51
	v_mul_f32_e32 v51, 0x3dd2d3e8, v56
	v_mul_f32_e32 v50, v50, v55
	v_fma_f32 v51, -v51, v56, s33
	v_mul_f32_e32 v53, 0x3dd2d3e8, v57
	v_exp_f32_e32 v50, v50
	v_mul_f32_e32 v51, v51, v56
	v_fma_f32 v53, -v53, v57, s33
	v_exp_f32_e32 v51, v51
	v_mul_f32_e32 v53, v53, v57
	v_exp_f32_e32 v53, v53
	v_add_f32_e32 v49, 1.0, v49
	v_rcp_f32_e32 v49, v49
	v_add_f32_e32 v50, 1.0, v50
	v_mul_f32_e32 v58, v47, v47
	v_rcp_f32_e32 v50, v50
	v_add_f32_e32 v51, 1.0, v51
	v_fmac_f32_e32 v58, v52, v52
	v_rcp_f32_e32 v51, v51
	v_add_f32_e32 v53, 1.0, v53
	v_fmac_f32_e32 v58, v46, v46
	v_rcp_f32_e32 v53, v53
	v_fmac_f32_e32 v58, v48, v48
	v_mul_f32_e32 v49, v49, v54
	v_fmac_f32_e32 v58, v49, v49
	v_mul_f32_e32 v50, v50, v55
	v_fmac_f32_e32 v58, v50, v50
	v_mul_f32_e32 v51, v51, v56
	v_fmac_f32_e32 v58, v51, v51
	v_mul_f32_e32 v53, v53, v57
	v_fmac_f32_e32 v58, v53, v53
	ds_bpermute_b32 v54, v68, v58
	s_waitcnt lgkmcnt(0)
	v_add_f32_e32 v54, v58, v54
	v_mov_b32_e32 v55, v54
	s_nop 1
	v_permlane16_swap_b32_e32 v55, v54
	s_waitcnt lgkmcnt(0)
	v_add_f32_e32 v54, v54, v55
	s_nop 1
	v_mov_b32_dpp v55, v54 row_ror:8 row_mask:0xf bank_mask:0xf
	s_waitcnt lgkmcnt(0)
	v_add_f32_e32 v54, v54, v55
	s_nop 1
	v_mov_b32_dpp v55, v54 row_shl:4 row_mask:0xf bank_mask:0x5
	v_mov_b32_dpp v55, v54 row_shr:4 row_mask:0xf bank_mask:0xa
	s_waitcnt lgkmcnt(0)
	v_add_f32_e32 v54, v54, v55
	s_nop 1
	v_mov_b32_dpp v55, v54 quad_perm:[2,3,0,1] row_mask:0xf bank_mask:0xf
	s_waitcnt lgkmcnt(0)
	v_add_f32_e32 v54, v54, v55
	s_nop 1
	v_mov_b32_dpp v55, v54 quad_perm:[1,0,3,2] row_mask:0xf bank_mask:0xf
	s_and_saveexec_b64 s[0:1], vcc
	s_cbranch_execz .LBB0_1270
	s_waitcnt lgkmcnt(0)
	v_add_f32_e32 v54, v54, v55
	v_fmamk_f32 v54, v54, 0x3b000000, v246
	s_mov_b32 s2, 0x800000
	v_cmp_gt_f32_e64 s[2:3], s2, v54
	v_mul_f32_e32 v55, 0x4b800000, v54
	s_nop 0
	v_cndmask_b32_e64 v54, v54, v55, s[2:3]
	v_rsq_f32_e32 v54, v54
	s_nop 0
	v_mul_f32_e32 v55, 0x45800000, v54
	v_cndmask_b32_e64 v74, v54, v55, s[2:3]
	global_load_dwordx4 v[54:57], v[62:63], off offset:16
	global_load_dwordx4 v[58:61], v[62:63], off
	v_mul_f32_e32 v46, v46, v74
	v_mul_f32_e32 v52, v52, v74
	v_mul_f32_e32 v47, v47, v74
	s_waitcnt vmcnt(0)
	v_mul_f32_e32 v46, v46, v60
	v_cvt_pk_bf16_f32 v46, v46, s0
	ds_write_b16 v67, v46 offset:35368
	v_mul_f32_e32 v46, v48, v74
	v_mul_f32_e32 v46, v46, v61
	v_cvt_pk_bf16_f32 v46, v46, s0
	ds_write_b16 v67, v46 offset:35640
	v_mul_f32_e32 v46, v49, v74
	v_mul_f32_e32 v46, v46, v54
	v_cvt_pk_bf16_f32 v46, v46, s0
	ds_write_b16 v67, v46 offset:35912
	v_mul_f32_e32 v46, v50, v74
	v_mul_f32_e32 v46, v46, v55
	v_cvt_pk_bf16_f32 v46, v46, s0
	ds_write_b16 v67, v46 offset:36184
	v_mul_f32_e32 v46, v51, v74
	v_mul_f32_e32 v46, v46, v56
	v_cvt_pk_bf16_f32 v46, v46, s0
	ds_write_b16 v67, v46 offset:36456
	v_mul_f32_e32 v46, v53, v74
	v_mul_f32_e32 v52, v52, v58
	v_mul_f32_e32 v47, v47, v59
	v_mul_f32_e32 v46, v46, v57
	v_cvt_pk_bf16_f32 v52, v52, s0
	v_cvt_pk_bf16_f32 v47, v47, s0
	v_cvt_pk_bf16_f32 v46, v46, s0
	ds_write_b16 v67, v52 offset:34824
	ds_write_b16 v67, v47 offset:35096
	ds_write_b16 v67, v46 offset:36728

; #define LAS __attribute__((address_space(3)))
; __device__ __forceinline__ void sgu_unit(const Params& p, int l, int un, LAS unsigned char* lds) {
;     ...
;     const int cc = un >> 2, h = un & 3; const int row0 = cc * 128;
;     LAS bf16_t* Wl = (LAS bf16_t*)lds;
;     LAS bf16_t* Vl = (LAS bf16_t*)(lds + 128 * 136 * 2);
;     const float* Wg = p.in[I_SGUW] + ((size_t)l * 4 + h) * 128 * 128;
;     f32x4 wq[8]; u32x4 vv[16];
; #pragma unroll
;     for (int i = 0; i < 8; ++i) wq[i] = *(const f32x4*)(Wg + (i * 512 + tid) * 4);
; #pragma unroll
;     for (int qi = 0; qi < 16; ++qi) vv[qi] = *(const u32x4*)(P + (size_t)(row0 + wave * 16 + qi) * INP + C_SGU_V + lane * 8);
; __global__ void __launch_bounds__(512, 2) fwd(Params p) {
;     ...
;             if (c < (l == 0 ? 72 : 64) || G != 256) pg8::gemm_phase(lds, pg8::Desc{512, 512, 512}, S, E);
;             else { const int un = (l == 0 ? 128 + (c - 72) : 160 + (c - 64)); if (un < (l == 0 ? B_SGU : 256)) sgu_unit(p, l, un, lds); }
.LBB0_1393:
	s_andn2_b64 vcc, exec, s[0:1]
	s_cbranch_vccnz .LBB0_1501
	v_readlane_b32 s0, v252, 5
	v_readlane_b32 s1, v252, 6
	s_lshl_b32 s4, s0, 9
	v_readlane_b32 s0, v252, 20
	v_readlane_b32 s1, v252, 21
	s_and_b64 s[0:1], s[0:1], exec
	s_cselect_b32 s0, 0x48, 64
	s_cmp_ge_i32 s92, s0
	v_readlane_b32 s12, v255, 40
	s_cselect_b64 s[2:3], -1, 0
	v_readlane_b32 s13, v255, 41
	s_and_b64 s[2:3], s[12:13], s[2:3]
	s_mov_b64 s[0:1], -1
	s_and_b64 vcc, exec, s[2:3]
	s_cbranch_vccz .LBB0_1430
	v_readlane_b32 s2, v252, 20
	v_readlane_b32 s3, v252, 21
	s_and_b64 s[0:1], s[2:3], exec
	s_cselect_b32 s0, 56, 0x60
	s_add_i32 s0, s0, s92
	s_and_b64 s[2:3], s[2:3], exec
	s_movk_i32 s1, 0x120
	s_cselect_b32 s1, s1, 0x100
	s_cmp_ge_u32 s0, s1
	s_cbranch_scc1 .LBB0_1429
	v_readlane_b32 s44, v251, 16
	s_lshl_b32 s12, s0, 5
	v_readlane_b32 s0, v253, 39
	v_readlane_b32 s48, v251, 20
	v_readlane_b32 s49, v251, 21
	s_or_b32 s40, s4, s0
	s_mov_b32 s41, s5
	v_readlane_b32 s50, v251, 22
	v_readlane_b32 s51, v251, 23
	v_readlane_b32 s52, v251, 24
	v_readlane_b32 s53, v251, 25
	v_readlane_b32 s54, v251, 26
	v_readlane_b32 s55, v251, 27
	s_mov_b64 s[16:17], s[48:49]
	s_lshl_b64 s[0:1], s[40:41], 9
	s_mov_b64 s[18:19], s[50:51]
	s_waitcnt vmcnt(0)
	v_mov_b32_e32 v64, v0
	s_add_u32 s2, s18, s0
	s_addc_u32 s3, s19, s1
	v_lshlrev_b32_e32 v2, 2, v64
	v_ashrrev_i32_e32 v3, 31, v2
	v_add_u32_e32 v62, 0x800, v2
	s_mov_b64 s[14:15], 0
	v_lshl_add_u64 v[4:5], v[2:3], 2, s[2:3]
	v_ashrrev_i32_e32 v63, 31, v62
	v_lshl_add_u64 v[6:7], v[62:63], 2, s[2:3]
	global_load_dwordx4 v[66:69], v[4:5], off
	global_load_dwordx4 v[70:73], v[6:7], off
	v_add_u32_e32 v102, 0x1000, v2
	v_ashrrev_i32_e32 v103, 31, v102
	v_add_u32_e32 v104, 0x1800, v2
	v_lshl_add_u64 v[4:5], v[102:103], 2, s[2:3]
	v_ashrrev_i32_e32 v105, 31, v104
	v_lshl_add_u64 v[6:7], v[104:105], 2, s[2:3]
	global_load_dwordx4 v[74:77], v[4:5], off
	global_load_dwordx4 v[78:81], v[6:7], off
	s_and_b32 s12, s12, 0x7fffff80
	s_lshl_b64 s[0:1], s[4:5], 2
	v_readlane_b32 s13, v253, 41
	v_add_u32_e32 v106, 0x2000, v2
	s_add_u32 s0, s13, s0
	v_readlane_b32 s13, v253, 42
	v_ashrrev_i32_e32 v107, 31, v106
	v_add_u32_e32 v108, 0x2800, v2
	s_addc_u32 s1, s13, s1
	v_lshl_add_u64 v[4:5], v[106:107], 2, s[2:3]
	v_ashrrev_i32_e32 v109, 31, v108
	s_add_u32 s36, s84, s14
	v_lshl_add_u64 v[6:7], v[108:109], 2, s[2:3]
	global_load_dwordx4 v[82:85], v[4:5], off
	global_load_dwordx4 v[86:89], v[6:7], off
	s_addc_u32 s37, s85, s15
	v_add_u32_e32 v110, 0x3000, v2
	v_add_u32_e32 v112, 0x3800, v2
	s_add_u32 s38, s36, 0x1f1b8000
	v_ashrrev_i32_e32 v111, 31, v110
	v_ashrrev_i32_e32 v113, 31, v112
	v_ashrrev_i32_e32 v103, 6, v64
	s_addc_u32 s39, s37, 0
	v_lshl_add_u64 v[4:5], v[110:111], 2, s[2:3]
	v_lshl_add_u64 v[2:3], v[112:113], 2, s[2:3]
	v_lshlrev_b32_e32 v65, 4, v103
	v_and_b32_e32 v8, 63, v64
	global_load_dwordx4 v[90:93], v[4:5], off
	global_load_dwordx4 v[94:97], v[2:3], off
	v_add_u32_e32 v9, s12, v65
	v_mov_b64_e32 v[2:3], s[38:39]
	s_movk_i32 s13, 0x1e00
	v_mad_i64_i32 v[4:5], s[2:3], v9, s13, v[2:3]
	v_lshlrev_b32_e32 v206, 4, v8
	v_or_b32_e32 v6, 1, v9
	v_lshl_add_u64 v[4:5], v[4:5], 0, v[206:207]
	v_mad_i64_i32 v[6:7], s[2:3], v6, s13, v[2:3]
	v_lshl_add_u64 v[6:7], v[6:7], 0, v[206:207]
	global_load_dwordx4 v[98:101], v[4:5], off offset:1024
	global_load_dwordx4 v[58:61], v[6:7], off offset:1024
	v_or_b32_e32 v4, 2, v9
	v_or_b32_e32 v6, 3, v9
	v_mad_i64_i32 v[4:5], s[2:3], v4, s13, v[2:3]
	v_mad_i64_i32 v[6:7], s[2:3], v6, s13, v[2:3]
	v_lshl_add_u64 v[4:5], v[4:5], 0, v[206:207]
	v_lshl_add_u64 v[6:7], v[6:7], 0, v[206:207]
	global_load_dwordx4 v[54:57], v[4:5], off offset:1024
	global_load_dwordx4 v[50:53], v[6:7], off offset:1024
	v_or_b32_e32 v4, 4, v9
	v_or_b32_e32 v6, 5, v9
	v_mad_i64_i32 v[4:5], s[2:3], v4, s13, v[2:3]
	v_mad_i64_i32 v[6:7], s[2:3], v6, s13, v[2:3]
	v_lshl_add_u64 v[4:5], v[4:5], 0, v[206:207]
	v_lshl_add_u64 v[6:7], v[6:7], 0, v[206:207]
	global_load_dwordx4 v[46:49], v[4:5], off offset:1024
	global_load_dwordx4 v[42:45], v[6:7], off offset:1024
	v_or_b32_e32 v4, 6, v9
	v_or_b32_e32 v6, 7, v9
	v_mad_i64_i32 v[4:5], s[2:3], v4, s13, v[2:3]
	v_mad_i64_i32 v[6:7], s[2:3], v6, s13, v[2:3]
	v_lshl_add_u64 v[4:5], v[4:5], 0, v[206:207]
	v_lshl_add_u64 v[6:7], v[6:7], 0, v[206:207]
	global_load_dwordx4 v[38:41], v[4:5], off offset:1024
	global_load_dwordx4 v[34:37], v[6:7], off offset:1024
	v_or_b32_e32 v4, 8, v9
	v_or_b32_e32 v6, 9, v9
	v_mad_i64_i32 v[4:5], s[2:3], v4, s13, v[2:3]
	v_mad_i64_i32 v[6:7], s[2:3], v6, s13, v[2:3]
	v_lshl_add_u64 v[4:5], v[4:5], 0, v[206:207]
	v_lshl_add_u64 v[6:7], v[6:7], 0, v[206:207]
	global_load_dwordx4 v[30:33], v[4:5], off offset:1024
	global_load_dwordx4 v[26:29], v[6:7], off offset:1024
	v_or_b32_e32 v4, 10, v9
	v_or_b32_e32 v6, 11, v9
	v_mad_i64_i32 v[4:5], s[2:3], v4, s13, v[2:3]
	v_mad_i64_i32 v[6:7], s[2:3], v6, s13, v[2:3]
	v_lshl_add_u64 v[4:5], v[4:5], 0, v[206:207]
	v_lshl_add_u64 v[6:7], v[6:7], 0, v[206:207]
	global_load_dwordx4 v[22:25], v[4:5], off offset:1024
	global_load_dwordx4 v[18:21], v[6:7], off offset:1024
	v_or_b32_e32 v4, 12, v9
	v_or_b32_e32 v6, 13, v9
	v_mad_i64_i32 v[4:5], s[2:3], v4, s13, v[2:3]
	v_mad_i64_i32 v[6:7], s[2:3], v6, s13, v[2:3]
	v_lshl_add_u64 v[4:5], v[4:5], 0, v[206:207]
	v_lshl_add_u64 v[6:7], v[6:7], 0, v[206:207]
	v_lshlrev_b32_e32 v105, 3, v64
	global_load_dwordx4 v[14:17], v[4:5], off offset:1024
	global_load_dwordx4 v[10:13], v[6:7], off offset:1024
	v_or_b32_e32 v4, 14, v9
	v_or_b32_e32 v6, 15, v9
	v_and_b32_e32 v63, 0xf8, v105
	v_mad_i64_i32 v[4:5], s[2:3], v4, s13, v[2:3]
	v_mad_i64_i32 v[2:3], s[2:3], v6, s13, v[2:3]
	v_add_u32_e32 v114, 0, v63
	v_bfe_i32 v63, v64, 5, 25
	s_movk_i32 s13, 0x110
	v_lshl_add_u64 v[4:5], v[4:5], 0, v[206:207]
	v_lshl_add_u64 v[2:3], v[2:3], 0, v[206:207]
	s_waitcnt vmcnt(21)
; #define LAS __attribute__((address_space(3)))
; __device__ __forceinline__ unsigned cvt_pk_bf16(float lo, float hi) { const f32x2 v = {lo, hi}; const bf16x2_t b = __builtin_convertvector(v, bf16x2_t); return __builtin_bit_cast(unsigned, b); }
; __device__ __forceinline__ float bflo(unsigned w) { return __uint_as_float(w << 16); }
; __device__ __forceinline__ float bfhi(unsigned w) { return __uint_as_float(w & 0xffff0000u); }
; __device__ __forceinline__ float wave_sum(float v) {
; #pragma unroll
;     for (int o = 32; o >= 1; o >>= 1) v += __shfl_xor(v, o);
;     return v;
; }
; __device__ __forceinline__ void sgu_unit(const Params& p, int l, int un, LAS unsigned char* lds) {
;     ...
;     for (int i = 0; i < 8; ++i) { const int e4 = (i * 512 + tid) * 4, r = e4 >> 7, c = e4 & 127; const f32x4 v = wq[i];
;         u32x2 w; w.x = cvt_pk_bf16(v[0], v[1]); w.y = cvt_pk_bf16(v[2], v[3]); *(LAS u32x2*)(Wl + r * 136 + c) = w; }
; #pragma unroll
;     for (int qi = 0; qi < 16; ++qi) { const int q = wave * 16 + qi;
;         const u32x4 v = vv[qi]; float f[8] = {bflo(v.x), bfhi(v.x), bflo(v.y), bfhi(v.y), bflo(v.z), bfhi(v.z), bflo(v.w), bfhi(v.w)}; float ss = 0.f;
; #pragma unroll
;         for (int j = 0; j < 8; ++j) { f[j] = gelu_tanh(f[j]); ss += f[j] * f[j]; }
;         ss = wave_sum(ss); const float rinv = rsqrtf(ss * (1.0f / 512.0f) + EPS);
	v_cvt_pk_bf16_f32 v66, v66, v67
	v_cvt_pk_bf16_f32 v67, v68, v69
	v_mad_u64_u32 v[68:69], s[2:3], v63, s13, v[114:115]
	global_load_dwordx4 v[6:9], v[4:5], off offset:1024
	s_nop 0
	global_load_dwordx4 v[2:5], v[2:3], off offset:1024
	ds_write_b64 v68, v[66:67]
	v_ashrrev_i32_e32 v66, 7, v62
	s_waitcnt vmcnt(22)
	v_cvt_pk_bf16_f32 v62, v70, v71
	v_cvt_pk_bf16_f32 v63, v72, v73
	v_mad_u64_u32 v[66:67], s[2:3], v66, s13, v[114:115]
	ds_write_b64 v66, v[62:63]
	v_ashrrev_i32_e32 v66, 7, v102
	s_waitcnt vmcnt(21)
	v_cvt_pk_bf16_f32 v62, v74, v75
	v_cvt_pk_bf16_f32 v63, v76, v77
	v_mad_u64_u32 v[66:67], s[2:3], v66, s13, v[114:115]
	ds_write_b64 v66, v[62:63]
	v_ashrrev_i32_e32 v66, 7, v104
	s_waitcnt vmcnt(20)
	v_cvt_pk_bf16_f32 v62, v78, v79
	v_cvt_pk_bf16_f32 v63, v80, v81
	v_mad_u64_u32 v[66:67], s[2:3], v66, s13, v[114:115]
	ds_write_b64 v66, v[62:63]
	v_ashrrev_i32_e32 v66, 7, v106
	s_waitcnt vmcnt(19)
	v_cvt_pk_bf16_f32 v62, v82, v83
	v_cvt_pk_bf16_f32 v63, v84, v85
	v_mad_u64_u32 v[66:67], s[2:3], v66, s13, v[114:115]
	ds_write_b64 v66, v[62:63]
	v_ashrrev_i32_e32 v66, 7, v108
	s_waitcnt vmcnt(18)
	v_cvt_pk_bf16_f32 v62, v86, v87
	v_cvt_pk_bf16_f32 v63, v88, v89
	v_mad_u64_u32 v[66:67], s[2:3], v66, s13, v[114:115]
	ds_write_b64 v66, v[62:63]
	v_ashrrev_i32_e32 v66, 7, v110
	s_waitcnt vmcnt(17)
	v_cvt_pk_bf16_f32 v62, v90, v91
	v_cvt_pk_bf16_f32 v63, v92, v93
	v_mad_u64_u32 v[66:67], s[2:3], v66, s13, v[114:115]
	ds_write_b64 v66, v[62:63]
	v_ashrrev_i32_e32 v66, 7, v112
	v_mad_u64_u32 v[66:67], s[2:3], v66, s13, v[114:115]
	s_waitcnt vmcnt(15)
	v_and_b32_e32 v67, 0xffff0000, v98
	v_mul_f32_e32 v73, 0x3dd2d3e8, v67
	v_fma_f32 v73, -v73, v67, s33
	v_mul_f32_e32 v73, v73, v67
	v_exp_f32_e32 v73, v73
	v_cvt_pk_bf16_f32 v62, v94, v95
	v_cvt_pk_bf16_f32 v63, v96, v97
	ds_write_b64 v66, v[62:63]
	v_lshlrev_b32_e32 v66, 16, v98
	v_add_f32_e32 v73, 1.0, v73
	v_mul_f32_e32 v72, 0x3dd2d3e8, v66
	v_rcp_f32_e32 v73, v73
	v_fma_f32 v72, -v72, v66, s33
	v_mul_f32_e32 v72, v72, v66
	v_lshlrev_b32_e32 v69, 16, v99
	v_exp_f32_e32 v72, v72
	v_mul_f32_e32 v79, v73, v67
	v_mul_f32_e32 v67, 0x3dd2d3e8, v69
	v_fma_f32 v67, -v67, v69, s33
	v_mul_f32_e32 v67, v67, v69
	v_add_f32_e32 v72, 1.0, v72
	v_exp_f32_e32 v67, v67
	v_rcp_f32_e32 v72, v72
	v_lshlrev_b32_e32 v71, 16, v100
	v_and_b32_e32 v70, 0xffff0000, v99
	v_add_f32_e32 v67, 1.0, v67
	v_mul_f32_e32 v73, 0x3dd2d3e8, v71
	v_mul_f32_e32 v81, v72, v66
	v_mul_f32_e32 v72, 0x3dd2d3e8, v70
	v_rcp_f32_e32 v67, v67
	v_fma_f32 v73, -v73, v71, s33
	v_fma_f32 v72, -v72, v70, s33
	v_mul_f32_e32 v73, v73, v71
	v_mul_f32_e32 v72, v72, v70
	v_exp_f32_e32 v73, v73
	v_and_b32_e32 v74, 0xffff0000, v100
	v_exp_f32_e32 v72, v72
	v_mul_f32_e32 v80, v67, v69
	v_mul_f32_e32 v69, 0x3dd2d3e8, v74
	v_fma_f32 v69, -v69, v74, s33
	v_add_f32_e32 v67, 1.0, v73
	v_mul_f32_e32 v69, v69, v74
	v_add_f32_e32 v72, 1.0, v72
	v_rcp_f32_e32 v67, v67
	v_exp_f32_e32 v69, v69
	v_rcp_f32_e32 v72, v72
	v_lshlrev_b32_e32 v75, 16, v101
	v_and_b32_e32 v82, 0xffff0000, v101
	v_mul_f32_e32 v76, v67, v71
	v_add_f32_e32 v67, 1.0, v69
	v_mul_f32_e32 v69, 0x3dd2d3e8, v75
	v_mul_f32_e32 v78, v72, v70
	v_fma_f32 v69, -v69, v75, s33
	v_mul_f32_e32 v70, 0x3dd2d3e8, v82
	v_mul_f32_e32 v69, v69, v75
	v_fma_f32 v70, -v70, v82, s33
	v_rcp_f32_e32 v67, v67
	v_exp_f32_e32 v69, v69
	v_mul_f32_e32 v70, v70, v82
	v_exp_f32_e32 v70, v70
	v_mul_f32_e32 v66, v79, v79
	v_mul_f32_e32 v77, v67, v74
	v_add_f32_e32 v67, 1.0, v69
	v_fmac_f32_e32 v66, v81, v81
	v_rcp_f32_e32 v67, v67
	v_add_f32_e32 v69, 1.0, v70
	v_fmac_f32_e32 v66, v80, v80
	v_rcp_f32_e32 v69, v69
	v_and_b32_e32 v62, 64, v249
	v_fmac_f32_e32 v66, v78, v78
	v_add_u32_e32 v62, 64, v62
	v_xor_b32_e32 v63, 32, v249
	v_fmac_f32_e32 v66, v76, v76
	v_cmp_lt_i32_e32 vcc, v63, v62
	v_fmac_f32_e32 v66, v77, v77
	v_mul_f32_e32 v75, v67, v75
	v_cndmask_b32_e32 v63, v249, v63, vcc
	v_fmac_f32_e32 v66, v75, v75
	v_mul_f32_e32 v74, v69, v82
	v_lshlrev_b32_e32 v68, 2, v63
	v_fmac_f32_e32 v66, v74, v74
	v_mov_b32_e32 v67, v66
	s_nop 1
	v_permlane32_swap_b32_e32 v67, v66
	v_xor_b32_e32 v63, 16, v249
	v_cmp_lt_i32_e32 vcc, v63, v62
	v_and_b32_e32 v84, 0x78, v105
	v_readlane_b32 s2, v253, 40
	v_cndmask_b32_e32 v63, v249, v63, vcc
	v_lshlrev_b32_e32 v69, 2, v63
	s_waitcnt lgkmcnt(0)
	v_add_f32_e32 v66, v66, v67
	v_mov_b32_e32 v67, v66
	s_nop 1
	v_permlane16_swap_b32_e32 v67, v66
	v_xor_b32_e32 v63, 8, v249
	v_cmp_lt_i32_e32 vcc, v63, v62
	v_lshlrev_b32_e32 v206, 2, v84
	v_readlane_b32 s45, v251, 17
	v_cndmask_b32_e32 v63, v249, v63, vcc
	v_lshlrev_b32_e32 v70, 2, v63
	s_waitcnt lgkmcnt(0)
	v_add_f32_e32 v66, v66, v67
	s_nop 1
	v_mov_b32_dpp v67, v66 row_ror:8 row_mask:0xf bank_mask:0xf
	v_xor_b32_e32 v63, 4, v249
	v_cmp_lt_i32_e32 vcc, v63, v62
	v_readlane_b32 s46, v251, 18
	v_readlane_b32 s47, v251, 19
	v_cndmask_b32_e32 v63, v249, v63, vcc
	v_lshlrev_b32_e32 v71, 2, v63
	s_waitcnt lgkmcnt(0)
	v_add_f32_e32 v66, v66, v67
	v_xor_b32_e32 v63, 2, v249
	s_nop 1
	v_mov_b32_dpp v67, v66 row_shl:4 row_mask:0xf bank_mask:0x5
	v_mov_b32_dpp v67, v66 row_shr:4 row_mask:0xf bank_mask:0xa
	v_cmp_lt_i32_e32 vcc, v63, v62
	v_readlane_b32 s56, v251, 28
	v_readlane_b32 s57, v251, 29
	v_cndmask_b32_e32 v63, v249, v63, vcc
	v_lshlrev_b32_e32 v72, 2, v63
	v_xor_b32_e32 v63, 1, v249
	v_cmp_lt_i32_e32 vcc, v63, v62
	v_readlane_b32 s58, v251, 30
	v_readlane_b32 s59, v251, 31
	v_cndmask_b32_e32 v62, v249, v63, vcc
	s_waitcnt lgkmcnt(0)
	v_add_f32_e32 v63, v66, v67
	s_nop 1
	v_mov_b32_dpp v67, v63 quad_perm:[2,3,0,1] row_mask:0xf bank_mask:0xf
	v_lshlrev_b32_e32 v73, 2, v62
	v_bfe_u32 v66, v64, 4, 2
	v_cmp_eq_u32_e32 vcc, s2, v66
	s_mov_b64 s[20:21], s[52:53]
	s_waitcnt lgkmcnt(0)
	v_add_f32_e32 v82, v63, v67
	s_nop 1
	v_mov_b32_dpp v83, v82 quad_perm:[1,0,3,2] row_mask:0xf bank_mask:0xf
	v_lshl_add_u32 v67, v103, 5, 0
	v_lshl_add_u64 v[62:63], s[0:1], 0, v[206:207]
	v_mad_u32_u24 v67, v84, s13, v67
	s_mov_b64 s[22:23], s[54:55]
	s_and_saveexec_b64 s[0:1], vcc
	s_cbranch_execz .LBB0_1398
; __device__ __forceinline__ unsigned short f2bf(float f) { return (unsigned short)(cvt_pk_bf16(f, 0.f) & 0xffffu); }
; __device__ __forceinline__ void sgu_unit(const Params& p, int l, int un, LAS unsigned char* lds) {
;     ...
;         if ((lane >> 4) == h) { const int c0 = (lane & 15) * 8; const float* g = p.in[I_SGUNG] + l * 512 + h * 128 + c0;
; #pragma unroll
;             for (int j = 0; j < 8; ++j) Vl[(c0 + j) * 136 + q] = f2bf(f[j] * rinv * g[j]); } }
	s_waitcnt lgkmcnt(0)
	v_add_f32_e32 v82, v82, v83
	v_fmamk_f32 v82, v82, 0x3b000000, v246
	s_mov_b32 s2, 0x800000
	v_cmp_gt_f32_e64 s[2:3], s2, v82
	v_mul_f32_e32 v83, 0x4b800000, v82
	s_nop 0
	v_cndmask_b32_e64 v82, v82, v83, s[2:3]
	v_rsq_f32_e32 v82, v82
	s_nop 0
	v_mul_f32_e32 v83, 0x45800000, v82
	v_cndmask_b32_e64 v90, v82, v83, s[2:3]
	global_load_dwordx4 v[82:85], v[62:63], off offset:16
	global_load_dwordx4 v[86:89], v[62:63], off
	v_mul_f32_e32 v79, v79, v90
	v_mul_f32_e32 v76, v76, v90
	v_mul_f32_e32 v81, v81, v90
	v_mul_f32_e32 v78, v78, v90
	v_mul_f32_e32 v75, v75, v90
	v_mul_f32_e32 v74, v74, v90
	s_waitcnt vmcnt(1)
	v_mul_f32_e32 v76, v76, v82
	s_waitcnt vmcnt(0)
	v_mul_f32_e32 v79, v79, v87
	v_cvt_pk_bf16_f32 v79, v79, s0
	v_cvt_pk_bf16_f32 v76, v76, s0
	ds_write_b16 v67, v79 offset:35088
	v_mul_f32_e32 v79, v80, v90
	ds_write_b16 v67, v76 offset:35904
	v_mul_f32_e32 v76, v77, v90
	v_mul_f32_e32 v81, v81, v86
	v_mul_f32_e32 v79, v79, v88
	v_mul_f32_e32 v78, v78, v89
	v_mul_f32_e32 v76, v76, v83
	v_mul_f32_e32 v75, v75, v84
	v_mul_f32_e32 v74, v74, v85
	v_cvt_pk_bf16_f32 v81, v81, s0
	v_cvt_pk_bf16_f32 v79, v79, s0
	v_cvt_pk_bf16_f32 v78, v78, s0
	v_cvt_pk_bf16_f32 v76, v76, s0
	v_cvt_pk_bf16_f32 v75, v75, s0
	v_cvt_pk_bf16_f32 v74, v74, s0
	ds_write_b16 v67, v81 offset:34816
	ds_write_b16 v67, v79 offset:35360
	ds_write_b16 v67, v78 offset:35632
	ds_write_b16 v67, v76 offset:36176
	ds_write_b16 v67, v75 offset:36448
	ds_write_b16 v67, v74 offset:36720

; __device__ __forceinline__ unsigned cvt_pk_bf16(float lo, float hi) { const f32x2 v = {lo, hi}; const bf16x2_t b = __builtin_convertvector(v, bf16x2_t); return __builtin_bit_cast(unsigned, b); }
; __device__ __forceinline__ float bflo(unsigned w) { return __uint_as_float(w << 16); }
; __device__ __forceinline__ void ph_norm2_router(const Params& p, int l, LAS unsigned char* lds) {
;     ...
;     for (int it = blockIdx.x; it < nrows / 8; it += gridDim.x) {
;         const int row = it * 8 + wave; const int rr = row < NLAT ? (row >> 11) : 4;
;         const float* m = mod + (size_t)rr * 12288 + lane * 8; const float* gp = n2g + lane * 8;
;         u32x4 xv[4];
; #pragma unroll
;         for (int j = 0; j < 4; ++j) xv[j] = xn[j];
;         { const int itn = it + (int)gridDim.x; if (itn < nrows / 8) { const bf16_t* xr = (const bf16_t*)(ws + WS_XB) + (size_t)(itn * 8 + wave) * DM + lane * 8;
; #pragma unroll
;             for (int j = 0; j < 4; ++j) xn[j] = *(const u32x4*)(xr + j * 512); } }
;         float x[4][8]; float ss = 0.f;
; #pragma unroll
;         for (int j = 0; j < 4; ++j) { x[j][0] = bflo(xv[j].x); x[j][1] = bfhi(xv[j].x); x[j][2] = bflo(xv[j].y); x[j][3] = bfhi(xv[j].y); x[j][4] = bflo(xv[j].z); x[j][5] = bfhi(xv[j].z); x[j][6] = bflo(xv[j].w); x[j][7] = bfhi(xv[j].w);
; #pragma unroll
;             for (int i = 0; i < 8; ++i) ss += x[j][i] * x[j][i]; }
;         ss = wave_sum(ss); const float rinv = rsqrtf(ss * (1.0f / DM) + EPS);
;         bf16_t* orow = (bf16_t*)(ws + WS_H) + (size_t)row * DM + lane * 8;
;         f32x4 lg[4];
; #pragma unroll
;         for (int e4 = 0; e4 < 4; ++e4) lg[e4] = (f32x4){0.f, 0.f, 0.f, 0.f};
;         f32x4 mv[2][6];
;     ...
;         H_MLOAD(mv[0], 0);
; #pragma unroll
;         for (int j = 0; j < 4; ++j) {
;             if (j < 3) H_MLOAD(mv[(j + 1) & 1], j + 1);
;             const f32x4 ga = mv[j & 1][0], gb = mv[j & 1][1], sa = mv[j & 1][2], sb = mv[j & 1][3], ha = mv[j & 1][4], hb = mv[j & 1][5];
;             float y[8];
; #pragma unroll
;             for (int i = 0; i < 8; ++i) y[i] = x[j][i] * rinv * (i < 4 ? ga[i] : gb[i - 4]) * (1.0f + (i < 4 ? sa[i] : sb[i - 4])) + (i < 4 ? ha[i] : hb[i - 4]);
;             u32x4 h; h.x = cvt_pk_bf16(y[0], y[1]); h.y = cvt_pk_bf16(y[2], y[3]); h.z = cvt_pk_bf16(y[4], y[5]); h.w = cvt_pk_bf16(y[6], y[7]);
;             *(u32x4*)(orow + j * 512) = h;
.LBB0_1760:
	v_readlane_b32 s0, v253, 61
	global_load_dwordx4 v[46:49], v[68:69], off offset:16
	global_load_dwordx4 v[54:57], v[68:69], off
	v_add_u32_e32 v80, s0, v93
	v_min_i32_e32 v18, 0x2000, v80
	v_ashrrev_i32_e32 v18, 11, v18
	v_mul_hi_i32_i24_e32 v19, 0xc000, v18
	v_mul_i32_i24_e32 v18, 0xc000, v18
	v_lshl_add_u64 v[58:59], v[66:67], 0, v[18:19]
	s_mov_b64 s[0:1], 0x8000
	v_lshl_add_u64 v[26:27], v[58:59], 0, s[0:1]
	s_mov_b32 s0, 0x8000
	v_add_co_u32_e32 v28, vcc, s0, v58
	s_mov_b32 s0, 0x9000
	s_nop 0
	v_addc_co_u32_e32 v29, vcc, 0, v59, vcc
	v_add_co_u32_e32 v94, vcc, s0, v58
	s_mov_b64 s[0:1], 0x6000
	s_nop 0
	v_addc_co_u32_e32 v95, vcc, 0, v59, vcc
	v_lshl_add_u64 v[30:31], v[58:59], 0, s[0:1]
	s_movk_i32 s0, 0x6000
	v_add_co_u32_e32 v32, vcc, s0, v58
	s_movk_i32 s0, 0x7000
	s_nop 0
	v_addc_co_u32_e32 v33, vcc, 0, v59, vcc
	v_add_co_u32_e32 v96, vcc, s0, v58
	v_lshlrev_b32_e32 v236, 16, v50
	s_nop 0
	v_addc_co_u32_e32 v97, vcc, 0, v59, vcc
	global_load_dwordx4 v[60:63], v[94:95], off offset:-4096
	global_load_dwordx4 v[194:197], v[96:97], off offset:-4096
	s_waitcnt lgkmcnt(0)
	global_load_dwordx4 v[18:21], v[68:69], off offset:2064
	global_load_dwordx4 v[22:25], v[68:69], off offset:2048
	global_load_dwordx4 v[106:109], v[26:27], off offset:16
	global_load_dwordx4 v[118:121], v[28:29], off offset:2048
	v_and_b32_e32 v237, 0xffff0000, v50
	v_lshlrev_b32_e32 v214, 16, v51
	v_and_b32_e32 v215, 0xffff0000, v51
	v_pk_mul_f32 v[208:209], v[236:237], v[236:237]
	s_mov_b64 s[0:1], 0x8800
	v_pk_mul_f32 v[116:117], v[214:215], v[214:215]
	v_add_f32_e32 v81, v208, v209
	v_lshl_add_u64 v[64:65], v[58:59], 0, s[0:1]
	s_mov_b64 s[0:1], 0x6800
	v_lshlrev_b32_e32 v212, 16, v52
	v_and_b32_e32 v213, 0xffff0000, v52
	v_add_f32_e32 v81, v116, v81
	v_lshl_add_u64 v[26:27], v[58:59], 0, s[0:1]
	v_pk_mul_f32 v[114:115], v[212:213], v[212:213]
	v_add_f32_e32 v81, v117, v81
	global_load_dwordx4 v[198:201], v[30:31], off offset:16
	s_nop 0
	global_load_dwordx4 v[30:33], v[32:33], off offset:2048
	s_nop 0
	global_load_dwordx4 v[202:205], v[64:65], off offset:16
	s_nop 0
	global_load_dwordx4 v[26:29], v[26:27], off offset:16
	v_lshlrev_b32_e32 v64, 16, v53
	v_and_b32_e32 v65, 0xffff0000, v53
	v_add_f32_e32 v81, v114, v81
	v_pk_mul_f32 v[90:91], v[64:65], v[64:65]
	v_add_f32_e32 v81, v115, v81
	v_lshlrev_b32_e32 v112, 16, v42
	v_and_b32_e32 v113, 0xffff0000, v42
	v_add_f32_e32 v81, v90, v81
	v_lshlrev_b32_e32 v110, 16, v43
	v_and_b32_e32 v111, 0xffff0000, v43
	v_pk_mul_f32 v[42:43], v[112:113], v[112:113]
	v_add_f32_e32 v81, v91, v81
	v_add_f32_e32 v42, v42, v81
	v_pk_mul_f32 v[216:217], v[110:111], v[110:111]
	v_add_f32_e32 v42, v43, v42
	v_lshlrev_b32_e32 v52, 16, v44
	v_and_b32_e32 v53, 0xffff0000, v44
	v_add_f32_e32 v42, v216, v42
	v_lshlrev_b32_e32 v50, 16, v45
	v_and_b32_e32 v51, 0xffff0000, v45
	v_pk_mul_f32 v[44:45], v[52:53], v[52:53]
	v_add_f32_e32 v42, v217, v42
	v_add_f32_e32 v42, v44, v42
	v_pk_mul_f32 v[210:211], v[50:51], v[50:51]
	v_add_f32_e32 v42, v45, v42
	v_lshlrev_b32_e32 v104, 16, v38
	v_and_b32_e32 v105, 0xffff0000, v38
	v_add_f32_e32 v42, v210, v42
	v_lshlrev_b32_e32 v102, 16, v39
	v_and_b32_e32 v103, 0xffff0000, v39
	v_pk_mul_f32 v[38:39], v[104:105], v[104:105]
	v_add_f32_e32 v42, v211, v42
	v_add_f32_e32 v38, v38, v42
	v_pk_mul_f32 v[220:221], v[102:103], v[102:103]
	v_add_f32_e32 v38, v39, v38
	v_lshlrev_b32_e32 v100, 16, v40
	v_and_b32_e32 v101, 0xffff0000, v40
	v_add_f32_e32 v38, v220, v38
	v_lshlrev_b32_e32 v98, 16, v41
	v_and_b32_e32 v99, 0xffff0000, v41
	v_pk_mul_f32 v[40:41], v[100:101], v[100:101]
	v_add_f32_e32 v38, v221, v38
	v_add_f32_e32 v38, v40, v38
	v_pk_mul_f32 v[218:219], v[98:99], v[98:99]
	v_add_f32_e32 v38, v41, v38
	v_lshlrev_b32_e32 v88, 16, v34
	v_and_b32_e32 v89, 0xffff0000, v34
	v_add_f32_e32 v38, v218, v38
	v_lshlrev_b32_e32 v86, 16, v35
	v_and_b32_e32 v87, 0xffff0000, v35
	v_pk_mul_f32 v[34:35], v[88:89], v[88:89]
	v_add_f32_e32 v38, v219, v38
	v_add_f32_e32 v34, v34, v38
	v_pk_mul_f32 v[224:225], v[86:87], v[86:87]
	v_add_f32_e32 v34, v35, v34
	v_lshlrev_b32_e32 v84, 16, v36
	v_and_b32_e32 v85, 0xffff0000, v36
	v_add_f32_e32 v34, v224, v34
	v_lshlrev_b32_e32 v82, 16, v37
	v_and_b32_e32 v83, 0xffff0000, v37
	v_pk_mul_f32 v[36:37], v[84:85], v[84:85]
	v_add_f32_e32 v34, v225, v34
	v_add_f32_e32 v34, v36, v34
	v_pk_mul_f32 v[222:223], v[82:83], v[82:83]
	v_add_f32_e32 v34, v37, v34
	v_add_f32_e32 v34, v222, v34
	v_add_f32_e32 v34, v223, v34
	v_mov_b32_e32 v35, v34
	s_nop 1
	v_permlane32_swap_b32_e32 v35, v34
	v_ashrrev_i32_e32 v81, 31, v80
	s_mov_b64 s[0:1], 0x9000
	s_waitcnt vmcnt(5)
	v_pk_add_f32 v[240:241], v[108:109], 1.0 op_sel_hi:[1,0]
	v_pk_add_f32 v[238:239], v[60:61], 1.0 op_sel_hi:[1,0]
	s_waitcnt lgkmcnt(0)
	v_add_f32_e32 v36, v34, v35
	v_mov_b32_e32 v37, v36
	s_nop 1
	v_permlane16_swap_b32_e32 v37, v36
	v_lshlrev_b64 v[34:35], 12, v[80:81]
	v_lshl_add_u64 v[90:91], v[72:73], 0, v[34:35]
	v_pk_add_f32 v[34:35], v[106:107], 1.0 op_sel_hi:[1,0]
	s_waitcnt vmcnt(4)
	v_pk_add_f32 v[116:117], v[120:121], 1.0 op_sel_hi:[1,0]
	s_waitcnt lgkmcnt(0)
	v_add_f32_e32 v38, v36, v37
	s_nop 1
	v_mov_b32_dpp v39, v38 row_ror:8 row_mask:0xf bank_mask:0xf
	v_pk_add_f32 v[36:37], v[62:63], 1.0 op_sel_hi:[1,0]
	ds_read_b128 v[42:45], v128
	ds_read_b128 v[60:63], v128 offset:4096
	ds_read_b128 v[208:211], v128 offset:32768
	ds_read_b128 v[216:219], v128 offset:36864
	ds_read_b128 v[220:223], v129
	ds_read_b128 v[224:227], v130
	ds_read_b128 v[228:231], v131
	ds_read_b128 v[232:235], v132
	s_waitcnt vmcnt(1)
	v_pk_add_f32 v[114:115], v[202:203], 1.0 op_sel_hi:[1,0]
	s_waitcnt lgkmcnt(8)
; #define LAS __attribute__((address_space(3)))
; __device__ __forceinline__ unsigned cvt_pk_bf16(float lo, float hi) { const f32x2 v = {lo, hi}; const bf16x2_t b = __builtin_convertvector(v, bf16x2_t); return __builtin_bit_cast(unsigned, b); }
; #define H_MLOAD(dst, jj) do { dst[0] = *(const f32x4*)(gp + (jj) * 512); dst[1] = *(const f32x4*)(gp + (jj) * 512 + 4); dst[2] = *(const f32x4*)(m + 4 * DM + (jj) * 512); dst[3] = *(const f32x4*)(m + 4 * DM + (jj) * 512 + 4); \
;             dst[4] = *(const f32x4*)(m + 3 * DM + (jj) * 512); dst[5] = *(const f32x4*)(m + 3 * DM + (jj) * 512 + 4); } while (0)
; __device__ __forceinline__ void ph_norm2_router(const Params& p, int l, LAS unsigned char* lds) {
;     ...
;         ss = wave_sum(ss); const float rinv = rsqrtf(ss * (1.0f / DM) + EPS);
;         bf16_t* orow = (bf16_t*)(ws + WS_H) + (size_t)row * DM + lane * 8;
;         f32x4 lg[4];
; #pragma unroll
;         for (int e4 = 0; e4 < 4; ++e4) lg[e4] = (f32x4){0.f, 0.f, 0.f, 0.f};
;         f32x4 mv[2][6];
;     ...
;         H_MLOAD(mv[0], 0);
; #pragma unroll
;         for (int j = 0; j < 4; ++j) {
;             if (j < 3) H_MLOAD(mv[(j + 1) & 1], j + 1);
;             const f32x4 ga = mv[j & 1][0], gb = mv[j & 1][1], sa = mv[j & 1][2], sb = mv[j & 1][3], ha = mv[j & 1][4], hb = mv[j & 1][5];
;             float y[8];
; #pragma unroll
;             for (int i = 0; i < 8; ++i) y[i] = x[j][i] * rinv * (i < 4 ? ga[i] : gb[i - 4]) * (1.0f + (i < 4 ? sa[i] : sb[i - 4])) + (i < 4 ? ha[i] : hb[i - 4]);
;             u32x4 h; h.x = cvt_pk_bf16(y[0], y[1]); h.y = cvt_pk_bf16(y[2], y[3]); h.z = cvt_pk_bf16(y[4], y[5]); h.w = cvt_pk_bf16(y[6], y[7]);
;             *(u32x4*)(orow + j * 512) = h;
; #pragma unroll
;             for (int i2 = 0; i2 < 8; i2 += 2) {
; #pragma unroll
;                 for (int e4 = 0; e4 < 4; ++e4) { const f32x4 w0 = *(const LAS f32x4*)(lds + (size_t)(((e4 * 8 + i2) * 256 + j * 64 + lane) * 16)); const f32x4 w1 = *(const LAS f32x4*)(lds + (size_t)(((e4 * 8 + i2 + 1) * 256 + j * 64 + lane) * 16));
;                     lg[e4] = __builtin_elementwise_fma(w0, (f32x4){y[i2], y[i2], y[i2], y[i2]}, lg[e4]); lg[e4] = __builtin_elementwise_fma(w1, (f32x4){y[i2 + 1], y[i2 + 1], y[i2 + 1], y[i2 + 1]}, lg[e4]); }
	v_add_f32_e32 v38, v38, v39
	s_nop 1
	v_mov_b32_dpp v39, v38 row_shl:4 row_mask:0xf bank_mask:0x5
	v_mov_b32_dpp v39, v38 row_shr:4 row_mask:0xf bank_mask:0xa
	v_pk_add_f32 v[118:119], v[118:119], 1.0 op_sel_hi:[1,0]
	v_pk_add_f32 v[120:121], v[204:205], 1.0 op_sel_hi:[1,0]
	s_waitcnt lgkmcnt(0)
	v_add_f32_e32 v40, v38, v39
	s_nop 1
	v_mov_b32_dpp v41, v40 quad_perm:[2,3,0,1] row_mask:0xf bank_mask:0xf
	v_lshl_add_u64 v[38:39], v[58:59], 0, s[0:1]
	s_mov_b64 s[0:1], 0x7000
	s_waitcnt lgkmcnt(0)
	v_add_f32_e32 v92, v40, v41
	s_nop 1
	v_mov_b32_dpp v106, v92 quad_perm:[1,0,3,2] row_mask:0xf bank_mask:0xf
	v_lshl_add_u64 v[40:41], v[58:59], 0, s[0:1]
	s_mov_b32 s0, 0x800000
	s_waitcnt lgkmcnt(0)
	v_add_f32_e32 v92, v92, v106
	v_fmamk_f32 v92, v92, 0x3a000000, v246
	v_mul_f32_e32 v106, 0x4b800000, v92
	v_cmp_gt_f32_e32 vcc, s0, v92
	s_mov_b64 s[0:1], 0x9800
	s_nop 0
	v_cndmask_b32_e32 v92, v92, v106, vcc
	v_rsq_f32_e32 v92, v92
	v_lshl_add_u64 v[106:107], v[58:59], 0, s[0:1]
	s_mov_b64 s[0:1], 0x7800
	v_lshl_add_u64 v[108:109], v[58:59], 0, s[0:1]
	v_mul_f32_e32 v58, 0x45800000, v92
	v_cndmask_b32_e32 v92, v92, v58, vcc
	v_pk_mul_f32 v[58:59], v[92:93], v[236:237] op_sel_hi:[0,1]
	v_pk_mul_f32 v[54:55], v[54:55], v[58:59]
	v_pk_mul_f32 v[58:59], v[92:93], v[214:215] op_sel_hi:[0,1]
	v_pk_mul_f32 v[56:57], v[56:57], v[58:59]
	v_pk_fma_f32 v[54:55], v[238:239], v[54:55], v[194:195]
	v_pk_fma_f32 v[56:57], v[36:37], v[56:57], v[196:197]
	v_pk_mul_f32 v[36:37], v[92:93], v[212:213] op_sel_hi:[0,1]
	v_pk_mul_f32 v[36:37], v[46:47], v[36:37]
	v_pk_fma_f32 v[42:43], v[42:43], v[54:55], 0 op_sel_hi:[1,0,0]
	v_pk_fma_f32 v[36:37], v[34:35], v[36:37], v[198:199]
	v_pk_mul_f32 v[34:35], v[92:93], v[64:65] op_sel_hi:[0,1]
	v_pk_fma_f32 v[44:45], v[44:45], v[54:55], 0 op_sel_hi:[1,0,0]
	v_pk_mul_f32 v[34:35], v[48:49], v[34:35]
	v_pk_fma_f32 v[58:59], v[62:63], v[54:55], v[44:45] op_sel:[0,1,0]
	v_pk_fma_f32 v[60:61], v[60:61], v[54:55], v[42:43] op_sel:[0,1,0]
	v_pk_fma_f32 v[42:43], v[208:209], v[54:55], 0 op_sel_hi:[1,0,0]
	v_pk_fma_f32 v[44:45], v[210:211], v[54:55], 0 op_sel_hi:[1,0,0]
	v_pk_fma_f32 v[34:35], v[240:241], v[34:35], v[200:201]
	v_pk_fma_f32 v[62:63], v[218:219], v[54:55], v[44:45] op_sel:[0,1,0]
	v_pk_fma_f32 v[64:65], v[216:217], v[54:55], v[42:43] op_sel:[0,1,0]
	v_pk_fma_f32 v[42:43], v[220:221], v[54:55], 0 op_sel_hi:[1,0,0]
	v_pk_fma_f32 v[44:45], v[222:223], v[54:55], 0 op_sel_hi:[1,0,0]
	v_cvt_pk_bf16_f32 v46, v54, v55
	v_cvt_pk_bf16_f32 v47, v56, v57
	v_cvt_pk_bf16_f32 v48, v36, v37
	v_cvt_pk_bf16_f32 v49, v34, v35
	v_pk_fma_f32 v[194:195], v[226:227], v[54:55], v[44:45] op_sel:[0,1,0]
	v_pk_fma_f32 v[196:197], v[224:225], v[54:55], v[42:43] op_sel:[0,1,0]
	v_pk_fma_f32 v[42:43], v[228:229], v[54:55], 0 op_sel_hi:[1,0,0]
	v_pk_fma_f32 v[44:45], v[230:231], v[54:55], 0 op_sel_hi:[1,0,0]
	global_store_dwordx4 v[90:91], v[46:49], off
	v_pk_fma_f32 v[198:199], v[234:235], v[54:55], v[44:45] op_sel:[0,1,0]
	v_pk_fma_f32 v[54:55], v[232:233], v[54:55], v[42:43] op_sel:[0,1,0]
	ds_read_b128 v[42:45], v128 offset:8192
	ds_read_b128 v[46:49], v128 offset:12288
	s_waitcnt lgkmcnt(1)
	v_pk_fma_f32 v[42:43], v[42:43], v[56:57], v[60:61] op_sel_hi:[1,0,1]
	v_pk_fma_f32 v[44:45], v[44:45], v[56:57], v[58:59] op_sel_hi:[1,0,1]
	s_waitcnt lgkmcnt(0)
	v_pk_fma_f32 v[60:61], v[46:47], v[56:57], v[42:43] op_sel:[0,1,0]
	v_pk_fma_f32 v[58:59], v[48:49], v[56:57], v[44:45] op_sel:[0,1,0]
	ds_read_b128 v[42:45], v128 offset:40960
	ds_read_b128 v[46:49], v128 offset:45056
	s_waitcnt lgkmcnt(1)
	v_pk_fma_f32 v[42:43], v[42:43], v[56:57], v[64:65] op_sel_hi:[1,0,1]
	v_pk_fma_f32 v[44:45], v[44:45], v[56:57], v[62:63] op_sel_hi:[1,0,1]
	s_waitcnt lgkmcnt(0)
	v_pk_fma_f32 v[64:65], v[46:47], v[56:57], v[42:43] op_sel:[0,1,0]
	v_pk_fma_f32 v[62:63], v[48:49], v[56:57], v[44:45] op_sel:[0,1,0]
	ds_read_b128 v[42:45], v133
	ds_read_b128 v[46:49], v134
	s_waitcnt lgkmcnt(1)
	v_pk_fma_f32 v[42:43], v[42:43], v[56:57], v[196:197] op_sel_hi:[1,0,1]
	v_pk_fma_f32 v[44:45], v[44:45], v[56:57], v[194:195] op_sel_hi:[1,0,1]
	s_waitcnt lgkmcnt(0)
	v_pk_fma_f32 v[196:197], v[46:47], v[56:57], v[42:43] op_sel:[0,1,0]
	v_pk_fma_f32 v[194:195], v[48:49], v[56:57], v[44:45] op_sel:[0,1,0]
	ds_read_b128 v[42:45], v135
	ds_read_b128 v[46:49], v136
	s_waitcnt lgkmcnt(1)
	v_pk_fma_f32 v[42:43], v[42:43], v[56:57], v[54:55] op_sel_hi:[1,0,1]
	v_pk_fma_f32 v[44:45], v[44:45], v[56:57], v[198:199] op_sel_hi:[1,0,1]
	s_waitcnt lgkmcnt(0)
	v_pk_fma_f32 v[54:55], v[48:49], v[56:57], v[44:45] op_sel:[0,1,0]
	v_pk_fma_f32 v[56:57], v[46:47], v[56:57], v[42:43] op_sel:[0,1,0]
	ds_read_b128 v[42:45], v128 offset:16384
	ds_read_b128 v[46:49], v128 offset:20480
	s_waitcnt lgkmcnt(1)
	v_pk_fma_f32 v[42:43], v[42:43], v[36:37], v[60:61] op_sel_hi:[1,0,1]
	v_pk_fma_f32 v[44:45], v[44:45], v[36:37], v[58:59] op_sel_hi:[1,0,1]
	s_waitcnt lgkmcnt(0)
	v_pk_fma_f32 v[60:61], v[46:47], v[36:37], v[42:43] op_sel:[0,1,0]
	v_pk_fma_f32 v[58:59], v[48:49], v[36:37], v[44:45] op_sel:[0,1,0]
	ds_read_b128 v[42:45], v128 offset:49152
	ds_read_b128 v[46:49], v128 offset:53248
	s_waitcnt lgkmcnt(1)
	v_pk_fma_f32 v[42:43], v[42:43], v[36:37], v[64:65] op_sel_hi:[1,0,1]
	v_pk_fma_f32 v[44:45], v[44:45], v[36:37], v[62:63] op_sel_hi:[1,0,1]
	s_waitcnt lgkmcnt(0)
	v_pk_fma_f32 v[64:65], v[46:47], v[36:37], v[42:43] op_sel:[0,1,0]
	v_pk_fma_f32 v[62:63], v[48:49], v[36:37], v[44:45] op_sel:[0,1,0]
	ds_read_b128 v[42:45], v137
	ds_read_b128 v[46:49], v138
	s_waitcnt lgkmcnt(1)
	v_pk_fma_f32 v[42:43], v[42:43], v[36:37], v[196:197] op_sel_hi:[1,0,1]
	v_pk_fma_f32 v[44:45], v[44:45], v[36:37], v[194:195] op_sel_hi:[1,0,1]
	s_waitcnt lgkmcnt(0)
; #define LAS __attribute__((address_space(3)))
; __device__ __forceinline__ unsigned cvt_pk_bf16(float lo, float hi) { const f32x2 v = {lo, hi}; const bf16x2_t b = __builtin_convertvector(v, bf16x2_t); return __builtin_bit_cast(unsigned, b); }
; #define H_MLOAD(dst, jj) do { dst[0] = *(const f32x4*)(gp + (jj) * 512); dst[1] = *(const f32x4*)(gp + (jj) * 512 + 4); dst[2] = *(const f32x4*)(m + 4 * DM + (jj) * 512); dst[3] = *(const f32x4*)(m + 4 * DM + (jj) * 512 + 4); \
;             dst[4] = *(const f32x4*)(m + 3 * DM + (jj) * 512); dst[5] = *(const f32x4*)(m + 3 * DM + (jj) * 512 + 4); } while (0)
; __device__ __forceinline__ void ph_norm2_router(const Params& p, int l, LAS unsigned char* lds) {
;     ...
;         for (int j = 0; j < 4; ++j) {
;             if (j < 3) H_MLOAD(mv[(j + 1) & 1], j + 1);
;             const f32x4 ga = mv[j & 1][0], gb = mv[j & 1][1], sa = mv[j & 1][2], sb = mv[j & 1][3], ha = mv[j & 1][4], hb = mv[j & 1][5];
;             float y[8];
; #pragma unroll
;             for (int i = 0; i < 8; ++i) y[i] = x[j][i] * rinv * (i < 4 ? ga[i] : gb[i - 4]) * (1.0f + (i < 4 ? sa[i] : sb[i - 4])) + (i < 4 ? ha[i] : hb[i - 4]);
;             u32x4 h; h.x = cvt_pk_bf16(y[0], y[1]); h.y = cvt_pk_bf16(y[2], y[3]); h.z = cvt_pk_bf16(y[4], y[5]); h.w = cvt_pk_bf16(y[6], y[7]);
;             *(u32x4*)(orow + j * 512) = h;
; #pragma unroll
;             for (int i2 = 0; i2 < 8; i2 += 2) {
; #pragma unroll
;                 for (int e4 = 0; e4 < 4; ++e4) { const f32x4 w0 = *(const LAS f32x4*)(lds + (size_t)(((e4 * 8 + i2) * 256 + j * 64 + lane) * 16)); const f32x4 w1 = *(const LAS f32x4*)(lds + (size_t)(((e4 * 8 + i2 + 1) * 256 + j * 64 + lane) * 16));
;                     lg[e4] = __builtin_elementwise_fma(w0, (f32x4){y[i2], y[i2], y[i2], y[i2]}, lg[e4]); lg[e4] = __builtin_elementwise_fma(w1, (f32x4){y[i2 + 1], y[i2 + 1], y[i2 + 1], y[i2 + 1]}, lg[e4]); }
;                 __builtin_amdgcn_sched_barrier(0); } }
	v_pk_fma_f32 v[196:197], v[46:47], v[36:37], v[42:43] op_sel:[0,1,0]
	v_pk_fma_f32 v[194:195], v[48:49], v[36:37], v[44:45] op_sel:[0,1,0]
	ds_read_b128 v[42:45], v139
	ds_read_b128 v[46:49], v140
	s_waitcnt lgkmcnt(1)
	v_pk_fma_f32 v[42:43], v[42:43], v[36:37], v[56:57] op_sel_hi:[1,0,1]
	v_pk_fma_f32 v[44:45], v[44:45], v[36:37], v[54:55] op_sel_hi:[1,0,1]
	s_waitcnt lgkmcnt(0)
	v_pk_fma_f32 v[54:55], v[48:49], v[36:37], v[44:45] op_sel:[0,1,0]
	v_pk_fma_f32 v[36:37], v[46:47], v[36:37], v[42:43] op_sel:[0,1,0]
	ds_read_b128 v[42:45], v128 offset:24576
	ds_read_b128 v[46:49], v128 offset:28672
	s_waitcnt lgkmcnt(1)
	v_pk_fma_f32 v[42:43], v[42:43], v[34:35], v[60:61] op_sel_hi:[1,0,1]
	v_pk_fma_f32 v[44:45], v[44:45], v[34:35], v[58:59] op_sel_hi:[1,0,1]
	s_waitcnt lgkmcnt(0)
	v_pk_fma_f32 v[200:201], v[46:47], v[34:35], v[42:43] op_sel:[0,1,0]
	v_pk_fma_f32 v[198:199], v[48:49], v[34:35], v[44:45] op_sel:[0,1,0]
	ds_read_b128 v[42:45], v128 offset:57344
	ds_read_b128 v[46:49], v128 offset:61440
	s_waitcnt lgkmcnt(1)
	v_pk_fma_f32 v[42:43], v[42:43], v[34:35], v[64:65] op_sel_hi:[1,0,1]
	v_pk_fma_f32 v[44:45], v[44:45], v[34:35], v[62:63] op_sel_hi:[1,0,1]
	s_waitcnt lgkmcnt(0)
	v_pk_fma_f32 v[204:205], v[46:47], v[34:35], v[42:43] op_sel:[0,1,0]
	v_pk_fma_f32 v[202:203], v[48:49], v[34:35], v[44:45] op_sel:[0,1,0]
	ds_read_b128 v[42:45], v141
	ds_read_b128 v[46:49], v142
	s_waitcnt lgkmcnt(1)
	v_pk_fma_f32 v[42:43], v[42:43], v[34:35], v[196:197] op_sel_hi:[1,0,1]
	v_pk_fma_f32 v[44:45], v[44:45], v[34:35], v[194:195] op_sel_hi:[1,0,1]
	s_waitcnt lgkmcnt(0)
	v_pk_fma_f32 v[196:197], v[46:47], v[34:35], v[42:43] op_sel:[0,1,0]
	v_pk_fma_f32 v[194:195], v[48:49], v[34:35], v[44:45] op_sel:[0,1,0]
	ds_read_b128 v[42:45], v143
	ds_read_b128 v[46:49], v144
	s_waitcnt lgkmcnt(1)
	v_pk_fma_f32 v[36:37], v[42:43], v[34:35], v[36:37] op_sel_hi:[1,0,1]
	v_pk_fma_f32 v[42:43], v[44:45], v[34:35], v[54:55] op_sel_hi:[1,0,1]
	s_waitcnt lgkmcnt(0)
	v_pk_fma_f32 v[210:211], v[46:47], v[34:35], v[36:37] op_sel:[0,1,0]
	v_pk_fma_f32 v[208:209], v[48:49], v[34:35], v[42:43] op_sel:[0,1,0]
	global_load_dwordx4 v[34:37], v[76:77], off offset:16
	global_load_dwordx4 v[62:65], v[76:77], off
	global_load_dwordx4 v[58:61], v[94:95], off
	global_load_dwordx4 v[54:57], v[96:97], off
	global_load_dwordx4 v[42:45], v[38:39], off offset:16
	s_nop 0
	global_load_dwordx4 v[38:41], v[40:41], off offset:16
	v_pk_mul_f32 v[46:47], v[92:93], v[112:113] op_sel_hi:[0,1]
	v_pk_mul_f32 v[22:23], v[22:23], v[46:47]
	ds_read_b128 v[46:49], v128 offset:5120
	v_pk_fma_f32 v[112:113], v[22:23], v[118:119], v[30:31]
	v_pk_mul_f32 v[22:23], v[92:93], v[110:111] op_sel_hi:[0,1]
	v_pk_mul_f32 v[22:23], v[24:25], v[22:23]
	v_cvt_pk_bf16_f32 v24, v112, v113
	v_pk_fma_f32 v[32:33], v[22:23], v[116:117], v[32:33]
	v_pk_mul_f32 v[22:23], v[92:93], v[52:53] op_sel_hi:[0,1]
	v_pk_mul_f32 v[18:19], v[18:19], v[22:23]
	v_cvt_pk_bf16_f32 v25, v32, v33
	s_waitcnt vmcnt(7)
	v_pk_fma_f32 v[22:23], v[18:19], v[114:115], v[26:27]
	v_pk_mul_f32 v[18:19], v[92:93], v[50:51] op_sel_hi:[0,1]
	v_pk_mul_f32 v[18:19], v[20:21], v[18:19]
	v_cvt_pk_bf16_f32 v26, v22, v23
	v_pk_fma_f32 v[18:19], v[18:19], v[120:121], v[28:29]
	ds_read_b128 v[28:31], v128 offset:1024
	v_cvt_pk_bf16_f32 v27, v18, v19
	global_store_dwordx4 v[90:91], v[24:27], off offset:1024
	ds_read_b128 v[24:27], v128 offset:33792
	s_waitcnt lgkmcnt(1)
	v_pk_fma_f32 v[20:21], v[28:29], v[112:113], v[200:201] op_sel_hi:[1,0,1]
	v_pk_fma_f32 v[28:29], v[30:31], v[112:113], v[198:199] op_sel_hi:[1,0,1]
	v_pk_fma_f32 v[20:21], v[46:47], v[112:113], v[20:21] op_sel:[0,1,0]
	v_pk_fma_f32 v[50:51], v[48:49], v[112:113], v[28:29] op_sel:[0,1,0]
	ds_read_b128 v[28:31], v128 offset:37888
	ds_read_b128 v[46:49], v145
	s_waitcnt lgkmcnt(2)
	v_pk_fma_f32 v[24:25], v[24:25], v[112:113], v[204:205] op_sel_hi:[1,0,1]
	v_pk_fma_f32 v[26:27], v[26:27], v[112:113], v[202:203] op_sel_hi:[1,0,1]
	s_waitcnt lgkmcnt(1)
	v_pk_fma_f32 v[110:111], v[28:29], v[112:113], v[24:25] op_sel:[0,1,0]
	v_pk_fma_f32 v[52:53], v[30:31], v[112:113], v[26:27] op_sel:[0,1,0]
	ds_read_b128 v[24:27], v146
	ds_read_b128 v[28:31], v147
	s_waitcnt lgkmcnt(2)
	v_pk_fma_f32 v[114:115], v[46:47], v[112:113], v[196:197] op_sel_hi:[1,0,1]
	v_pk_fma_f32 v[116:117], v[48:49], v[112:113], v[194:195] op_sel_hi:[1,0,1]
	ds_read_b128 v[46:49], v148
	s_waitcnt lgkmcnt(2)
	v_pk_fma_f32 v[116:117], v[26:27], v[112:113], v[116:117] op_sel:[0,1,0]
	v_pk_fma_f32 v[114:115], v[24:25], v[112:113], v[114:115] op_sel:[0,1,0]
	s_waitcnt lgkmcnt(1)
	v_pk_fma_f32 v[24:25], v[28:29], v[112:113], v[210:211] op_sel_hi:[1,0,1]
	v_pk_fma_f32 v[26:27], v[30:31], v[112:113], v[208:209] op_sel_hi:[1,0,1]
	s_waitcnt lgkmcnt(0)
	v_pk_fma_f32 v[46:47], v[46:47], v[112:113], v[24:25] op_sel:[0,1,0]
	v_pk_fma_f32 v[48:49], v[48:49], v[112:113], v[26:27] op_sel:[0,1,0]
	ds_read_b128 v[24:27], v128 offset:9216
	ds_read_b128 v[28:31], v128 offset:13312
	s_waitcnt lgkmcnt(1)
	v_pk_fma_f32 v[20:21], v[24:25], v[32:33], v[20:21] op_sel_hi:[1,0,1]
	v_pk_fma_f32 v[24:25], v[26:27], v[32:33], v[50:51] op_sel_hi:[1,0,1]
	s_waitcnt lgkmcnt(0)
	v_pk_fma_f32 v[20:21], v[28:29], v[32:33], v[20:21] op_sel:[0,1,0]
	v_pk_fma_f32 v[50:51], v[30:31], v[32:33], v[24:25] op_sel:[0,1,0]
	ds_read_b128 v[24:27], v128 offset:41984
	ds_read_b128 v[28:31], v128 offset:46080
	s_waitcnt lgkmcnt(1)
	v_pk_fma_f32 v[24:25], v[24:25], v[32:33], v[110:111] op_sel_hi:[1,0,1]
	v_pk_fma_f32 v[26:27], v[26:27], v[32:33], v[52:53] op_sel_hi:[1,0,1]
	s_waitcnt lgkmcnt(0)
; #define LAS __attribute__((address_space(3)))
; __device__ __forceinline__ unsigned cvt_pk_bf16(float lo, float hi) { const f32x2 v = {lo, hi}; const bf16x2_t b = __builtin_convertvector(v, bf16x2_t); return __builtin_bit_cast(unsigned, b); }
; #define H_MLOAD(dst, jj) do { dst[0] = *(const f32x4*)(gp + (jj) * 512); dst[1] = *(const f32x4*)(gp + (jj) * 512 + 4); dst[2] = *(const f32x4*)(m + 4 * DM + (jj) * 512); dst[3] = *(const f32x4*)(m + 4 * DM + (jj) * 512 + 4); \
;             dst[4] = *(const f32x4*)(m + 3 * DM + (jj) * 512); dst[5] = *(const f32x4*)(m + 3 * DM + (jj) * 512 + 4); } while (0)
; __device__ __forceinline__ void ph_norm2_router(const Params& p, int l, LAS unsigned char* lds) {
;     ...
;         for (int j = 0; j < 4; ++j) {
;             if (j < 3) H_MLOAD(mv[(j + 1) & 1], j + 1);
;             const f32x4 ga = mv[j & 1][0], gb = mv[j & 1][1], sa = mv[j & 1][2], sb = mv[j & 1][3], ha = mv[j & 1][4], hb = mv[j & 1][5];
;             float y[8];
; #pragma unroll
;             for (int i = 0; i < 8; ++i) y[i] = x[j][i] * rinv * (i < 4 ? ga[i] : gb[i - 4]) * (1.0f + (i < 4 ? sa[i] : sb[i - 4])) + (i < 4 ? ha[i] : hb[i - 4]);
;             u32x4 h; h.x = cvt_pk_bf16(y[0], y[1]); h.y = cvt_pk_bf16(y[2], y[3]); h.z = cvt_pk_bf16(y[4], y[5]); h.w = cvt_pk_bf16(y[6], y[7]);
;             *(u32x4*)(orow + j * 512) = h;
; #pragma unroll
;             for (int i2 = 0; i2 < 8; i2 += 2) {
; #pragma unroll
;                 for (int e4 = 0; e4 < 4; ++e4) { const f32x4 w0 = *(const LAS f32x4*)(lds + (size_t)(((e4 * 8 + i2) * 256 + j * 64 + lane) * 16)); const f32x4 w1 = *(const LAS f32x4*)(lds + (size_t)(((e4 * 8 + i2 + 1) * 256 + j * 64 + lane) * 16));
;                     lg[e4] = __builtin_elementwise_fma(w0, (f32x4){y[i2], y[i2], y[i2], y[i2]}, lg[e4]); lg[e4] = __builtin_elementwise_fma(w1, (f32x4){y[i2 + 1], y[i2 + 1], y[i2 + 1], y[i2 + 1]}, lg[e4]); }
;                 __builtin_amdgcn_sched_barrier(0); } }
	v_pk_fma_f32 v[110:111], v[28:29], v[32:33], v[24:25] op_sel:[0,1,0]
	v_pk_fma_f32 v[52:53], v[30:31], v[32:33], v[26:27] op_sel:[0,1,0]
	ds_read_b128 v[24:27], v149
	ds_read_b128 v[28:31], v150
	s_waitcnt lgkmcnt(1)
	v_pk_fma_f32 v[24:25], v[24:25], v[32:33], v[114:115] op_sel_hi:[1,0,1]
	v_pk_fma_f32 v[26:27], v[26:27], v[32:33], v[116:117] op_sel_hi:[1,0,1]
	s_waitcnt lgkmcnt(0)
	v_pk_fma_f32 v[114:115], v[28:29], v[32:33], v[24:25] op_sel:[0,1,0]
	v_pk_fma_f32 v[112:113], v[30:31], v[32:33], v[26:27] op_sel:[0,1,0]
	ds_read_b128 v[24:27], v151
	ds_read_b128 v[28:31], v152
	s_waitcnt lgkmcnt(1)
	v_pk_fma_f32 v[24:25], v[24:25], v[32:33], v[46:47] op_sel_hi:[1,0,1]
	v_pk_fma_f32 v[26:27], v[26:27], v[32:33], v[48:49] op_sel_hi:[1,0,1]
	s_waitcnt lgkmcnt(0)
	v_pk_fma_f32 v[46:47], v[30:31], v[32:33], v[26:27] op_sel:[0,1,0]
	v_pk_fma_f32 v[32:33], v[28:29], v[32:33], v[24:25] op_sel:[0,1,0]
	ds_read_b128 v[24:27], v128 offset:17408
	ds_read_b128 v[28:31], v128 offset:21504
	s_waitcnt lgkmcnt(1)
	v_pk_fma_f32 v[20:21], v[24:25], v[22:23], v[20:21] op_sel_hi:[1,0,1]
	v_pk_fma_f32 v[24:25], v[26:27], v[22:23], v[50:51] op_sel_hi:[1,0,1]
	s_waitcnt lgkmcnt(0)
	v_pk_fma_f32 v[50:51], v[28:29], v[22:23], v[20:21] op_sel:[0,1,0]
	v_pk_fma_f32 v[48:49], v[30:31], v[22:23], v[24:25] op_sel:[0,1,0]
	ds_read_b128 v[24:27], v128 offset:50176
	ds_read_b128 v[28:31], v128 offset:54272
	s_waitcnt lgkmcnt(1)
	v_pk_fma_f32 v[20:21], v[24:25], v[22:23], v[110:111] op_sel_hi:[1,0,1]
	v_pk_fma_f32 v[24:25], v[26:27], v[22:23], v[52:53] op_sel_hi:[1,0,1]
	s_waitcnt lgkmcnt(0)
	v_pk_fma_f32 v[110:111], v[28:29], v[22:23], v[20:21] op_sel:[0,1,0]
	v_pk_fma_f32 v[52:53], v[30:31], v[22:23], v[24:25] op_sel:[0,1,0]
	ds_read_b128 v[24:27], v153
	ds_read_b128 v[28:31], v154
	s_waitcnt lgkmcnt(1)
	v_pk_fma_f32 v[20:21], v[24:25], v[22:23], v[114:115] op_sel_hi:[1,0,1]
	v_pk_fma_f32 v[24:25], v[26:27], v[22:23], v[112:113] op_sel_hi:[1,0,1]
	s_waitcnt lgkmcnt(0)
	v_pk_fma_f32 v[114:115], v[28:29], v[22:23], v[20:21] op_sel:[0,1,0]
	v_pk_fma_f32 v[112:113], v[30:31], v[22:23], v[24:25] op_sel:[0,1,0]
	ds_read_b128 v[24:27], v155
	ds_read_b128 v[28:31], v156
	s_waitcnt lgkmcnt(1)
	v_pk_fma_f32 v[20:21], v[24:25], v[22:23], v[32:33] op_sel_hi:[1,0,1]
	v_pk_fma_f32 v[24:25], v[26:27], v[22:23], v[46:47] op_sel_hi:[1,0,1]
	s_waitcnt lgkmcnt(0)
	v_pk_fma_f32 v[28:29], v[28:29], v[22:23], v[20:21] op_sel:[0,1,0]
	v_pk_fma_f32 v[30:31], v[30:31], v[22:23], v[24:25] op_sel:[0,1,0]
	ds_read_b128 v[20:23], v128 offset:25600
	ds_read_b128 v[24:27], v128 offset:29696
	s_waitcnt lgkmcnt(1)
	v_pk_fma_f32 v[20:21], v[20:21], v[18:19], v[50:51] op_sel_hi:[1,0,1]
	v_pk_fma_f32 v[22:23], v[22:23], v[18:19], v[48:49] op_sel_hi:[1,0,1]
	s_waitcnt lgkmcnt(0)
	v_pk_fma_f32 v[118:119], v[24:25], v[18:19], v[20:21] op_sel:[0,1,0]
	v_pk_fma_f32 v[116:117], v[26:27], v[18:19], v[22:23] op_sel:[0,1,0]
	ds_read_b128 v[20:23], v128 offset:58368
	ds_read_b128 v[24:27], v128 offset:62464
	s_waitcnt lgkmcnt(1)
	v_pk_fma_f32 v[20:21], v[20:21], v[18:19], v[110:111] op_sel_hi:[1,0,1]
	v_pk_fma_f32 v[22:23], v[22:23], v[18:19], v[52:53] op_sel_hi:[1,0,1]
	s_waitcnt lgkmcnt(0)
	v_pk_fma_f32 v[120:121], v[24:25], v[18:19], v[20:21] op_sel:[0,1,0]
	v_pk_fma_f32 v[110:111], v[26:27], v[18:19], v[22:23] op_sel:[0,1,0]
	ds_read_b128 v[20:23], v157
	ds_read_b128 v[24:27], v158
	s_waitcnt lgkmcnt(1)
	v_pk_fma_f32 v[20:21], v[20:21], v[18:19], v[114:115] op_sel_hi:[1,0,1]
	v_pk_fma_f32 v[22:23], v[22:23], v[18:19], v[112:113] op_sel_hi:[1,0,1]
	s_waitcnt lgkmcnt(0)
	v_pk_fma_f32 v[114:115], v[24:25], v[18:19], v[20:21] op_sel:[0,1,0]
	v_pk_fma_f32 v[112:113], v[26:27], v[18:19], v[22:23] op_sel:[0,1,0]
	ds_read_b128 v[20:23], v159
	ds_read_b128 v[24:27], v160
	s_waitcnt lgkmcnt(1)
	v_pk_fma_f32 v[20:21], v[20:21], v[18:19], v[28:29] op_sel_hi:[1,0,1]
	v_pk_fma_f32 v[22:23], v[22:23], v[18:19], v[30:31] op_sel_hi:[1,0,1]
	s_waitcnt lgkmcnt(0)
	v_pk_fma_f32 v[196:197], v[24:25], v[18:19], v[20:21] op_sel:[0,1,0]
	v_pk_fma_f32 v[194:195], v[26:27], v[18:19], v[22:23] op_sel:[0,1,0]
	global_load_dwordx4 v[18:21], v[78:79], off offset:16
	global_load_dwordx4 v[50:53], v[78:79], off
	global_load_dwordx4 v[46:49], v[94:95], off offset:2048
	global_load_dwordx4 v[30:33], v[96:97], off offset:2048
	global_load_dwordx4 v[26:29], v[106:107], off offset:16
	global_load_dwordx4 v[22:25], v[108:109], off offset:16
	v_pk_mul_f32 v[94:95], v[92:93], v[104:105] op_sel_hi:[0,1]
	s_waitcnt vmcnt(11)
	v_pk_mul_f32 v[62:63], v[94:95], v[62:63]
	s_waitcnt vmcnt(10)
	v_pk_add_f32 v[58:59], v[58:59], 1.0 op_sel_hi:[1,0]
	s_waitcnt vmcnt(8)
	v_pk_add_f32 v[42:43], v[42:43], 1.0 op_sel_hi:[1,0]
	v_pk_fma_f32 v[62:63], v[62:63], v[58:59], v[54:55]
	v_pk_mul_f32 v[54:55], v[92:93], v[102:103] op_sel_hi:[0,1]
	v_pk_mul_f32 v[54:55], v[54:55], v[64:65]
	v_pk_add_f32 v[58:59], v[60:61], 1.0 op_sel_hi:[1,0]
	s_nop 0
	v_pk_fma_f32 v[64:65], v[54:55], v[58:59], v[56:57]
	v_pk_mul_f32 v[54:55], v[92:93], v[100:101] op_sel_hi:[0,1]
	v_pk_mul_f32 v[34:35], v[54:55], v[34:35]
	ds_read_b128 v[54:57], v128 offset:2048
	ds_read_b128 v[58:61], v128 offset:6144
	s_waitcnt vmcnt(7)
	v_pk_fma_f32 v[38:39], v[34:35], v[42:43], v[38:39]
	v_pk_mul_f32 v[34:35], v[92:93], v[98:99] op_sel_hi:[0,1]
	v_pk_mul_f32 v[34:35], v[34:35], v[36:37]
	v_pk_add_f32 v[36:37], v[44:45], 1.0 op_sel_hi:[1,0]
	v_cvt_pk_bf16_f32 v42, v38, v39
	v_pk_fma_f32 v[34:35], v[34:35], v[36:37], v[40:41]
	v_cvt_pk_bf16_f32 v40, v62, v63
	v_cvt_pk_bf16_f32 v41, v64, v65
	v_cvt_pk_bf16_f32 v43, v34, v35
	global_store_dwordx4 v[90:91], v[40:43], off offset:2048
	ds_read_b128 v[40:43], v128 offset:34816
	s_waitcnt lgkmcnt(2)
; #define LAS __attribute__((address_space(3)))
; __device__ __forceinline__ void ph_norm2_router(const Params& p, int l, LAS unsigned char* lds) {
;     ...
;             for (int i2 = 0; i2 < 8; i2 += 2) {
; #pragma unroll
;                 for (int e4 = 0; e4 < 4; ++e4) { const f32x4 w0 = *(const LAS f32x4*)(lds + (size_t)(((e4 * 8 + i2) * 256 + j * 64 + lane) * 16)); const f32x4 w1 = *(const LAS f32x4*)(lds + (size_t)(((e4 * 8 + i2 + 1) * 256 + j * 64 + lane) * 16));
;                     lg[e4] = __builtin_elementwise_fma(w0, (f32x4){y[i2], y[i2], y[i2], y[i2]}, lg[e4]); lg[e4] = __builtin_elementwise_fma(w1, (f32x4){y[i2 + 1], y[i2 + 1], y[i2 + 1], y[i2 + 1]}, lg[e4]); }
;                 __builtin_amdgcn_sched_barrier(0); } }
	v_pk_fma_f32 v[36:37], v[54:55], v[62:63], v[118:119] op_sel_hi:[1,0,1]
	v_pk_fma_f32 v[44:45], v[56:57], v[62:63], v[116:117] op_sel_hi:[1,0,1]
	ds_read_b128 v[54:57], v128 offset:38912
	s_waitcnt lgkmcnt(2)
	v_pk_fma_f32 v[44:45], v[60:61], v[62:63], v[44:45] op_sel:[0,1,0]
	v_pk_fma_f32 v[36:37], v[58:59], v[62:63], v[36:37] op_sel:[0,1,0]
	ds_read_b128 v[58:61], v161
	s_waitcnt lgkmcnt(2)
	v_pk_fma_f32 v[40:41], v[40:41], v[62:63], v[120:121] op_sel_hi:[1,0,1]
	v_pk_fma_f32 v[42:43], v[42:43], v[62:63], v[110:111] op_sel_hi:[1,0,1]
	s_waitcnt lgkmcnt(1)
	v_pk_fma_f32 v[96:97], v[54:55], v[62:63], v[40:41] op_sel:[0,1,0]
	v_pk_fma_f32 v[94:95], v[56:57], v[62:63], v[42:43] op_sel:[0,1,0]
	ds_read_b128 v[40:43], v162
	ds_read_b128 v[54:57], v163
	s_waitcnt lgkmcnt(2)
	v_pk_fma_f32 v[98:99], v[58:59], v[62:63], v[114:115] op_sel_hi:[1,0,1]
	v_pk_fma_f32 v[100:101], v[60:61], v[62:63], v[112:113] op_sel_hi:[1,0,1]
	ds_read_b128 v[58:61], v164
	s_waitcnt lgkmcnt(2)
	v_pk_fma_f32 v[100:101], v[42:43], v[62:63], v[100:101] op_sel:[0,1,0]
	v_pk_fma_f32 v[98:99], v[40:41], v[62:63], v[98:99] op_sel:[0,1,0]
	s_waitcnt lgkmcnt(1)
	v_pk_fma_f32 v[40:41], v[54:55], v[62:63], v[196:197] op_sel_hi:[1,0,1]
	v_pk_fma_f32 v[42:43], v[56:57], v[62:63], v[194:195] op_sel_hi:[1,0,1]
	s_waitcnt lgkmcnt(0)
	v_pk_fma_f32 v[58:59], v[58:59], v[62:63], v[40:41] op_sel:[0,1,0]
	v_pk_fma_f32 v[60:61], v[60:61], v[62:63], v[42:43] op_sel:[0,1,0]
	ds_read_b128 v[40:43], v128 offset:10240
	ds_read_b128 v[54:57], v128 offset:14336
	s_waitcnt lgkmcnt(1)
	v_pk_fma_f32 v[36:37], v[40:41], v[64:65], v[36:37] op_sel_hi:[1,0,1]
	v_pk_fma_f32 v[40:41], v[42:43], v[64:65], v[44:45] op_sel_hi:[1,0,1]
	s_waitcnt lgkmcnt(0)
	v_pk_fma_f32 v[36:37], v[54:55], v[64:65], v[36:37] op_sel:[0,1,0]
	v_pk_fma_f32 v[44:45], v[56:57], v[64:65], v[40:41] op_sel:[0,1,0]
	ds_read_b128 v[40:43], v128 offset:43008
	ds_read_b128 v[54:57], v128 offset:47104
	s_waitcnt lgkmcnt(1)
	v_pk_fma_f32 v[40:41], v[40:41], v[64:65], v[96:97] op_sel_hi:[1,0,1]
	v_pk_fma_f32 v[42:43], v[42:43], v[64:65], v[94:95] op_sel_hi:[1,0,1]
	s_waitcnt lgkmcnt(0)
	v_pk_fma_f32 v[94:95], v[54:55], v[64:65], v[40:41] op_sel:[0,1,0]
	v_pk_fma_f32 v[62:63], v[56:57], v[64:65], v[42:43] op_sel:[0,1,0]
	ds_read_b128 v[40:43], v165
	ds_read_b128 v[54:57], v166
	s_waitcnt lgkmcnt(1)
	v_pk_fma_f32 v[40:41], v[40:41], v[64:65], v[98:99] op_sel_hi:[1,0,1]
	v_pk_fma_f32 v[42:43], v[42:43], v[64:65], v[100:101] op_sel_hi:[1,0,1]
	s_waitcnt lgkmcnt(0)
	v_pk_fma_f32 v[98:99], v[54:55], v[64:65], v[40:41] op_sel:[0,1,0]
	v_pk_fma_f32 v[96:97], v[56:57], v[64:65], v[42:43] op_sel:[0,1,0]
	ds_read_b128 v[40:43], v167
	ds_read_b128 v[54:57], v168
	s_waitcnt lgkmcnt(1)
	v_pk_fma_f32 v[40:41], v[40:41], v[64:65], v[58:59] op_sel_hi:[1,0,1]
	v_pk_fma_f32 v[42:43], v[42:43], v[64:65], v[60:61] op_sel_hi:[1,0,1]
	s_waitcnt lgkmcnt(0)
	v_pk_fma_f32 v[60:61], v[54:55], v[64:65], v[40:41] op_sel:[0,1,0]
	v_pk_fma_f32 v[58:59], v[56:57], v[64:65], v[42:43] op_sel:[0,1,0]
	ds_read_b128 v[40:43], v128 offset:18432
	ds_read_b128 v[54:57], v128 offset:22528
	s_waitcnt lgkmcnt(1)
	v_pk_fma_f32 v[36:37], v[40:41], v[38:39], v[36:37] op_sel_hi:[1,0,1]
	v_pk_fma_f32 v[40:41], v[42:43], v[38:39], v[44:45] op_sel_hi:[1,0,1]
	s_waitcnt lgkmcnt(0)
	v_pk_fma_f32 v[64:65], v[54:55], v[38:39], v[36:37] op_sel:[0,1,0]
	v_pk_fma_f32 v[44:45], v[56:57], v[38:39], v[40:41] op_sel:[0,1,0]
	ds_read_b128 v[40:43], v128 offset:51200
	ds_read_b128 v[54:57], v128 offset:55296
	s_waitcnt lgkmcnt(1)
	v_pk_fma_f32 v[36:37], v[40:41], v[38:39], v[94:95] op_sel_hi:[1,0,1]
	v_pk_fma_f32 v[40:41], v[42:43], v[38:39], v[62:63] op_sel_hi:[1,0,1]
	s_waitcnt lgkmcnt(0)
	v_pk_fma_f32 v[94:95], v[54:55], v[38:39], v[36:37] op_sel:[0,1,0]
	v_pk_fma_f32 v[62:63], v[56:57], v[38:39], v[40:41] op_sel:[0,1,0]
	ds_read_b128 v[40:43], v169
	ds_read_b128 v[54:57], v170
	s_waitcnt lgkmcnt(1)
	v_pk_fma_f32 v[36:37], v[40:41], v[38:39], v[98:99] op_sel_hi:[1,0,1]
	v_pk_fma_f32 v[40:41], v[42:43], v[38:39], v[96:97] op_sel_hi:[1,0,1]
	s_waitcnt lgkmcnt(0)
	v_pk_fma_f32 v[98:99], v[54:55], v[38:39], v[36:37] op_sel:[0,1,0]
	v_pk_fma_f32 v[96:97], v[56:57], v[38:39], v[40:41] op_sel:[0,1,0]
	ds_read_b128 v[40:43], v171
	ds_read_b128 v[54:57], v172
	s_waitcnt lgkmcnt(1)
	v_pk_fma_f32 v[36:37], v[40:41], v[38:39], v[60:61] op_sel_hi:[1,0,1]
	v_pk_fma_f32 v[40:41], v[42:43], v[38:39], v[58:59] op_sel_hi:[1,0,1]
	s_waitcnt lgkmcnt(0)
	v_pk_fma_f32 v[54:55], v[54:55], v[38:39], v[36:37] op_sel:[0,1,0]
	v_pk_fma_f32 v[56:57], v[56:57], v[38:39], v[40:41] op_sel:[0,1,0]
	ds_read_b128 v[36:39], v128 offset:26624
	ds_read_b128 v[40:43], v128 offset:30720
	s_waitcnt lgkmcnt(1)
	v_pk_fma_f32 v[36:37], v[36:37], v[34:35], v[64:65] op_sel_hi:[1,0,1]
	v_pk_fma_f32 v[38:39], v[38:39], v[34:35], v[44:45] op_sel_hi:[1,0,1]
	s_waitcnt lgkmcnt(0)
	v_pk_fma_f32 v[58:59], v[40:41], v[34:35], v[36:37] op_sel:[0,1,0]
	v_pk_fma_f32 v[44:45], v[42:43], v[34:35], v[38:39] op_sel:[0,1,0]
	ds_read_b128 v[36:39], v128 offset:59392
	ds_read_b128 v[40:43], v128 offset:63488
	s_waitcnt lgkmcnt(1)
	v_pk_fma_f32 v[36:37], v[36:37], v[34:35], v[94:95] op_sel_hi:[1,0,1]
	v_pk_fma_f32 v[38:39], v[38:39], v[34:35], v[62:63] op_sel_hi:[1,0,1]
	s_waitcnt lgkmcnt(0)
	v_pk_fma_f32 v[62:63], v[40:41], v[34:35], v[36:37] op_sel:[0,1,0]
	v_pk_fma_f32 v[60:61], v[42:43], v[34:35], v[38:39] op_sel:[0,1,0]
	ds_read_b128 v[36:39], v173
	ds_read_b128 v[40:43], v174
	s_waitcnt lgkmcnt(1)
	v_pk_fma_f32 v[36:37], v[36:37], v[34:35], v[98:99] op_sel_hi:[1,0,1]
	v_pk_fma_f32 v[38:39], v[38:39], v[34:35], v[96:97] op_sel_hi:[1,0,1]
	s_waitcnt lgkmcnt(0)
; #define LAS __attribute__((address_space(3)))
; __device__ __forceinline__ unsigned cvt_pk_bf16(float lo, float hi) { const f32x2 v = {lo, hi}; const bf16x2_t b = __builtin_convertvector(v, bf16x2_t); return __builtin_bit_cast(unsigned, b); }
; #define H_MLOAD(dst, jj) do { dst[0] = *(const f32x4*)(gp + (jj) * 512); dst[1] = *(const f32x4*)(gp + (jj) * 512 + 4); dst[2] = *(const f32x4*)(m + 4 * DM + (jj) * 512); dst[3] = *(const f32x4*)(m + 4 * DM + (jj) * 512 + 4); \
;             dst[4] = *(const f32x4*)(m + 3 * DM + (jj) * 512); dst[5] = *(const f32x4*)(m + 3 * DM + (jj) * 512 + 4); } while (0)
; __device__ __forceinline__ void ph_norm2_router(const Params& p, int l, LAS unsigned char* lds) {
;     ...
;         for (int j = 0; j < 4; ++j) {
;             if (j < 3) H_MLOAD(mv[(j + 1) & 1], j + 1);
;             const f32x4 ga = mv[j & 1][0], gb = mv[j & 1][1], sa = mv[j & 1][2], sb = mv[j & 1][3], ha = mv[j & 1][4], hb = mv[j & 1][5];
;             float y[8];
; #pragma unroll
;             for (int i = 0; i < 8; ++i) y[i] = x[j][i] * rinv * (i < 4 ? ga[i] : gb[i - 4]) * (1.0f + (i < 4 ? sa[i] : sb[i - 4])) + (i < 4 ? ha[i] : hb[i - 4]);
;             u32x4 h; h.x = cvt_pk_bf16(y[0], y[1]); h.y = cvt_pk_bf16(y[2], y[3]); h.z = cvt_pk_bf16(y[4], y[5]); h.w = cvt_pk_bf16(y[6], y[7]);
;             *(u32x4*)(orow + j * 512) = h;
; #pragma unroll
;             for (int i2 = 0; i2 < 8; i2 += 2) {
; #pragma unroll
;                 for (int e4 = 0; e4 < 4; ++e4) { const f32x4 w0 = *(const LAS f32x4*)(lds + (size_t)(((e4 * 8 + i2) * 256 + j * 64 + lane) * 16)); const f32x4 w1 = *(const LAS f32x4*)(lds + (size_t)(((e4 * 8 + i2 + 1) * 256 + j * 64 + lane) * 16));
;                     lg[e4] = __builtin_elementwise_fma(w0, (f32x4){y[i2], y[i2], y[i2], y[i2]}, lg[e4]); lg[e4] = __builtin_elementwise_fma(w1, (f32x4){y[i2 + 1], y[i2 + 1], y[i2 + 1], y[i2 + 1]}, lg[e4]); }
;                 __builtin_amdgcn_sched_barrier(0); } }
	v_pk_fma_f32 v[94:95], v[40:41], v[34:35], v[36:37] op_sel:[0,1,0]
	v_pk_fma_f32 v[64:65], v[42:43], v[34:35], v[38:39] op_sel:[0,1,0]
	ds_read_b128 v[36:39], v175
	ds_read_b128 v[40:43], v176
	s_waitcnt lgkmcnt(1)
	v_pk_fma_f32 v[36:37], v[36:37], v[34:35], v[54:55] op_sel_hi:[1,0,1]
	v_pk_fma_f32 v[38:39], v[38:39], v[34:35], v[56:57] op_sel_hi:[1,0,1]
	s_waitcnt lgkmcnt(0)
	v_pk_fma_f32 v[36:37], v[40:41], v[34:35], v[36:37] op_sel:[0,1,0]
	v_pk_fma_f32 v[38:39], v[42:43], v[34:35], v[38:39] op_sel:[0,1,0]
	v_pk_mul_f32 v[34:35], v[92:93], v[88:89] op_sel_hi:[0,1]
	s_waitcnt vmcnt(5)
	v_pk_mul_f32 v[34:35], v[34:35], v[50:51]
	s_waitcnt vmcnt(4)
	v_pk_add_f32 v[40:41], v[46:47], 1.0 op_sel_hi:[1,0]
	s_waitcnt vmcnt(2)
	v_pk_add_f32 v[26:27], v[26:27], 1.0 op_sel_hi:[1,0]
	v_pk_fma_f32 v[40:41], v[34:35], v[40:41], v[30:31]
	v_pk_mul_f32 v[30:31], v[92:93], v[86:87] op_sel_hi:[0,1]
	v_pk_mul_f32 v[30:31], v[30:31], v[52:53]
	v_pk_add_f32 v[34:35], v[48:49], 1.0 op_sel_hi:[1,0]
	s_nop 0
	v_pk_fma_f32 v[42:43], v[30:31], v[34:35], v[32:33]
	v_pk_mul_f32 v[30:31], v[92:93], v[84:85] op_sel_hi:[0,1]
	v_pk_mul_f32 v[18:19], v[30:31], v[18:19]
	ds_read_b128 v[32:35], v128 offset:7168
	s_waitcnt vmcnt(1)
	v_pk_fma_f32 v[22:23], v[18:19], v[26:27], v[22:23]
	v_pk_mul_f32 v[18:19], v[92:93], v[82:83] op_sel_hi:[0,1]
	v_pk_mul_f32 v[18:19], v[18:19], v[20:21]
	v_pk_add_f32 v[20:21], v[28:29], 1.0 op_sel_hi:[1,0]
	ds_read_b128 v[28:31], v128 offset:3072
	v_pk_fma_f32 v[18:19], v[18:19], v[20:21], v[24:25]
	v_cvt_pk_bf16_f32 v24, v40, v41
	v_cvt_pk_bf16_f32 v25, v42, v43
	v_cvt_pk_bf16_f32 v26, v22, v23
	v_cvt_pk_bf16_f32 v27, v18, v19
	global_store_dwordx4 v[90:91], v[24:27], off offset:3072
	s_waitcnt lgkmcnt(0)
	v_pk_fma_f32 v[20:21], v[28:29], v[40:41], v[58:59] op_sel_hi:[1,0,1]
	ds_read_b128 v[24:27], v128 offset:35840
	v_pk_fma_f32 v[28:29], v[30:31], v[40:41], v[44:45] op_sel_hi:[1,0,1]
	v_pk_fma_f32 v[20:21], v[32:33], v[40:41], v[20:21] op_sel:[0,1,0]
	v_pk_fma_f32 v[44:45], v[34:35], v[40:41], v[28:29] op_sel:[0,1,0]
	ds_read_b128 v[28:31], v128 offset:39936
	ds_read_b128 v[32:35], v177
	s_waitcnt lgkmcnt(2)
	v_pk_fma_f32 v[24:25], v[24:25], v[40:41], v[62:63] op_sel_hi:[1,0,1]
	v_pk_fma_f32 v[26:27], v[26:27], v[40:41], v[60:61] op_sel_hi:[1,0,1]
	s_waitcnt lgkmcnt(1)
	v_pk_fma_f32 v[48:49], v[28:29], v[40:41], v[24:25] op_sel:[0,1,0]
	v_pk_fma_f32 v[46:47], v[30:31], v[40:41], v[26:27] op_sel:[0,1,0]
	ds_read_b128 v[24:27], v178
	ds_read_b128 v[28:31], v179
	s_waitcnt lgkmcnt(2)
	v_pk_fma_f32 v[50:51], v[32:33], v[40:41], v[94:95] op_sel_hi:[1,0,1]
	v_pk_fma_f32 v[52:53], v[34:35], v[40:41], v[64:65] op_sel_hi:[1,0,1]
	ds_read_b128 v[32:35], v180
	s_waitcnt lgkmcnt(2)
	v_pk_fma_f32 v[52:53], v[26:27], v[40:41], v[52:53] op_sel:[0,1,0]
	v_pk_fma_f32 v[50:51], v[24:25], v[40:41], v[50:51] op_sel:[0,1,0]
	s_waitcnt lgkmcnt(1)
	v_pk_fma_f32 v[24:25], v[28:29], v[40:41], v[36:37] op_sel_hi:[1,0,1]
	v_pk_fma_f32 v[26:27], v[30:31], v[40:41], v[38:39] op_sel_hi:[1,0,1]
	s_waitcnt lgkmcnt(0)
	v_pk_fma_f32 v[32:33], v[32:33], v[40:41], v[24:25] op_sel:[0,1,0]
	v_pk_fma_f32 v[34:35], v[34:35], v[40:41], v[26:27] op_sel:[0,1,0]
	ds_read_b128 v[24:27], v128 offset:11264
	ds_read_b128 v[28:31], v128 offset:15360
	s_waitcnt lgkmcnt(1)
	v_pk_fma_f32 v[20:21], v[24:25], v[42:43], v[20:21] op_sel_hi:[1,0,1]
	v_pk_fma_f32 v[24:25], v[26:27], v[42:43], v[44:45] op_sel_hi:[1,0,1]
	s_waitcnt lgkmcnt(0)
	v_pk_fma_f32 v[20:21], v[28:29], v[42:43], v[20:21] op_sel:[0,1,0]
	v_pk_fma_f32 v[36:37], v[30:31], v[42:43], v[24:25] op_sel:[0,1,0]
	ds_read_b128 v[24:27], v128 offset:44032
	ds_read_b128 v[28:31], v128 offset:48128
	s_waitcnt lgkmcnt(1)
	v_pk_fma_f32 v[24:25], v[24:25], v[42:43], v[48:49] op_sel_hi:[1,0,1]
	v_pk_fma_f32 v[26:27], v[26:27], v[42:43], v[46:47] op_sel_hi:[1,0,1]
	s_waitcnt lgkmcnt(0)
	v_pk_fma_f32 v[40:41], v[28:29], v[42:43], v[24:25] op_sel:[0,1,0]
	v_pk_fma_f32 v[38:39], v[30:31], v[42:43], v[26:27] op_sel:[0,1,0]
	ds_read_b128 v[24:27], v181
	ds_read_b128 v[28:31], v182
	s_waitcnt lgkmcnt(1)
	v_pk_fma_f32 v[24:25], v[24:25], v[42:43], v[50:51] op_sel_hi:[1,0,1]
	v_pk_fma_f32 v[26:27], v[26:27], v[42:43], v[52:53] op_sel_hi:[1,0,1]
	s_waitcnt lgkmcnt(0)
	v_pk_fma_f32 v[46:47], v[28:29], v[42:43], v[24:25] op_sel:[0,1,0]
	v_pk_fma_f32 v[44:45], v[30:31], v[42:43], v[26:27] op_sel:[0,1,0]
	ds_read_b128 v[24:27], v183
	ds_read_b128 v[28:31], v184
	s_waitcnt lgkmcnt(1)
	v_pk_fma_f32 v[24:25], v[24:25], v[42:43], v[32:33] op_sel_hi:[1,0,1]
	v_pk_fma_f32 v[26:27], v[26:27], v[42:43], v[34:35] op_sel_hi:[1,0,1]
	s_waitcnt lgkmcnt(0)
	v_pk_fma_f32 v[34:35], v[28:29], v[42:43], v[24:25] op_sel:[0,1,0]
	v_pk_fma_f32 v[32:33], v[30:31], v[42:43], v[26:27] op_sel:[0,1,0]
	ds_read_b128 v[24:27], v128 offset:19456
	ds_read_b128 v[28:31], v128 offset:23552
	s_waitcnt lgkmcnt(1)
	v_pk_fma_f32 v[20:21], v[24:25], v[22:23], v[20:21] op_sel_hi:[1,0,1]
	v_pk_fma_f32 v[24:25], v[26:27], v[22:23], v[36:37] op_sel_hi:[1,0,1]
	s_waitcnt lgkmcnt(0)
	v_pk_fma_f32 v[42:43], v[28:29], v[22:23], v[20:21] op_sel:[0,1,0]
	v_pk_fma_f32 v[36:37], v[30:31], v[22:23], v[24:25] op_sel:[0,1,0]
	ds_read_b128 v[24:27], v128 offset:52224
	ds_read_b128 v[28:31], v128 offset:56320
	s_waitcnt lgkmcnt(1)
	v_pk_fma_f32 v[20:21], v[24:25], v[22:23], v[40:41] op_sel_hi:[1,0,1]
	v_pk_fma_f32 v[24:25], v[26:27], v[22:23], v[38:39] op_sel_hi:[1,0,1]
	s_waitcnt lgkmcnt(0)
	v_pk_fma_f32 v[40:41], v[28:29], v[22:23], v[20:21] op_sel:[0,1,0]
	v_pk_fma_f32 v[38:39], v[30:31], v[22:23], v[24:25] op_sel:[0,1,0]
	ds_read_b128 v[24:27], v185
	ds_read_b128 v[28:31], v186
	s_waitcnt lgkmcnt(1)
; #define LAS __attribute__((address_space(3)))
; __device__ __forceinline__ void ph_norm2_router(const Params& p, int l, LAS unsigned char* lds) {
;     ...
;                 for (int e4 = 0; e4 < 4; ++e4) { const f32x4 w0 = *(const LAS f32x4*)(lds + (size_t)(((e4 * 8 + i2) * 256 + j * 64 + lane) * 16)); const f32x4 w1 = *(const LAS f32x4*)(lds + (size_t)(((e4 * 8 + i2 + 1) * 256 + j * 64 + lane) * 16));
;                     lg[e4] = __builtin_elementwise_fma(w0, (f32x4){y[i2], y[i2], y[i2], y[i2]}, lg[e4]); lg[e4] = __builtin_elementwise_fma(w1, (f32x4){y[i2 + 1], y[i2 + 1], y[i2 + 1], y[i2 + 1]}, lg[e4]); }
;                 __builtin_amdgcn_sched_barrier(0); } }
;         float v8[8], v4[4], v2[2], v1;
; #pragma unroll
;         for (int e = 0; e < 8; ++e) { const float lo = lg[e >> 2][e & 3], hi_ = lg[(e + 8) >> 2][e & 3]; const float snd = (lane & 32) ? lo : hi_, kp = (lane & 32) ? hi_ : lo; v8[e] = kp + __shfl_xor(snd, 32); }
; #pragma unroll
;         for (int e = 0; e < 4; ++e) { const float snd = (lane & 16) ? v8[e] : v8[e + 4], kp = (lane & 16) ? v8[e + 4] : v8[e]; v4[e] = kp + __shfl_xor(snd, 16); }
; #pragma unroll
;         for (int e = 0; e < 2; ++e) { const float snd = (lane & 8) ? v4[e] : v4[e + 2], kp = (lane & 8) ? v4[e + 2] : v4[e]; v2[e] = kp + __shfl_xor(snd, 8); }
;         { const float snd = (lane & 4) ? v2[0] : v2[1], kp = (lane & 4) ? v2[1] : v2[0]; v1 = kp + __shfl_xor(snd, 4); }
;         v1 += __shfl_xor(v1, 1); v1 += __shfl_xor(v1, 2);
;         float mx = v1; mx = fmaxf(mx, __shfl_xor(mx, 4)); mx = fmaxf(mx, __shfl_xor(mx, 8)); mx = fmaxf(mx, __shfl_xor(mx, 16)); mx = fmaxf(mx, __shfl_xor(mx, 32));
;         const float ex = __expf(v1 - mx); float se = ex; se += __shfl_xor(se, 4); se += __shfl_xor(se, 8); se += __shfl_xor(se, 16); se += __shfl_xor(se, 32);
;         if ((lane & 3) == 0) ((float*)(ws + WS_AFF))[(size_t)row * 16 + (lane >> 2)] = ex / se;
	v_pk_fma_f32 v[20:21], v[24:25], v[22:23], v[46:47] op_sel_hi:[1,0,1]
	v_pk_fma_f32 v[24:25], v[26:27], v[22:23], v[44:45] op_sel_hi:[1,0,1]
	s_waitcnt lgkmcnt(0)
	v_pk_fma_f32 v[46:47], v[28:29], v[22:23], v[20:21] op_sel:[0,1,0]
	v_pk_fma_f32 v[44:45], v[30:31], v[22:23], v[24:25] op_sel:[0,1,0]
	ds_read_b128 v[24:27], v187
	ds_read_b128 v[28:31], v188
	s_waitcnt lgkmcnt(1)
	v_pk_fma_f32 v[20:21], v[24:25], v[22:23], v[34:35] op_sel_hi:[1,0,1]
	v_pk_fma_f32 v[24:25], v[26:27], v[22:23], v[32:33] op_sel_hi:[1,0,1]
	s_waitcnt lgkmcnt(0)
	v_pk_fma_f32 v[28:29], v[28:29], v[22:23], v[20:21] op_sel:[0,1,0]
	v_pk_fma_f32 v[30:31], v[30:31], v[22:23], v[24:25] op_sel:[0,1,0]
	ds_read_b128 v[20:23], v128 offset:27648
	ds_read_b128 v[24:27], v128 offset:31744
	s_waitcnt lgkmcnt(1)
	v_pk_fma_f32 v[20:21], v[20:21], v[18:19], v[42:43] op_sel_hi:[1,0,1]
	v_pk_fma_f32 v[22:23], v[22:23], v[18:19], v[36:37] op_sel_hi:[1,0,1]
	s_waitcnt lgkmcnt(0)
	v_pk_fma_f32 v[34:35], v[24:25], v[18:19], v[20:21] op_sel:[0,1,0]
	v_pk_fma_f32 v[32:33], v[26:27], v[18:19], v[22:23] op_sel:[0,1,0]
	ds_read_b128 v[20:23], v128 offset:60416
	ds_read_b128 v[24:27], v128 offset:64512
	s_waitcnt lgkmcnt(1)
	v_pk_fma_f32 v[20:21], v[20:21], v[18:19], v[40:41] op_sel_hi:[1,0,1]
	v_pk_fma_f32 v[22:23], v[22:23], v[18:19], v[38:39] op_sel_hi:[1,0,1]
	s_waitcnt lgkmcnt(0)
	v_pk_fma_f32 v[38:39], v[24:25], v[18:19], v[20:21] op_sel:[0,1,0]
	v_pk_fma_f32 v[36:37], v[26:27], v[18:19], v[22:23] op_sel:[0,1,0]
	ds_read_b128 v[20:23], v189
	ds_read_b128 v[24:27], v190
	s_waitcnt lgkmcnt(1)
	v_pk_fma_f32 v[20:21], v[20:21], v[18:19], v[46:47] op_sel_hi:[1,0,1]
	v_pk_fma_f32 v[22:23], v[22:23], v[18:19], v[44:45] op_sel_hi:[1,0,1]
	s_waitcnt lgkmcnt(0)
	v_pk_fma_f32 v[42:43], v[24:25], v[18:19], v[20:21] op_sel:[0,1,0]
	v_pk_fma_f32 v[40:41], v[26:27], v[18:19], v[22:23] op_sel:[0,1,0]
	ds_read_b128 v[20:23], v191
	ds_read_b128 v[24:27], v192
	s_waitcnt lgkmcnt(1)
	v_pk_fma_f32 v[20:21], v[20:21], v[18:19], v[28:29] op_sel_hi:[1,0,1]
	v_pk_fma_f32 v[22:23], v[22:23], v[18:19], v[30:31] op_sel_hi:[1,0,1]
	s_waitcnt lgkmcnt(0)
	v_pk_fma_f32 v[22:23], v[26:27], v[18:19], v[22:23] op_sel:[0,1,0]
	v_pk_fma_f32 v[18:19], v[24:25], v[18:19], v[20:21] op_sel:[0,1,0]
	v_cndmask_b32_e64 v20, v34, v42, s[36:37]
	ds_bpermute_b32 v20, v122, v20
	v_cndmask_b32_e64 v21, v42, v34, s[36:37]
	v_cndmask_b32_e64 v24, v43, v35, s[36:37]
	v_cndmask_b32_e64 v25, v40, v32, s[36:37]
	v_cndmask_b32_e64 v26, v41, v33, s[36:37]
	s_waitcnt lgkmcnt(0)
	v_add_f32_e32 v20, v21, v20
	v_cndmask_b32_e64 v21, v35, v43, s[36:37]
	ds_bpermute_b32 v21, v122, v21
	s_waitcnt lgkmcnt(0)
	v_add_f32_e32 v21, v24, v21
	v_cndmask_b32_e64 v24, v32, v40, s[36:37]
	ds_bpermute_b32 v24, v122, v24
	s_waitcnt lgkmcnt(0)
	v_add_f32_e32 v24, v25, v24
	v_cndmask_b32_e64 v25, v33, v41, s[36:37]
	ds_bpermute_b32 v25, v122, v25
	s_waitcnt lgkmcnt(0)
	v_add_f32_e32 v25, v26, v25
	v_cndmask_b32_e64 v26, v38, v18, s[36:37]
	ds_bpermute_b32 v26, v122, v26
	v_cndmask_b32_e64 v18, v18, v38, s[36:37]
	s_waitcnt lgkmcnt(0)
	v_add_f32_e32 v18, v18, v26
	v_cndmask_b32_e64 v26, v39, v19, s[36:37]
	ds_bpermute_b32 v26, v122, v26
	v_cndmask_b32_e64 v19, v19, v39, s[36:37]
	s_waitcnt lgkmcnt(0)
	v_add_f32_e32 v19, v19, v26
	v_cndmask_b32_e64 v26, v36, v22, s[36:37]
	ds_bpermute_b32 v26, v122, v26
	v_cndmask_b32_e64 v22, v22, v36, s[36:37]
	s_waitcnt lgkmcnt(0)
	v_add_f32_e32 v22, v22, v26
	v_cndmask_b32_e64 v26, v37, v23, s[36:37]
	ds_bpermute_b32 v26, v122, v26
	v_cndmask_b32_e64 v23, v23, v37, s[36:37]
	s_waitcnt lgkmcnt(0)
	v_add_f32_e32 v23, v23, v26
	v_cndmask_b32_e64 v26, v20, v18, s[38:39]
	v_cndmask_b32_e64 v18, v18, v20, s[38:39]
	ds_bpermute_b32 v20, v123, v26
	s_waitcnt lgkmcnt(0)
	v_add_f32_e32 v18, v18, v20
	v_cndmask_b32_e64 v20, v21, v19, s[38:39]
	ds_bpermute_b32 v20, v123, v20
	v_cndmask_b32_e64 v19, v19, v21, s[38:39]
	v_cndmask_b32_e64 v21, v22, v24, s[38:39]
	s_waitcnt lgkmcnt(0)
	v_add_f32_e32 v19, v19, v20
	v_cndmask_b32_e64 v20, v24, v22, s[38:39]
	ds_bpermute_b32 v20, v123, v20
	v_cndmask_b32_e64 v22, v23, v25, s[38:39]
	s_waitcnt lgkmcnt(0)
	v_add_f32_e32 v20, v21, v20
	v_cndmask_b32_e64 v21, v25, v23, s[38:39]
	ds_bpermute_b32 v21, v123, v21
	s_waitcnt lgkmcnt(0)
	v_add_f32_e32 v21, v22, v21
	v_cndmask_b32_e64 v22, v18, v20, s[40:41]
	v_cndmask_b32_e64 v18, v20, v18, s[40:41]
	s_nop 1
	v_mov_b32_dpp v20, v22 row_ror:8 row_mask:0xf bank_mask:0xf
	s_waitcnt lgkmcnt(0)
	v_add_f32_e32 v18, v18, v20
	v_cndmask_b32_e64 v20, v19, v21, s[40:41]
	ds_bpermute_b32 v20, v124, v20
	v_cndmask_b32_e64 v19, v21, v19, s[40:41]
	s_waitcnt lgkmcnt(0)
	v_add_f32_e32 v19, v19, v20
	v_cndmask_b32_e64 v20, v18, v19, s[42:43]
	v_cndmask_b32_e64 v18, v19, v18, s[42:43]
	s_nop 1
	v_mov_b32_dpp v19, v20 row_shl:4 row_mask:0xf bank_mask:0x5
	v_mov_b32_dpp v19, v20 row_shr:4 row_mask:0xf bank_mask:0xa
	s_waitcnt lgkmcnt(0)
	v_add_f32_e32 v18, v18, v19
	s_nop 1
	v_mov_b32_dpp v19, v18 quad_perm:[1,0,3,2] row_mask:0xf bank_mask:0xf
	s_waitcnt lgkmcnt(0)
	v_add_f32_e32 v18, v18, v19
	s_nop 1
	v_mov_b32_dpp v19, v18 quad_perm:[2,3,0,1] row_mask:0xf bank_mask:0xf
	s_waitcnt lgkmcnt(0)
	v_add_f32_e32 v18, v18, v19
	s_nop 1
	v_mov_b32_dpp v19, v18 row_shl:4 row_mask:0xf bank_mask:0x5
	v_mov_b32_dpp v19, v18 row_shr:4 row_mask:0xf bank_mask:0xa
	s_waitcnt lgkmcnt(0)
	v_max_f32_e32 v19, v19, v19
	v_max_f32_e32 v19, v18, v19
	s_nop 1
	v_mov_b32_dpp v20, v19 row_ror:8 row_mask:0xf bank_mask:0xf
	s_waitcnt lgkmcnt(0)
	v_max_f32_e32 v20, v20, v20
	v_max_f32_e32 v19, v19, v20
	v_mov_b32_e32 v20, v19
	s_nop 1
	v_permlane16_swap_b32_e32 v20, v19
	s_waitcnt lgkmcnt(0)
	v_max_f32_e32 v20, v20, v20
	v_max_f32_e32 v19, v19, v20
	v_mov_b32_e32 v20, v19
	s_nop 1
	v_permlane32_swap_b32_e32 v20, v19
	s_waitcnt lgkmcnt(0)
	v_max_f32_e32 v20, v20, v20
	v_max_f32_e32 v19, v19, v20
	v_sub_f32_e32 v18, v18, v19
	v_mul_f32_e32 v18, 0x3fb8aa3b, v18
	v_exp_f32_e32 v18, v18
	s_nop 1
	v_mov_b32_dpp v19, v18 row_shl:4 row_mask:0xf bank_mask:0x5
	v_mov_b32_dpp v19, v18 row_shr:4 row_mask:0xf bank_mask:0xa
	s_waitcnt lgkmcnt(0)
	v_add_f32_e32 v19, v18, v19
	s_nop 1
	v_mov_b32_dpp v20, v19 row_ror:8 row_mask:0xf bank_mask:0xf
	s_waitcnt lgkmcnt(0)
	v_add_f32_e32 v19, v19, v20
	v_mov_b32_e32 v20, v19
	s_nop 1
	v_permlane16_swap_b32_e32 v20, v19
	s_waitcnt lgkmcnt(0)
	v_add_f32_e32 v19, v19, v20
	ds_bpermute_b32 v20, v122, v19
	s_and_saveexec_b64 s[0:1], s[44:45]
	s_cbranch_execz .LBB0_1757
	s_waitcnt lgkmcnt(0)
	v_add_f32_e32 v19, v19, v20
	v_div_scale_f32 v20, s[14:15], v19, v19, v18
	v_rcp_f32_e32 v21, v20
	v_div_scale_f32 v22, vcc, v18, v19, v18
	v_fma_f32 v23, -v20, v21, 1.0
	v_fmac_f32_e32 v21, v23, v21
	v_mul_f32_e32 v23, v22, v21
	v_fma_f32 v24, -v20, v23, v22
	v_fmac_f32_e32 v23, v24, v21
	v_fma_f32 v20, -v20, v23, v22
	v_div_fmas_f32 v20, v20, v21, v23
	v_div_fixup_f32 v20, v20, v19, v18
	v_lshlrev_b64 v[18:19], 6, v[80:81]
	v_lshl_add_u64 v[18:19], v[74:75], 0, v[18:19]
	global_store_dword v[18:19], v20, off
	s_branch .LBB0_1757

; #define M_UNPACK(dst, v) do { dst[0] = bflo(v.x); dst[1] = bfhi(v.x); dst[2] = bflo(v.y); dst[3] = bfhi(v.y); dst[4] = bflo(v.z); dst[5] = bfhi(v.z); dst[6] = bflo(v.w); dst[7] = bfhi(v.w); } while (0)
; __device__ __forceinline__ void ph_combine(const Params& p, int l) {
;     ...
;         for (int j = 0; j < 4; ++j) { M_UNPACK(x[j], xv[j]);
; #pragma unroll
;             for (int i = 0; i < 8; ++i) s[j][i] = 0.f; }
;         unsigned msk = (unsigned)__ballot(myinv >= 0);
;         while (msk) {
;             const int e0 = __builtin_ctz(msk); msk &= msk - 1; const bool two = msk != 0u; const int e1 = two ? __builtin_ctz(msk) : e0; if (two) msk &= msk - 1;
;             const int r0 = __shfl(myinv, e0), r1 = __shfl(myinv, e1);
;             const bf16_t* y0 = YS + ((size_t)e0 * EROWS + r0) * DM + lane * 8; const bf16_t* y1 = YS + ((size_t)e1 * EROWS + r1) * DM + lane * 8;
;             u32x4 v0[4], v1[4];
; #pragma unroll
;             for (int j = 0; j < 4; ++j) { v0[j] = *(const u32x4*)(y0 + j * 512); v1[j] = *(const u32x4*)(y1 + j * 512); }
;             const float f1 = two ? 1.0f : 0.0f;
; #pragma unroll
;             for (int j = 0; j < 4; ++j) { float a[8], b[8]; M_UNPACK(a, v0[j]); M_UNPACK(b, v1[j]);
; #pragma unroll
;                 for (int i = 0; i < 8; ++i) s[j][i] += a[i] + f1 * b[i]; }
;         }
;         const float* gate = mod + (size_t)(l * 5 + rr) * 12288 + 5 * DM + lane * 8;
;         float ss = 0.f;
; #pragma unroll
;         for (int j = 0; j < 4; ++j) { const f32x4 g0 = *(const f32x4*)(gate + j * 512), g1 = *(const f32x4*)(gate + j * 512 + 4);
; #pragma unroll
;             for (int i = 0; i < 8; ++i) { x[j][i] += (i < 4 ? g0[i] : g1[i - 4]) * s[j][i]; ss += x[j][i] * x[j][i]; } }
;         ss = wave_sum(ss); const float rinv = rsqrtf(ss * (1.0f / DM) + EPS);
.LBB0_2689:
	v_lshlrev_b32_e32 v118, 16, v30
	v_and_b32_e32 v119, 0xffff0000, v30
	v_lshl_add_u32 v30, s25, 3, v124
	v_lshlrev_b32_e32 v116, 16, v32
	v_and_b32_e32 v117, 0xffff0000, v32
	v_lshlrev_b32_e32 v114, 16, v33
	v_and_b32_e32 v115, 0xffff0000, v33
	v_lshlrev_b32_e32 v32, 16, v20
	v_and_b32_e32 v33, 0xffff0000, v20
	v_min_i32_e32 v20, 0x2000, v30
	v_ashrrev_i32_e32 v120, 11, v20
	v_add_u32_e32 v20, s13, v120
	v_lshlrev_b32_e32 v98, 16, v18
	v_and_b32_e32 v99, 0xffff0000, v18
	v_lshlrev_b32_e32 v96, 16, v19
	v_and_b32_e32 v97, 0xffff0000, v19
	v_lshlrev_b32_e32 v18, 16, v21
	v_and_b32_e32 v19, 0xffff0000, v21
	v_mul_hi_i32_i24_e32 v21, 0xc000, v20
	v_mul_i32_i24_e32 v20, 0xc000, v20
	v_lshl_add_u64 v[20:21], s[2:3], 0, v[20:21]
	v_lshl_add_u64 v[122:123], v[20:21], 0, v[206:207]
	s_mov_b64 s[0:1], 0xa000
	v_lshl_add_u64 v[138:139], v[122:123], 0, s[0:1]
	s_mov_b32 s0, 0xb000
	v_add_co_u32_e32 v140, vcc, s0, v122
	v_lshlrev_b32_e32 v94, 16, v22
	s_nop 0
	v_addc_co_u32_e32 v141, vcc, 0, v123, vcc
	v_and_b32_e32 v95, 0xffff0000, v22
	v_lshlrev_b32_e32 v92, 16, v23
	v_and_b32_e32 v93, 0xffff0000, v23
	global_load_dwordx4 v[20:23], v[140:141], off offset:-4096
	global_load_dwordx4 v[134:137], v[138:139], off offset:16
	v_lshlrev_b32_e32 v108, 16, v31
	v_and_b32_e32 v109, 0xffff0000, v31
	v_lshlrev_b32_e32 v112, 16, v26
	v_and_b32_e32 v113, 0xffff0000, v26
	v_lshlrev_b32_e32 v110, 16, v27
	v_and_b32_e32 v111, 0xffff0000, v27
	v_lshlrev_b32_e32 v106, 16, v28
	v_and_b32_e32 v107, 0xffff0000, v28
	v_lshlrev_b32_e32 v104, 16, v29
	v_and_b32_e32 v105, 0xffff0000, v29
	v_lshlrev_b32_e32 v102, 16, v24
	v_and_b32_e32 v103, 0xffff0000, v24
	v_lshlrev_b32_e32 v100, 16, v25
	v_and_b32_e32 v101, 0xffff0000, v25
	s_mov_b64 s[0:1], 0xb000
	v_readlane_b32 s14, v255, 57
	v_readlane_b32 s15, v255, 58
	v_ashrrev_i32_e32 v31, 31, v30
	s_waitcnt vmcnt(1)
	v_pk_fma_f32 v[28:29], v[90:91], v[20:21], v[118:119]
	v_pk_fma_f32 v[26:27], v[88:89], v[22:23], v[108:109]
	s_waitcnt vmcnt(0)
	v_pk_fma_f32 v[24:25], v[60:61], v[134:135], v[116:117]
	v_pk_fma_f32 v[22:23], v[58:59], v[136:137], v[114:115]
	global_load_dwordx4 v[88:91], v[138:139], off offset:2064
	global_load_dwordx4 v[114:117], v[138:139], off offset:2048
	v_pk_mul_f32 v[20:21], v[28:29], v[28:29]
	v_pk_mul_f32 v[108:109], v[26:27], v[26:27]
	v_add_f32_e32 v20, v20, v21
	v_add_f32_e32 v20, v108, v20
	v_pk_mul_f32 v[60:61], v[24:25], v[24:25]
	v_add_f32_e32 v20, v109, v20
	v_add_f32_e32 v20, v60, v20
	v_pk_mul_f32 v[58:59], v[22:23], v[22:23]
	v_add_f32_e32 v20, v61, v20
	v_add_f32_e32 v20, v58, v20
	v_add_f32_e32 v20, v59, v20
	s_waitcnt vmcnt(1)
	v_pk_fma_f32 v[106:107], v[52:53], v[88:89], v[106:107]
	s_waitcnt vmcnt(0)
	v_pk_fma_f32 v[112:113], v[56:57], v[114:115], v[112:113]
	v_lshl_add_u64 v[114:115], v[122:123], 0, s[0:1]
	v_pk_fma_f32 v[110:111], v[54:55], v[116:117], v[110:111]
	v_pk_fma_f32 v[104:105], v[50:51], v[90:91], v[104:105]
	global_load_dwordx4 v[88:91], v[140:141], off
	s_nop 0
	global_load_dwordx4 v[114:117], v[114:115], off offset:16
	s_mov_b64 s[0:1], 0xb800
	v_pk_mul_f32 v[56:57], v[112:113], v[112:113]
	v_pk_mul_f32 v[54:55], v[110:111], v[110:111]
	v_add_f32_e32 v20, v56, v20
	v_add_f32_e32 v20, v57, v20
	v_add_f32_e32 v20, v54, v20
	v_pk_mul_f32 v[52:53], v[106:107], v[106:107]
	v_add_f32_e32 v20, v55, v20
	v_add_f32_e32 v20, v52, v20
	v_pk_mul_f32 v[50:51], v[104:105], v[104:105]
	v_add_f32_e32 v20, v53, v20
	v_add_f32_e32 v20, v50, v20
	v_add_f32_e32 v20, v51, v20
	s_waitcnt vmcnt(1)
	v_pk_fma_f32 v[92:93], v[46:47], v[90:91], v[92:93]
	s_waitcnt vmcnt(0)
	v_pk_fma_f32 v[90:91], v[44:45], v[114:115], v[102:103]
	v_lshl_add_u64 v[114:115], v[122:123], 0, s[0:1]
	v_pk_fma_f32 v[94:95], v[48:49], v[88:89], v[94:95]
	v_pk_fma_f32 v[88:89], v[42:43], v[116:117], v[100:101]
	global_load_dwordx4 v[100:103], v[140:141], off offset:2048
	s_nop 0
	global_load_dwordx4 v[114:117], v[114:115], off offset:16
	v_pk_mul_f32 v[48:49], v[94:95], v[94:95]
	v_pk_mul_f32 v[46:47], v[92:93], v[92:93]
	v_add_f32_e32 v20, v48, v20
	v_add_f32_e32 v20, v49, v20
	v_add_f32_e32 v20, v46, v20
	v_pk_mul_f32 v[44:45], v[90:91], v[90:91]
	v_add_f32_e32 v20, v47, v20
	v_add_f32_e32 v20, v44, v20
	v_pk_mul_f32 v[42:43], v[88:89], v[88:89]
	v_add_f32_e32 v20, v45, v20
	v_add_f32_e32 v20, v42, v20
	v_add_f32_e32 v20, v43, v20
	s_mov_b32 s0, 0x800000
	s_waitcnt vmcnt(1)
	v_pk_fma_f32 v[98:99], v[40:41], v[100:101], v[98:99]
	s_nop 0
	v_pk_mul_f32 v[40:41], v[98:99], v[98:99]
	v_pk_fma_f32 v[96:97], v[38:39], v[102:103], v[96:97]
	v_add_f32_e32 v20, v40, v20
	v_pk_mul_f32 v[38:39], v[96:97], v[96:97]
	v_add_f32_e32 v20, v41, v20
	s_waitcnt vmcnt(0)
	v_pk_fma_f32 v[102:103], v[36:37], v[114:115], v[32:33]
	v_add_f32_e32 v20, v38, v20
	v_pk_mul_f32 v[32:33], v[102:103], v[102:103]
	v_add_f32_e32 v20, v39, v20
	v_pk_fma_f32 v[100:101], v[34:35], v[116:117], v[18:19]
	v_add_f32_e32 v20, v32, v20
	v_pk_mul_f32 v[18:19], v[100:101], v[100:101]
	v_add_f32_e32 v20, v33, v20
	v_add_f32_e32 v18, v18, v20
	v_add_f32_e32 v18, v19, v18
	v_mov_b32_e32 v19, v18
	s_nop 1
	v_permlane32_swap_b32_e32 v19, v18
	s_waitcnt lgkmcnt(0)
	v_add_f32_e32 v18, v18, v19
	v_mov_b32_e32 v19, v18
	s_nop 1
	v_permlane16_swap_b32_e32 v19, v18
	s_waitcnt lgkmcnt(0)
	v_add_f32_e32 v18, v18, v19
	s_nop 1
	v_mov_b32_dpp v19, v18 row_ror:8 row_mask:0xf bank_mask:0xf
	s_waitcnt lgkmcnt(0)
	v_add_f32_e32 v18, v18, v19
	s_nop 1
	v_mov_b32_dpp v19, v18 row_shl:4 row_mask:0xf bank_mask:0x5
	v_mov_b32_dpp v19, v18 row_shr:4 row_mask:0xf bank_mask:0xa
	s_waitcnt lgkmcnt(0)
	v_add_f32_e32 v18, v18, v19
	s_nop 1
	v_mov_b32_dpp v19, v18 quad_perm:[2,3,0,1] row_mask:0xf bank_mask:0xf
	s_waitcnt lgkmcnt(0)
	v_add_f32_e32 v18, v18, v19
	s_nop 1
	v_mov_b32_dpp v19, v18 quad_perm:[1,0,3,2] row_mask:0xf bank_mask:0xf
	s_waitcnt lgkmcnt(0)
	v_add_f32_e32 v18, v18, v19
	v_fmamk_f32 v18, v18, 0x3a000000, v246
	v_cmp_gt_f32_e32 vcc, s0, v18
	v_mul_f32_e32 v19, 0x4b800000, v18
	s_mov_b64 s[0:1], -1
	v_cndmask_b32_e32 v18, v18, v19, vcc
	v_rsq_f32_e32 v18, v18
	s_nop 0
	v_mul_f32_e32 v19, 0x45800000, v18
	v_cndmask_b32_e32 v108, v18, v19, vcc
	s_and_b64 vcc, exec, s[14:15]
	s_cbranch_vccz .LBB0_2691
; __device__ __forceinline__ void ph_combine(const Params& p, int l) {
;     ...
;             float* orow = p.out + (size_t)row * DM + lane * 8; const float* g = p.in[I_FNG] + lane * 8;
;             f32x4 gq[8];
; #pragma unroll
;             for (int j = 0; j < 4; ++j) { gq[2 * j] = *(const f32x4*)(g + j * 512); gq[2 * j + 1] = *(const f32x4*)(g + j * 512 + 4); }
; #pragma unroll
;             for (int j = 0; j < 4; ++j) { const f32x4 ga = gq[2 * j], gb = gq[2 * j + 1];
;                 *(f32x4*)(orow + j * 512) = (f32x4){x[j][0] * rinv * ga[0], x[j][1] * rinv * ga[1], x[j][2] * rinv * ga[2], x[j][3] * rinv * ga[3]};
;                 *(f32x4*)(orow + j * 512 + 4) = (f32x4){x[j][4] * rinv * gb[0], x[j][5] * rinv * gb[1], x[j][6] * rinv * gb[2], x[j][7] * rinv * gb[3]}; }
	global_load_dwordx4 v[32:35], v[76:77], off offset:16
	global_load_dwordx4 v[36:39], v[76:77], off
	global_load_dwordx4 v[40:43], v[76:77], off offset:2064
	global_load_dwordx4 v[44:47], v[76:77], off offset:2048
	global_load_dwordx4 v[48:51], v[78:79], off offset:16
	global_load_dwordx4 v[52:55], v[78:79], off
	global_load_dwordx4 v[18:21], v[80:81], off offset:16
	global_load_dwordx4 v[56:59], v[80:81], off
	v_lshlrev_b64 v[60:61], 13, v[30:31]
	v_pk_mul_f32 v[114:115], v[28:29], v[108:109] op_sel_hi:[1,0]
	v_pk_mul_f32 v[116:117], v[26:27], v[108:109] op_sel_hi:[1,0]
	v_lshl_add_u64 v[60:61], v[74:75], 0, v[60:61]
	s_movk_i32 s0, 0x1000
	s_waitcnt vmcnt(6)
	v_pk_mul_f32 v[38:39], v[116:117], v[38:39]
	v_pk_mul_f32 v[36:37], v[114:115], v[36:37]
	global_store_dwordx4 v[60:61], v[36:39], off
	s_nop 1
	v_pk_mul_f32 v[36:37], v[24:25], v[108:109] op_sel_hi:[1,0]
	v_pk_mul_f32 v[38:39], v[22:23], v[108:109] op_sel_hi:[1,0]
	v_pk_mul_f32 v[32:33], v[36:37], v[32:33]
	v_pk_mul_f32 v[34:35], v[38:39], v[34:35]
	global_store_dwordx4 v[60:61], v[32:35], off offset:16
	v_add_co_u32_e32 v36, vcc, s0, v60
	s_nop 0
	v_pk_mul_f32 v[32:33], v[112:113], v[108:109] op_sel_hi:[1,0]
	v_pk_mul_f32 v[34:35], v[110:111], v[108:109] op_sel_hi:[1,0]
	s_waitcnt vmcnt(6)
	v_pk_mul_f32 v[32:33], v[32:33], v[44:45]
	v_pk_mul_f32 v[34:35], v[34:35], v[46:47]
	global_store_dwordx4 v[60:61], v[32:35], off offset:2048
	v_addc_co_u32_e32 v37, vcc, 0, v61, vcc
	s_nop 0
	v_pk_mul_f32 v[32:33], v[106:107], v[108:109] op_sel_hi:[1,0]
	v_pk_mul_f32 v[34:35], v[104:105], v[108:109] op_sel_hi:[1,0]
	v_pk_mul_f32 v[32:33], v[32:33], v[40:41]
	v_pk_mul_f32 v[34:35], v[34:35], v[42:43]
	global_store_dwordx4 v[60:61], v[32:35], off offset:2064
	s_mov_b64 s[0:1], 0
	s_nop 0
	v_pk_mul_f32 v[32:33], v[94:95], v[108:109] op_sel_hi:[1,0]
	v_pk_mul_f32 v[34:35], v[92:93], v[108:109] op_sel_hi:[1,0]
	s_waitcnt vmcnt(6)
	v_pk_mul_f32 v[32:33], v[32:33], v[52:53]
	v_pk_mul_f32 v[34:35], v[34:35], v[54:55]
	global_store_dwordx4 v[36:37], v[32:35], off
	s_nop 1
	v_pk_mul_f32 v[32:33], v[90:91], v[108:109] op_sel_hi:[1,0]
	v_pk_mul_f32 v[34:35], v[88:89], v[108:109] op_sel_hi:[1,0]
	v_pk_mul_f32 v[32:33], v[32:33], v[48:49]
	v_pk_mul_f32 v[34:35], v[34:35], v[50:51]
	global_store_dwordx4 v[36:37], v[32:35], off offset:16
	s_nop 1
	v_pk_mul_f32 v[32:33], v[98:99], v[108:109] op_sel_hi:[1,0]
	v_pk_mul_f32 v[34:35], v[96:97], v[108:109] op_sel_hi:[1,0]
	s_waitcnt vmcnt(6)
	v_pk_mul_f32 v[32:33], v[32:33], v[56:57]
	v_pk_mul_f32 v[34:35], v[34:35], v[58:59]
	global_store_dwordx4 v[36:37], v[32:35], off offset:2048
	s_nop 1
	v_pk_mul_f32 v[32:33], v[102:103], v[108:109] op_sel_hi:[1,0]
	v_pk_mul_f32 v[34:35], v[100:101], v[108:109] op_sel_hi:[1,0]
	v_pk_mul_f32 v[18:19], v[32:33], v[18:19]
	v_pk_mul_f32 v[20:21], v[34:35], v[20:21]
	global_store_dwordx4 v[36:37], v[18:21], off offset:2064
